# all packed f32 VALU ops (v_pk_mul/add/fma_f32, 2043 sites, mostly GEMM epilogues) split into two scalar f32 ops (bit-exact); plus DSA table mask and trims
# baseline (speedup 1.0000x reference)
.LBB0_27:
	s_add_u32 s16, s15, s86
	s_addc_u32 s17, s34, s87
	s_add_u32 s36, s16, 0xd0000
	s_addc_u32 s37, s17, 0
	global_load_dwordx4 v[18:21], v1, s[36:37] offset:16
	global_load_dwordx4 v[62:65], v228, s[16:17]
	v_lshl_add_u64 v[38:39], v[26:27], 0, s[86:87]
	global_load_dwordx2 v[68:69], v[38:39], off offset:-1024
	global_load_dwordx2 v[70:71], v[38:39], off offset:-512
	global_load_dwordx2 v[72:73], v[38:39], off
	global_load_dwordx2 v[74:75], v[38:39], off offset:512
	v_lshl_add_u64 v[38:39], v[36:37], 0, s[86:87]
	global_load_dwordx2 v[60:61], v[38:39], off offset:-1024
	global_load_dwordx2 v[58:59], v[38:39], off offset:-512
	global_load_dwordx2 v[56:57], v[38:39], off
	global_load_dwordx2 v[54:55], v[38:39], off offset:512
	v_lshl_add_u64 v[38:39], v[32:33], 0, s[86:87]
	global_load_dwordx2 v[52:53], v[38:39], off offset:-1024
	global_load_dwordx2 v[50:51], v[38:39], off offset:-512
	global_load_dwordx2 v[48:49], v[38:39], off
	global_load_dwordx2 v[46:47], v[38:39], off offset:512
	s_add_i32 s16, s14, 3
	s_ashr_i32 s17, s16, 31
	s_lshl_b64 s[36:37], s[16:17], 11
	v_lshl_add_u64 v[38:39], v[22:23], 0, s[36:37]
	global_load_dwordx2 v[44:45], v[38:39], off
	global_load_dwordx2 v[42:43], v[38:39], off offset:512
	global_load_dwordx2 v[40:41], v[38:39], off offset:1024
	s_nop 0
	global_load_dwordx2 v[38:39], v[38:39], off offset:1536
	s_lshl_b64 s[16:17], s[16:17], 12
	s_add_i32 s14, s14, 4
	s_add_u32 s15, s15, 32
	s_addc_u32 s34, s34, 0
	v_lshl_add_u64 v[26:27], v[26:27], 0, s[38:39]
	v_lshl_add_u64 v[32:33], v[32:33], 0, s[38:39]
	v_lshl_add_u64 v[36:37], v[36:37], 0, s[38:39]
	s_cmp_ge_i32 s14, s31
	s_waitcnt vmcnt(15)
	v_lshlrev_b32_e32 v66, 16, v68
	v_ffbh_u32_e32 v0, v63
	v_min_u32_e32 v0, 32, v0
	v_lshlrev_b64 v[62:63], v0, v[62:63]
	v_min_u32_e32 v62, 1, v62
	v_or_b32_e32 v62, v63, v62
	v_cvt_f32_u32_e32 v62, v62
	v_sub_u32_e32 v0, 32, v0
	v_and_b32_e32 v67, 0xffff0000, v68
	v_lshlrev_b32_e32 v68, 16, v69
	v_ldexp_f32 v0, v62, v0
	v_fmamk_f32 v0, v0, 0x32800000, v196
	v_cmp_gt_f32_e32 vcc, s96, v0
	v_mul_f32_e32 v62, 0x4b800000, v0
	v_and_b32_e32 v69, 0xffff0000, v69
	v_cndmask_b32_e32 v0, v0, v62, vcc
	v_rsq_f32_e32 v0, v0
	s_nop 0
	v_mul_f32_e32 v62, 0x45800000, v0
	v_cndmask_b32_e32 v0, v0, v62, vcc
	v_mul_f32_e32 v66, v0, v66
	v_mul_f32_e32 v67, v0, v67
	v_mul_f32_e32 v68, v0, v68
	v_mul_f32_e32 v69, v0, v69
	v_lshl_add_u64 v[62:63], v[30:31], 0, s[0:1]
	v_mul_f32_e32 v66, v14, v66
	v_mul_f32_e32 v67, v15, v67
	v_mul_f32_e32 v68, v16, v68
	v_mul_f32_e32 v69, v17, v69
	global_store_dwordx4 v[62:63], v[66:69], off
	v_lshl_add_u64 v[30:31], v[30:31], 0, s[40:41]
	s_waitcnt vmcnt(15)
	v_lshlrev_b32_e32 v66, 16, v70
	v_and_b32_e32 v67, 0xffff0000, v70
	v_lshlrev_b32_e32 v68, 16, v71
	v_and_b32_e32 v69, 0xffff0000, v71
	v_mul_f32_e32 v66, v0, v66
	v_mul_f32_e32 v67, v0, v67
	v_mul_f32_e32 v68, v0, v68
	v_mul_f32_e32 v69, v0, v69
	v_mul_f32_e32 v66, v10, v66
	v_mul_f32_e32 v67, v11, v67
	v_mul_f32_e32 v68, v12, v68
	v_mul_f32_e32 v69, v13, v69
	global_store_dwordx4 v[62:63], v[66:69], off offset:1024
	s_waitcnt vmcnt(15)
	s_nop 0
	v_lshlrev_b32_e32 v66, 16, v72
	v_and_b32_e32 v67, 0xffff0000, v72
	v_lshlrev_b32_e32 v68, 16, v73
	v_and_b32_e32 v69, 0xffff0000, v73
	v_mul_f32_e32 v66, v0, v66
	v_mul_f32_e32 v67, v0, v67
	v_mul_f32_e32 v68, v0, v68
	v_mul_f32_e32 v69, v0, v69
	v_mul_f32_e32 v66, v6, v66
	v_mul_f32_e32 v67, v7, v67
	v_mul_f32_e32 v68, v8, v68
	v_mul_f32_e32 v69, v9, v69
	global_store_dwordx4 v[62:63], v[66:69], off offset:2048
	s_waitcnt vmcnt(15)
	s_nop 0
	v_lshlrev_b32_e32 v66, 16, v74
	v_and_b32_e32 v67, 0xffff0000, v74
	v_lshlrev_b32_e32 v68, 16, v75
	v_and_b32_e32 v69, 0xffff0000, v75
	v_mul_f32_e32 v66, v0, v66
	v_mul_f32_e32 v67, v0, v67
	v_mul_f32_e32 v68, v0, v68
	v_mul_f32_e32 v69, v0, v69
	v_ffbh_u32_e32 v0, v65
	v_mul_f32_e32 v66, v2, v66
	v_mul_f32_e32 v67, v3, v67
	v_mul_f32_e32 v68, v4, v68
	v_mul_f32_e32 v69, v5, v69
	v_min_u32_e32 v0, 32, v0
	global_store_dwordx4 v[62:63], v[66:69], off offset:3072
	v_lshlrev_b64 v[62:63], v0, v[64:65]
	v_min_u32_e32 v62, 1, v62
	v_or_b32_e32 v62, v63, v62
	v_cvt_f32_u32_e32 v62, v62
	v_sub_u32_e32 v0, 32, v0
	s_waitcnt vmcnt(15)
	v_and_b32_e32 v63, 0xffff0000, v60
	v_lshl_add_u64 v[66:67], v[34:35], 0, s[0:1]
	v_ldexp_f32 v0, v62, v0
	v_fmamk_f32 v0, v0, 0x32800000, v196
	v_cmp_gt_f32_e32 vcc, s96, v0
	v_mul_f32_e32 v62, 0x4b800000, v0
	v_lshl_add_u64 v[34:35], v[34:35], 0, s[40:41]
	v_cndmask_b32_e32 v0, v0, v62, vcc
	v_rsq_f32_e32 v0, v0
	s_nop 0
	v_mul_f32_e32 v62, 0x45800000, v0
	v_cndmask_b32_e32 v0, v0, v62, vcc
	v_lshlrev_b32_e32 v62, 16, v60
	v_lshlrev_b32_e32 v60, 16, v61
	v_and_b32_e32 v61, 0xffff0000, v61
	v_mul_f32_e32 v60, v0, v60
	v_mul_f32_e32 v61, v0, v61
	v_mul_f32_e32 v62, v0, v62
	v_mul_f32_e32 v63, v0, v63
	v_mul_f32_e32 v64, v16, v60
	v_mul_f32_e32 v65, v17, v61
	s_waitcnt vmcnt(14)
	v_lshlrev_b32_e32 v60, 16, v58
	v_and_b32_e32 v61, 0xffff0000, v58
	v_lshlrev_b32_e32 v58, 16, v59
	v_and_b32_e32 v59, 0xffff0000, v59
	v_mul_f32_e32 v62, v14, v62
	v_mul_f32_e32 v63, v15, v63
	v_mul_f32_e32 v58, v0, v58
	v_mul_f32_e32 v59, v0, v59
	global_store_dwordx4 v[66:67], v[62:65], off
	v_mul_f32_e32 v60, v0, v60
	v_mul_f32_e32 v61, v0, v61
	v_mul_f32_e32 v60, v10, v60
	v_mul_f32_e32 v61, v11, v61
	v_mul_f32_e32 v62, v12, v58
	v_mul_f32_e32 v63, v13, v59
	s_waitcnt vmcnt(14)
	v_lshlrev_b32_e32 v58, 16, v56
	v_and_b32_e32 v59, 0xffff0000, v56
	v_lshlrev_b32_e32 v56, 16, v57
	v_and_b32_e32 v57, 0xffff0000, v57
	v_mul_f32_e32 v56, v0, v56
	v_mul_f32_e32 v57, v0, v57
	global_store_dwordx4 v[66:67], v[60:63], off offset:1024
	v_mul_f32_e32 v58, v0, v58
	v_mul_f32_e32 v59, v0, v59
	v_mul_f32_e32 v58, v6, v58
	v_mul_f32_e32 v59, v7, v59
	v_mul_f32_e32 v60, v8, v56
	v_mul_f32_e32 v61, v9, v57
	s_waitcnt vmcnt(14)
	v_lshlrev_b32_e32 v56, 16, v54
	v_and_b32_e32 v57, 0xffff0000, v54
	v_lshlrev_b32_e32 v54, 16, v55
	v_and_b32_e32 v55, 0xffff0000, v55
	v_mul_f32_e32 v56, v0, v56
	v_mul_f32_e32 v57, v0, v57
	v_mul_f32_e32 v54, v0, v54
	v_mul_f32_e32 v55, v0, v55
	v_ffbh_u32_e32 v0, v19
	v_min_u32_e32 v0, 32, v0
	v_lshlrev_b64 v[18:19], v0, v[18:19]
	v_min_u32_e32 v18, 1, v18
	v_or_b32_e32 v18, v19, v18
	v_cvt_f32_u32_e32 v18, v18
	v_sub_u32_e32 v0, 32, v0
	global_store_dwordx4 v[66:67], v[58:61], off offset:2048
	v_mul_f32_e32 v56, v2, v56
	v_mul_f32_e32 v57, v3, v57
	v_ldexp_f32 v0, v18, v0
	v_fmamk_f32 v0, v0, 0x32800000, v196
	v_cmp_gt_f32_e32 vcc, s96, v0
	v_mul_f32_e32 v18, 0x4b800000, v0
	v_mul_f32_e32 v58, v4, v54
	v_mul_f32_e32 v59, v5, v55
	v_cndmask_b32_e32 v0, v0, v18, vcc
	v_rsq_f32_e32 v0, v0
	s_waitcnt vmcnt(14)
	v_lshlrev_b32_e32 v54, 16, v52
	v_and_b32_e32 v55, 0xffff0000, v52
	v_lshlrev_b32_e32 v52, 16, v53
	v_mul_f32_e32 v18, 0x45800000, v0
	v_cndmask_b32_e32 v0, v0, v18, vcc
	v_and_b32_e32 v53, 0xffff0000, v53
	v_mul_f32_e32 v52, v0, v52
	v_mul_f32_e32 v53, v0, v53
	global_store_dwordx4 v[66:67], v[56:59], off offset:3072
	v_mul_f32_e32 v54, v0, v54
	v_mul_f32_e32 v55, v0, v55
	v_lshl_add_u64 v[18:19], v[28:29], 0, s[0:1]
	v_mul_f32_e32 v56, v16, v52
	v_mul_f32_e32 v57, v17, v53
	s_waitcnt vmcnt(14)
	v_lshlrev_b32_e32 v52, 16, v50
	v_and_b32_e32 v53, 0xffff0000, v50
	v_lshlrev_b32_e32 v50, 16, v51
	v_and_b32_e32 v51, 0xffff0000, v51
	v_mul_f32_e32 v54, v14, v54
	v_mul_f32_e32 v55, v15, v55
	v_mul_f32_e32 v50, v0, v50
	v_mul_f32_e32 v51, v0, v51
	global_store_dwordx4 v[18:19], v[54:57], off
	v_mul_f32_e32 v52, v0, v52
	v_mul_f32_e32 v53, v0, v53
	v_mul_f32_e32 v52, v10, v52
	v_mul_f32_e32 v53, v11, v53
	v_mul_f32_e32 v54, v12, v50
	v_mul_f32_e32 v55, v13, v51
	s_waitcnt vmcnt(14)
	v_lshlrev_b32_e32 v50, 16, v48
	v_and_b32_e32 v51, 0xffff0000, v48
	v_lshlrev_b32_e32 v48, 16, v49
	v_and_b32_e32 v49, 0xffff0000, v49
	v_mul_f32_e32 v48, v0, v48
	v_mul_f32_e32 v49, v0, v49
	global_store_dwordx4 v[18:19], v[52:55], off offset:1024
	v_mul_f32_e32 v50, v0, v50
	v_mul_f32_e32 v51, v0, v51
	v_mul_f32_e32 v50, v6, v50
	v_mul_f32_e32 v51, v7, v51
	v_mul_f32_e32 v52, v8, v48
	v_mul_f32_e32 v53, v9, v49
	s_waitcnt vmcnt(14)
	v_lshlrev_b32_e32 v48, 16, v46
	v_and_b32_e32 v49, 0xffff0000, v46
	v_lshlrev_b32_e32 v46, 16, v47
	v_and_b32_e32 v47, 0xffff0000, v47
	v_mul_f32_e32 v48, v0, v48
	v_mul_f32_e32 v49, v0, v49
	v_mul_f32_e32 v46, v0, v46
	v_mul_f32_e32 v47, v0, v47
	v_ffbh_u32_e32 v0, v21
	global_store_dwordx4 v[18:19], v[50:53], off offset:2048
	v_mul_f32_e32 v48, v2, v48
	v_mul_f32_e32 v49, v3, v49
	v_min_u32_e32 v0, 32, v0
	v_mul_f32_e32 v50, v4, v46
	v_mul_f32_e32 v51, v5, v47
	global_store_dwordx4 v[18:19], v[48:51], off offset:3072
	v_lshlrev_b64 v[18:19], v0, v[20:21]
	v_min_u32_e32 v18, 1, v18
	v_or_b32_e32 v18, v19, v18
	v_cvt_f32_u32_e32 v18, v18
	v_sub_u32_e32 v0, 32, v0
	s_waitcnt vmcnt(15)
	v_and_b32_e32 v19, 0xffff0000, v44
	v_lshlrev_b32_e32 v20, 16, v45
	v_ldexp_f32 v0, v18, v0
	v_fmamk_f32 v0, v0, 0x32800000, v196
	v_cmp_gt_f32_e32 vcc, s96, v0
	v_mul_f32_e32 v18, 0x4b800000, v0
	v_and_b32_e32 v21, 0xffff0000, v45
	v_cndmask_b32_e32 v0, v0, v18, vcc
	v_rsq_f32_e32 v0, v0
	v_lshl_add_u64 v[46:47], v[24:25], 0, s[16:17]
	v_lshl_add_u64 v[28:29], v[28:29], 0, s[40:41]
	v_mul_f32_e32 v18, 0x45800000, v0
	v_cndmask_b32_e32 v0, v0, v18, vcc
	v_lshlrev_b32_e32 v18, 16, v44
	v_mul_f32_e32 v18, v0, v18
	v_mul_f32_e32 v19, v0, v19
	v_mul_f32_e32 v20, v0, v20
	v_mul_f32_e32 v21, v0, v21
	v_mul_f32_e32 v18, v14, v18
	v_mul_f32_e32 v19, v15, v19
	v_mul_f32_e32 v20, v16, v20
	v_mul_f32_e32 v21, v17, v21
	global_store_dwordx4 v[46:47], v[18:21], off
	s_waitcnt vmcnt(15)
	s_nop 0
	v_lshlrev_b32_e32 v18, 16, v42
	v_and_b32_e32 v19, 0xffff0000, v42
	v_lshlrev_b32_e32 v20, 16, v43
	v_and_b32_e32 v21, 0xffff0000, v43
	v_mul_f32_e32 v18, v0, v18
	v_mul_f32_e32 v19, v0, v19
	v_mul_f32_e32 v20, v0, v20
	v_mul_f32_e32 v21, v0, v21
	v_mul_f32_e32 v18, v10, v18
	v_mul_f32_e32 v19, v11, v19
	v_mul_f32_e32 v20, v12, v20
	v_mul_f32_e32 v21, v13, v21
	global_store_dwordx4 v[46:47], v[18:21], off offset:1024
	s_waitcnt vmcnt(15)
	s_nop 0
	v_lshlrev_b32_e32 v18, 16, v40
	v_and_b32_e32 v19, 0xffff0000, v40
	v_lshlrev_b32_e32 v20, 16, v41
	v_and_b32_e32 v21, 0xffff0000, v41
	v_mul_f32_e32 v18, v0, v18
	v_mul_f32_e32 v19, v0, v19
	v_mul_f32_e32 v20, v0, v20
	v_mul_f32_e32 v21, v0, v21
	v_mul_f32_e32 v18, v6, v18
	v_mul_f32_e32 v19, v7, v19
	v_mul_f32_e32 v20, v8, v20
	v_mul_f32_e32 v21, v9, v21
	global_store_dwordx4 v[46:47], v[18:21], off offset:2048
	s_waitcnt vmcnt(15)
	s_nop 0
	v_lshlrev_b32_e32 v18, 16, v38
	v_and_b32_e32 v19, 0xffff0000, v38
	v_lshlrev_b32_e32 v20, 16, v39
	v_and_b32_e32 v21, 0xffff0000, v39
	v_mul_f32_e32 v18, v0, v18
	v_mul_f32_e32 v19, v0, v19
	v_mul_f32_e32 v20, v0, v20
	v_mul_f32_e32 v21, v0, v21
	v_mul_f32_e32 v18, v2, v18
	v_mul_f32_e32 v19, v3, v19
	v_mul_f32_e32 v20, v4, v20
	v_mul_f32_e32 v21, v5, v21
	global_store_dwordx4 v[46:47], v[18:21], off offset:3072
	s_cbranch_scc0 .LBB0_27

.LBB0_77:
	s_or_b64 exec, exec, s[64:65]
	v_lshlrev_b64 v[70:71], 2, v[74:75]
	v_lshl_add_u64 v[2:3], s[56:57], 0, v[70:71]
	v_lshl_or_b32 v0, v66, 6, v67
	global_load_dwordx4 v[66:69], v[2:3], off offset:16
	global_load_dwordx4 v[86:89], v[2:3], off
	v_lshl_add_u64 v[2:3], s[60:61], 0, v[70:71]
	v_lshl_add_u64 v[72:73], s[62:63], 0, v[70:71]
	v_lshl_add_u64 v[76:77], s[58:59], 0, v[70:71]
	global_load_dwordx4 v[62:65], v[2:3], off offset:16
	global_load_dwordx4 v[90:93], v[2:3], off
	s_nop 0
	global_load_dwordx4 v[2:5], v[72:73], off offset:16
	global_load_dwordx4 v[94:97], v[72:73], off
	s_nop 0
	global_load_dwordx4 v[70:73], v[76:77], off offset:16
	global_load_dwordx4 v[98:101], v[76:77], off
	v_lshlrev_b32_e32 v76, 16, v58
	v_and_b32_e32 v77, 0xffff0000, v58
	v_lshlrev_b32_e32 v58, 16, v59
	v_and_b32_e32 v59, 0xffff0000, v59
	s_waitcnt vmcnt(0)
	v_fma_f32 v76, v86, v76, v98
	v_fma_f32 v77, v87, v77, v99
	v_lshlrev_b32_e32 v86, 16, v14
	v_and_b32_e32 v87, 0xffff0000, v14
	v_fma_f32 v76, v90, v86, v76
	v_fma_f32 v77, v91, v87, v77
	v_lshlrev_b32_e32 v86, 16, v54
	v_and_b32_e32 v87, 0xffff0000, v54
	v_fma_f32 v76, v94, v86, v76
	v_fma_f32 v77, v95, v87, v77
	v_fma_f32 v58, v88, v58, v100
	v_fma_f32 v59, v89, v59, v101
	v_mul_f32_e32 v14, 0x3d372713, v76
	v_mul_f32_e32 v14, v76, v14
	v_fma_f32 v14, v76, v14, v76
	v_mul_f32_e32 v14, 0xc0135761, v14
	v_exp_f32_e32 v14, v14
	v_lshlrev_b32_e32 v54, 16, v55
	v_and_b32_e32 v55, 0xffff0000, v55
	v_add_f32_e32 v14, 1.0, v14
	v_rcp_f32_e32 v86, v14
	v_mul_f32_e32 v14, 0x3d372713, v77
	v_mul_f32_e32 v14, v77, v14
	v_fma_f32 v14, v77, v14, v77
	v_mul_f32_e32 v14, 0xc0135761, v14
	v_exp_f32_e32 v14, v14
	s_nop 0
	v_add_f32_e32 v14, 1.0, v14
	v_rcp_f32_e32 v87, v14
	v_lshlrev_b32_e32 v14, 16, v15
	v_and_b32_e32 v15, 0xffff0000, v15
	v_fma_f32 v14, v92, v14, v58
	v_fma_f32 v15, v93, v15, v59
	v_mul_f32_e32 v76, v76, v86
	v_mul_f32_e32 v77, v77, v87
	v_fma_f32 v14, v96, v54, v14
	v_fma_f32 v15, v97, v55, v15
	v_lshlrev_b32_e32 v86, 16, v50
	v_and_b32_e32 v87, 0xffff0000, v50
	v_mul_f32_e32 v50, 0x3d372713, v14
	v_mul_f32_e32 v50, v14, v50
	v_fma_f32 v50, v14, v50, v14
	v_mul_f32_e32 v50, 0xc0135761, v50
	v_exp_f32_e32 v50, v50
	v_mul_f32_e32 v76, v76, v86
	v_mul_f32_e32 v77, v77, v87
	v_add_f32_e32 v50, 1.0, v50
	v_rcp_f32_e32 v54, v50
	v_mul_f32_e32 v50, 0x3d372713, v15
	v_mul_f32_e32 v50, v15, v50
	v_fma_f32 v50, v15, v50, v15
	v_mul_f32_e32 v50, 0xc0135761, v50
	v_exp_f32_e32 v50, v50
	s_nop 0
	v_add_f32_e32 v50, 1.0, v50
	v_rcp_f32_e32 v55, v50
	v_lshlrev_b32_e32 v50, 16, v51
	v_and_b32_e32 v51, 0xffff0000, v51
	v_mul_f32_e32 v14, v14, v54
	v_mul_f32_e32 v15, v15, v55
	s_nop 0
	v_mul_f32_e32 v14, v14, v50
	v_mul_f32_e32 v15, v15, v51
	v_lshlrev_b32_e32 v50, 16, v60
	v_and_b32_e32 v51, 0xffff0000, v60
	v_fma_f32 v50, v66, v50, v70
	v_fma_f32 v51, v67, v51, v71
	v_lshlrev_b32_e32 v54, 16, v16
	v_and_b32_e32 v55, 0xffff0000, v16
	v_fma_f32 v50, v62, v54, v50
	v_fma_f32 v51, v63, v55, v51
	v_lshlrev_b32_e32 v54, 16, v56
	v_and_b32_e32 v55, 0xffff0000, v56
	v_fma_f32 v2, v2, v54, v50
	v_fma_f32 v3, v3, v55, v51
	s_nop 0
	v_mul_f32_e32 v16, 0x3d372713, v2
	v_mul_f32_e32 v16, v2, v16
	v_fma_f32 v16, v2, v16, v2
	v_mul_f32_e32 v16, 0xc0135761, v16
	v_exp_f32_e32 v16, v16
	s_nop 0
	v_add_f32_e32 v16, 1.0, v16
	v_rcp_f32_e32 v50, v16
	v_mul_f32_e32 v16, 0x3d372713, v3
	v_mul_f32_e32 v16, v3, v16
	v_fma_f32 v16, v3, v16, v3
	v_mul_f32_e32 v16, 0xc0135761, v16
	v_exp_f32_e32 v16, v16
	s_nop 0
	v_add_f32_e32 v16, 1.0, v16
	v_rcp_f32_e32 v51, v16
	v_lshlrev_b32_e32 v16, 16, v17
	v_and_b32_e32 v17, 0xffff0000, v17
	v_mul_f32_e32 v2, v2, v50
	v_mul_f32_e32 v3, v3, v51
	v_lshlrev_b32_e32 v50, 16, v52
	v_and_b32_e32 v51, 0xffff0000, v52
	v_mul_f32_e32 v2, v2, v50
	v_mul_f32_e32 v3, v3, v51
	v_lshlrev_b32_e32 v50, 16, v61
	v_and_b32_e32 v51, 0xffff0000, v61
	v_fma_f32 v50, v68, v50, v72
	v_fma_f32 v51, v69, v51, v73
	v_cvt_pk_bf16_f32 v52, v2, v3
	v_fma_f32 v16, v64, v16, v50
	v_fma_f32 v17, v65, v17, v51
	v_lshlrev_b32_e32 v50, 16, v57
	v_and_b32_e32 v51, 0xffff0000, v57
	v_fma_f32 v4, v4, v50, v16
	v_fma_f32 v5, v5, v51, v17
	v_mov_b64_e32 v[2:3], s[0:1]
	v_mul_f32_e32 v16, 0x3d372713, v4
	v_mul_f32_e32 v17, 0x3d372713, v5
	v_mul_f32_e32 v16, v4, v16
	v_mul_f32_e32 v17, v5, v17
	v_fma_f32 v16, v4, v16, v4
	v_fma_f32 v17, v5, v17, v5
	v_mul_f32_e32 v16, 0xc0135761, v16
	v_mul_f32_e32 v17, 0xc0135761, v17
	v_exp_f32_e32 v16, v16
	v_exp_f32_e32 v17, v17
	v_mad_i64_i32 v[2:3], s[42:43], v0, s2, v[2:3]
	v_add_f32_e32 v16, 1.0, v16
	v_add_f32_e32 v17, 1.0, v17
	v_rcp_f32_e32 v16, v16
	v_rcp_f32_e32 v17, v17
	v_cvt_pk_bf16_f32 v50, v76, v77
	v_cvt_pk_bf16_f32 v51, v14, v15
	v_lshl_add_u64 v[2:3], v[74:75], 1, v[2:3]
	v_mul_f32_e32 v4, v4, v16
	v_mul_f32_e32 v5, v5, v17
	v_lshlrev_b32_e32 v16, 16, v53
	v_and_b32_e32 v17, 0xffff0000, v53
	v_mul_f32_e32 v4, v4, v16
	v_mul_f32_e32 v5, v5, v17
	s_nop 0
	v_cvt_pk_bf16_f32 v53, v4, v5
	global_store_dwordx4 v[2:3], v[50:53], off
	s_and_saveexec_b64 s[42:43], s[40:41]
	s_cbranch_execz .LBB0_79
	v_add_u32_e32 v0, v84, v83
	v_mad_i32_i24 v2, v0, s90, v80
	v_lshl_add_u32 v58, v2, 3, v234
	v_lshrrev_b32_e32 v2, 1, v0
	v_ashrrev_i32_e32 v59, 31, v58
	v_add_u32_e32 v2, s34, v2
	v_and_b32_e32 v0, 1, v0
	v_lshlrev_b64 v[54:55], 2, v[58:59]
	v_lshl_or_b32 v0, v2, 6, v0
	v_lshl_add_u64 v[2:3], s[56:57], 0, v[54:55]
	global_load_dwordx4 v[50:53], v[2:3], off offset:16
	global_load_dwordx4 v[60:63], v[2:3], off
	v_lshl_add_u64 v[2:3], s[60:61], 0, v[54:55]
	v_lshl_add_u64 v[56:57], s[62:63], 0, v[54:55]
	v_lshl_add_u64 v[72:73], s[58:59], 0, v[54:55]
	global_load_dwordx4 v[14:17], v[2:3], off offset:16
	global_load_dwordx4 v[64:67], v[2:3], off
	s_nop 0
	global_load_dwordx4 v[2:5], v[56:57], off offset:16
	global_load_dwordx4 v[68:71], v[56:57], off
	s_nop 0
	global_load_dwordx4 v[54:57], v[72:73], off offset:16
	s_nop 0
	global_load_dwordx4 v[72:75], v[72:73], off
	v_lshlrev_b32_e32 v76, 16, v38
	v_and_b32_e32 v77, 0xffff0000, v38
	s_waitcnt vmcnt(0)
	v_fma_f32 v60, v60, v76, v72
	v_fma_f32 v61, v61, v77, v73
	v_lshlrev_b32_e32 v72, 16, v18
	v_and_b32_e32 v73, 0xffff0000, v18
	v_fma_f32 v60, v64, v72, v60
	v_fma_f32 v61, v65, v73, v61
	v_lshlrev_b32_e32 v64, 16, v26
	v_and_b32_e32 v65, 0xffff0000, v26
	v_fma_f32 v60, v68, v64, v60
	v_fma_f32 v61, v69, v65, v61
	s_nop 0
	v_mul_f32_e32 v18, 0x3d372713, v60
	v_mul_f32_e32 v18, v60, v18
	v_fma_f32 v18, v60, v18, v60
	v_mul_f32_e32 v18, 0xc0135761, v18
	v_exp_f32_e32 v18, v18
	s_nop 0
	v_add_f32_e32 v18, 1.0, v18
	v_rcp_f32_e32 v64, v18
	v_mul_f32_e32 v18, 0x3d372713, v61
	v_mul_f32_e32 v18, v61, v18
	v_fma_f32 v18, v61, v18, v61
	v_mul_f32_e32 v18, 0xc0135761, v18
	v_exp_f32_e32 v18, v18
	s_nop 0
	v_add_f32_e32 v18, 1.0, v18
	v_rcp_f32_e32 v65, v18
	v_lshlrev_b32_e32 v18, 16, v19
	v_and_b32_e32 v19, 0xffff0000, v19
	v_mul_f32_e32 v60, v60, v64
	v_mul_f32_e32 v61, v61, v65
	v_lshlrev_b32_e32 v64, 16, v46
	v_and_b32_e32 v65, 0xffff0000, v46
	v_mul_f32_e32 v60, v60, v64
	v_mul_f32_e32 v61, v61, v65
	v_lshlrev_b32_e32 v64, 16, v39
	v_and_b32_e32 v65, 0xffff0000, v39
	v_fma_f32 v62, v62, v64, v74
	v_fma_f32 v63, v63, v65, v75
	s_nop 0
	v_fma_f32 v18, v66, v18, v62
	v_fma_f32 v19, v67, v19, v63
	v_lshlrev_b32_e32 v62, 16, v27
	v_and_b32_e32 v63, 0xffff0000, v27
	v_fma_f32 v18, v70, v62, v18
	v_fma_f32 v19, v71, v63, v19
	s_nop 0
	v_mul_f32_e32 v62, 0x3d372713, v18
	v_mul_f32_e32 v63, 0x3d372713, v19
	v_mul_f32_e32 v62, v18, v62
	v_mul_f32_e32 v63, v19, v63
	v_fma_f32 v62, v18, v62, v18
	v_fma_f32 v63, v19, v63, v19
	v_mul_f32_e32 v62, 0xc0135761, v62
	v_mul_f32_e32 v63, 0xc0135761, v63
	v_exp_f32_e32 v62, v62
	v_exp_f32_e32 v63, v63
	v_add_f32_e32 v62, 1.0, v62
	v_add_f32_e32 v63, 1.0, v63
	v_rcp_f32_e32 v62, v62
	v_rcp_f32_e32 v63, v63
	s_nop 0
	v_mul_f32_e32 v18, v18, v62
	v_mul_f32_e32 v19, v19, v63
	v_lshlrev_b32_e32 v62, 16, v47
	v_and_b32_e32 v63, 0xffff0000, v47
	v_mul_f32_e32 v18, v18, v62
	v_mul_f32_e32 v19, v19, v63
	v_lshlrev_b32_e32 v62, 16, v40
	v_and_b32_e32 v63, 0xffff0000, v40
	v_fma_f32 v50, v50, v62, v54
	v_fma_f32 v51, v51, v63, v55
	v_lshlrev_b32_e32 v54, 16, v20
	v_and_b32_e32 v55, 0xffff0000, v20
	v_fma_f32 v14, v14, v54, v50
	v_fma_f32 v15, v15, v55, v51
	v_lshlrev_b32_e32 v50, 16, v28
	v_and_b32_e32 v51, 0xffff0000, v28
	v_fma_f32 v2, v2, v50, v14
	v_fma_f32 v3, v3, v51, v15
	v_lshlrev_b32_e32 v20, 16, v21
	v_mul_f32_e32 v14, 0x3d372713, v2
	v_mul_f32_e32 v15, 0x3d372713, v3
	v_mul_f32_e32 v14, v2, v14
	v_mul_f32_e32 v15, v3, v15
	v_fma_f32 v14, v2, v14, v2
	v_fma_f32 v15, v3, v15, v3
	v_mul_f32_e32 v14, 0xc0135761, v14
	v_mul_f32_e32 v15, 0xc0135761, v15
	v_exp_f32_e32 v14, v14
	v_exp_f32_e32 v15, v15
	v_and_b32_e32 v21, 0xffff0000, v21
	v_add_f32_e32 v14, 1.0, v14
	v_add_f32_e32 v15, 1.0, v15
	v_rcp_f32_e32 v14, v14
	v_rcp_f32_e32 v15, v15
	s_nop 0
	v_mul_f32_e32 v2, v2, v14
	v_mul_f32_e32 v3, v3, v15
	v_lshlrev_b32_e32 v14, 16, v48
	v_and_b32_e32 v15, 0xffff0000, v48
	v_mul_f32_e32 v2, v2, v14
	v_mul_f32_e32 v3, v3, v15
	v_lshlrev_b32_e32 v14, 16, v41
	v_and_b32_e32 v15, 0xffff0000, v41
	v_fma_f32 v14, v52, v14, v56
	v_fma_f32 v15, v53, v15, v57
	s_nop 0
	v_fma_f32 v14, v16, v20, v14
	v_fma_f32 v15, v17, v21, v15
	v_lshlrev_b32_e32 v16, 16, v29
	v_and_b32_e32 v17, 0xffff0000, v29
	v_fma_f32 v4, v4, v16, v14
	v_fma_f32 v5, v5, v17, v15
	v_cvt_pk_bf16_f32 v16, v2, v3
	v_mul_f32_e32 v14, 0x3d372713, v4
	v_mul_f32_e32 v15, 0x3d372713, v5
	v_mul_f32_e32 v14, v4, v14
	v_mul_f32_e32 v15, v5, v15
	v_fma_f32 v14, v4, v14, v4
	v_fma_f32 v15, v5, v15, v5
	v_mul_f32_e32 v14, 0xc0135761, v14
	v_mul_f32_e32 v15, 0xc0135761, v15
	v_exp_f32_e32 v14, v14
	v_exp_f32_e32 v15, v15
	v_mov_b64_e32 v[2:3], s[0:1]
	v_mad_i64_i32 v[2:3], s[40:41], v0, s2, v[2:3]
	v_add_f32_e32 v14, 1.0, v14
	v_add_f32_e32 v15, 1.0, v15
	v_rcp_f32_e32 v14, v14
	v_rcp_f32_e32 v15, v15
	v_lshl_add_u64 v[2:3], v[58:59], 1, v[2:3]
	v_mul_f32_e32 v4, v4, v14
	v_mul_f32_e32 v5, v5, v15
	v_lshlrev_b32_e32 v14, 16, v49
	v_and_b32_e32 v15, 0xffff0000, v49
	v_mul_f32_e32 v4, v4, v14
	v_mul_f32_e32 v5, v5, v15
	v_cvt_pk_bf16_f32 v14, v60, v61
	v_cvt_pk_bf16_f32 v15, v18, v19
	v_cvt_pk_bf16_f32 v17, v4, v5
	global_store_dwordx4 v[2:3], v[14:17], off
.LBB0_79:
	s_or_b64 exec, exec, s[42:43]
	s_and_saveexec_b64 s[40:41], s[38:39]
	s_cbranch_execz .LBB0_42
	v_add_u32_e32 v0, v82, v81
	v_mad_i32_i24 v2, v0, s90, v80
	v_lshl_add_u32 v54, v2, 3, v230
	v_lshrrev_b32_e32 v2, 1, v0
	v_ashrrev_i32_e32 v55, 31, v54
	v_add_u32_e32 v2, s34, v2
	v_and_b32_e32 v0, 1, v0
	v_lshlrev_b64 v[50:51], 2, v[54:55]
	v_lshl_or_b32 v0, v2, 6, v0
	v_lshl_add_u64 v[2:3], s[56:57], 0, v[50:51]
	global_load_dwordx4 v[18:21], v[2:3], off offset:16
	global_load_dwordx4 v[56:59], v[2:3], off
	v_lshl_add_u64 v[2:3], s[60:61], 0, v[50:51]
	v_lshl_add_u64 v[52:53], s[62:63], 0, v[50:51]
	v_lshl_add_u64 v[68:69], s[58:59], 0, v[50:51]
	global_load_dwordx4 v[14:17], v[2:3], off offset:16
	global_load_dwordx4 v[60:63], v[2:3], off
	s_nop 0
	global_load_dwordx4 v[2:5], v[52:53], off offset:16
	global_load_dwordx4 v[64:67], v[52:53], off
	s_nop 0
	global_load_dwordx4 v[50:53], v[68:69], off offset:16
	s_nop 0
	global_load_dwordx4 v[68:71], v[68:69], off
	v_lshlrev_b32_e32 v72, 16, v34
	v_and_b32_e32 v73, 0xffff0000, v34
	s_waitcnt vmcnt(0)
	v_fma_f32 v56, v56, v72, v68
	v_fma_f32 v57, v57, v73, v69
	v_lshlrev_b32_e32 v68, 16, v22
	v_and_b32_e32 v69, 0xffff0000, v22
	v_fma_f32 v56, v60, v68, v56
	v_fma_f32 v57, v61, v69, v57
	v_lshlrev_b32_e32 v60, 16, v30
	v_and_b32_e32 v61, 0xffff0000, v30
	v_fma_f32 v56, v64, v60, v56
	v_fma_f32 v57, v65, v61, v57
	s_nop 0
	v_mul_f32_e32 v22, 0x3d372713, v56
	v_mul_f32_e32 v22, v56, v22
	v_fma_f32 v22, v56, v22, v56
	v_mul_f32_e32 v22, 0xc0135761, v22
	v_exp_f32_e32 v22, v22
	s_nop 0
	v_add_f32_e32 v22, 1.0, v22
	v_rcp_f32_e32 v60, v22
	v_mul_f32_e32 v22, 0x3d372713, v57
	v_mul_f32_e32 v22, v57, v22
	v_fma_f32 v22, v57, v22, v57
	v_mul_f32_e32 v22, 0xc0135761, v22
	v_exp_f32_e32 v22, v22
	s_nop 0
	v_add_f32_e32 v22, 1.0, v22
	v_rcp_f32_e32 v61, v22
	v_lshlrev_b32_e32 v22, 16, v23
	v_and_b32_e32 v23, 0xffff0000, v23
	v_mul_f32_e32 v56, v56, v60
	v_mul_f32_e32 v57, v57, v61
	v_lshlrev_b32_e32 v60, 16, v42
	v_and_b32_e32 v61, 0xffff0000, v42
	v_mul_f32_e32 v56, v56, v60
	v_mul_f32_e32 v57, v57, v61
	v_lshlrev_b32_e32 v60, 16, v35
	v_and_b32_e32 v61, 0xffff0000, v35
	v_fma_f32 v58, v58, v60, v70
	v_fma_f32 v59, v59, v61, v71
	s_nop 0
	v_fma_f32 v22, v62, v22, v58
	v_fma_f32 v23, v63, v23, v59
	v_lshlrev_b32_e32 v58, 16, v31
	v_and_b32_e32 v59, 0xffff0000, v31
	v_fma_f32 v22, v66, v58, v22
	v_fma_f32 v23, v67, v59, v23
	s_nop 0
	v_mul_f32_e32 v58, 0x3d372713, v22
	v_mul_f32_e32 v59, 0x3d372713, v23
	v_mul_f32_e32 v58, v22, v58
	v_mul_f32_e32 v59, v23, v59
	v_fma_f32 v58, v22, v58, v22
	v_fma_f32 v59, v23, v59, v23
	v_mul_f32_e32 v58, 0xc0135761, v58
	v_mul_f32_e32 v59, 0xc0135761, v59
	v_exp_f32_e32 v58, v58
	v_exp_f32_e32 v59, v59
	v_add_f32_e32 v58, 1.0, v58
	v_add_f32_e32 v59, 1.0, v59
	v_rcp_f32_e32 v58, v58
	v_rcp_f32_e32 v59, v59
	s_nop 0
	v_mul_f32_e32 v22, v22, v58
	v_mul_f32_e32 v23, v23, v59
	v_lshlrev_b32_e32 v58, 16, v43
	v_and_b32_e32 v59, 0xffff0000, v43
	v_mul_f32_e32 v22, v22, v58
	v_mul_f32_e32 v23, v23, v59
	v_lshlrev_b32_e32 v58, 16, v36
	v_and_b32_e32 v59, 0xffff0000, v36
	v_fma_f32 v18, v18, v58, v50
	v_fma_f32 v19, v19, v59, v51
	v_lshlrev_b32_e32 v50, 16, v24
	v_and_b32_e32 v51, 0xffff0000, v24
	v_fma_f32 v14, v14, v50, v18
	v_fma_f32 v15, v15, v51, v19
	v_lshlrev_b32_e32 v18, 16, v32
	v_and_b32_e32 v19, 0xffff0000, v32
	v_fma_f32 v2, v2, v18, v14
	v_fma_f32 v3, v3, v19, v15
	v_lshlrev_b32_e32 v18, 16, v25
	v_mul_f32_e32 v14, 0x3d372713, v2
	v_mul_f32_e32 v15, 0x3d372713, v3
	v_mul_f32_e32 v14, v2, v14
	v_mul_f32_e32 v15, v3, v15
	v_fma_f32 v14, v2, v14, v2
	v_fma_f32 v15, v3, v15, v3
	v_mul_f32_e32 v14, 0xc0135761, v14
	v_mul_f32_e32 v15, 0xc0135761, v15
	v_exp_f32_e32 v14, v14
	v_exp_f32_e32 v15, v15
	v_and_b32_e32 v19, 0xffff0000, v25
	v_add_f32_e32 v14, 1.0, v14
	v_add_f32_e32 v15, 1.0, v15
	v_rcp_f32_e32 v14, v14
	v_rcp_f32_e32 v15, v15
	s_nop 0
	v_mul_f32_e32 v2, v2, v14
	v_mul_f32_e32 v3, v3, v15
	v_lshlrev_b32_e32 v14, 16, v44
	v_and_b32_e32 v15, 0xffff0000, v44
	v_mul_f32_e32 v2, v2, v14
	v_mul_f32_e32 v3, v3, v15
	v_lshlrev_b32_e32 v14, 16, v37
	v_and_b32_e32 v15, 0xffff0000, v37
	v_fma_f32 v14, v20, v14, v52
	v_fma_f32 v15, v21, v15, v53
	s_nop 0
	v_fma_f32 v14, v16, v18, v14
	v_fma_f32 v15, v17, v19, v15
	v_lshlrev_b32_e32 v16, 16, v33
	v_and_b32_e32 v17, 0xffff0000, v33
	v_fma_f32 v4, v4, v16, v14
	v_fma_f32 v5, v5, v17, v15
	v_cvt_pk_bf16_f32 v16, v2, v3
	v_mul_f32_e32 v14, 0x3d372713, v4
	v_mul_f32_e32 v15, 0x3d372713, v5
	v_mul_f32_e32 v14, v4, v14
	v_mul_f32_e32 v15, v5, v15
	v_fma_f32 v14, v4, v14, v4
	v_fma_f32 v15, v5, v15, v5
	v_mul_f32_e32 v14, 0xc0135761, v14
	v_mul_f32_e32 v15, 0xc0135761, v15
	v_exp_f32_e32 v14, v14
	v_exp_f32_e32 v15, v15
	v_mov_b64_e32 v[2:3], s[0:1]
	v_mad_i64_i32 v[2:3], s[38:39], v0, s2, v[2:3]
	v_add_f32_e32 v14, 1.0, v14
	v_add_f32_e32 v15, 1.0, v15
	v_rcp_f32_e32 v14, v14
	v_rcp_f32_e32 v15, v15
	v_lshl_add_u64 v[2:3], v[54:55], 1, v[2:3]
	v_mul_f32_e32 v4, v4, v14
	v_mul_f32_e32 v5, v5, v15
	v_lshlrev_b32_e32 v14, 16, v45
	v_and_b32_e32 v15, 0xffff0000, v45
	v_mul_f32_e32 v4, v4, v14
	v_mul_f32_e32 v5, v5, v15
	v_cvt_pk_bf16_f32 v14, v56, v57
	v_cvt_pk_bf16_f32 v15, v22, v23
	v_cvt_pk_bf16_f32 v17, v4, v5
	global_store_dwordx4 v[2:3], v[14:17], off
	s_branch .LBB0_42

.LBB0_105:
	s_add_u32 s16, s74, 0x2200000
	v_readlane_b32 s0, v253, 39
	s_addc_u32 s17, s75, 0
	v_readlane_b32 s1, v253, 40
	s_and_b64 s[0:1], s[0:1], exec
	v_readlane_b32 s0, v253, 34
	s_cselect_b32 s14, s0, s16
	s_mov_b32 s0, -1
	v_readlane_b32 s1, v253, 35
	s_waitcnt vmcnt(0)
	s_barrier
	s_cselect_b32 s15, s1, s17
	v_mbcnt_lo_u32_b32 v0, s0, 0
	v_mbcnt_hi_u32_b32 v170, s0, v0
	s_ashr_i32 s39, s38, 31
	s_lshl_b32 s1, s62, 5
	s_lshl_b64 s[34:35], s[38:39], 8
	v_lshrrev_b32_e32 v0, 1, v170
	s_lshl_b32 s0, s91, 8
	s_or_b32 s34, s34, s1
	v_and_b32_e32 v0, 56, v0
	v_and_b32_e32 v131, 64, v231
	v_and_b32_e32 v130, 15, v170
	s_add_i32 s29, s0, s63
	v_lshl_add_u64 v[158:159], s[34:35], 0, v[0:1]
	v_xor_b32_e32 v0, 16, v231
	v_add_u32_e32 v131, 64, v131
	v_or_b32_e32 v160, s29, v130
	v_cmp_lt_i32_e32 vcc, v0, v131
	v_lshlrev_b64 v[176:177], 1, v[158:159]
	v_ashrrev_i32_e32 v161, 31, v160
	v_cndmask_b32_e32 v0, v231, v0, vcc
	v_lshlrev_b32_e32 v171, 2, v0
	v_xor_b32_e32 v0, 32, v231
	v_lshl_add_u64 v[162:163], s[16:17], 0, v[176:177]
	v_lshlrev_b64 v[178:179], 11, v[160:161]
	v_cmp_lt_i32_e32 vcc, v0, v131
	v_or_b32_e32 v182, s63, v130
	v_lshl_add_u64 v[130:131], v[162:163], 0, v[178:179]
	global_load_dwordx4 v[172:175], v[130:131], off
	global_load_dwordx4 v[154:157], v[130:131], off offset:256
	v_or_b32_e32 v130, 16, v160
	v_ashrrev_i32_e32 v131, 31, v130
	v_lshlrev_b64 v[168:169], 11, v[130:131]
	v_lshl_add_u64 v[130:131], v[162:163], 0, v[168:169]
	global_load_dwordx4 v[150:153], v[130:131], off
	global_load_dwordx4 v[146:149], v[130:131], off offset:256
	v_or_b32_e32 v130, 32, v160
	v_ashrrev_i32_e32 v131, 31, v130
	v_lshlrev_b64 v[166:167], 11, v[130:131]
	v_lshl_add_u64 v[130:131], v[162:163], 0, v[166:167]
	global_load_dwordx4 v[142:145], v[130:131], off
	global_load_dwordx4 v[138:141], v[130:131], off offset:256
	v_or_b32_e32 v130, 48, v160
	v_ashrrev_i32_e32 v131, 31, v130
	v_lshlrev_b64 v[164:165], 11, v[130:131]
	v_lshl_add_u64 v[130:131], v[162:163], 0, v[164:165]
	global_load_dwordx4 v[134:137], v[130:131], off
	s_nop 0
	global_load_dwordx4 v[130:133], v[130:131], off offset:256
	v_lshl_add_u64 v[178:179], s[14:15], 0, v[178:179]
	v_lshl_add_u64 v[176:177], v[178:179], 0, v[176:177]
	v_cndmask_b32_e32 v0, v231, v0, vcc
	v_lshlrev_b32_e32 v0, 2, v0
	s_lshl_b32 s1, s62, 2
	v_cmp_gt_u32_e32 vcc, 16, v170
	s_waitcnt vmcnt(0)
	v_lshlrev_b32_e32 v180, 16, v172
	v_and_b32_e32 v181, 0xffff0000, v172
	v_lshlrev_b32_e32 v172, 16, v173
	v_and_b32_e32 v173, 0xffff0000, v173
	v_add_f32_e32 v128, v128, v172
	v_add_f32_e32 v129, v129, v173
	v_lshlrev_b32_e32 v172, 16, v174
	v_and_b32_e32 v173, 0xffff0000, v174
	v_add_f32_e32 v172, v122, v172
	v_add_f32_e32 v173, v123, v173
	v_lshlrev_b32_e32 v122, 16, v175
	v_and_b32_e32 v123, 0xffff0000, v175
	v_add_f32_e32 v126, v126, v180
	v_add_f32_e32 v127, v127, v181
	v_add_f32_e32 v174, v124, v122
	v_add_f32_e32 v175, v125, v123
	v_cvt_pk_bf16_f32 v122, v126, v127
	v_cvt_pk_bf16_f32 v123, v128, v129
	v_cvt_pk_bf16_f32 v124, v172, v173
	v_cvt_pk_bf16_f32 v125, v174, v175
	global_store_dwordx4 v[176:177], v[122:125], off
	s_nop 1
	v_mul_f32_e32 v122, v126, v126
	v_mul_f32_e32 v123, v127, v127
	v_mul_f32_e32 v126, v172, v172
	v_mul_f32_e32 v127, v173, v173
	v_lshlrev_b32_e32 v172, 16, v154
	v_and_b32_e32 v173, 0xffff0000, v154
	v_lshlrev_b32_e32 v154, 16, v155
	v_and_b32_e32 v155, 0xffff0000, v155
	v_add_f32_e32 v120, v120, v154
	v_add_f32_e32 v121, v121, v155
	v_lshlrev_b32_e32 v154, 16, v156
	v_and_b32_e32 v155, 0xffff0000, v156
	v_add_f32_e32 v154, v114, v154
	v_add_f32_e32 v155, v115, v155
	v_lshlrev_b32_e32 v114, 16, v157
	v_and_b32_e32 v115, 0xffff0000, v157
	v_add_f32_e32 v118, v118, v172
	v_add_f32_e32 v119, v119, v173
	v_add_f32_e32 v156, v116, v114
	v_add_f32_e32 v157, v117, v115
	v_cvt_pk_bf16_f32 v114, v118, v119
	v_cvt_pk_bf16_f32 v115, v120, v121
	v_cvt_pk_bf16_f32 v116, v154, v155
	v_cvt_pk_bf16_f32 v117, v156, v157
	global_store_dwordx4 v[176:177], v[114:117], off offset:256
	v_mul_f32_e32 v124, v128, v128
	v_mul_f32_e32 v125, v129, v129
	v_mul_f32_e32 v128, v174, v174
	v_mul_f32_e32 v129, v175, v175
	v_mul_f32_e32 v114, v118, v118
	v_mul_f32_e32 v115, v119, v119
	v_mul_f32_e32 v116, v120, v120
	v_mul_f32_e32 v117, v121, v121
	v_add_f32_e32 v114, v114, v115
	v_add_f32_e32 v116, v116, v117
	v_mul_f32_e32 v118, v154, v154
	v_mul_f32_e32 v119, v155, v155
	v_mul_f32_e32 v120, v156, v156
	v_mul_f32_e32 v121, v157, v157
	v_add_f32_e32 v114, v114, v116
	v_add_f32_e32 v115, v128, v129
	v_add_f32_e32 v116, v126, v127
	v_add_f32_e32 v120, v120, v121
	v_add_f32_e32 v118, v118, v119
	v_add_f32_e32 v115, v116, v115
	v_add_f32_e32 v116, v124, v125
	v_add_f32_e32 v117, v122, v123
	v_add_f32_e32 v118, v118, v120
	v_add_f32_e32 v116, v117, v116
	v_add_f32_e32 v114, v114, v118
	v_add_f32_e32 v115, v116, v115
	v_add_f32_e32 v114, v115, v114
	ds_bpermute_b32 v115, v171, v114
	s_waitcnt lgkmcnt(0)
	v_add_f32_e32 v115, v114, v115
	ds_bpermute_b32 v116, v0, v115
	v_lshl_or_b32 v114, v182, 4, s1
	s_and_saveexec_b64 s[16:17], vcc
	s_cbranch_execz .LBB0_107
	s_waitcnt lgkmcnt(0)
	v_add_f32_e32 v115, v115, v116
	ds_write_b32 v114, v115
.LBB0_107:
	s_or_b64 exec, exec, s[16:17]
	s_waitcnt lgkmcnt(0)
	v_lshlrev_b32_e32 v116, 16, v150
	v_and_b32_e32 v117, 0xffff0000, v150
	v_add_f32_e32 v110, v110, v116
	v_add_f32_e32 v111, v111, v117
	v_lshlrev_b32_e32 v116, 16, v151
	v_and_b32_e32 v117, 0xffff0000, v151
	v_add_f32_e32 v112, v112, v116
	v_add_f32_e32 v113, v113, v117
	v_lshlrev_b32_e32 v116, 16, v152
	v_and_b32_e32 v117, 0xffff0000, v152
	v_add_f32_e32 v116, v106, v116
	v_add_f32_e32 v117, v107, v117
	v_lshlrev_b32_e32 v106, 16, v153
	v_and_b32_e32 v107, 0xffff0000, v153
	v_add_f32_e32 v118, v108, v106
	v_add_f32_e32 v119, v109, v107
	v_lshl_add_u64 v[120:121], s[14:15], 0, v[168:169]
	v_cvt_pk_bf16_f32 v106, v110, v111
	v_cvt_pk_bf16_f32 v107, v112, v113
	v_cvt_pk_bf16_f32 v108, v116, v117
	v_cvt_pk_bf16_f32 v109, v118, v119
	v_lshl_add_u64 v[120:121], v[158:159], 1, v[120:121]
	global_store_dwordx4 v[120:121], v[106:109], off
	s_nop 1
	v_mul_f32_e32 v106, v110, v110
	v_mul_f32_e32 v107, v111, v111
	v_mul_f32_e32 v110, v116, v116
	v_mul_f32_e32 v111, v117, v117
	v_lshlrev_b32_e32 v116, 16, v146
	v_and_b32_e32 v117, 0xffff0000, v146
	v_add_f32_e32 v102, v102, v116
	v_add_f32_e32 v103, v103, v117
	v_lshlrev_b32_e32 v116, 16, v147
	v_and_b32_e32 v117, 0xffff0000, v147
	v_add_f32_e32 v104, v104, v116
	v_add_f32_e32 v105, v105, v117
	v_lshlrev_b32_e32 v116, 16, v148
	v_and_b32_e32 v117, 0xffff0000, v148
	v_add_f32_e32 v116, v98, v116
	v_add_f32_e32 v117, v99, v117
	v_lshlrev_b32_e32 v98, 16, v149
	v_and_b32_e32 v99, 0xffff0000, v149
	v_mul_f32_e32 v108, v112, v112
	v_mul_f32_e32 v109, v113, v113
	v_mul_f32_e32 v112, v118, v118
	v_mul_f32_e32 v113, v119, v119
	v_add_f32_e32 v118, v100, v98
	v_add_f32_e32 v119, v101, v99
	v_cvt_pk_bf16_f32 v98, v102, v103
	v_cvt_pk_bf16_f32 v99, v104, v105
	v_cvt_pk_bf16_f32 v100, v116, v117
	v_cvt_pk_bf16_f32 v101, v118, v119
	global_store_dwordx4 v[120:121], v[98:101], off offset:256
	s_nop 1
	v_mul_f32_e32 v98, v102, v102
	v_mul_f32_e32 v99, v103, v103
	v_mul_f32_e32 v100, v104, v104
	v_mul_f32_e32 v101, v105, v105
	v_add_f32_e32 v98, v98, v99
	v_add_f32_e32 v100, v100, v101
	v_mul_f32_e32 v102, v116, v116
	v_mul_f32_e32 v103, v117, v117
	v_mul_f32_e32 v104, v118, v118
	v_mul_f32_e32 v105, v119, v119
	v_add_f32_e32 v98, v98, v100
	v_add_f32_e32 v99, v112, v113
	v_add_f32_e32 v100, v110, v111
	v_add_f32_e32 v104, v104, v105
	v_add_f32_e32 v102, v102, v103
	v_add_f32_e32 v99, v100, v99
	v_add_f32_e32 v100, v108, v109
	v_add_f32_e32 v101, v106, v107
	v_add_f32_e32 v102, v102, v104
	v_add_f32_e32 v100, v101, v100
	v_add_f32_e32 v98, v98, v102
	v_add_f32_e32 v99, v100, v99
	v_add_f32_e32 v98, v99, v98
	ds_bpermute_b32 v99, v171, v98
	s_waitcnt lgkmcnt(0)
	v_add_f32_e32 v98, v98, v99
	ds_bpermute_b32 v99, v0, v98
	s_and_saveexec_b64 s[16:17], vcc
	v_readlane_b32 s91, v253, 27
	v_readlane_b32 s92, v253, 28
	s_mov_b32 s89, 0x2e8ba2e9
	s_movk_i32 s90, 0xfea0
	s_movk_i32 s94, 0x2000
	v_readlane_b32 s93, v253, 29
	s_cbranch_execz .LBB0_109
	s_waitcnt lgkmcnt(0)
	v_add_f32_e32 v98, v98, v99
	ds_write_b32 v114, v98 offset:256
.LBB0_109:
	s_or_b64 exec, exec, s[16:17]
	v_lshlrev_b32_e32 v98, 16, v142
	s_waitcnt lgkmcnt(0)
	v_and_b32_e32 v99, 0xffff0000, v142
	v_add_f32_e32 v94, v94, v98
	v_add_f32_e32 v95, v95, v99
	v_lshlrev_b32_e32 v98, 16, v143
	v_and_b32_e32 v99, 0xffff0000, v143
	v_add_f32_e32 v96, v96, v98
	v_add_f32_e32 v97, v97, v99
	v_lshlrev_b32_e32 v98, 16, v144
	v_and_b32_e32 v99, 0xffff0000, v144
	v_add_f32_e32 v98, v90, v98
	v_add_f32_e32 v99, v91, v99
	v_lshlrev_b32_e32 v90, 16, v145
	v_and_b32_e32 v91, 0xffff0000, v145
	v_add_f32_e32 v100, v92, v90
	v_add_f32_e32 v101, v93, v91
	v_lshl_add_u64 v[102:103], s[14:15], 0, v[166:167]
	v_cvt_pk_bf16_f32 v90, v94, v95
	v_cvt_pk_bf16_f32 v91, v96, v97
	v_cvt_pk_bf16_f32 v92, v98, v99
	v_cvt_pk_bf16_f32 v93, v100, v101
	v_lshl_add_u64 v[102:103], v[158:159], 1, v[102:103]
	global_store_dwordx4 v[102:103], v[90:93], off
	s_nop 1
	v_mul_f32_e32 v90, v94, v94
	v_mul_f32_e32 v91, v95, v95
	v_mul_f32_e32 v94, v98, v98
	v_mul_f32_e32 v95, v99, v99
	v_lshlrev_b32_e32 v98, 16, v138
	v_and_b32_e32 v99, 0xffff0000, v138
	v_add_f32_e32 v86, v86, v98
	v_add_f32_e32 v87, v87, v99
	v_lshlrev_b32_e32 v98, 16, v139
	v_and_b32_e32 v99, 0xffff0000, v139
	v_add_f32_e32 v88, v88, v98
	v_add_f32_e32 v89, v89, v99
	v_lshlrev_b32_e32 v98, 16, v140
	v_and_b32_e32 v99, 0xffff0000, v140
	v_add_f32_e32 v98, v82, v98
	v_add_f32_e32 v99, v83, v99
	v_lshlrev_b32_e32 v82, 16, v141
	v_and_b32_e32 v83, 0xffff0000, v141
	v_mul_f32_e32 v92, v96, v96
	v_mul_f32_e32 v93, v97, v97
	v_mul_f32_e32 v96, v100, v100
	v_mul_f32_e32 v97, v101, v101
	v_add_f32_e32 v100, v84, v82
	v_add_f32_e32 v101, v85, v83
	v_cvt_pk_bf16_f32 v82, v86, v87
	v_cvt_pk_bf16_f32 v83, v88, v89
	v_cvt_pk_bf16_f32 v84, v98, v99
	v_cvt_pk_bf16_f32 v85, v100, v101
	global_store_dwordx4 v[102:103], v[82:85], off offset:256
	s_nop 1
	v_mul_f32_e32 v82, v86, v86
	v_mul_f32_e32 v83, v87, v87
	v_mul_f32_e32 v84, v88, v88
	v_mul_f32_e32 v85, v89, v89
	v_add_f32_e32 v82, v82, v83
	v_add_f32_e32 v84, v84, v85
	v_mul_f32_e32 v86, v98, v98
	v_mul_f32_e32 v87, v99, v99
	v_mul_f32_e32 v88, v100, v100
	v_mul_f32_e32 v89, v101, v101
	v_add_f32_e32 v82, v82, v84
	v_add_f32_e32 v83, v96, v97
	v_add_f32_e32 v84, v94, v95
	v_add_f32_e32 v88, v88, v89
	v_add_f32_e32 v86, v86, v87
	v_add_f32_e32 v83, v84, v83
	v_add_f32_e32 v84, v92, v93
	v_add_f32_e32 v85, v90, v91
	v_add_f32_e32 v86, v86, v88
	v_add_f32_e32 v84, v85, v84
	v_add_f32_e32 v82, v82, v86
	v_add_f32_e32 v83, v84, v83
	v_add_f32_e32 v82, v83, v82
	ds_bpermute_b32 v83, v171, v82
	s_waitcnt lgkmcnt(0)
	v_add_f32_e32 v82, v82, v83
	ds_bpermute_b32 v83, v0, v82
	s_and_saveexec_b64 s[16:17], vcc
	s_cbranch_execz .LBB0_111
	s_waitcnt lgkmcnt(0)
	v_add_f32_e32 v82, v82, v83
	ds_write_b32 v114, v82 offset:512
.LBB0_111:
	s_or_b64 exec, exec, s[16:17]
	v_lshlrev_b32_e32 v82, 16, v134
	s_waitcnt lgkmcnt(0)
	v_and_b32_e32 v83, 0xffff0000, v134
	v_add_f32_e32 v78, v78, v82
	v_add_f32_e32 v79, v79, v83
	v_lshlrev_b32_e32 v82, 16, v135
	v_and_b32_e32 v83, 0xffff0000, v135
	v_add_f32_e32 v80, v80, v82
	v_add_f32_e32 v81, v81, v83
	v_lshlrev_b32_e32 v82, 16, v136
	v_and_b32_e32 v83, 0xffff0000, v136
	v_add_f32_e32 v82, v74, v82
	v_add_f32_e32 v83, v75, v83
	v_lshlrev_b32_e32 v74, 16, v137
	v_and_b32_e32 v75, 0xffff0000, v137
	v_add_f32_e32 v84, v76, v74
	v_add_f32_e32 v85, v77, v75
	v_lshl_add_u64 v[86:87], s[14:15], 0, v[164:165]
	v_cvt_pk_bf16_f32 v74, v78, v79
	v_cvt_pk_bf16_f32 v75, v80, v81
	v_cvt_pk_bf16_f32 v76, v82, v83
	v_cvt_pk_bf16_f32 v77, v84, v85
	v_lshl_add_u64 v[86:87], v[158:159], 1, v[86:87]
	global_store_dwordx4 v[86:87], v[74:77], off
	s_nop 1
	v_mul_f32_e32 v74, v78, v78
	v_mul_f32_e32 v75, v79, v79
	v_mul_f32_e32 v78, v82, v82
	v_mul_f32_e32 v79, v83, v83
	v_lshlrev_b32_e32 v82, 16, v130
	v_and_b32_e32 v83, 0xffff0000, v130
	v_add_f32_e32 v70, v70, v82
	v_add_f32_e32 v71, v71, v83
	v_lshlrev_b32_e32 v82, 16, v131
	v_and_b32_e32 v83, 0xffff0000, v131
	v_add_f32_e32 v72, v72, v82
	v_add_f32_e32 v73, v73, v83
	v_lshlrev_b32_e32 v82, 16, v132
	v_and_b32_e32 v83, 0xffff0000, v132
	v_add_f32_e32 v82, v66, v82
	v_add_f32_e32 v83, v67, v83
	v_lshlrev_b32_e32 v66, 16, v133
	v_and_b32_e32 v67, 0xffff0000, v133
	v_mul_f32_e32 v76, v80, v80
	v_mul_f32_e32 v77, v81, v81
	v_mul_f32_e32 v80, v84, v84
	v_mul_f32_e32 v81, v85, v85
	v_add_f32_e32 v84, v68, v66
	v_add_f32_e32 v85, v69, v67
	v_cvt_pk_bf16_f32 v66, v70, v71
	v_cvt_pk_bf16_f32 v67, v72, v73
	v_cvt_pk_bf16_f32 v68, v82, v83
	v_cvt_pk_bf16_f32 v69, v84, v85
	global_store_dwordx4 v[86:87], v[66:69], off offset:256
	s_nop 1
	v_mul_f32_e32 v66, v70, v70
	v_mul_f32_e32 v67, v71, v71
	v_mul_f32_e32 v68, v72, v72
	v_mul_f32_e32 v69, v73, v73
	v_add_f32_e32 v66, v66, v67
	v_add_f32_e32 v68, v68, v69
	v_mul_f32_e32 v70, v82, v82
	v_mul_f32_e32 v71, v83, v83
	v_mul_f32_e32 v72, v84, v84
	v_mul_f32_e32 v73, v85, v85
	v_add_f32_e32 v66, v66, v68
	v_add_f32_e32 v67, v80, v81
	v_add_f32_e32 v68, v78, v79
	v_add_f32_e32 v72, v72, v73
	v_add_f32_e32 v70, v70, v71
	v_add_f32_e32 v67, v68, v67
	v_add_f32_e32 v68, v76, v77
	v_add_f32_e32 v69, v74, v75
	v_add_f32_e32 v70, v70, v72
	v_add_f32_e32 v68, v69, v68
	v_add_f32_e32 v66, v66, v70
	v_add_f32_e32 v67, v68, v67
	v_add_f32_e32 v66, v67, v66
	ds_bpermute_b32 v67, v171, v66
	s_waitcnt lgkmcnt(0)
	v_add_f32_e32 v66, v66, v67
	ds_bpermute_b32 v67, v0, v66
	s_and_saveexec_b64 s[16:17], vcc
	s_cbranch_execz .LBB0_113
	s_waitcnt lgkmcnt(0)
	v_add_f32_e32 v66, v66, v67
	ds_write_b32 v114, v66 offset:768
.LBB0_113:
	s_or_b64 exec, exec, s[16:17]
	s_waitcnt lgkmcnt(0)
	v_lshlrev_b64 v[66:67], 11, v[160:161]
	v_lshl_add_u64 v[104:105], v[66:67], 0, s[20:21]
	v_lshl_add_u64 v[68:69], v[162:163], 0, v[104:105]
	global_load_dwordx4 v[96:99], v[68:69], off
	global_load_dwordx4 v[100:103], v[68:69], off offset:256
	s_mov_b64 s[16:17], 0x48000
	v_lshl_add_u64 v[94:95], v[66:67], 0, s[16:17]
	s_mov_b64 s[16:17], 0x58000
	v_lshl_add_u64 v[68:69], v[162:163], 0, v[94:95]
	v_lshl_add_u64 v[92:93], v[66:67], 0, s[22:23]
	v_lshl_add_u64 v[90:91], v[66:67], 0, s[16:17]
	global_load_dwordx4 v[86:89], v[68:69], off
	global_load_dwordx4 v[82:85], v[68:69], off offset:256
	v_lshl_add_u64 v[68:69], v[162:163], 0, v[92:93]
	v_lshl_add_u64 v[66:67], v[162:163], 0, v[90:91]
	global_load_dwordx4 v[78:81], v[68:69], off
	global_load_dwordx4 v[74:77], v[68:69], off offset:256
	global_load_dwordx4 v[70:73], v[66:67], off
	s_nop 0
	global_load_dwordx4 v[66:69], v[66:67], off offset:256
	v_lshl_add_u64 v[104:105], s[14:15], 0, v[104:105]
	v_lshl_add_u64 v[104:105], v[158:159], 1, v[104:105]
	s_waitcnt vmcnt(7)
	v_lshlrev_b32_e32 v106, 16, v96
	v_and_b32_e32 v107, 0xffff0000, v96
	v_lshlrev_b32_e32 v96, 16, v97
	v_and_b32_e32 v97, 0xffff0000, v97
	v_add_f32_e32 v64, v64, v96
	v_add_f32_e32 v65, v65, v97
	v_lshlrev_b32_e32 v96, 16, v98
	v_and_b32_e32 v97, 0xffff0000, v98
	v_add_f32_e32 v96, v58, v96
	v_add_f32_e32 v97, v59, v97
	v_lshlrev_b32_e32 v58, 16, v99
	v_and_b32_e32 v59, 0xffff0000, v99
	v_add_f32_e32 v62, v62, v106
	v_add_f32_e32 v63, v63, v107
	v_add_f32_e32 v98, v60, v58
	v_add_f32_e32 v99, v61, v59
	v_cvt_pk_bf16_f32 v58, v62, v63
	v_cvt_pk_bf16_f32 v59, v64, v65
	v_cvt_pk_bf16_f32 v60, v96, v97
	v_cvt_pk_bf16_f32 v61, v98, v99
	global_store_dwordx4 v[104:105], v[58:61], off
	s_nop 1
	v_mul_f32_e32 v58, v62, v62
	v_mul_f32_e32 v59, v63, v63
	v_mul_f32_e32 v62, v96, v96
	v_mul_f32_e32 v63, v97, v97
	s_waitcnt vmcnt(7)
	v_lshlrev_b32_e32 v96, 16, v100
	v_and_b32_e32 v97, 0xffff0000, v100
	v_add_f32_e32 v54, v54, v96
	v_add_f32_e32 v55, v55, v97
	v_lshlrev_b32_e32 v96, 16, v101
	v_and_b32_e32 v97, 0xffff0000, v101
	v_add_f32_e32 v56, v56, v96
	v_add_f32_e32 v57, v57, v97
	v_lshlrev_b32_e32 v96, 16, v102
	v_and_b32_e32 v97, 0xffff0000, v102
	v_add_f32_e32 v96, v50, v96
	v_add_f32_e32 v97, v51, v97
	v_lshlrev_b32_e32 v50, 16, v103
	v_and_b32_e32 v51, 0xffff0000, v103
	v_mul_f32_e32 v60, v64, v64
	v_mul_f32_e32 v61, v65, v65
	v_mul_f32_e32 v64, v98, v98
	v_mul_f32_e32 v65, v99, v99
	v_add_f32_e32 v98, v52, v50
	v_add_f32_e32 v99, v53, v51
	v_cvt_pk_bf16_f32 v50, v54, v55
	v_cvt_pk_bf16_f32 v51, v56, v57
	v_cvt_pk_bf16_f32 v52, v96, v97
	v_cvt_pk_bf16_f32 v53, v98, v99
	global_store_dwordx4 v[104:105], v[50:53], off offset:256
	s_nop 1
	v_mul_f32_e32 v50, v54, v54
	v_mul_f32_e32 v51, v55, v55
	v_mul_f32_e32 v52, v56, v56
	v_mul_f32_e32 v53, v57, v57
	v_add_f32_e32 v50, v50, v51
	v_add_f32_e32 v52, v52, v53
	v_mul_f32_e32 v54, v96, v96
	v_mul_f32_e32 v55, v97, v97
	v_mul_f32_e32 v56, v98, v98
	v_mul_f32_e32 v57, v99, v99
	v_add_f32_e32 v50, v50, v52
	v_add_f32_e32 v51, v64, v65
	v_add_f32_e32 v52, v62, v63
	v_add_f32_e32 v56, v56, v57
	v_add_f32_e32 v54, v54, v55
	v_add_f32_e32 v51, v52, v51
	v_add_f32_e32 v52, v60, v61
	v_add_f32_e32 v53, v58, v59
	v_add_f32_e32 v54, v54, v56
	v_add_f32_e32 v52, v53, v52
	v_add_f32_e32 v50, v50, v54
	v_add_f32_e32 v51, v52, v51
	v_add_f32_e32 v50, v51, v50
	ds_bpermute_b32 v51, v171, v50
	s_waitcnt lgkmcnt(0)
	v_add_f32_e32 v50, v50, v51
	ds_bpermute_b32 v51, v0, v50
	s_and_saveexec_b64 s[16:17], vcc
	s_cbranch_execz .LBB0_115
	s_waitcnt lgkmcnt(0)
	v_add_f32_e32 v50, v50, v51
	ds_write_b32 v114, v50 offset:2048
.LBB0_115:
	s_or_b64 exec, exec, s[16:17]
	s_waitcnt vmcnt(7)
	v_lshlrev_b32_e32 v50, 16, v86
	s_waitcnt lgkmcnt(0)
	v_and_b32_e32 v51, 0xffff0000, v86
	v_add_f32_e32 v46, v46, v50
	v_add_f32_e32 v47, v47, v51
	v_lshlrev_b32_e32 v50, 16, v87
	v_and_b32_e32 v51, 0xffff0000, v87
	v_add_f32_e32 v48, v48, v50
	v_add_f32_e32 v49, v49, v51
	v_lshlrev_b32_e32 v50, 16, v88
	v_and_b32_e32 v51, 0xffff0000, v88
	v_add_f32_e32 v50, v42, v50
	v_add_f32_e32 v51, v43, v51
	v_lshlrev_b32_e32 v42, 16, v89
	v_and_b32_e32 v43, 0xffff0000, v89
	v_add_f32_e32 v52, v44, v42
	v_add_f32_e32 v53, v45, v43
	v_lshl_add_u64 v[54:55], s[14:15], 0, v[94:95]
	v_cvt_pk_bf16_f32 v42, v46, v47
	v_cvt_pk_bf16_f32 v43, v48, v49
	v_cvt_pk_bf16_f32 v44, v50, v51
	v_cvt_pk_bf16_f32 v45, v52, v53
	v_lshl_add_u64 v[54:55], v[158:159], 1, v[54:55]
	global_store_dwordx4 v[54:55], v[42:45], off
	s_nop 1
	v_mul_f32_e32 v42, v46, v46
	v_mul_f32_e32 v43, v47, v47
	v_mul_f32_e32 v46, v50, v50
	v_mul_f32_e32 v47, v51, v51
	s_waitcnt vmcnt(7)
	v_lshlrev_b32_e32 v50, 16, v82
	v_and_b32_e32 v51, 0xffff0000, v82
	v_add_f32_e32 v38, v38, v50
	v_add_f32_e32 v39, v39, v51
	v_lshlrev_b32_e32 v50, 16, v83
	v_and_b32_e32 v51, 0xffff0000, v83
	v_add_f32_e32 v40, v40, v50
	v_add_f32_e32 v41, v41, v51
	v_lshlrev_b32_e32 v50, 16, v84
	v_and_b32_e32 v51, 0xffff0000, v84
	v_add_f32_e32 v50, v34, v50
	v_add_f32_e32 v51, v35, v51
	v_lshlrev_b32_e32 v34, 16, v85
	v_and_b32_e32 v35, 0xffff0000, v85
	v_mul_f32_e32 v44, v48, v48
	v_mul_f32_e32 v45, v49, v49
	v_mul_f32_e32 v48, v52, v52
	v_mul_f32_e32 v49, v53, v53
	v_add_f32_e32 v52, v36, v34
	v_add_f32_e32 v53, v37, v35
	v_cvt_pk_bf16_f32 v34, v38, v39
	v_cvt_pk_bf16_f32 v35, v40, v41
	v_cvt_pk_bf16_f32 v36, v50, v51
	v_cvt_pk_bf16_f32 v37, v52, v53
	global_store_dwordx4 v[54:55], v[34:37], off offset:256
	s_nop 1
	v_mul_f32_e32 v34, v38, v38
	v_mul_f32_e32 v35, v39, v39
	v_mul_f32_e32 v36, v40, v40
	v_mul_f32_e32 v37, v41, v41
	v_add_f32_e32 v34, v34, v35
	v_add_f32_e32 v36, v36, v37
	v_mul_f32_e32 v38, v50, v50
	v_mul_f32_e32 v39, v51, v51
	v_mul_f32_e32 v40, v52, v52
	v_mul_f32_e32 v41, v53, v53
	v_add_f32_e32 v34, v34, v36
	v_add_f32_e32 v35, v48, v49
	v_add_f32_e32 v36, v46, v47
	v_add_f32_e32 v40, v40, v41
	v_add_f32_e32 v38, v38, v39
	v_add_f32_e32 v35, v36, v35
	v_add_f32_e32 v36, v44, v45
	v_add_f32_e32 v37, v42, v43
	v_add_f32_e32 v38, v38, v40
	v_add_f32_e32 v36, v37, v36
	v_add_f32_e32 v34, v34, v38
	v_add_f32_e32 v35, v36, v35
	v_add_f32_e32 v34, v35, v34
	ds_bpermute_b32 v35, v171, v34
	s_waitcnt lgkmcnt(0)
	v_add_f32_e32 v34, v34, v35
	ds_bpermute_b32 v35, v0, v34
	s_and_saveexec_b64 s[16:17], vcc
	s_cbranch_execz .LBB0_117
	s_waitcnt lgkmcnt(0)
	v_add_f32_e32 v34, v34, v35
	ds_write_b32 v114, v34 offset:2304
.LBB0_117:
	s_or_b64 exec, exec, s[16:17]
	s_waitcnt vmcnt(7)
	v_lshlrev_b32_e32 v34, 16, v78
	s_waitcnt lgkmcnt(0)
	v_and_b32_e32 v35, 0xffff0000, v78
	v_add_f32_e32 v30, v30, v34
	v_add_f32_e32 v31, v31, v35
	v_lshlrev_b32_e32 v34, 16, v79
	v_and_b32_e32 v35, 0xffff0000, v79
	v_add_f32_e32 v32, v32, v34
	v_add_f32_e32 v33, v33, v35
	v_lshlrev_b32_e32 v34, 16, v80
	v_and_b32_e32 v35, 0xffff0000, v80
	v_add_f32_e32 v34, v26, v34
	v_add_f32_e32 v35, v27, v35
	v_lshlrev_b32_e32 v26, 16, v81
	v_and_b32_e32 v27, 0xffff0000, v81
	v_add_f32_e32 v36, v28, v26
	v_add_f32_e32 v37, v29, v27
	v_lshl_add_u64 v[38:39], s[14:15], 0, v[92:93]
	v_cvt_pk_bf16_f32 v26, v30, v31
	v_cvt_pk_bf16_f32 v27, v32, v33
	v_cvt_pk_bf16_f32 v28, v34, v35
	v_cvt_pk_bf16_f32 v29, v36, v37
	v_lshl_add_u64 v[38:39], v[158:159], 1, v[38:39]
	global_store_dwordx4 v[38:39], v[26:29], off
	s_nop 1
	v_mul_f32_e32 v26, v30, v30
	v_mul_f32_e32 v27, v31, v31
	v_mul_f32_e32 v30, v34, v34
	v_mul_f32_e32 v31, v35, v35
	s_waitcnt vmcnt(7)
	v_lshlrev_b32_e32 v34, 16, v74
	v_and_b32_e32 v35, 0xffff0000, v74
	v_add_f32_e32 v22, v22, v34
	v_add_f32_e32 v23, v23, v35
	v_lshlrev_b32_e32 v34, 16, v75
	v_and_b32_e32 v35, 0xffff0000, v75
	v_add_f32_e32 v24, v24, v34
	v_add_f32_e32 v25, v25, v35
	v_lshlrev_b32_e32 v34, 16, v76
	v_and_b32_e32 v35, 0xffff0000, v76
	v_add_f32_e32 v34, v18, v34
	v_add_f32_e32 v35, v19, v35
	v_lshlrev_b32_e32 v18, 16, v77
	v_and_b32_e32 v19, 0xffff0000, v77
	v_mul_f32_e32 v28, v32, v32
	v_mul_f32_e32 v29, v33, v33
	v_mul_f32_e32 v32, v36, v36
	v_mul_f32_e32 v33, v37, v37
	v_add_f32_e32 v36, v20, v18
	v_add_f32_e32 v37, v21, v19
	v_cvt_pk_bf16_f32 v18, v22, v23
	v_cvt_pk_bf16_f32 v19, v24, v25
	v_cvt_pk_bf16_f32 v20, v34, v35
	v_cvt_pk_bf16_f32 v21, v36, v37
	global_store_dwordx4 v[38:39], v[18:21], off offset:256
	s_nop 1
	v_mul_f32_e32 v18, v22, v22
	v_mul_f32_e32 v19, v23, v23
	v_mul_f32_e32 v20, v24, v24
	v_mul_f32_e32 v21, v25, v25
	v_add_f32_e32 v18, v18, v19
	v_add_f32_e32 v20, v20, v21
	v_mul_f32_e32 v22, v34, v34
	v_mul_f32_e32 v23, v35, v35
	v_mul_f32_e32 v24, v36, v36
	v_mul_f32_e32 v25, v37, v37
	v_add_f32_e32 v18, v18, v20
	v_add_f32_e32 v19, v32, v33
	v_add_f32_e32 v20, v30, v31
	v_add_f32_e32 v24, v24, v25
	v_add_f32_e32 v22, v22, v23
	v_add_f32_e32 v19, v20, v19
	v_add_f32_e32 v20, v28, v29
	v_add_f32_e32 v21, v26, v27
	v_add_f32_e32 v22, v22, v24
	v_add_f32_e32 v20, v21, v20
	v_add_f32_e32 v18, v18, v22
	v_add_f32_e32 v19, v20, v19
	v_add_f32_e32 v18, v19, v18
	ds_bpermute_b32 v19, v171, v18
	s_waitcnt lgkmcnt(0)
	v_add_f32_e32 v18, v18, v19
	ds_bpermute_b32 v19, v0, v18
	s_and_saveexec_b64 s[16:17], vcc
	s_cbranch_execz .LBB0_119
	s_waitcnt lgkmcnt(0)
	v_add_f32_e32 v18, v18, v19
	ds_write_b32 v114, v18 offset:2560
.LBB0_119:
	s_or_b64 exec, exec, s[16:17]
	s_waitcnt vmcnt(7)
	v_lshlrev_b32_e32 v18, 16, v70
	s_waitcnt lgkmcnt(0)
	v_and_b32_e32 v19, 0xffff0000, v70
	v_add_f32_e32 v14, v14, v18
	v_add_f32_e32 v15, v15, v19
	v_lshlrev_b32_e32 v18, 16, v71
	v_and_b32_e32 v19, 0xffff0000, v71
	v_add_f32_e32 v16, v16, v18
	v_add_f32_e32 v17, v17, v19
	v_lshlrev_b32_e32 v18, 16, v72
	v_and_b32_e32 v19, 0xffff0000, v72
	v_add_f32_e32 v18, v10, v18
	v_add_f32_e32 v19, v11, v19
	v_lshlrev_b32_e32 v10, 16, v73
	v_and_b32_e32 v11, 0xffff0000, v73
	v_add_f32_e32 v20, v12, v10
	v_add_f32_e32 v21, v13, v11
	v_lshl_add_u64 v[22:23], s[14:15], 0, v[90:91]
	v_cvt_pk_bf16_f32 v10, v14, v15
	v_cvt_pk_bf16_f32 v11, v16, v17
	v_cvt_pk_bf16_f32 v12, v18, v19
	v_cvt_pk_bf16_f32 v13, v20, v21
	v_lshl_add_u64 v[22:23], v[158:159], 1, v[22:23]
	global_store_dwordx4 v[22:23], v[10:13], off
	s_nop 1
	v_mul_f32_e32 v10, v14, v14
	v_mul_f32_e32 v11, v15, v15
	v_mul_f32_e32 v14, v18, v18
	v_mul_f32_e32 v15, v19, v19
	s_waitcnt vmcnt(7)
	v_lshlrev_b32_e32 v18, 16, v66
	v_and_b32_e32 v19, 0xffff0000, v66
	v_add_f32_e32 v6, v6, v18
	v_add_f32_e32 v7, v7, v19
	v_lshlrev_b32_e32 v18, 16, v67
	v_and_b32_e32 v19, 0xffff0000, v67
	v_add_f32_e32 v8, v8, v18
	v_add_f32_e32 v9, v9, v19
	v_lshlrev_b32_e32 v18, 16, v68
	v_and_b32_e32 v19, 0xffff0000, v68
	v_add_f32_e32 v18, v2, v18
	v_add_f32_e32 v19, v3, v19
	v_lshlrev_b32_e32 v2, 16, v69
	v_and_b32_e32 v3, 0xffff0000, v69
	v_mul_f32_e32 v12, v16, v16
	v_mul_f32_e32 v13, v17, v17
	v_mul_f32_e32 v16, v20, v20
	v_mul_f32_e32 v17, v21, v21
	v_add_f32_e32 v20, v4, v2
	v_add_f32_e32 v21, v5, v3
	v_cvt_pk_bf16_f32 v2, v6, v7
	v_cvt_pk_bf16_f32 v3, v8, v9
	v_cvt_pk_bf16_f32 v4, v18, v19
	v_cvt_pk_bf16_f32 v5, v20, v21
	global_store_dwordx4 v[22:23], v[2:5], off offset:256
	s_nop 1
	v_mul_f32_e32 v2, v6, v6
	v_mul_f32_e32 v3, v7, v7
	v_mul_f32_e32 v4, v8, v8
	v_mul_f32_e32 v5, v9, v9
	v_add_f32_e32 v2, v2, v3
	v_add_f32_e32 v4, v4, v5
	v_mul_f32_e32 v6, v18, v18
	v_mul_f32_e32 v7, v19, v19
	v_mul_f32_e32 v8, v20, v20
	v_mul_f32_e32 v9, v21, v21
	v_add_f32_e32 v2, v2, v4
	v_add_f32_e32 v3, v16, v17
	v_add_f32_e32 v4, v14, v15
	v_add_f32_e32 v8, v8, v9
	v_add_f32_e32 v6, v6, v7
	v_add_f32_e32 v3, v4, v3
	v_add_f32_e32 v4, v12, v13
	v_add_f32_e32 v5, v10, v11
	v_add_f32_e32 v6, v6, v8
	v_add_f32_e32 v4, v5, v4
	v_add_f32_e32 v2, v2, v6
	v_add_f32_e32 v3, v4, v3
	v_add_f32_e32 v2, v3, v2
	ds_bpermute_b32 v3, v171, v2
	s_waitcnt lgkmcnt(0)
	v_add_f32_e32 v2, v2, v3
	ds_bpermute_b32 v0, v0, v2
	s_and_saveexec_b64 s[14:15], vcc
	s_cbranch_execz .LBB0_121
	s_waitcnt lgkmcnt(0)
	v_add_f32_e32 v0, v2, v0
	ds_write_b32 v114, v0 offset:2816

.LBB0_155:
	v_readlane_b32 s38, v253, 32
	s_andn2_b64 vcc, exec, s[48:49]
	s_lshl_b32 s52, s38, 14
	v_readlane_b32 s39, v253, 33
	s_cbranch_vccnz .LBB0_159
	s_and_b64 vcc, exec, s[36:37]
	s_cbranch_vccnz .LBB0_158
	v_lshrrev_b32_e32 v0, 3, v198
	v_and_b32_e32 v67, 7, v235
	v_lshlrev_b32_e32 v98, 4, v67
	v_mul_u32_u24_e32 v69, 0x84, v0
	v_add3_u32 v69, s52, v98, v69
	s_waitcnt vmcnt(7)
	v_mul_f32_e32 v30, v30, v66
	v_mul_f32_e32 v31, v31, v66
	ds_write2_b32 v69, v30, v31 offset1:1
	v_mul_f32_e32 v30, v32, v66
	v_mul_f32_e32 v31, v33, v66
	ds_write2_b32 v69, v30, v31 offset0:2 offset1:3
	v_add_u32_e32 v32, 0x420, v69
	s_waitcnt vmcnt(6)
	v_mul_f32_e32 v30, v38, v68
	v_mul_f32_e32 v31, v39, v68
	ds_write2_b32 v32, v30, v31 offset1:1
	v_add_u32_e32 v32, 0x428, v69
	v_mul_f32_e32 v30, v40, v68
	v_mul_f32_e32 v31, v41, v68
	ds_write2_b32 v32, v30, v31 offset1:1
	v_add_u32_e32 v32, 0x840, v69
	s_waitcnt vmcnt(5)
	v_mul_f32_e32 v30, v34, v74
	v_mul_f32_e32 v31, v35, v74
	ds_write2_b32 v32, v30, v31 offset1:1
	v_add_u32_e32 v32, 0x848, v69
	v_mul_f32_e32 v30, v36, v74
	v_mul_f32_e32 v31, v37, v74
	ds_write2_b32 v32, v30, v31 offset1:1
	v_add_u32_e32 v32, 0xc60, v69
	s_waitcnt vmcnt(4)
	v_mul_f32_e32 v30, v46, v76
	v_mul_f32_e32 v31, v47, v76
	ds_write2_b32 v32, v30, v31 offset1:1
	v_add_u32_e32 v32, 0xc68, v69
	v_mul_f32_e32 v30, v48, v76
	v_mul_f32_e32 v31, v49, v76
	ds_write2_b32 v32, v30, v31 offset1:1
	v_add_u32_e32 v32, 0x1080, v69
	s_waitcnt vmcnt(3)
	v_mul_f32_e32 v30, v42, v82
	v_mul_f32_e32 v31, v43, v82
	ds_write2_b32 v32, v30, v31 offset1:1
	v_add_u32_e32 v32, 0x1088, v69
	v_mul_f32_e32 v30, v44, v82
	v_mul_f32_e32 v31, v45, v82
	ds_write2_b32 v32, v30, v31 offset1:1
	v_add_u32_e32 v32, 0x14a0, v69
	s_waitcnt vmcnt(2)
	v_mul_f32_e32 v30, v54, v84
	v_mul_f32_e32 v31, v55, v84
	ds_write2_b32 v32, v30, v31 offset1:1
	v_add_u32_e32 v32, 0x14a8, v69
	v_mul_f32_e32 v30, v56, v84
	v_mul_f32_e32 v31, v57, v84
	ds_write2_b32 v32, v30, v31 offset1:1
	v_add_u32_e32 v32, 0x18c0, v69
	s_waitcnt vmcnt(1)
	v_mul_f32_e32 v30, v50, v90
	v_mul_f32_e32 v31, v51, v90
	ds_write2_b32 v32, v30, v31 offset1:1
	v_add_u32_e32 v32, 0x18c8, v69
	v_mul_f32_e32 v30, v52, v90
	v_mul_f32_e32 v31, v53, v90
	ds_write2_b32 v32, v30, v31 offset1:1
	v_add_u32_e32 v32, 0x1ce0, v69
	s_waitcnt vmcnt(0)
	v_mul_f32_e32 v30, v58, v92
	v_mul_f32_e32 v31, v59, v92
	ds_write2_b32 v32, v30, v31 offset1:1
	v_add_u32_e32 v32, 0x1ce8, v69
	v_mul_f32_e32 v30, v60, v92
	v_mul_f32_e32 v31, v61, v92
	ds_write2_b32 v32, v30, v31 offset1:1
	s_waitcnt lgkmcnt(0)
	v_mul_u32_u24_e32 v30, 0x420, v67
	v_lshlrev_b32_e32 v31, 2, v0
	v_add3_u32 v52, s52, v30, v31
	ds_read2_b32 v[34:35], v52 offset0:33 offset1:41
	ds_read2_b32 v[36:37], v52 offset1:8
	ds_read2_b32 v[38:39], v52 offset0:66 offset1:74
	ds_read2_b32 v[40:41], v52 offset0:99 offset1:107
	ds_read2_b32 v[42:43], v52 offset0:132 offset1:140
	ds_read2_b32 v[44:45], v52 offset0:165 offset1:173
	ds_read2_b32 v[46:47], v52 offset0:198 offset1:206
	ds_read2_b32 v[48:49], v52 offset0:231 offset1:239
	v_lshlrev_b32_e32 v0, 11, v0
	v_lshl_add_u64 v[50:51], s[16:17], 0, v[0:1]
	v_mov_b32_e32 v99, v1
	s_waitcnt lgkmcnt(6)
	v_cvt_pk_bf16_f32 v30, v36, v34
	s_waitcnt lgkmcnt(4)
	v_cvt_pk_bf16_f32 v31, v38, v40
	s_waitcnt lgkmcnt(2)
	v_cvt_pk_bf16_f32 v32, v42, v44
	s_waitcnt lgkmcnt(0)
	v_cvt_pk_bf16_f32 v33, v46, v48
	v_lshl_add_u64 v[50:51], v[50:51], 0, v[98:99]
	global_store_dwordx4 v[50:51], v[30:33], off
	v_or_b32_e32 v34, 0x4000, v0
	s_nop 0
	v_cvt_pk_bf16_f32 v30, v37, v35
	v_cvt_pk_bf16_f32 v31, v39, v41
	v_cvt_pk_bf16_f32 v32, v43, v45
	v_cvt_pk_bf16_f32 v33, v47, v49
	v_mov_b32_e32 v35, v1
	ds_read2_b32 v[36:37], v52 offset0:49 offset1:57
	ds_read2_b32 v[38:39], v52 offset0:16 offset1:24
	ds_read2_b32 v[40:41], v52 offset0:82 offset1:90
	ds_read2_b32 v[42:43], v52 offset0:115 offset1:123
	ds_read2_b32 v[44:45], v52 offset0:148 offset1:156
	ds_read2_b32 v[46:47], v52 offset0:181 offset1:189
	ds_read2_b32 v[48:49], v52 offset0:214 offset1:222
	ds_read2_b32 v[50:51], v52 offset0:247 offset1:255
	v_lshl_add_u64 v[34:35], s[16:17], 0, v[34:35]
	v_lshl_add_u64 v[34:35], v[34:35], 0, v[98:99]
	global_store_dwordx4 v[34:35], v[30:33], off
	v_or_b32_e32 v34, 0x8000, v0
	v_mov_b32_e32 v35, v1
	v_lshl_add_u64 v[34:35], s[16:17], 0, v[34:35]
	s_waitcnt lgkmcnt(6)
	v_cvt_pk_bf16_f32 v30, v38, v36
	s_waitcnt lgkmcnt(4)
	v_cvt_pk_bf16_f32 v31, v40, v42
	s_waitcnt lgkmcnt(2)
	v_cvt_pk_bf16_f32 v32, v44, v46
	s_waitcnt lgkmcnt(0)
	v_cvt_pk_bf16_f32 v33, v48, v50
	v_lshl_add_u64 v[34:35], v[34:35], 0, v[98:99]
	v_or_b32_e32 v0, 0xc000, v0
	global_store_dwordx4 v[34:35], v[30:33], off
	v_lshl_add_u64 v[34:35], s[16:17], 0, v[0:1]
	v_lshl_add_u64 v[34:35], v[34:35], 0, v[98:99]
	v_cvt_pk_bf16_f32 v30, v39, v37
	v_cvt_pk_bf16_f32 v31, v41, v43
	v_cvt_pk_bf16_f32 v32, v45, v47
	v_cvt_pk_bf16_f32 v33, v49, v51
	global_store_dwordx4 v[34:35], v[30:33], off
	s_waitcnt lgkmcnt(0)

.LBB0_174:
	s_andn2_b64 vcc, exec, s[38:39]
	s_cbranch_vccnz .LBB0_178
	s_cmp_eq_u32 s31, 0
	s_cbranch_scc1 .LBB0_177
	v_lshrrev_b32_e32 v0, 3, v198
	s_waitcnt vmcnt(7)
	v_and_b32_e32 v31, 7, v235
	v_lshlrev_b32_e32 v30, 4, v31
	v_mul_u32_u24_e32 v32, 0x84, v0
	v_add3_u32 v32, s52, v30, v32
	v_mul_f32_e32 v2, v2, v70
	v_mul_f32_e32 v3, v3, v70
	ds_write2_b32 v32, v2, v3 offset1:1
	v_mul_f32_e32 v2, v4, v70
	v_mul_f32_e32 v3, v5, v70
	ds_write2_b32 v32, v2, v3 offset0:2 offset1:3
	v_add_u32_e32 v4, 0x420, v32
	s_waitcnt vmcnt(6)
	v_mul_f32_e32 v2, v10, v72
	v_mul_f32_e32 v3, v11, v72
	ds_write2_b32 v4, v2, v3 offset1:1
	v_add_u32_e32 v4, 0x428, v32
	v_mul_f32_e32 v2, v12, v72
	v_mul_f32_e32 v3, v13, v72
	ds_write2_b32 v4, v2, v3 offset1:1
	v_add_u32_e32 v4, 0x840, v32
	s_waitcnt vmcnt(5)
	v_mul_f32_e32 v2, v6, v78
	v_mul_f32_e32 v3, v7, v78
	ds_write2_b32 v4, v2, v3 offset1:1
	v_add_u32_e32 v4, 0x848, v32
	v_mul_f32_e32 v2, v8, v78
	v_mul_f32_e32 v3, v9, v78
	ds_write2_b32 v4, v2, v3 offset1:1
	v_add_u32_e32 v4, 0xc60, v32
	s_waitcnt vmcnt(4)
	v_mul_f32_e32 v2, v18, v80
	v_mul_f32_e32 v3, v19, v80
	ds_write2_b32 v4, v2, v3 offset1:1
	v_add_u32_e32 v4, 0xc68, v32
	v_mul_f32_e32 v2, v20, v80
	v_mul_f32_e32 v3, v21, v80
	ds_write2_b32 v4, v2, v3 offset1:1
	v_add_u32_e32 v4, 0x1080, v32
	s_waitcnt vmcnt(3)
	v_mul_f32_e32 v2, v14, v86
	v_mul_f32_e32 v3, v15, v86
	ds_write2_b32 v4, v2, v3 offset1:1
	v_add_u32_e32 v4, 0x1088, v32
	v_mul_f32_e32 v2, v16, v86
	v_mul_f32_e32 v3, v17, v86
	ds_write2_b32 v4, v2, v3 offset1:1
	v_add_u32_e32 v4, 0x14a0, v32
	s_waitcnt vmcnt(2)
	v_mul_f32_e32 v2, v26, v88
	v_mul_f32_e32 v3, v27, v88
	ds_write2_b32 v4, v2, v3 offset1:1
	v_add_u32_e32 v4, 0x14a8, v32
	v_mul_f32_e32 v2, v28, v88
	v_mul_f32_e32 v3, v29, v88
	ds_write2_b32 v4, v2, v3 offset1:1
	v_add_u32_e32 v4, 0x18c0, v32
	s_waitcnt vmcnt(1)
	v_mul_f32_e32 v2, v22, v94
	v_mul_f32_e32 v3, v23, v94
	ds_write2_b32 v4, v2, v3 offset1:1
	v_add_u32_e32 v4, 0x18c8, v32
	v_mul_f32_e32 v2, v24, v94
	v_mul_f32_e32 v3, v25, v94
	ds_write2_b32 v4, v2, v3 offset1:1
	v_add_u32_e32 v4, 0x1ce0, v32
	s_waitcnt vmcnt(0)
	v_mul_f32_e32 v2, v62, v96
	v_mul_f32_e32 v3, v63, v96
	ds_write2_b32 v4, v2, v3 offset1:1
	v_add_u32_e32 v4, 0x1ce8, v32
	v_mul_f32_e32 v2, v64, v96
	v_mul_f32_e32 v3, v65, v96
	ds_write2_b32 v4, v2, v3 offset1:1
	s_waitcnt lgkmcnt(0)
	v_mul_u32_u24_e32 v2, 0x420, v31
	v_lshlrev_b32_e32 v3, 2, v0
	v_add3_u32 v24, s52, v2, v3
	ds_read2_b32 v[6:7], v24 offset0:33 offset1:41
	ds_read2_b32 v[8:9], v24 offset1:8
	ds_read2_b32 v[10:11], v24 offset0:66 offset1:74
	ds_read2_b32 v[12:13], v24 offset0:99 offset1:107
	ds_read2_b32 v[14:15], v24 offset0:132 offset1:140
	ds_read2_b32 v[16:17], v24 offset0:165 offset1:173
	ds_read2_b32 v[18:19], v24 offset0:198 offset1:206
	ds_read2_b32 v[20:21], v24 offset0:231 offset1:239
	v_lshlrev_b32_e32 v0, 11, v0
	v_lshl_add_u64 v[22:23], s[14:15], 0, v[0:1]
	v_mov_b32_e32 v31, v1
	s_waitcnt lgkmcnt(6)
	v_cvt_pk_bf16_f32 v2, v8, v6
	s_waitcnt lgkmcnt(4)
	v_cvt_pk_bf16_f32 v3, v10, v12
	s_waitcnt lgkmcnt(2)
	v_cvt_pk_bf16_f32 v4, v14, v16
	s_waitcnt lgkmcnt(0)
	v_cvt_pk_bf16_f32 v5, v18, v20
	v_lshl_add_u64 v[22:23], v[22:23], 0, v[30:31]
	global_store_dwordx4 v[22:23], v[2:5], off
	v_or_b32_e32 v6, 0x4000, v0
	s_nop 0
	v_cvt_pk_bf16_f32 v2, v9, v7
	v_cvt_pk_bf16_f32 v3, v11, v13
	v_cvt_pk_bf16_f32 v4, v15, v17
	v_cvt_pk_bf16_f32 v5, v19, v21
	v_mov_b32_e32 v7, v1
	ds_read2_b32 v[8:9], v24 offset0:49 offset1:57
	ds_read2_b32 v[10:11], v24 offset0:16 offset1:24
	ds_read2_b32 v[12:13], v24 offset0:82 offset1:90
	ds_read2_b32 v[14:15], v24 offset0:115 offset1:123
	ds_read2_b32 v[16:17], v24 offset0:148 offset1:156
	ds_read2_b32 v[18:19], v24 offset0:181 offset1:189
	ds_read2_b32 v[20:21], v24 offset0:214 offset1:222
	ds_read2_b32 v[22:23], v24 offset0:247 offset1:255
	v_lshl_add_u64 v[6:7], s[14:15], 0, v[6:7]
	v_lshl_add_u64 v[6:7], v[6:7], 0, v[30:31]
	global_store_dwordx4 v[6:7], v[2:5], off
	v_or_b32_e32 v6, 0x8000, v0
	v_mov_b32_e32 v7, v1
	v_lshl_add_u64 v[6:7], s[14:15], 0, v[6:7]
	s_waitcnt lgkmcnt(6)
	v_cvt_pk_bf16_f32 v2, v10, v8
	s_waitcnt lgkmcnt(4)
	v_cvt_pk_bf16_f32 v3, v12, v14
	s_waitcnt lgkmcnt(2)
	v_cvt_pk_bf16_f32 v4, v16, v18
	s_waitcnt lgkmcnt(0)
	v_cvt_pk_bf16_f32 v5, v20, v22
	v_lshl_add_u64 v[6:7], v[6:7], 0, v[30:31]
	v_or_b32_e32 v0, 0xc000, v0
	global_store_dwordx4 v[6:7], v[2:5], off
	v_lshl_add_u64 v[6:7], s[14:15], 0, v[0:1]
	v_lshl_add_u64 v[6:7], v[6:7], 0, v[30:31]
	v_cvt_pk_bf16_f32 v2, v11, v9
	v_cvt_pk_bf16_f32 v3, v13, v15
	v_cvt_pk_bf16_f32 v4, v17, v19
	v_cvt_pk_bf16_f32 v5, v21, v23
	global_store_dwordx4 v[6:7], v[2:5], off
	s_waitcnt lgkmcnt(0)

.LBB0_193:
	s_andn2_b64 vcc, exec, s[38:39]
	s_cbranch_vccnz .LBB0_197
	s_cmp_eq_u32 s31, 0
	s_cbranch_scc1 .LBB0_196
	v_lshrrev_b32_e32 v0, 3, v198
	s_waitcnt vmcnt(0)
	v_and_b32_e32 v63, 7, v235
	v_lshlrev_b32_e32 v62, 4, v63
	v_mul_u32_u24_e32 v64, 0x84, v0
	v_add3_u32 v64, s52, v62, v64
	v_mul_f32_e32 v34, v34, v74
	v_mul_f32_e32 v35, v35, v74
	ds_write2_b32 v64, v34, v35 offset1:1
	v_mul_f32_e32 v34, v36, v74
	v_mul_f32_e32 v35, v37, v74
	ds_write2_b32 v64, v34, v35 offset0:2 offset1:3
	v_add_u32_e32 v36, 0x420, v64
	v_mul_f32_e32 v34, v42, v76
	v_mul_f32_e32 v35, v43, v76
	ds_write2_b32 v36, v34, v35 offset1:1
	v_add_u32_e32 v36, 0x428, v64
	v_mul_f32_e32 v34, v44, v76
	v_mul_f32_e32 v35, v45, v76
	ds_write2_b32 v36, v34, v35 offset1:1
	v_add_u32_e32 v36, 0x840, v64
	v_mul_f32_e32 v34, v38, v82
	v_mul_f32_e32 v35, v39, v82
	ds_write2_b32 v36, v34, v35 offset1:1
	v_add_u32_e32 v36, 0x848, v64
	v_mul_f32_e32 v34, v40, v82
	v_mul_f32_e32 v35, v41, v82
	ds_write2_b32 v36, v34, v35 offset1:1
	v_add_u32_e32 v36, 0xc60, v64
	v_mul_f32_e32 v34, v50, v84
	v_mul_f32_e32 v35, v51, v84
	ds_write2_b32 v36, v34, v35 offset1:1
	v_add_u32_e32 v36, 0xc68, v64
	v_mul_f32_e32 v34, v52, v84
	v_mul_f32_e32 v35, v53, v84
	ds_write2_b32 v36, v34, v35 offset1:1
	v_add_u32_e32 v36, 0x1080, v64
	v_mul_f32_e32 v34, v46, v90
	v_mul_f32_e32 v35, v47, v90
	ds_write2_b32 v36, v34, v35 offset1:1
	v_add_u32_e32 v36, 0x1088, v64
	v_mul_f32_e32 v34, v48, v90
	v_mul_f32_e32 v35, v49, v90
	ds_write2_b32 v36, v34, v35 offset1:1
	v_add_u32_e32 v36, 0x14a0, v64
	v_mul_f32_e32 v34, v58, v92
	v_mul_f32_e32 v35, v59, v92
	ds_write2_b32 v36, v34, v35 offset1:1
	v_add_u32_e32 v36, 0x14a8, v64
	v_mul_f32_e32 v34, v60, v92
	v_mul_f32_e32 v35, v61, v92
	ds_write2_b32 v36, v34, v35 offset1:1
	v_add_u32_e32 v36, 0x18c0, v64
	v_mul_f32_e32 v34, v54, v98
	v_mul_f32_e32 v35, v55, v98
	ds_write2_b32 v36, v34, v35 offset1:1
	v_add_u32_e32 v36, 0x18c8, v64
	v_mul_f32_e32 v34, v56, v98
	v_mul_f32_e32 v35, v57, v98
	ds_write2_b32 v36, v34, v35 offset1:1
	v_add_u32_e32 v36, 0x1ce0, v64
	v_mul_f32_e32 v34, v66, v100
	v_mul_f32_e32 v35, v67, v100
	ds_write2_b32 v36, v34, v35 offset1:1
	v_add_u32_e32 v36, 0x1ce8, v64
	v_mul_f32_e32 v34, v68, v100
	v_mul_f32_e32 v35, v69, v100
	ds_write2_b32 v36, v34, v35 offset1:1
	s_waitcnt lgkmcnt(0)
	v_mul_u32_u24_e32 v34, 0x420, v63
	v_lshlrev_b32_e32 v35, 2, v0
	v_add3_u32 v56, s52, v34, v35
	ds_read2_b32 v[38:39], v56 offset0:33 offset1:41
	ds_read2_b32 v[40:41], v56 offset1:8
	ds_read2_b32 v[42:43], v56 offset0:66 offset1:74
	ds_read2_b32 v[44:45], v56 offset0:99 offset1:107
	ds_read2_b32 v[46:47], v56 offset0:132 offset1:140
	ds_read2_b32 v[48:49], v56 offset0:165 offset1:173
	ds_read2_b32 v[50:51], v56 offset0:198 offset1:206
	ds_read2_b32 v[52:53], v56 offset0:231 offset1:239
	v_lshlrev_b32_e32 v0, 11, v0
	v_lshl_add_u64 v[54:55], s[16:17], 0, v[0:1]
	v_mov_b32_e32 v63, v1
	s_waitcnt lgkmcnt(6)
	v_cvt_pk_bf16_f32 v34, v40, v38
	s_waitcnt lgkmcnt(4)
	v_cvt_pk_bf16_f32 v35, v42, v44
	s_waitcnt lgkmcnt(2)
	v_cvt_pk_bf16_f32 v36, v46, v48
	s_waitcnt lgkmcnt(0)
	v_cvt_pk_bf16_f32 v37, v50, v52
	v_lshl_add_u64 v[54:55], v[54:55], 0, v[62:63]
	global_store_dwordx4 v[54:55], v[34:37], off
	v_or_b32_e32 v38, 0x4000, v0
	s_nop 0
	v_cvt_pk_bf16_f32 v34, v41, v39
	v_cvt_pk_bf16_f32 v35, v43, v45
	v_cvt_pk_bf16_f32 v36, v47, v49
	v_cvt_pk_bf16_f32 v37, v51, v53
	v_mov_b32_e32 v39, v1
	ds_read2_b32 v[40:41], v56 offset0:49 offset1:57
	ds_read2_b32 v[42:43], v56 offset0:16 offset1:24
	ds_read2_b32 v[44:45], v56 offset0:82 offset1:90
	ds_read2_b32 v[46:47], v56 offset0:115 offset1:123
	ds_read2_b32 v[48:49], v56 offset0:148 offset1:156
	ds_read2_b32 v[50:51], v56 offset0:181 offset1:189
	ds_read2_b32 v[52:53], v56 offset0:214 offset1:222
	ds_read2_b32 v[54:55], v56 offset0:247 offset1:255
	v_lshl_add_u64 v[38:39], s[16:17], 0, v[38:39]
	v_lshl_add_u64 v[38:39], v[38:39], 0, v[62:63]
	global_store_dwordx4 v[38:39], v[34:37], off
	v_or_b32_e32 v38, 0x8000, v0
	v_mov_b32_e32 v39, v1
	v_lshl_add_u64 v[38:39], s[16:17], 0, v[38:39]
	s_waitcnt lgkmcnt(6)
	v_cvt_pk_bf16_f32 v34, v42, v40
	s_waitcnt lgkmcnt(4)
	v_cvt_pk_bf16_f32 v35, v44, v46
	s_waitcnt lgkmcnt(2)
	v_cvt_pk_bf16_f32 v36, v48, v50
	s_waitcnt lgkmcnt(0)
	v_cvt_pk_bf16_f32 v37, v52, v54
	v_lshl_add_u64 v[38:39], v[38:39], 0, v[62:63]
	v_or_b32_e32 v0, 0xc000, v0
	global_store_dwordx4 v[38:39], v[34:37], off
	v_lshl_add_u64 v[38:39], s[16:17], 0, v[0:1]
	v_lshl_add_u64 v[38:39], v[38:39], 0, v[62:63]
	v_cvt_pk_bf16_f32 v34, v43, v41
	v_cvt_pk_bf16_f32 v35, v45, v47
	v_cvt_pk_bf16_f32 v36, v49, v51
	v_cvt_pk_bf16_f32 v37, v53, v55
	global_store_dwordx4 v[38:39], v[34:37], off
	s_waitcnt lgkmcnt(0)

.LBB0_215:
	s_andn2_b64 vcc, exec, s[50:51]
	s_cbranch_vccnz .LBB0_219
	s_cmp_eq_u32 s31, 0
	s_cbranch_scc1 .LBB0_218
	s_waitcnt vmcnt(6)
	v_mul_f32_e32 v2, v120, v2
	v_mul_f32_e32 v3, v120, v3
	ds_write2_b32 v101, v2, v3 offset1:1
	v_mul_f32_e32 v2, v120, v4
	v_mul_f32_e32 v3, v120, v5
	ds_write2_b32 v101, v2, v3 offset0:2 offset1:3
	s_waitcnt vmcnt(7)
	v_mul_f32_e32 v2, v118, v10
	v_mul_f32_e32 v3, v118, v11
	v_add_u32_e32 v0, 0x420, v101
	ds_write2_b32 v0, v2, v3 offset1:1
	v_mul_f32_e32 v2, v118, v12
	v_mul_f32_e32 v3, v118, v13
	v_add_u32_e32 v0, 0x428, v101
	ds_write2_b32 v0, v2, v3 offset1:1
	s_waitcnt vmcnt(6)
	v_mul_f32_e32 v2, v124, v6
	v_mul_f32_e32 v3, v124, v7
	v_add_u32_e32 v0, 0x840, v101
	ds_write2_b32 v0, v2, v3 offset1:1
	v_mul_f32_e32 v2, v124, v8
	v_mul_f32_e32 v3, v124, v9
	v_add_u32_e32 v0, 0x848, v101
	ds_write2_b32 v0, v2, v3 offset1:1
	s_waitcnt vmcnt(5)
	v_mul_f32_e32 v2, v122, v22
	v_mul_f32_e32 v3, v122, v23
	v_add_u32_e32 v0, 0xc60, v101
	ds_write2_b32 v0, v2, v3 offset1:1
	v_mul_f32_e32 v2, v122, v24
	v_mul_f32_e32 v3, v122, v25
	v_add_u32_e32 v0, 0xc68, v101
	ds_write2_b32 v0, v2, v3 offset1:1
	s_waitcnt vmcnt(4)
	v_mul_f32_e32 v2, v128, v14
	v_mul_f32_e32 v3, v128, v15
	v_add_u32_e32 v0, 0x1080, v101
	ds_write2_b32 v0, v2, v3 offset1:1
	v_mul_f32_e32 v2, v128, v16
	v_mul_f32_e32 v3, v128, v17
	v_add_u32_e32 v0, 0x1088, v101
	ds_write2_b32 v0, v2, v3 offset1:1
	s_waitcnt vmcnt(5)
	v_mul_f32_e32 v2, v126, v26
	v_mul_f32_e32 v3, v126, v27
	v_add_u32_e32 v0, 0x14a0, v101
	ds_write2_b32 v0, v2, v3 offset1:1
	v_mul_f32_e32 v2, v126, v28
	v_mul_f32_e32 v3, v126, v29
	v_add_u32_e32 v0, 0x14a8, v101
	ds_write2_b32 v0, v2, v3 offset1:1
	s_waitcnt vmcnt(4)
	v_mul_f32_e32 v2, v132, v18
	v_mul_f32_e32 v3, v132, v19
	v_add_u32_e32 v0, 0x18c0, v101
	ds_write2_b32 v0, v2, v3 offset1:1
	v_mul_f32_e32 v2, v132, v20
	v_mul_f32_e32 v3, v132, v21
	v_add_u32_e32 v0, 0x18c8, v101
	ds_write2_b32 v0, v2, v3 offset1:1
	s_waitcnt vmcnt(0)
	v_mul_f32_e32 v2, v130, v30
	v_mul_f32_e32 v3, v130, v31
	v_add_u32_e32 v0, 0x1ce0, v101
	ds_write2_b32 v0, v2, v3 offset1:1
	v_mul_f32_e32 v2, v130, v32
	v_mul_f32_e32 v3, v130, v33
	v_add_u32_e32 v0, 0x1ce8, v101
	ds_write2_b32 v0, v2, v3 offset1:1
	s_waitcnt lgkmcnt(0)
	ds_read2_b32 v[6:7], v99 offset0:33 offset1:41
	ds_read2_b32 v[8:9], v99 offset1:8
	ds_read2_b32 v[10:11], v99 offset0:66 offset1:74
	ds_read2_b32 v[12:13], v99 offset0:99 offset1:107
	ds_read2_b32 v[14:15], v99 offset0:132 offset1:140
	ds_read2_b32 v[16:17], v99 offset0:165 offset1:173
	ds_read2_b32 v[18:19], v99 offset0:198 offset1:206
	ds_read2_b32 v[20:21], v99 offset0:231 offset1:239
	v_lshl_add_u64 v[22:23], s[14:15], 0, v[116:117]
	v_lshlrev_b32_e32 v0, 1, v106
	s_waitcnt lgkmcnt(6)
	v_cvt_pk_bf16_f32 v2, v8, v6
	s_waitcnt lgkmcnt(4)
	v_cvt_pk_bf16_f32 v3, v10, v12
	s_waitcnt lgkmcnt(2)
	v_cvt_pk_bf16_f32 v4, v14, v16
	s_waitcnt lgkmcnt(0)
	v_cvt_pk_bf16_f32 v5, v18, v20
	v_lshl_add_u64 v[22:23], v[22:23], 0, v[0:1]
	global_store_dwordx4 v[22:23], v[2:5], off
	s_nop 1
	v_cvt_pk_bf16_f32 v2, v9, v7
	v_cvt_pk_bf16_f32 v3, v11, v13
	v_cvt_pk_bf16_f32 v4, v15, v17
	v_cvt_pk_bf16_f32 v5, v19, v21
	ds_read2_b32 v[8:9], v99 offset0:49 offset1:57
	ds_read2_b32 v[10:11], v99 offset0:16 offset1:24
	ds_read2_b32 v[12:13], v99 offset0:82 offset1:90
	ds_read2_b32 v[14:15], v99 offset0:115 offset1:123
	ds_read2_b32 v[16:17], v99 offset0:148 offset1:156
	ds_read2_b32 v[18:19], v99 offset0:181 offset1:189
	ds_read2_b32 v[20:21], v99 offset0:214 offset1:222
	ds_read2_b32 v[22:23], v99 offset0:247 offset1:255
	v_lshl_add_u64 v[6:7], s[14:15], 0, v[114:115]
	v_lshl_add_u64 v[6:7], v[6:7], 0, v[0:1]
	global_store_dwordx4 v[6:7], v[2:5], off
	v_lshl_add_u64 v[6:7], s[14:15], 0, v[112:113]
	v_lshl_add_u64 v[6:7], v[6:7], 0, v[0:1]
	s_waitcnt lgkmcnt(6)
	v_cvt_pk_bf16_f32 v2, v10, v8
	s_waitcnt lgkmcnt(4)
	v_cvt_pk_bf16_f32 v3, v12, v14
	s_waitcnt lgkmcnt(2)
	v_cvt_pk_bf16_f32 v4, v16, v18
	s_waitcnt lgkmcnt(0)
	v_cvt_pk_bf16_f32 v5, v20, v22
	global_store_dwordx4 v[6:7], v[2:5], off
	v_lshl_add_u64 v[6:7], s[14:15], 0, v[110:111]
	v_lshl_add_u64 v[6:7], v[6:7], 0, v[0:1]
	v_cvt_pk_bf16_f32 v2, v11, v9
	v_cvt_pk_bf16_f32 v3, v13, v15
	v_cvt_pk_bf16_f32 v4, v17, v19
	v_cvt_pk_bf16_f32 v5, v21, v23
	global_store_dwordx4 v[6:7], v[2:5], off
	s_waitcnt lgkmcnt(0)

.LBB0_233:
	s_andn2_b64 vcc, exec, s[50:51]
	s_cbranch_vccnz .LBB0_200
	s_cmp_eq_u32 s31, 0
	s_cbranch_scc1 .LBB0_199
	s_waitcnt vmcnt(6)
	v_mul_f32_e32 v2, v2, v120
	v_mul_f32_e32 v3, v3, v120
	ds_write2_b32 v101, v2, v3 offset1:1
	v_mul_f32_e32 v2, v4, v120
	v_mul_f32_e32 v3, v5, v120
	ds_write2_b32 v101, v2, v3 offset0:2 offset1:3
	v_mul_f32_e32 v2, v10, v118
	v_mul_f32_e32 v3, v11, v118
	v_add_u32_e32 v0, 0x420, v101
	ds_write2_b32 v0, v2, v3 offset1:1
	v_mul_f32_e32 v2, v12, v118
	v_mul_f32_e32 v3, v13, v118
	v_add_u32_e32 v0, 0x428, v101
	ds_write2_b32 v0, v2, v3 offset1:1
	v_mul_f32_e32 v2, v6, v124
	v_mul_f32_e32 v3, v7, v124
	v_add_u32_e32 v0, 0x840, v101
	ds_write2_b32 v0, v2, v3 offset1:1
	v_mul_f32_e32 v2, v8, v124
	v_mul_f32_e32 v3, v9, v124
	v_add_u32_e32 v0, 0x848, v101
	ds_write2_b32 v0, v2, v3 offset1:1
	s_waitcnt vmcnt(5)
	v_mul_f32_e32 v2, v22, v122
	v_mul_f32_e32 v3, v23, v122
	v_add_u32_e32 v0, 0xc60, v101
	ds_write2_b32 v0, v2, v3 offset1:1
	v_mul_f32_e32 v2, v24, v122
	v_mul_f32_e32 v3, v25, v122
	v_add_u32_e32 v0, 0xc68, v101
	ds_write2_b32 v0, v2, v3 offset1:1
	s_waitcnt vmcnt(4)
	v_mul_f32_e32 v2, v14, v128
	v_mul_f32_e32 v3, v15, v128
	v_add_u32_e32 v0, 0x1080, v101
	ds_write2_b32 v0, v2, v3 offset1:1
	v_mul_f32_e32 v2, v16, v128
	v_mul_f32_e32 v3, v17, v128
	v_add_u32_e32 v0, 0x1088, v101
	ds_write2_b32 v0, v2, v3 offset1:1
	v_mul_f32_e32 v2, v26, v126
	v_mul_f32_e32 v3, v27, v126
	v_add_u32_e32 v0, 0x14a0, v101
	ds_write2_b32 v0, v2, v3 offset1:1
	v_mul_f32_e32 v2, v28, v126
	v_mul_f32_e32 v3, v29, v126
	v_add_u32_e32 v0, 0x14a8, v101
	ds_write2_b32 v0, v2, v3 offset1:1
	v_mul_f32_e32 v2, v18, v132
	v_mul_f32_e32 v3, v19, v132
	v_add_u32_e32 v0, 0x18c0, v101
	ds_write2_b32 v0, v2, v3 offset1:1
	v_mul_f32_e32 v2, v20, v132
	v_mul_f32_e32 v3, v21, v132
	v_add_u32_e32 v0, 0x18c8, v101
	ds_write2_b32 v0, v2, v3 offset1:1
	s_waitcnt vmcnt(0)
	v_mul_f32_e32 v2, v30, v130
	v_mul_f32_e32 v3, v31, v130
	v_add_u32_e32 v0, 0x1ce0, v101
	ds_write2_b32 v0, v2, v3 offset1:1
	v_mul_f32_e32 v2, v32, v130
	v_mul_f32_e32 v3, v33, v130
	v_add_u32_e32 v0, 0x1ce8, v101
	ds_write2_b32 v0, v2, v3 offset1:1
	s_waitcnt lgkmcnt(0)
	ds_read2_b32 v[6:7], v99 offset0:33 offset1:41
	ds_read2_b32 v[8:9], v99 offset1:8
	ds_read2_b32 v[10:11], v99 offset0:66 offset1:74
	ds_read2_b32 v[12:13], v99 offset0:99 offset1:107
	ds_read2_b32 v[14:15], v99 offset0:132 offset1:140
	ds_read2_b32 v[16:17], v99 offset0:165 offset1:173
	ds_read2_b32 v[18:19], v99 offset0:198 offset1:206
	ds_read2_b32 v[20:21], v99 offset0:231 offset1:239
	v_lshl_add_u64 v[22:23], s[14:15], 0, v[116:117]
	v_lshlrev_b32_e32 v0, 1, v106
	s_waitcnt lgkmcnt(6)
	v_cvt_pk_bf16_f32 v2, v8, v6
	s_waitcnt lgkmcnt(4)
	v_cvt_pk_bf16_f32 v3, v10, v12
	s_waitcnt lgkmcnt(2)
	v_cvt_pk_bf16_f32 v4, v14, v16
	s_waitcnt lgkmcnt(0)
	v_cvt_pk_bf16_f32 v5, v18, v20
	v_lshl_add_u64 v[22:23], v[22:23], 0, v[0:1]
	global_store_dwordx4 v[22:23], v[2:5], off
	s_nop 1
	v_cvt_pk_bf16_f32 v2, v9, v7
	v_cvt_pk_bf16_f32 v3, v11, v13
	v_cvt_pk_bf16_f32 v4, v15, v17
	v_cvt_pk_bf16_f32 v5, v19, v21
	ds_read2_b32 v[8:9], v99 offset0:49 offset1:57
	ds_read2_b32 v[10:11], v99 offset0:16 offset1:24
	ds_read2_b32 v[12:13], v99 offset0:82 offset1:90
	ds_read2_b32 v[14:15], v99 offset0:115 offset1:123
	ds_read2_b32 v[16:17], v99 offset0:148 offset1:156
	ds_read2_b32 v[18:19], v99 offset0:181 offset1:189
	ds_read2_b32 v[20:21], v99 offset0:214 offset1:222
	ds_read2_b32 v[22:23], v99 offset0:247 offset1:255
	v_lshl_add_u64 v[6:7], s[14:15], 0, v[114:115]
	v_lshl_add_u64 v[6:7], v[6:7], 0, v[0:1]
	global_store_dwordx4 v[6:7], v[2:5], off
	v_lshl_add_u64 v[6:7], s[14:15], 0, v[112:113]
	v_lshl_add_u64 v[6:7], v[6:7], 0, v[0:1]
	s_waitcnt lgkmcnt(6)
	v_cvt_pk_bf16_f32 v2, v10, v8
	s_waitcnt lgkmcnt(4)
	v_cvt_pk_bf16_f32 v3, v12, v14
	s_waitcnt lgkmcnt(2)
	v_cvt_pk_bf16_f32 v4, v16, v18
	s_waitcnt lgkmcnt(0)
	v_cvt_pk_bf16_f32 v5, v20, v22
	global_store_dwordx4 v[6:7], v[2:5], off
	v_lshl_add_u64 v[6:7], s[14:15], 0, v[110:111]
	v_lshl_add_u64 v[6:7], v[6:7], 0, v[0:1]
	v_cvt_pk_bf16_f32 v2, v11, v9
	v_cvt_pk_bf16_f32 v3, v13, v15
	v_cvt_pk_bf16_f32 v4, v17, v19
	v_cvt_pk_bf16_f32 v5, v21, v23
	global_store_dwordx4 v[6:7], v[2:5], off
	s_waitcnt lgkmcnt(0)
	s_branch .LBB0_199

.LBB0_258:
	s_and_b64 vcc, exec, s[38:39]
	s_cbranch_vccz .LBB0_262
	s_cmp_eq_u32 s31, 0
	s_cbranch_scc1 .LBB0_261
	s_waitcnt vmcnt(6)
	v_mul_f32_e32 v2, v2, v120
	v_mul_f32_e32 v3, v3, v120
	ds_write2_b32 v101, v2, v3 offset1:1
	v_mul_f32_e32 v2, v4, v120
	v_mul_f32_e32 v3, v5, v120
	ds_write2_b32 v101, v2, v3 offset0:2 offset1:3
	v_mul_f32_e32 v2, v10, v118
	v_mul_f32_e32 v3, v11, v118
	v_add_u32_e32 v4, 0x420, v101
	ds_write2_b32 v4, v2, v3 offset1:1
	v_mul_f32_e32 v2, v12, v118
	v_mul_f32_e32 v3, v13, v118
	v_add_u32_e32 v4, 0x428, v101
	ds_write2_b32 v4, v2, v3 offset1:1
	v_mul_f32_e32 v2, v6, v124
	v_mul_f32_e32 v3, v7, v124
	v_add_u32_e32 v4, 0x840, v101
	ds_write2_b32 v4, v2, v3 offset1:1
	v_mul_f32_e32 v2, v8, v124
	v_mul_f32_e32 v3, v9, v124
	v_add_u32_e32 v4, 0x848, v101
	ds_write2_b32 v4, v2, v3 offset1:1
	s_waitcnt vmcnt(5)
	v_mul_f32_e32 v2, v22, v122
	v_mul_f32_e32 v3, v23, v122
	v_add_u32_e32 v4, 0xc60, v101
	ds_write2_b32 v4, v2, v3 offset1:1
	v_mul_f32_e32 v2, v24, v122
	v_mul_f32_e32 v3, v25, v122
	v_add_u32_e32 v4, 0xc68, v101
	ds_write2_b32 v4, v2, v3 offset1:1
	s_waitcnt vmcnt(4)
	v_mul_f32_e32 v2, v14, v128
	v_mul_f32_e32 v3, v15, v128
	v_add_u32_e32 v4, 0x1080, v101
	ds_write2_b32 v4, v2, v3 offset1:1
	v_mul_f32_e32 v2, v16, v128
	v_mul_f32_e32 v3, v17, v128
	v_add_u32_e32 v4, 0x1088, v101
	ds_write2_b32 v4, v2, v3 offset1:1
	v_mul_f32_e32 v2, v26, v126
	v_mul_f32_e32 v3, v27, v126
	v_add_u32_e32 v4, 0x14a0, v101
	ds_write2_b32 v4, v2, v3 offset1:1
	v_mul_f32_e32 v2, v28, v126
	v_mul_f32_e32 v3, v29, v126
	v_add_u32_e32 v4, 0x14a8, v101
	ds_write2_b32 v4, v2, v3 offset1:1
	v_mul_f32_e32 v2, v18, v132
	v_mul_f32_e32 v3, v19, v132
	v_add_u32_e32 v4, 0x18c0, v101
	ds_write2_b32 v4, v2, v3 offset1:1
	v_mul_f32_e32 v2, v20, v132
	v_mul_f32_e32 v3, v21, v132
	v_add_u32_e32 v4, 0x18c8, v101
	ds_write2_b32 v4, v2, v3 offset1:1
	s_waitcnt vmcnt(0)
	v_mul_f32_e32 v2, v30, v130
	v_mul_f32_e32 v3, v31, v130
	v_add_u32_e32 v4, 0x1ce0, v101
	ds_write2_b32 v4, v2, v3 offset1:1
	v_mul_f32_e32 v2, v32, v130
	v_mul_f32_e32 v3, v33, v130
	v_add_u32_e32 v4, 0x1ce8, v101
	ds_write2_b32 v4, v2, v3 offset1:1
	s_waitcnt lgkmcnt(0)
	ds_read2_b32 v[6:7], v99 offset0:33 offset1:41
	ds_read2_b32 v[8:9], v99 offset1:8
	ds_read2_b32 v[10:11], v99 offset0:66 offset1:74
	ds_read2_b32 v[12:13], v99 offset0:99 offset1:107
	ds_read2_b32 v[14:15], v99 offset0:132 offset1:140
	ds_read2_b32 v[16:17], v99 offset0:165 offset1:173
	ds_read2_b32 v[18:19], v99 offset0:198 offset1:206
	ds_read2_b32 v[20:21], v99 offset0:231 offset1:239
	v_lshl_add_u64 v[22:23], s[14:15], 0, v[116:117]
	v_lshlrev_b32_e32 v24, 1, v106
	v_mov_b32_e32 v25, v1
	s_waitcnt lgkmcnt(6)
	v_cvt_pk_bf16_f32 v2, v8, v6
	s_waitcnt lgkmcnt(4)
	v_cvt_pk_bf16_f32 v3, v10, v12
	s_waitcnt lgkmcnt(2)
	v_cvt_pk_bf16_f32 v4, v14, v16
	s_waitcnt lgkmcnt(0)
	v_cvt_pk_bf16_f32 v5, v18, v20
	v_lshl_add_u64 v[22:23], v[22:23], 0, v[24:25]
	global_store_dwordx4 v[22:23], v[2:5], off
	s_nop 1
	v_cvt_pk_bf16_f32 v2, v9, v7
	v_cvt_pk_bf16_f32 v3, v11, v13
	v_cvt_pk_bf16_f32 v4, v15, v17
	v_cvt_pk_bf16_f32 v5, v19, v21
	ds_read2_b32 v[8:9], v99 offset0:49 offset1:57
	ds_read2_b32 v[10:11], v99 offset0:16 offset1:24
	ds_read2_b32 v[12:13], v99 offset0:82 offset1:90
	ds_read2_b32 v[14:15], v99 offset0:115 offset1:123
	ds_read2_b32 v[16:17], v99 offset0:148 offset1:156
	ds_read2_b32 v[18:19], v99 offset0:181 offset1:189
	ds_read2_b32 v[20:21], v99 offset0:214 offset1:222
	ds_read2_b32 v[22:23], v99 offset0:247 offset1:255
	v_lshl_add_u64 v[6:7], s[14:15], 0, v[114:115]
	v_lshl_add_u64 v[6:7], v[6:7], 0, v[24:25]
	global_store_dwordx4 v[6:7], v[2:5], off
	v_lshl_add_u64 v[6:7], s[14:15], 0, v[112:113]
	v_lshl_add_u64 v[6:7], v[6:7], 0, v[24:25]
	s_waitcnt lgkmcnt(6)
	v_cvt_pk_bf16_f32 v2, v10, v8
	s_waitcnt lgkmcnt(4)
	v_cvt_pk_bf16_f32 v3, v12, v14
	s_waitcnt lgkmcnt(2)
	v_cvt_pk_bf16_f32 v4, v16, v18
	s_waitcnt lgkmcnt(0)
	v_cvt_pk_bf16_f32 v5, v20, v22
	global_store_dwordx4 v[6:7], v[2:5], off
	v_lshl_add_u64 v[6:7], s[14:15], 0, v[110:111]
	v_lshl_add_u64 v[6:7], v[6:7], 0, v[24:25]
	v_cvt_pk_bf16_f32 v2, v11, v9
	v_cvt_pk_bf16_f32 v3, v13, v15
	v_cvt_pk_bf16_f32 v4, v17, v19
	v_cvt_pk_bf16_f32 v5, v21, v23
	global_store_dwordx4 v[6:7], v[2:5], off
	s_waitcnt lgkmcnt(0)

.LBB0_277:
	s_andn2_b64 vcc, exec, s[38:39]
	s_cbranch_vccnz .LBB0_281
	s_cmp_eq_u32 s31, 0
	s_cbranch_scc1 .LBB0_280
	s_waitcnt vmcnt(0)
	v_mul_f32_e32 v2, v58, v134
	v_mul_f32_e32 v3, v59, v134
	ds_write2_b32 v101, v2, v3 offset1:1
	v_mul_f32_e32 v2, v60, v134
	v_mul_f32_e32 v3, v61, v134
	ds_write2_b32 v101, v2, v3 offset0:2 offset1:3
	v_mul_f32_e32 v2, v74, v136
	v_mul_f32_e32 v3, v75, v136
	v_add_u32_e32 v4, 0x420, v101
	ds_write2_b32 v4, v2, v3 offset1:1
	v_mul_f32_e32 v2, v76, v136
	v_mul_f32_e32 v3, v77, v136
	v_add_u32_e32 v4, 0x428, v101
	ds_write2_b32 v4, v2, v3 offset1:1
	v_mul_f32_e32 v2, v70, v138
	v_mul_f32_e32 v3, v71, v138
	v_add_u32_e32 v4, 0x840, v101
	ds_write2_b32 v4, v2, v3 offset1:1
	v_mul_f32_e32 v2, v72, v138
	v_mul_f32_e32 v3, v73, v138
	v_add_u32_e32 v4, 0x848, v101
	ds_write2_b32 v4, v2, v3 offset1:1
	v_mul_f32_e32 v2, v82, v140
	v_mul_f32_e32 v3, v83, v140
	v_add_u32_e32 v4, 0xc60, v101
	ds_write2_b32 v4, v2, v3 offset1:1
	v_mul_f32_e32 v2, v84, v140
	v_mul_f32_e32 v3, v85, v140
	v_add_u32_e32 v4, 0xc68, v101
	ds_write2_b32 v4, v2, v3 offset1:1
	v_mul_f32_e32 v2, v78, v142
	v_mul_f32_e32 v3, v79, v142
	v_add_u32_e32 v4, 0x1080, v101
	ds_write2_b32 v4, v2, v3 offset1:1
	v_mul_f32_e32 v2, v80, v142
	v_mul_f32_e32 v3, v81, v142
	v_add_u32_e32 v4, 0x1088, v101
	ds_write2_b32 v4, v2, v3 offset1:1
	v_mul_f32_e32 v2, v90, v144
	v_mul_f32_e32 v3, v91, v144
	v_add_u32_e32 v4, 0x14a0, v101
	ds_write2_b32 v4, v2, v3 offset1:1
	v_mul_f32_e32 v2, v92, v144
	v_mul_f32_e32 v3, v93, v144
	v_add_u32_e32 v4, 0x14a8, v101
	ds_write2_b32 v4, v2, v3 offset1:1
	v_mul_f32_e32 v2, v86, v146
	v_mul_f32_e32 v3, v87, v146
	v_add_u32_e32 v4, 0x18c0, v101
	ds_write2_b32 v4, v2, v3 offset1:1
	v_mul_f32_e32 v2, v88, v146
	v_mul_f32_e32 v3, v89, v146
	v_add_u32_e32 v4, 0x18c8, v101
	ds_write2_b32 v4, v2, v3 offset1:1
	v_mul_f32_e32 v2, v94, v148
	v_mul_f32_e32 v3, v95, v148
	v_add_u32_e32 v4, 0x1ce0, v101
	ds_write2_b32 v4, v2, v3 offset1:1
	v_mul_f32_e32 v2, v96, v148
	v_mul_f32_e32 v3, v97, v148
	v_add_u32_e32 v4, 0x1ce8, v101
	ds_write2_b32 v4, v2, v3 offset1:1
	s_waitcnt lgkmcnt(0)
	ds_read2_b32 v[6:7], v99 offset0:33 offset1:41
	ds_read2_b32 v[8:9], v99 offset1:8
	ds_read2_b32 v[10:11], v99 offset0:66 offset1:74
	ds_read2_b32 v[12:13], v99 offset0:99 offset1:107
	ds_read2_b32 v[14:15], v99 offset0:132 offset1:140
	ds_read2_b32 v[16:17], v99 offset0:165 offset1:173
	ds_read2_b32 v[18:19], v99 offset0:198 offset1:206
	ds_read2_b32 v[20:21], v99 offset0:231 offset1:239
	v_lshl_add_u64 v[22:23], s[16:17], 0, v[116:117]
	v_lshlrev_b32_e32 v24, 1, v106
	v_mov_b32_e32 v25, v1
	s_waitcnt lgkmcnt(6)
	v_cvt_pk_bf16_f32 v2, v8, v6
	s_waitcnt lgkmcnt(4)
	v_cvt_pk_bf16_f32 v3, v10, v12
	s_waitcnt lgkmcnt(2)
	v_cvt_pk_bf16_f32 v4, v14, v16
	s_waitcnt lgkmcnt(0)
	v_cvt_pk_bf16_f32 v5, v18, v20
	v_lshl_add_u64 v[22:23], v[22:23], 0, v[24:25]
	global_store_dwordx4 v[22:23], v[2:5], off
	s_nop 1
	v_cvt_pk_bf16_f32 v2, v9, v7
	v_cvt_pk_bf16_f32 v3, v11, v13
	v_cvt_pk_bf16_f32 v4, v15, v17
	v_cvt_pk_bf16_f32 v5, v19, v21
	ds_read2_b32 v[8:9], v99 offset0:49 offset1:57
	ds_read2_b32 v[10:11], v99 offset0:16 offset1:24
	ds_read2_b32 v[12:13], v99 offset0:82 offset1:90
	ds_read2_b32 v[14:15], v99 offset0:115 offset1:123
	ds_read2_b32 v[16:17], v99 offset0:148 offset1:156
	ds_read2_b32 v[18:19], v99 offset0:181 offset1:189
	ds_read2_b32 v[20:21], v99 offset0:214 offset1:222
	ds_read2_b32 v[22:23], v99 offset0:247 offset1:255
	v_lshl_add_u64 v[6:7], s[16:17], 0, v[114:115]
	v_lshl_add_u64 v[6:7], v[6:7], 0, v[24:25]
	global_store_dwordx4 v[6:7], v[2:5], off
	v_lshl_add_u64 v[6:7], s[16:17], 0, v[112:113]
	v_lshl_add_u64 v[6:7], v[6:7], 0, v[24:25]
	s_waitcnt lgkmcnt(6)
	v_cvt_pk_bf16_f32 v2, v10, v8
	s_waitcnt lgkmcnt(4)
	v_cvt_pk_bf16_f32 v3, v12, v14
	s_waitcnt lgkmcnt(2)
	v_cvt_pk_bf16_f32 v4, v16, v18
	s_waitcnt lgkmcnt(0)
	v_cvt_pk_bf16_f32 v5, v20, v22
	global_store_dwordx4 v[6:7], v[2:5], off
	v_lshl_add_u64 v[6:7], s[16:17], 0, v[110:111]
	v_lshl_add_u64 v[6:7], v[6:7], 0, v[24:25]
	v_cvt_pk_bf16_f32 v2, v11, v9
	v_cvt_pk_bf16_f32 v3, v13, v15
	v_cvt_pk_bf16_f32 v4, v17, v19
	v_cvt_pk_bf16_f32 v5, v21, v23
	global_store_dwordx4 v[6:7], v[2:5], off
	s_waitcnt lgkmcnt(0)

.LBB0_287:
	s_andn2_b64 vcc, exec, s[36:37]
	s_cbranch_vccnz .LBB0_284
	s_cmp_eq_u32 s31, 0
	s_cbranch_scc1 .LBB0_283
	s_waitcnt vmcnt(6)
	v_mul_f32_e32 v34, v124, v34
	v_mul_f32_e32 v35, v124, v35
	ds_write2_b32 v101, v34, v35 offset1:1
	v_mul_f32_e32 v34, v124, v36
	v_mul_f32_e32 v35, v124, v37
	ds_write2_b32 v101, v34, v35 offset0:2 offset1:3
	s_waitcnt vmcnt(5)
	v_mul_f32_e32 v34, v126, v42
	v_mul_f32_e32 v35, v126, v43
	v_add_u32_e32 v36, 0x420, v101
	ds_write2_b32 v36, v34, v35 offset1:1
	v_mul_f32_e32 v34, v126, v44
	v_mul_f32_e32 v35, v126, v45
	v_add_u32_e32 v36, 0x428, v101
	ds_write2_b32 v36, v34, v35 offset1:1
	s_waitcnt vmcnt(4)
	v_mul_f32_e32 v34, v132, v38
	v_mul_f32_e32 v35, v132, v39
	v_add_u32_e32 v36, 0x840, v101
	ds_write2_b32 v36, v34, v35 offset1:1
	v_mul_f32_e32 v34, v132, v40
	v_mul_f32_e32 v35, v132, v41
	v_add_u32_e32 v36, 0x848, v101
	ds_write2_b32 v36, v34, v35 offset1:1
	v_mul_f32_e32 v34, v122, v50
	v_mul_f32_e32 v35, v122, v51
	v_add_u32_e32 v36, 0xc60, v101
	ds_write2_b32 v36, v34, v35 offset1:1
	v_mul_f32_e32 v34, v122, v52
	v_mul_f32_e32 v35, v122, v53
	v_add_u32_e32 v36, 0xc68, v101
	ds_write2_b32 v36, v34, v35 offset1:1
	s_waitcnt vmcnt(3)
	v_mul_f32_e32 v34, v130, v46
	v_mul_f32_e32 v35, v130, v47
	v_add_u32_e32 v36, 0x1080, v101
	ds_write2_b32 v36, v34, v35 offset1:1
	v_mul_f32_e32 v34, v130, v48
	v_mul_f32_e32 v35, v130, v49
	v_add_u32_e32 v36, 0x1088, v101
	ds_write2_b32 v36, v34, v35 offset1:1
	s_waitcnt vmcnt(0)
	v_mul_f32_e32 v34, v120, v62
	v_mul_f32_e32 v35, v120, v63
	v_add_u32_e32 v36, 0x14a0, v101
	ds_write2_b32 v36, v34, v35 offset1:1
	v_mul_f32_e32 v34, v120, v64
	v_mul_f32_e32 v35, v120, v65
	v_add_u32_e32 v36, 0x14a8, v101
	ds_write2_b32 v36, v34, v35 offset1:1
	v_mul_f32_e32 v34, v128, v54
	v_mul_f32_e32 v35, v128, v55
	v_add_u32_e32 v36, 0x18c0, v101
	ds_write2_b32 v36, v34, v35 offset1:1
	v_mul_f32_e32 v34, v128, v56
	v_mul_f32_e32 v35, v128, v57
	v_add_u32_e32 v36, 0x18c8, v101
	ds_write2_b32 v36, v34, v35 offset1:1
	v_mul_f32_e32 v34, v118, v66
	v_mul_f32_e32 v35, v118, v67
	v_add_u32_e32 v36, 0x1ce0, v101
	ds_write2_b32 v36, v34, v35 offset1:1
	v_mul_f32_e32 v34, v118, v68
	v_mul_f32_e32 v35, v118, v69
	v_add_u32_e32 v36, 0x1ce8, v101
	ds_write2_b32 v36, v34, v35 offset1:1
	s_waitcnt lgkmcnt(0)
	ds_read2_b32 v[38:39], v99 offset0:33 offset1:41
	ds_read2_b32 v[40:41], v99 offset1:8
	ds_read2_b32 v[42:43], v99 offset0:66 offset1:74
	ds_read2_b32 v[44:45], v99 offset0:99 offset1:107
	ds_read2_b32 v[46:47], v99 offset0:132 offset1:140
	ds_read2_b32 v[48:49], v99 offset0:165 offset1:173
	ds_read2_b32 v[50:51], v99 offset0:198 offset1:206
	ds_read2_b32 v[52:53], v99 offset0:231 offset1:239
	v_mad_u64_u32 v[54:55], s[36:37], s34, v104, 0
	v_lshl_add_u64 v[54:55], v[54:55], 1, s[14:15]
	v_lshlrev_b32_e32 v56, 1, v106
	v_mov_b32_e32 v57, v1
	s_waitcnt lgkmcnt(6)
	v_cvt_pk_bf16_f32 v34, v40, v38
	s_waitcnt lgkmcnt(4)
	v_cvt_pk_bf16_f32 v35, v42, v44
	s_waitcnt lgkmcnt(2)
	v_cvt_pk_bf16_f32 v36, v46, v48
	s_waitcnt lgkmcnt(0)
	v_cvt_pk_bf16_f32 v37, v50, v52
	v_lshl_add_u64 v[54:55], v[54:55], 0, v[56:57]
	global_store_dwordx4 v[54:55], v[34:37], off
	s_nop 1
	v_cvt_pk_bf16_f32 v34, v41, v39
	v_cvt_pk_bf16_f32 v35, v43, v45
	v_cvt_pk_bf16_f32 v36, v47, v49
	v_cvt_pk_bf16_f32 v37, v51, v53
	v_mad_u64_u32 v[38:39], s[36:37], s34, v102, 0
	ds_read2_b32 v[40:41], v99 offset0:16 offset1:24
	ds_read2_b32 v[42:43], v99 offset0:49 offset1:57
	ds_read2_b32 v[44:45], v99 offset0:82 offset1:90
	ds_read2_b32 v[46:47], v99 offset0:115 offset1:123
	ds_read2_b32 v[48:49], v99 offset0:148 offset1:156
	ds_read2_b32 v[50:51], v99 offset0:181 offset1:189
	ds_read2_b32 v[52:53], v99 offset0:214 offset1:222
	ds_read2_b32 v[54:55], v99 offset0:247 offset1:255
	v_lshl_add_u64 v[38:39], v[38:39], 1, s[14:15]
	v_lshl_add_u64 v[38:39], v[38:39], 0, v[56:57]
	global_store_dwordx4 v[38:39], v[34:37], off
	v_mad_u64_u32 v[38:39], s[36:37], s34, v100, 0
	v_lshl_add_u64 v[38:39], v[38:39], 1, s[14:15]
	s_waitcnt lgkmcnt(6)
	v_cvt_pk_bf16_f32 v34, v40, v42
	s_waitcnt lgkmcnt(4)
	v_cvt_pk_bf16_f32 v35, v44, v46
	s_waitcnt lgkmcnt(2)
	v_cvt_pk_bf16_f32 v36, v48, v50
	s_waitcnt lgkmcnt(0)
	v_cvt_pk_bf16_f32 v37, v52, v54
	v_lshl_add_u64 v[38:39], v[38:39], 0, v[56:57]
	global_store_dwordx4 v[38:39], v[34:37], off
	v_mad_u64_u32 v[38:39], s[36:37], s34, v98, 0
	v_lshl_add_u64 v[38:39], v[38:39], 1, s[14:15]
	v_cvt_pk_bf16_f32 v34, v41, v43
	v_cvt_pk_bf16_f32 v35, v45, v47
	v_cvt_pk_bf16_f32 v36, v49, v51
	v_cvt_pk_bf16_f32 v37, v53, v55
	v_lshl_add_u64 v[38:39], v[38:39], 0, v[56:57]
	global_store_dwordx4 v[38:39], v[34:37], off
	s_waitcnt lgkmcnt(0)
	s_branch .LBB0_283

.LBB0_292:
	s_and_b64 vcc, exec, s[16:17]
	s_cbranch_vccz .LBB0_296
	s_cmp_eq_u32 s31, 0
	s_cbranch_scc1 .LBB0_295
	s_waitcnt vmcnt(6)
	v_mul_f32_e32 v34, v34, v124
	v_mul_f32_e32 v35, v35, v124
	ds_write2_b32 v101, v34, v35 offset1:1
	v_mul_f32_e32 v34, v36, v124
	v_mul_f32_e32 v35, v37, v124
	ds_write2_b32 v101, v34, v35 offset0:2 offset1:3
	s_waitcnt vmcnt(5)
	v_mul_f32_e32 v34, v42, v126
	v_mul_f32_e32 v35, v43, v126
	v_add_u32_e32 v0, 0x420, v101
	ds_write2_b32 v0, v34, v35 offset1:1
	v_mul_f32_e32 v34, v44, v126
	v_mul_f32_e32 v35, v45, v126
	v_add_u32_e32 v0, 0x428, v101
	ds_write2_b32 v0, v34, v35 offset1:1
	s_waitcnt vmcnt(4)
	v_mul_f32_e32 v34, v38, v132
	v_mul_f32_e32 v35, v39, v132
	v_add_u32_e32 v0, 0x840, v101
	ds_write2_b32 v0, v34, v35 offset1:1
	v_mul_f32_e32 v34, v40, v132
	v_mul_f32_e32 v35, v41, v132
	v_add_u32_e32 v0, 0x848, v101
	ds_write2_b32 v0, v34, v35 offset1:1
	v_mul_f32_e32 v34, v50, v122
	v_mul_f32_e32 v35, v51, v122
	v_add_u32_e32 v0, 0xc60, v101
	ds_write2_b32 v0, v34, v35 offset1:1
	v_mul_f32_e32 v34, v52, v122
	v_mul_f32_e32 v35, v53, v122
	v_add_u32_e32 v0, 0xc68, v101
	ds_write2_b32 v0, v34, v35 offset1:1
	s_waitcnt vmcnt(3)
	v_mul_f32_e32 v34, v46, v130
	v_mul_f32_e32 v35, v47, v130
	v_add_u32_e32 v0, 0x1080, v101
	ds_write2_b32 v0, v34, v35 offset1:1
	v_mul_f32_e32 v34, v48, v130
	v_mul_f32_e32 v35, v49, v130
	v_add_u32_e32 v0, 0x1088, v101
	ds_write2_b32 v0, v34, v35 offset1:1
	s_waitcnt vmcnt(0)
	v_mul_f32_e32 v34, v62, v120
	v_mul_f32_e32 v35, v63, v120
	v_add_u32_e32 v0, 0x14a0, v101
	ds_write2_b32 v0, v34, v35 offset1:1
	v_mul_f32_e32 v34, v64, v120
	v_mul_f32_e32 v35, v65, v120
	v_add_u32_e32 v0, 0x14a8, v101
	ds_write2_b32 v0, v34, v35 offset1:1
	v_mul_f32_e32 v34, v54, v128
	v_mul_f32_e32 v35, v55, v128
	v_add_u32_e32 v0, 0x18c0, v101
	ds_write2_b32 v0, v34, v35 offset1:1
	v_mul_f32_e32 v34, v56, v128
	v_mul_f32_e32 v35, v57, v128
	v_add_u32_e32 v0, 0x18c8, v101
	ds_write2_b32 v0, v34, v35 offset1:1
	v_mul_f32_e32 v34, v66, v118
	v_mul_f32_e32 v35, v67, v118
	v_add_u32_e32 v0, 0x1ce0, v101
	ds_write2_b32 v0, v34, v35 offset1:1
	v_mul_f32_e32 v34, v68, v118
	v_mul_f32_e32 v35, v69, v118
	v_add_u32_e32 v0, 0x1ce8, v101
	ds_write2_b32 v0, v34, v35 offset1:1
	s_waitcnt lgkmcnt(0)
	ds_read2_b32 v[38:39], v99 offset0:33 offset1:41
	ds_read2_b32 v[40:41], v99 offset1:8
	ds_read2_b32 v[42:43], v99 offset0:66 offset1:74
	ds_read2_b32 v[44:45], v99 offset0:99 offset1:107
	ds_read2_b32 v[46:47], v99 offset0:132 offset1:140
	ds_read2_b32 v[48:49], v99 offset0:165 offset1:173
	ds_read2_b32 v[50:51], v99 offset0:198 offset1:206
	ds_read2_b32 v[52:53], v99 offset0:231 offset1:239
	v_mul_u32_u24_e32 v0, s34, v104
	v_lshlrev_b32_e32 v0, 1, v0
	v_lshl_add_u64 v[54:55], s[14:15], 0, v[0:1]
	v_lshlrev_b32_e32 v0, 1, v106
	s_lshl_b32 s14, s34, 3
	s_waitcnt lgkmcnt(6)
	v_cvt_pk_bf16_f32 v34, v40, v38
	s_waitcnt lgkmcnt(4)
	v_cvt_pk_bf16_f32 v35, v42, v44
	s_waitcnt lgkmcnt(2)
	v_cvt_pk_bf16_f32 v36, v46, v48
	s_waitcnt lgkmcnt(0)
	v_cvt_pk_bf16_f32 v37, v50, v52
	v_lshl_add_u64 v[56:57], v[54:55], 0, v[0:1]
	s_ashr_i32 s15, s14, 31
	global_store_dwordx4 v[56:57], v[34:37], off
	s_lshl_b64 s[14:15], s[14:15], 1
	s_nop 0
	v_cvt_pk_bf16_f32 v34, v41, v39
	v_cvt_pk_bf16_f32 v35, v43, v45
	v_cvt_pk_bf16_f32 v36, v47, v49
	v_cvt_pk_bf16_f32 v37, v51, v53
	v_lshl_add_u64 v[38:39], v[54:55], 0, s[14:15]
	ds_read2_b32 v[42:43], v99 offset0:16 offset1:24
	ds_read2_b32 v[44:45], v99 offset0:49 offset1:57
	ds_read2_b32 v[46:47], v99 offset0:82 offset1:90
	ds_read2_b32 v[48:49], v99 offset0:115 offset1:123
	ds_read2_b32 v[50:51], v99 offset0:148 offset1:156
	ds_read2_b32 v[52:53], v99 offset0:181 offset1:189
	ds_read2_b32 v[54:55], v99 offset0:214 offset1:222
	ds_read2_b32 v[56:57], v99 offset0:247 offset1:255
	v_lshl_add_u64 v[40:41], v[38:39], 0, v[0:1]
	v_lshl_add_u64 v[38:39], v[38:39], 0, s[14:15]
	global_store_dwordx4 v[40:41], v[34:37], off
	v_lshl_add_u64 v[40:41], v[38:39], 0, v[0:1]
	v_lshl_add_u64 v[38:39], v[38:39], 0, s[14:15]
	s_waitcnt lgkmcnt(6)
	v_cvt_pk_bf16_f32 v34, v42, v44
	s_waitcnt lgkmcnt(4)
	v_cvt_pk_bf16_f32 v35, v46, v48
	s_waitcnt lgkmcnt(2)
	v_cvt_pk_bf16_f32 v36, v50, v52
	s_waitcnt lgkmcnt(0)
	v_cvt_pk_bf16_f32 v37, v54, v56
	global_store_dwordx4 v[40:41], v[34:37], off
	v_lshl_add_u64 v[38:39], v[38:39], 0, v[0:1]
	s_nop 0
	v_cvt_pk_bf16_f32 v34, v43, v45
	v_cvt_pk_bf16_f32 v35, v47, v49
	v_cvt_pk_bf16_f32 v36, v51, v53
	v_cvt_pk_bf16_f32 v37, v55, v57
	global_store_dwordx4 v[38:39], v[34:37], off
	s_waitcnt lgkmcnt(0)

.LBB0_314:
	s_andn2_b64 vcc, exec, s[44:45]
	s_cbranch_vccnz .LBB0_318
	s_cmp_eq_u32 s31, 0
	s_cbranch_scc1 .LBB0_317
	s_waitcnt vmcnt(1)
	v_mul_f32_e32 v26, v126, v26
	v_mul_f32_e32 v27, v126, v27
	v_add_u32_e32 v0, 0x420, v101
	ds_write2_b32 v0, v26, v27 offset1:1
	v_mul_f32_e32 v26, v126, v28
	v_mul_f32_e32 v27, v126, v29
	v_add_u32_e32 v0, 0x428, v101
	ds_write2_b32 v0, v26, v27 offset1:1
	v_mul_f32_e32 v22, v132, v22
	v_mul_f32_e32 v23, v132, v23
	v_add_u32_e32 v0, 0x840, v101
	ds_write2_b32 v0, v22, v23 offset1:1
	v_mul_f32_e32 v22, v132, v24
	v_mul_f32_e32 v23, v132, v25
	v_add_u32_e32 v0, 0x848, v101
	ds_write2_b32 v0, v22, v23 offset1:1
	v_mul_f32_e32 v18, v122, v18
	v_mul_f32_e32 v19, v122, v19
	v_add_u32_e32 v0, 0xc60, v101
	ds_write2_b32 v0, v18, v19 offset1:1
	v_mul_f32_e32 v18, v122, v20
	v_mul_f32_e32 v19, v122, v21
	v_add_u32_e32 v0, 0xc68, v101
	ds_write2_b32 v0, v18, v19 offset1:1
	v_mul_f32_e32 v14, v130, v14
	v_mul_f32_e32 v15, v130, v15
	v_add_u32_e32 v0, 0x1080, v101
	ds_write2_b32 v0, v14, v15 offset1:1
	v_mul_f32_e32 v14, v130, v16
	v_mul_f32_e32 v15, v130, v17
	v_add_u32_e32 v0, 0x1088, v101
	ds_write2_b32 v0, v14, v15 offset1:1
	v_mul_f32_e32 v10, v120, v10
	v_mul_f32_e32 v11, v120, v11
	v_add_u32_e32 v0, 0x14a0, v101
	ds_write2_b32 v0, v10, v11 offset1:1
	v_mul_f32_e32 v10, v120, v12
	v_mul_f32_e32 v11, v120, v13
	v_add_u32_e32 v0, 0x14a8, v101
	ds_write2_b32 v0, v10, v11 offset1:1
	v_mul_f32_e32 v6, v128, v6
	v_mul_f32_e32 v7, v128, v7
	v_add_u32_e32 v0, 0x18c0, v101
	ds_write2_b32 v0, v6, v7 offset1:1
	v_mul_f32_e32 v6, v128, v8
	v_mul_f32_e32 v7, v128, v9
	v_add_u32_e32 v0, 0x18c8, v101
	s_waitcnt vmcnt(0)
	v_mul_f32_e32 v30, v124, v30
	v_mul_f32_e32 v31, v124, v31
	ds_write2_b32 v0, v6, v7 offset1:1
	v_mul_f32_e32 v2, v118, v2
	v_mul_f32_e32 v3, v118, v3
	v_add_u32_e32 v0, 0x1ce0, v101
	ds_write2_b32 v101, v30, v31 offset1:1
	v_mul_f32_e32 v30, v124, v32
	v_mul_f32_e32 v31, v124, v33
	ds_write2_b32 v0, v2, v3 offset1:1
	v_mul_f32_e32 v2, v118, v4
	v_mul_f32_e32 v3, v118, v5
	v_add_u32_e32 v0, 0x1ce8, v101
	ds_write2_b32 v101, v30, v31 offset0:2 offset1:3
	ds_write2_b32 v0, v2, v3 offset1:1
	s_waitcnt lgkmcnt(0)
	ds_read2_b32 v[6:7], v99 offset0:33 offset1:41
	ds_read2_b32 v[8:9], v99 offset1:8
	ds_read2_b32 v[10:11], v99 offset0:66 offset1:74
	ds_read2_b32 v[12:13], v99 offset0:99 offset1:107
	ds_read2_b32 v[14:15], v99 offset0:132 offset1:140
	ds_read2_b32 v[16:17], v99 offset0:165 offset1:173
	ds_read2_b32 v[18:19], v99 offset0:198 offset1:206
	ds_read2_b32 v[20:21], v99 offset0:231 offset1:239
	v_mad_u64_u32 v[22:23], s[44:45], s34, v104, 0
	v_lshl_add_u64 v[22:23], v[22:23], 1, s[0:1]
	v_lshlrev_b32_e32 v0, 1, v106
	s_waitcnt lgkmcnt(6)
	v_cvt_pk_bf16_f32 v2, v8, v6
	s_waitcnt lgkmcnt(4)
	v_cvt_pk_bf16_f32 v3, v10, v12
	s_waitcnt lgkmcnt(2)
	v_cvt_pk_bf16_f32 v4, v14, v16
	s_waitcnt lgkmcnt(0)
	v_cvt_pk_bf16_f32 v5, v18, v20
	v_lshl_add_u64 v[22:23], v[22:23], 0, v[0:1]
	global_store_dwordx4 v[22:23], v[2:5], off
	s_nop 1
	v_cvt_pk_bf16_f32 v2, v9, v7
	v_cvt_pk_bf16_f32 v3, v11, v13
	v_cvt_pk_bf16_f32 v4, v15, v17
	v_cvt_pk_bf16_f32 v5, v19, v21
	v_mad_u64_u32 v[6:7], s[44:45], s34, v102, 0
	ds_read2_b32 v[8:9], v99 offset0:16 offset1:24
	ds_read2_b32 v[10:11], v99 offset0:49 offset1:57
	ds_read2_b32 v[12:13], v99 offset0:82 offset1:90
	ds_read2_b32 v[14:15], v99 offset0:115 offset1:123
	ds_read2_b32 v[16:17], v99 offset0:148 offset1:156
	ds_read2_b32 v[18:19], v99 offset0:181 offset1:189
	ds_read2_b32 v[20:21], v99 offset0:214 offset1:222
	ds_read2_b32 v[22:23], v99 offset0:247 offset1:255
	v_lshl_add_u64 v[6:7], v[6:7], 1, s[0:1]
	v_lshl_add_u64 v[6:7], v[6:7], 0, v[0:1]
	global_store_dwordx4 v[6:7], v[2:5], off
	v_mad_u64_u32 v[6:7], s[44:45], s34, v100, 0
	v_lshl_add_u64 v[6:7], v[6:7], 1, s[0:1]
	s_waitcnt lgkmcnt(6)
	v_cvt_pk_bf16_f32 v2, v8, v10
	s_waitcnt lgkmcnt(4)
	v_cvt_pk_bf16_f32 v3, v12, v14
	s_waitcnt lgkmcnt(2)
	v_cvt_pk_bf16_f32 v4, v16, v18
	s_waitcnt lgkmcnt(0)
	v_cvt_pk_bf16_f32 v5, v20, v22
	v_lshl_add_u64 v[6:7], v[6:7], 0, v[0:1]
	global_store_dwordx4 v[6:7], v[2:5], off
	v_mad_u64_u32 v[6:7], s[44:45], s34, v98, 0
	v_lshl_add_u64 v[6:7], v[6:7], 1, s[0:1]
	v_cvt_pk_bf16_f32 v2, v9, v11
	v_cvt_pk_bf16_f32 v3, v13, v15
	v_cvt_pk_bf16_f32 v4, v17, v19
	v_cvt_pk_bf16_f32 v5, v21, v23
	v_lshl_add_u64 v[6:7], v[6:7], 0, v[0:1]
	global_store_dwordx4 v[6:7], v[2:5], off
	s_waitcnt lgkmcnt(0)

.LBB0_332:
	s_andn2_b64 vcc, exec, s[44:45]
	s_cbranch_vccnz .LBB0_299
	s_cmp_eq_u32 s31, 0
	s_cbranch_scc1 .LBB0_298
	s_waitcnt vmcnt(1)
	v_mul_f32_e32 v26, v26, v126
	v_mul_f32_e32 v27, v27, v126
	v_add_u32_e32 v0, 0x420, v101
	ds_write2_b32 v0, v26, v27 offset1:1
	v_mul_f32_e32 v26, v28, v126
	v_mul_f32_e32 v27, v29, v126
	v_add_u32_e32 v0, 0x428, v101
	ds_write2_b32 v0, v26, v27 offset1:1
	v_mul_f32_e32 v22, v22, v132
	v_mul_f32_e32 v23, v23, v132
	v_add_u32_e32 v0, 0x840, v101
	ds_write2_b32 v0, v22, v23 offset1:1
	v_mul_f32_e32 v22, v24, v132
	v_mul_f32_e32 v23, v25, v132
	v_add_u32_e32 v0, 0x848, v101
	ds_write2_b32 v0, v22, v23 offset1:1
	v_mul_f32_e32 v18, v18, v122
	v_mul_f32_e32 v19, v19, v122
	v_add_u32_e32 v0, 0xc60, v101
	ds_write2_b32 v0, v18, v19 offset1:1
	v_mul_f32_e32 v18, v20, v122
	v_mul_f32_e32 v19, v21, v122
	v_add_u32_e32 v0, 0xc68, v101
	ds_write2_b32 v0, v18, v19 offset1:1
	v_mul_f32_e32 v14, v14, v130
	v_mul_f32_e32 v15, v15, v130
	v_add_u32_e32 v0, 0x1080, v101
	ds_write2_b32 v0, v14, v15 offset1:1
	v_mul_f32_e32 v14, v16, v130
	v_mul_f32_e32 v15, v17, v130
	v_add_u32_e32 v0, 0x1088, v101
	ds_write2_b32 v0, v14, v15 offset1:1
	v_mul_f32_e32 v10, v10, v120
	v_mul_f32_e32 v11, v11, v120
	v_add_u32_e32 v0, 0x14a0, v101
	ds_write2_b32 v0, v10, v11 offset1:1
	v_mul_f32_e32 v10, v12, v120
	v_mul_f32_e32 v11, v13, v120
	v_add_u32_e32 v0, 0x14a8, v101
	ds_write2_b32 v0, v10, v11 offset1:1
	v_mul_f32_e32 v6, v6, v128
	v_mul_f32_e32 v7, v7, v128
	v_add_u32_e32 v0, 0x18c0, v101
	ds_write2_b32 v0, v6, v7 offset1:1
	v_mul_f32_e32 v6, v8, v128
	v_mul_f32_e32 v7, v9, v128
	v_add_u32_e32 v0, 0x18c8, v101
	s_waitcnt vmcnt(0)
	v_mul_f32_e32 v30, v30, v124
	v_mul_f32_e32 v31, v31, v124
	ds_write2_b32 v0, v6, v7 offset1:1
	v_mul_f32_e32 v2, v2, v118
	v_mul_f32_e32 v3, v3, v118
	v_add_u32_e32 v0, 0x1ce0, v101
	ds_write2_b32 v101, v30, v31 offset1:1
	v_mul_f32_e32 v30, v32, v124
	v_mul_f32_e32 v31, v33, v124
	ds_write2_b32 v0, v2, v3 offset1:1
	v_mul_f32_e32 v2, v4, v118
	v_mul_f32_e32 v3, v5, v118
	v_add_u32_e32 v0, 0x1ce8, v101
	ds_write2_b32 v101, v30, v31 offset0:2 offset1:3
	ds_write2_b32 v0, v2, v3 offset1:1
	s_waitcnt lgkmcnt(0)
	ds_read2_b32 v[6:7], v99 offset0:33 offset1:41
	ds_read2_b32 v[8:9], v99 offset1:8
	ds_read2_b32 v[10:11], v99 offset0:66 offset1:74
	ds_read2_b32 v[12:13], v99 offset0:99 offset1:107
	ds_read2_b32 v[14:15], v99 offset0:132 offset1:140
	ds_read2_b32 v[16:17], v99 offset0:165 offset1:173
	ds_read2_b32 v[18:19], v99 offset0:198 offset1:206
	ds_read2_b32 v[20:21], v99 offset0:231 offset1:239
	v_mad_u64_u32 v[22:23], s[36:37], s34, v104, 0
	v_lshl_add_u64 v[22:23], v[22:23], 1, s[0:1]
	v_lshlrev_b32_e32 v0, 1, v106
	s_waitcnt lgkmcnt(6)
	v_cvt_pk_bf16_f32 v2, v8, v6
	s_waitcnt lgkmcnt(4)
	v_cvt_pk_bf16_f32 v3, v10, v12
	s_waitcnt lgkmcnt(2)
	v_cvt_pk_bf16_f32 v4, v14, v16
	s_waitcnt lgkmcnt(0)
	v_cvt_pk_bf16_f32 v5, v18, v20
	v_lshl_add_u64 v[22:23], v[22:23], 0, v[0:1]
	global_store_dwordx4 v[22:23], v[2:5], off
	s_nop 1
	v_cvt_pk_bf16_f32 v2, v9, v7
	v_cvt_pk_bf16_f32 v3, v11, v13
	v_cvt_pk_bf16_f32 v4, v15, v17
	v_cvt_pk_bf16_f32 v5, v19, v21
	v_mad_u64_u32 v[6:7], s[36:37], s34, v102, 0
	ds_read2_b32 v[8:9], v99 offset0:16 offset1:24
	ds_read2_b32 v[10:11], v99 offset0:49 offset1:57
	ds_read2_b32 v[12:13], v99 offset0:82 offset1:90
	ds_read2_b32 v[14:15], v99 offset0:115 offset1:123
	ds_read2_b32 v[16:17], v99 offset0:148 offset1:156
	ds_read2_b32 v[18:19], v99 offset0:181 offset1:189
	ds_read2_b32 v[20:21], v99 offset0:214 offset1:222
	ds_read2_b32 v[22:23], v99 offset0:247 offset1:255
	v_lshl_add_u64 v[6:7], v[6:7], 1, s[0:1]
	v_lshl_add_u64 v[6:7], v[6:7], 0, v[0:1]
	global_store_dwordx4 v[6:7], v[2:5], off
	v_mad_u64_u32 v[6:7], s[36:37], s34, v100, 0
	v_lshl_add_u64 v[6:7], v[6:7], 1, s[0:1]
	s_waitcnt lgkmcnt(6)
	v_cvt_pk_bf16_f32 v2, v8, v10
	s_waitcnt lgkmcnt(4)
	v_cvt_pk_bf16_f32 v3, v12, v14
	s_waitcnt lgkmcnt(2)
	v_cvt_pk_bf16_f32 v4, v16, v18
	s_waitcnt lgkmcnt(0)
	v_cvt_pk_bf16_f32 v5, v20, v22
	v_lshl_add_u64 v[6:7], v[6:7], 0, v[0:1]
	global_store_dwordx4 v[6:7], v[2:5], off
	v_mad_u64_u32 v[6:7], s[36:37], s34, v98, 0
	v_lshl_add_u64 v[6:7], v[6:7], 1, s[0:1]
	v_cvt_pk_bf16_f32 v2, v9, v11
	v_cvt_pk_bf16_f32 v3, v13, v15
	v_cvt_pk_bf16_f32 v4, v17, v19
	v_cvt_pk_bf16_f32 v5, v21, v23
	v_lshl_add_u64 v[6:7], v[6:7], 0, v[0:1]
	global_store_dwordx4 v[6:7], v[2:5], off
	s_waitcnt lgkmcnt(0)
	s_branch .LBB0_298

.LBB0_343:
	s_cmp_eq_u32 s31, 0
	s_cbranch_scc1 .LBB0_345
	s_waitcnt vmcnt(1)
	v_mul_f32_e32 v26, v26, v126
	v_mul_f32_e32 v27, v27, v126
	v_add_u32_e32 v0, 0x420, v101
	ds_write2_b32 v0, v26, v27 offset1:1
	v_mul_f32_e32 v26, v28, v126
	v_mul_f32_e32 v27, v29, v126
	v_add_u32_e32 v0, 0x428, v101
	ds_write2_b32 v0, v26, v27 offset1:1
	v_mul_f32_e32 v22, v22, v132
	v_mul_f32_e32 v23, v23, v132
	v_add_u32_e32 v0, 0x840, v101
	ds_write2_b32 v0, v22, v23 offset1:1
	v_mul_f32_e32 v22, v24, v132
	v_mul_f32_e32 v23, v25, v132
	v_add_u32_e32 v0, 0x848, v101
	ds_write2_b32 v0, v22, v23 offset1:1
	v_mul_f32_e32 v18, v18, v122
	v_mul_f32_e32 v19, v19, v122
	v_add_u32_e32 v0, 0xc60, v101
	ds_write2_b32 v0, v18, v19 offset1:1
	v_mul_f32_e32 v18, v20, v122
	v_mul_f32_e32 v19, v21, v122
	v_add_u32_e32 v0, 0xc68, v101
	ds_write2_b32 v0, v18, v19 offset1:1
	v_mul_f32_e32 v14, v14, v130
	v_mul_f32_e32 v15, v15, v130
	v_add_u32_e32 v0, 0x1080, v101
	ds_write2_b32 v0, v14, v15 offset1:1
	v_mul_f32_e32 v14, v16, v130
	v_mul_f32_e32 v15, v17, v130
	v_add_u32_e32 v0, 0x1088, v101
	ds_write2_b32 v0, v14, v15 offset1:1
	v_mul_f32_e32 v10, v10, v120
	v_mul_f32_e32 v11, v11, v120
	v_add_u32_e32 v0, 0x14a0, v101
	ds_write2_b32 v0, v10, v11 offset1:1
	v_mul_f32_e32 v10, v12, v120
	v_mul_f32_e32 v11, v13, v120
	v_add_u32_e32 v0, 0x14a8, v101
	ds_write2_b32 v0, v10, v11 offset1:1
	v_mul_f32_e32 v6, v6, v128
	v_mul_f32_e32 v7, v7, v128
	v_add_u32_e32 v0, 0x18c0, v101
	ds_write2_b32 v0, v6, v7 offset1:1
	v_mul_f32_e32 v6, v8, v128
	v_mul_f32_e32 v7, v9, v128
	v_add_u32_e32 v0, 0x18c8, v101
	s_waitcnt vmcnt(0)
	v_mul_f32_e32 v30, v30, v124
	v_mul_f32_e32 v31, v31, v124
	ds_write2_b32 v0, v6, v7 offset1:1
	v_mul_f32_e32 v2, v2, v118
	v_mul_f32_e32 v3, v3, v118
	v_add_u32_e32 v0, 0x1ce0, v101
	ds_write2_b32 v101, v30, v31 offset1:1
	v_mul_f32_e32 v30, v32, v124
	v_mul_f32_e32 v31, v33, v124
	ds_write2_b32 v0, v2, v3 offset1:1
	v_mul_f32_e32 v2, v4, v118
	v_mul_f32_e32 v3, v5, v118
	v_add_u32_e32 v0, 0x1ce8, v101
	ds_write2_b32 v101, v30, v31 offset0:2 offset1:3
	ds_write2_b32 v0, v2, v3 offset1:1
	s_waitcnt lgkmcnt(0)
	ds_read2_b32 v[6:7], v99 offset0:33 offset1:41
	ds_read2_b32 v[8:9], v99 offset1:8
	ds_read2_b32 v[10:11], v99 offset0:66 offset1:74
	ds_read2_b32 v[12:13], v99 offset0:99 offset1:107
	ds_read2_b32 v[14:15], v99 offset0:132 offset1:140
	ds_read2_b32 v[16:17], v99 offset0:165 offset1:173
	ds_read2_b32 v[18:19], v99 offset0:198 offset1:206
	ds_read2_b32 v[20:21], v99 offset0:231 offset1:239
	v_mad_u64_u32 v[22:23], s[14:15], s34, v104, 0
	v_lshl_add_u64 v[22:23], v[22:23], 1, s[0:1]
	v_lshlrev_b32_e32 v0, 1, v106
	s_waitcnt lgkmcnt(6)
	v_cvt_pk_bf16_f32 v2, v8, v6
	s_waitcnt lgkmcnt(4)
	v_cvt_pk_bf16_f32 v3, v10, v12
	s_waitcnt lgkmcnt(2)
	v_cvt_pk_bf16_f32 v4, v14, v16
	s_waitcnt lgkmcnt(0)
	v_cvt_pk_bf16_f32 v5, v18, v20
	v_lshl_add_u64 v[22:23], v[22:23], 0, v[0:1]
	global_store_dwordx4 v[22:23], v[2:5], off
	s_nop 1
	v_cvt_pk_bf16_f32 v2, v9, v7
	v_cvt_pk_bf16_f32 v3, v11, v13
	v_cvt_pk_bf16_f32 v4, v15, v17
	v_cvt_pk_bf16_f32 v5, v19, v21
	v_mad_u64_u32 v[6:7], s[14:15], s34, v102, 0
	ds_read2_b32 v[8:9], v99 offset0:16 offset1:24
	ds_read2_b32 v[10:11], v99 offset0:49 offset1:57
	ds_read2_b32 v[12:13], v99 offset0:82 offset1:90
	ds_read2_b32 v[14:15], v99 offset0:115 offset1:123
	ds_read2_b32 v[16:17], v99 offset0:148 offset1:156
	ds_read2_b32 v[18:19], v99 offset0:181 offset1:189
	ds_read2_b32 v[20:21], v99 offset0:214 offset1:222
	ds_read2_b32 v[22:23], v99 offset0:247 offset1:255
	v_lshl_add_u64 v[6:7], v[6:7], 1, s[0:1]
	v_lshl_add_u64 v[6:7], v[6:7], 0, v[0:1]
	global_store_dwordx4 v[6:7], v[2:5], off
	v_mad_u64_u32 v[6:7], s[14:15], s34, v100, 0
	v_lshl_add_u64 v[6:7], v[6:7], 1, s[0:1]
	s_waitcnt lgkmcnt(6)
	v_cvt_pk_bf16_f32 v2, v8, v10
	s_waitcnt lgkmcnt(4)
	v_cvt_pk_bf16_f32 v3, v12, v14
	s_waitcnt lgkmcnt(2)
	v_cvt_pk_bf16_f32 v4, v16, v18
	s_waitcnt lgkmcnt(0)
	v_cvt_pk_bf16_f32 v5, v20, v22
	v_lshl_add_u64 v[6:7], v[6:7], 0, v[0:1]
	global_store_dwordx4 v[6:7], v[2:5], off
	v_mad_u64_u32 v[6:7], s[14:15], s34, v98, 0
	v_lshl_add_u64 v[6:7], v[6:7], 1, s[0:1]
	v_cvt_pk_bf16_f32 v2, v9, v11
	v_cvt_pk_bf16_f32 v3, v13, v15
	v_cvt_pk_bf16_f32 v4, v17, v19
	v_cvt_pk_bf16_f32 v5, v21, v23
	v_lshl_add_u64 v[6:7], v[6:7], 0, v[0:1]
	global_store_dwordx4 v[6:7], v[2:5], off
	s_waitcnt lgkmcnt(0)

.LBB0_360:
	s_mov_b32 s29, -1
	s_ashr_i32 s37, s36, 31
	v_mbcnt_lo_u32_b32 v0, s29, 0
	v_mbcnt_hi_u32_b32 v0, s29, v0
	s_lshl_b64 s[36:37], s[36:37], 7
	v_lshrrev_b32_e32 v46, 1, v0
	s_or_b64 s[36:37], s[36:37], s[80:81]
	v_and_b32_e32 v46, 56, v46
	v_mov_b32_e32 v47, v1
	v_lshl_add_u64 v[182:183], s[36:37], 0, v[46:47]
	v_lshlrev_b64 v[46:47], 2, v[182:183]
	v_lshl_add_u64 v[50:51], s[46:47], 0, v[46:47]
	v_lshl_add_u64 v[58:59], s[52:53], 0, v[46:47]
	v_lshl_add_u64 v[62:63], s[54:55], 0, v[46:47]
	v_lshl_add_u64 v[86:87], s[48:49], 0, v[46:47]
	global_load_dwordx4 v[46:49], v[50:51], off offset:16
	global_load_dwordx4 v[74:77], v[50:51], off
	s_nop 0
	global_load_dwordx4 v[50:53], v[58:59], off offset:16
	global_load_dwordx4 v[78:81], v[58:59], off
	s_nop 0
	global_load_dwordx4 v[58:61], v[62:63], off offset:16
	global_load_dwordx4 v[82:85], v[62:63], off
	s_nop 0
	global_load_dwordx4 v[62:65], v[86:87], off offset:16
	s_nop 0
	global_load_dwordx4 v[86:89], v[86:87], off
	s_waitcnt vmcnt(0)
	v_ffbh_u32_e32 v192, v191
	v_min_u32_e32 v192, 32, v192
	v_lshlrev_b64 v[190:191], v192, v[190:191]
	v_min_u32_e32 v190, 1, v190
	v_or_b32_e32 v190, v191, v190
	v_ffbh_u32_e32 v191, v189
	v_min_u32_e32 v191, 32, v191
	v_lshlrev_b64 v[188:189], v191, v[188:189]
	v_min_u32_e32 v188, 1, v188
	v_cvt_f32_u32_e32 v190, v190
	v_or_b32_e32 v188, v189, v188
	v_cvt_f32_u32_e32 v188, v188
	v_sub_u32_e32 v189, 32, v192
	v_ldexp_f32 v189, v190, v189
	v_sub_u32_e32 v190, 32, v191
	v_ldexp_f32 v188, v188, v190
	s_mov_b32 s36, 0x32800000
	v_fma_f32 v192, v188, s36, v196
	v_fma_f32 v193, v189, s36, v196
	s_lshl_b32 s29, s38, 8
	v_mul_f32_e32 v188, 0x4b800000, v193
	v_cmp_gt_f32_e64 s[36:37], s96, v193
	v_readlane_b32 s39, v253, 47
	s_add_i32 s29, s29, s39
	v_cndmask_b32_e64 v188, v193, v188, s[36:37]
	v_rsq_f32_e32 v188, v188
	s_ashr_i32 s39, s38, 31
	v_and_b32_e32 v0, 15, v0
	v_cmp_gt_f32_e32 vcc, s96, v192
	v_mul_f32_e32 v189, 0x45800000, v188
	v_cndmask_b32_e64 v194, v188, v189, s[36:37]
	s_lshl_b64 s[36:37], s[38:39], 2
	s_add_u32 s66, s36, s85
	v_mul_f32_e32 v188, v194, v160
	v_mul_f32_e32 v189, v194, v161
	v_mul_f32_e32 v190, v194, v158
	v_mul_f32_e32 v191, v194, v159
	v_mul_f32_e32 v158, v194, v156
	v_mul_f32_e32 v159, v194, v157
	v_mul_f32_e32 v160, v194, v154
	v_mul_f32_e32 v161, v194, v155
	v_or_b32_e32 v193, s29, v0
	s_addc_u32 s67, s37, s84
	v_cmp_lt_u32_e64 s[36:37], 1, v0
	v_mov_b32_dpp v202, v190 row_shr:1 row_mask:0xf bank_mask:0xf bound_ctrl:1
	v_mov_b32_dpp v204, v190 row_shr:2 row_mask:0xf bank_mask:0xf bound_ctrl:1
	v_mov_b32_dpp v203, v191 row_shr:1 row_mask:0xf bank_mask:0xf bound_ctrl:1
	v_mov_b32_dpp v205, v191 row_shr:2 row_mask:0xf bank_mask:0xf bound_ctrl:1
	v_mov_b32_dpp v206, v188 row_shr:1 row_mask:0xf bank_mask:0xf bound_ctrl:1
	v_mov_b32_dpp v208, v188 row_shr:2 row_mask:0xf bank_mask:0xf bound_ctrl:1
	v_mov_b32_dpp v207, v189 row_shr:1 row_mask:0xf bank_mask:0xf bound_ctrl:1
	v_mov_b32_dpp v209, v189 row_shr:2 row_mask:0xf bank_mask:0xf bound_ctrl:1
	v_mov_b32_dpp v210, v160 row_shr:1 row_mask:0xf bank_mask:0xf bound_ctrl:1
	v_mov_b32_dpp v212, v160 row_shr:2 row_mask:0xf bank_mask:0xf bound_ctrl:1
	v_mov_b32_dpp v211, v161 row_shr:1 row_mask:0xf bank_mask:0xf bound_ctrl:1
	v_mov_b32_dpp v213, v161 row_shr:2 row_mask:0xf bank_mask:0xf bound_ctrl:1
	v_mov_b32_dpp v214, v158 row_shr:1 row_mask:0xf bank_mask:0xf bound_ctrl:1
	v_mov_b32_dpp v216, v158 row_shr:2 row_mask:0xf bank_mask:0xf bound_ctrl:1
	v_mov_b32_dpp v215, v159 row_shr:1 row_mask:0xf bank_mask:0xf bound_ctrl:1
	v_mov_b32_dpp v217, v159 row_shr:2 row_mask:0xf bank_mask:0xf bound_ctrl:1
	s_and_saveexec_b64 s[38:39], s[36:37]
	s_xor_b64 s[38:39], exec, s[38:39]
	s_cbranch_execz .LBB0_362
	v_fma_f32 v154, v48, v216, v64
	v_fma_f32 v155, v49, v217, v65
	v_fma_f32 v212, v46, v212, v62
	v_fma_f32 v213, v47, v213, v63
	v_fma_f32 v154, v52, v214, v154
	v_fma_f32 v155, v53, v215, v155
	v_fma_f32 v210, v50, v210, v212
	v_fma_f32 v211, v51, v211, v213
	v_fma_f32 v154, v158, v60, v154
	v_fma_f32 v155, v159, v61, v155
	v_fma_f32 v210, v160, v58, v210
	v_fma_f32 v211, v161, v59, v211
	v_mul_f32_e32 v156, 0x3d372713, v154
	v_mul_f32_e32 v157, 0x3d372713, v155
	v_mul_f32_e32 v200, v194, v148
	v_mul_f32_e32 v201, v194, v149
	v_mul_f32_e32 v195, 0x3d372713, v210
	v_mul_f32_e32 v156, v154, v156
	v_mul_f32_e32 v157, v155, v157
	v_mul_f32_e32 v195, v210, v195
	v_mul_f32_e32 v212, 0x3d372713, v211
	v_fma_f32 v156, v154, v156, v154
	v_fma_f32 v157, v155, v157, v155
	v_fma_f32 v195, v210, v195, v210
	v_mul_f32_e32 v212, v211, v212
	v_mul_f32_e32 v156, 0xc0135761, v156
	v_mul_f32_e32 v157, 0xc0135761, v157
	v_mul_f32_e32 v195, 0xc0135761, v195
	v_fma_f32 v212, v211, v212, v211
	v_exp_f32_e32 v156, v156
	v_exp_f32_e32 v157, v157
	v_exp_f32_e32 v195, v195
	v_mul_f32_e32 v212, 0xc0135761, v212
	v_exp_f32_e32 v213, v212
	v_add_f32_e32 v156, 1.0, v156
	v_add_f32_e32 v157, 1.0, v157
	v_add_f32_e32 v195, 1.0, v195
	v_rcp_f32_e32 v156, v156
	v_rcp_f32_e32 v157, v157
	v_rcp_f32_e32 v212, v195
	v_add_f32_e32 v195, 1.0, v213
	v_rcp_f32_e32 v213, v195
	v_mul_f32_e32 v154, v154, v156
	v_mul_f32_e32 v155, v155, v157
	v_fma_f32 v204, v74, v204, v86
	v_fma_f32 v205, v75, v205, v87
	v_mul_f32_e32 v200, v200, v154
	v_mul_f32_e32 v201, v201, v155
	v_mul_f32_e32 v154, v194, v146
	v_mul_f32_e32 v155, v194, v147
	v_mul_f32_e32 v156, v210, v212
	v_mul_f32_e32 v157, v211, v213
	v_fma_f32 v202, v78, v202, v204
	v_fma_f32 v203, v79, v203, v205
	v_mul_f32_e32 v156, v154, v156
	v_mul_f32_e32 v157, v155, v157
	v_fma_f32 v154, v76, v208, v88
	v_fma_f32 v155, v77, v209, v89
	v_fma_f32 v202, v190, v82, v202
	v_fma_f32 v203, v191, v83, v203
	v_fma_f32 v154, v80, v206, v154
	v_fma_f32 v155, v81, v207, v155
	v_mul_f32_e32 v204, 0x3d372713, v202
	v_fma_f32 v154, v188, v84, v154
	v_fma_f32 v155, v189, v85, v155
	v_mul_f32_e32 v204, v202, v204
	v_mul_f32_e32 v195, 0x3d372713, v154
	v_mul_f32_e32 v195, v154, v195
	v_mul_f32_e32 v206, 0x3d372713, v155
	v_fma_f32 v195, v154, v195, v154
	v_mul_f32_e32 v206, v155, v206
	v_mul_f32_e32 v195, 0xc0135761, v195
	v_fma_f32 v206, v155, v206, v155
	v_mul_f32_e32 v205, 0x3d372713, v203
	v_exp_f32_e32 v195, v195
	v_mul_f32_e32 v206, 0xc0135761, v206
	v_fma_f32 v204, v202, v204, v202
	v_mul_f32_e32 v205, v203, v205
	v_exp_f32_e32 v207, v206
	v_mul_f32_e32 v204, 0xc0135761, v204
	v_fma_f32 v205, v203, v205, v203
	v_exp_f32_e32 v204, v204
	v_mul_f32_e32 v205, 0xc0135761, v205
	v_exp_f32_e32 v205, v205
	v_add_f32_e32 v195, 1.0, v195
	v_rcp_f32_e32 v206, v195
	v_mul_f32_e32 v208, v194, v152
	v_mul_f32_e32 v209, v194, v153
	v_add_f32_e32 v195, 1.0, v207
	v_rcp_f32_e32 v207, v195
	v_add_f32_e32 v195, 1.0, v204
	v_rcp_f32_e32 v204, v195
	v_add_f32_e32 v195, 1.0, v205
	v_rcp_f32_e32 v205, v195
	v_mul_f32_e32 v154, v154, v206
	v_mul_f32_e32 v155, v155, v207
	v_cvt_pk_bf16_f32 v156, v156, v157
	v_mul_f32_e32 v206, v208, v154
	v_mul_f32_e32 v207, v209, v155
	v_mul_f32_e32 v154, v194, v150
	v_mul_f32_e32 v155, v194, v151
	v_mul_f32_e32 v194, v202, v204
	v_mul_f32_e32 v195, v203, v205
	v_cvt_pk_bf16_f32 v157, v200, v201
	v_mul_f32_e32 v154, v154, v194
	v_mul_f32_e32 v155, v155, v195
	v_mov_b64_e32 v[194:195], s[16:17]
	v_cvt_pk_bf16_f32 v154, v154, v155
	v_cvt_pk_bf16_f32 v155, v206, v207
	v_mad_i64_i32 v[200:201], s[40:41], v193, s2, v[194:195]
.LBB0_362:
	s_or_saveexec_b64 s[38:39], s[38:39]
	s_lshl_b64 s[40:41], s[66:67], 2
	s_xor_b64 exec, exec, s[38:39]
	s_cbranch_execz .LBB0_364
	v_or_b32_e32 v203, s40, v0
	v_mov_b64_e32 v[200:201], s[42:43]
	v_mad_u64_u32 v[200:201], s[82:83], v203, s2, v[200:201]
	v_mov_b32_e32 v195, v194
	v_mad_i32_i24 v201, s41, v232, v201
	s_lshl_b64 s[50:51], s[66:67], 1
	v_cvt_pk_bf16_f32 v154, v190, v191
	v_cvt_pk_bf16_f32 v155, v188, v189
	v_cvt_pk_bf16_f32 v156, v160, v161
	v_cvt_pk_bf16_f32 v157, v158, v159
	v_lshl_add_u64 v[200:201], v[182:183], 1, v[200:201]
	v_mul_f32_e32 v146, v194, v146
	v_mul_f32_e32 v147, v195, v147
	v_or_b32_e32 v202, s50, v0
	global_store_dwordx4 v[200:201], v[154:157], off
	v_mul_f32_e32 v150, v194, v150
	v_mul_f32_e32 v151, v195, v151
	s_nop 0
	v_mov_b32_e32 v154, v194
	v_mov_b32_e32 v155, v194
	v_cvt_pk_bf16_f32 v156, v146, v147
	v_mov_b64_e32 v[146:147], s[44:45]
	v_mul_f32_e32 v152, v154, v152
	v_mul_f32_e32 v153, v155, v153
	v_mul_f32_e32 v148, v154, v148
	v_mul_f32_e32 v149, v155, v149
	v_mad_u64_u32 v[200:201], s[82:83], v202, s2, v[146:147]
	v_cvt_pk_bf16_f32 v154, v150, v151
	v_cvt_pk_bf16_f32 v155, v152, v153
	v_cvt_pk_bf16_f32 v157, v148, v149
	v_mad_i32_i24 v201, s51, v232, v201
.LBB0_364:
	s_or_b64 exec, exec, s[38:39]
	v_mul_f32_e32 v146, 0x4b800000, v192
	v_cndmask_b32_e32 v146, v192, v146, vcc
	v_rsq_f32_e32 v146, v146
	s_mov_b32 s38, 0x32800000
	v_mul_f32_e32 v147, 0x45800000, v146
	v_cndmask_b32_e32 v192, v146, v147, vcc
	v_ffbh_u32_e32 v146, v187
	v_min_u32_e32 v148, 32, v146
	v_lshlrev_b64 v[146:147], v148, v[186:187]
	v_min_u32_e32 v146, 1, v146
	v_or_b32_e32 v146, v147, v146
	v_cvt_f32_u32_e32 v146, v146
	v_sub_u32_e32 v147, 32, v148
	v_mul_f32_e32 v142, v192, v142
	v_mul_f32_e32 v143, v192, v143
	v_mul_f32_e32 v134, v192, v134
	v_mul_f32_e32 v135, v192, v135
	v_ldexp_f32 v147, v146, v147
	v_ffbh_u32_e32 v146, v185
	v_min_u32_e32 v146, 32, v146
	v_lshlrev_b64 v[148:149], v146, v[184:185]
	v_min_u32_e32 v148, 1, v148
	v_or_b32_e32 v148, v149, v148
	v_cvt_f32_u32_e32 v148, v148
	v_sub_u32_e32 v146, 32, v146
	v_mul_f32_e32 v144, v192, v144
	v_mul_f32_e32 v145, v192, v145
	v_mul_f32_e32 v136, v192, v136
	v_mul_f32_e32 v137, v192, v137
	v_ldexp_f32 v146, v148, v146
	v_fma_f32 v146, v146, s38, v196
	v_fma_f32 v147, v147, s38, v196
	v_mul_f32_e32 v130, v192, v130
	v_mul_f32_e32 v131, v192, v131
	v_mul_f32_e32 v148, 0x4b800000, v147
	v_cmp_gt_f32_e64 s[38:39], s96, v147
	v_mul_f32_e32 v132, v192, v132
	v_mul_f32_e32 v133, v192, v133
	v_cmp_gt_f32_e32 vcc, s96, v146
	v_cndmask_b32_e64 v147, v147, v148, s[38:39]
	v_rsq_f32_e32 v147, v147
	s_nop 0
	v_mul_f32_e32 v148, 0x45800000, v147
	v_cndmask_b32_e64 v152, v147, v148, s[38:39]
	v_lshlrev_b64 v[148:149], 1, v[182:183]
	v_lshl_add_u64 v[184:185], v[200:201], 0, v[148:149]
	global_store_dwordx4 v[184:185], v[154:157], off
	v_mul_f32_e32 v126, v152, v126
	v_mul_f32_e32 v127, v152, v127
	v_mul_f32_e32 v118, v152, v118
	v_mul_f32_e32 v119, v152, v119
	v_mov_b32_e32 v156, v1
	v_mov_b32_e32 v157, v1
	v_mov_b32_e32 v154, v1
	v_mov_b32_dpp v156, v190 row_ror:2 row_mask:0xf bank_mask:0xf
	v_mov_b32_e32 v155, v1
	v_mov_b32_dpp v157, v191 row_ror:2 row_mask:0xf bank_mask:0xf
	v_mov_b32_dpp v154, v190 row_ror:1 row_mask:0xf bank_mask:0xf
	v_mov_b32_dpp v156, v142 row_shr:2 row_mask:0xf bank_mask:0xf
	v_mov_b32_dpp v155, v191 row_ror:1 row_mask:0xf bank_mask:0xf
	v_mov_b32_dpp v157, v143 row_shr:2 row_mask:0xf bank_mask:0xf
	v_mov_b32_dpp v154, v142 row_shr:1 row_mask:0xf bank_mask:0xf
	v_mov_b32_dpp v155, v143 row_shr:1 row_mask:0xf bank_mask:0xf
	v_fma_f32 v156, v74, v156, v86
	v_fma_f32 v157, v75, v157, v87
	v_mul_f32_e32 v128, v152, v128
	v_mul_f32_e32 v129, v152, v129
	v_fma_f32 v154, v78, v154, v156
	v_fma_f32 v155, v79, v155, v157
	v_mul_f32_e32 v120, v152, v120
	v_mul_f32_e32 v121, v152, v121
	v_fma_f32 v154, v142, v82, v154
	v_fma_f32 v155, v143, v83, v155
	v_mul_f32_e32 v114, v152, v114
	v_mul_f32_e32 v115, v152, v115
	v_mul_f32_e32 v151, 0x3d372713, v154
	v_mul_f32_e32 v151, v154, v151
	v_fma_f32 v151, v154, v151, v154
	v_mul_f32_e32 v151, 0xc0135761, v151
	v_exp_f32_e32 v151, v151
	v_mul_f32_e32 v147, 0x4b800000, v146
	v_cndmask_b32_e32 v146, v146, v147, vcc
	v_rsq_f32_e32 v146, v146
	v_add_f32_e32 v151, 1.0, v151
	v_rcp_f32_e32 v156, v151
	v_mul_f32_e32 v151, 0x3d372713, v155
	v_mul_f32_e32 v151, v155, v151
	v_fma_f32 v151, v155, v151, v155
	v_mul_f32_e32 v151, 0xc0135761, v151
	v_exp_f32_e32 v151, v151
	v_mul_f32_e32 v116, v152, v116
	v_mul_f32_e32 v117, v152, v117
	v_mul_f32_e32 v147, 0x45800000, v146
	v_cndmask_b32_e32 v150, v146, v147, vcc
	v_add_f32_e32 v151, 1.0, v151
	v_rcp_f32_e32 v157, v151
	v_cmp_lt_u32_e32 vcc, 13, v0
	v_lshl_add_u64 v[146:147], v[0:1], 0, -12
	v_mul_f32_e32 v154, v154, v156
	v_mul_f32_e32 v155, v155, v157
	v_mov_b32_e32 v156, v1
	v_mov_b32_e32 v157, v1
	v_mul_f32_e32 v154, v134, v154
	v_mul_f32_e32 v155, v135, v155
	v_mov_b32_e32 v134, v1
	v_mov_b32_dpp v156, v188 row_ror:2 row_mask:0xf bank_mask:0xf
	v_mov_b32_e32 v135, v1
	v_mov_b32_dpp v157, v189 row_ror:2 row_mask:0xf bank_mask:0xf
	v_mov_b32_dpp v134, v188 row_ror:1 row_mask:0xf bank_mask:0xf
	v_mov_b32_dpp v156, v144 row_shr:2 row_mask:0xf bank_mask:0xf
	v_mov_b32_dpp v135, v189 row_ror:1 row_mask:0xf bank_mask:0xf
	v_mov_b32_dpp v157, v145 row_shr:2 row_mask:0xf bank_mask:0xf
	v_mov_b32_dpp v134, v144 row_shr:1 row_mask:0xf bank_mask:0xf
	v_mov_b32_dpp v135, v145 row_shr:1 row_mask:0xf bank_mask:0xf
	v_fma_f32 v156, v76, v156, v88
	v_fma_f32 v157, v77, v157, v89
	s_nop 0
	v_fma_f32 v134, v80, v134, v156
	v_fma_f32 v135, v81, v135, v157
	s_nop 0
	v_fma_f32 v134, v144, v84, v134
	v_fma_f32 v135, v145, v85, v135
	s_nop 0
	v_mul_f32_e32 v151, 0x3d372713, v134
	v_mul_f32_e32 v151, v134, v151
	v_fma_f32 v151, v134, v151, v134
	v_mul_f32_e32 v151, 0xc0135761, v151
	v_exp_f32_e32 v151, v151
	s_nop 0
	v_add_f32_e32 v151, 1.0, v151
	v_rcp_f32_e32 v156, v151
	v_mul_f32_e32 v151, 0x3d372713, v135
	v_mul_f32_e32 v151, v135, v151
	v_fma_f32 v151, v135, v151, v135
	v_mul_f32_e32 v151, 0xc0135761, v151
	v_exp_f32_e32 v151, v151
	s_nop 0
	v_add_f32_e32 v151, 1.0, v151
	v_rcp_f32_e32 v157, v151
	v_mul_f32_e32 v110, v150, v110
	v_mul_f32_e32 v111, v150, v111
	v_mul_f32_e32 v102, v150, v102
	v_mul_f32_e32 v103, v150, v103
	v_mul_f32_e32 v112, v150, v112
	v_mul_f32_e32 v113, v150, v113
	v_mul_f32_e32 v134, v134, v156
	v_mul_f32_e32 v135, v135, v157
	v_mul_f32_e32 v104, v150, v104
	v_mul_f32_e32 v105, v150, v105
	v_mul_f32_e32 v156, v136, v134
	v_mul_f32_e32 v157, v137, v135
	v_mul_f32_e32 v134, v192, v140
	v_mul_f32_e32 v135, v192, v141
	v_mov_b32_e32 v140, v1
	v_mov_b32_e32 v141, v1
	v_mul_f32_e32 v136, v192, v138
	v_mul_f32_e32 v137, v192, v139
	v_mov_b32_e32 v138, v1
	v_mov_b32_dpp v140, v160 row_ror:2 row_mask:0xf bank_mask:0xf
	v_mov_b32_e32 v139, v1
	v_mov_b32_dpp v141, v161 row_ror:2 row_mask:0xf bank_mask:0xf
	v_mov_b32_dpp v138, v160 row_ror:1 row_mask:0xf bank_mask:0xf
	v_mov_b32_dpp v140, v136 row_shr:2 row_mask:0xf bank_mask:0xf
	v_mov_b32_dpp v139, v161 row_ror:1 row_mask:0xf bank_mask:0xf
	v_mov_b32_dpp v141, v137 row_shr:2 row_mask:0xf bank_mask:0xf
	v_mov_b32_dpp v138, v136 row_shr:1 row_mask:0xf bank_mask:0xf
	v_mov_b32_dpp v139, v137 row_shr:1 row_mask:0xf bank_mask:0xf
	v_fma_f32 v140, v46, v140, v62
	v_fma_f32 v141, v47, v141, v63
	v_mul_f32_e32 v98, v150, v98
	v_mul_f32_e32 v99, v150, v99
	v_fma_f32 v138, v50, v138, v140
	v_fma_f32 v139, v51, v139, v141
	v_mul_f32_e32 v100, v150, v100
	v_mul_f32_e32 v101, v150, v101
	v_fma_f32 v138, v136, v58, v138
	v_fma_f32 v139, v137, v59, v139
	s_nop 0
	v_mul_f32_e32 v140, 0x3d372713, v138
	v_mul_f32_e32 v141, 0x3d372713, v139
	v_mul_f32_e32 v140, v138, v140
	v_mul_f32_e32 v141, v139, v141
	v_fma_f32 v140, v138, v140, v138
	v_fma_f32 v141, v139, v141, v139
	v_mul_f32_e32 v140, 0xc0135761, v140
	v_mul_f32_e32 v141, 0xc0135761, v141
	v_exp_f32_e32 v140, v140
	v_exp_f32_e32 v141, v141
	v_add_f32_e32 v140, 1.0, v140
	v_add_f32_e32 v141, 1.0, v141
	v_rcp_f32_e32 v140, v140
	v_rcp_f32_e32 v141, v141
	s_nop 0
	v_mul_f32_e32 v138, v138, v140
	v_mul_f32_e32 v139, v139, v141
	v_mov_b32_e32 v140, v1
	v_mov_b32_e32 v141, v1
	v_mul_f32_e32 v130, v130, v138
	v_mul_f32_e32 v131, v131, v139
	v_mov_b32_e32 v138, v1
	v_mov_b32_dpp v140, v158 row_ror:2 row_mask:0xf bank_mask:0xf
	v_mov_b32_e32 v139, v1
	v_mov_b32_dpp v141, v159 row_ror:2 row_mask:0xf bank_mask:0xf
	v_mov_b32_dpp v138, v158 row_ror:1 row_mask:0xf bank_mask:0xf
	v_mov_b32_dpp v140, v134 row_shr:2 row_mask:0xf bank_mask:0xf
	v_mov_b32_dpp v139, v159 row_ror:1 row_mask:0xf bank_mask:0xf
	v_mov_b32_dpp v141, v135 row_shr:2 row_mask:0xf bank_mask:0xf
	v_mov_b32_dpp v138, v134 row_shr:1 row_mask:0xf bank_mask:0xf
	v_mov_b32_dpp v139, v135 row_shr:1 row_mask:0xf bank_mask:0xf
	v_fma_f32 v140, v48, v140, v64
	v_fma_f32 v141, v49, v141, v65
	s_nop 0
	v_fma_f32 v138, v52, v138, v140
	v_fma_f32 v139, v53, v139, v141
	s_nop 0
	v_fma_f32 v138, v134, v60, v138
	v_fma_f32 v139, v135, v61, v139
	s_nop 0
	v_mul_f32_e32 v140, 0x3d372713, v138
	v_mul_f32_e32 v141, 0x3d372713, v139
	v_mul_f32_e32 v140, v138, v140
	v_mul_f32_e32 v141, v139, v141
	v_fma_f32 v140, v138, v140, v138
	v_fma_f32 v141, v139, v141, v139
	v_mul_f32_e32 v140, 0xc0135761, v140
	v_mul_f32_e32 v141, 0xc0135761, v141
	v_exp_f32_e32 v140, v140
	v_exp_f32_e32 v141, v141
	v_add_f32_e32 v140, 1.0, v140
	v_add_f32_e32 v141, 1.0, v141
	v_rcp_f32_e32 v140, v140
	v_rcp_f32_e32 v141, v141
	s_nop 0
	v_mul_f32_e32 v138, v138, v140
	v_mul_f32_e32 v139, v139, v141
	s_nop 0
	v_mul_f32_e32 v132, v132, v138
	v_mul_f32_e32 v133, v133, v139
	v_cvt_pk_bf16_f32 v140, v130, v131
	v_cvt_pk_bf16_f32 v141, v132, v133
	v_or_b32_e32 v132, 16, v193
	v_mov_b64_e32 v[130:131], s[16:17]
	v_mad_i64_i32 v[132:133], s[38:39], v132, s2, v[130:131]
	v_cvt_pk_bf16_f32 v138, v154, v155
	v_cvt_pk_bf16_f32 v139, v156, v157
	v_lshl_add_u64 v[132:133], v[132:133], 0, v[148:149]
	global_store_dwordx4 v[132:133], v[138:141], off
	v_mov_b32_e32 v132, v1
	v_mov_b32_e32 v133, v1
	v_mov_b32_e32 v138, v1
	v_mov_b32_e32 v139, v1
	v_mov_b32_dpp v132, v142 row_ror:1 row_mask:0xf bank_mask:0xf
	v_mov_b32_dpp v138, v142 row_ror:2 row_mask:0xf bank_mask:0xf
	v_mov_b32_dpp v139, v143 row_ror:2 row_mask:0xf bank_mask:0xf
	v_mov_b32_dpp v133, v143 row_ror:1 row_mask:0xf bank_mask:0xf
	v_mov_b32_dpp v138, v126 row_shr:2 row_mask:0xf bank_mask:0xf
	v_mov_b32_dpp v139, v127 row_shr:2 row_mask:0xf bank_mask:0xf
	v_mov_b32_dpp v132, v126 row_shr:1 row_mask:0xf bank_mask:0xf
	v_mov_b32_dpp v133, v127 row_shr:1 row_mask:0xf bank_mask:0xf
	v_fma_f32 v138, v74, v138, v86
	v_fma_f32 v139, v75, v139, v87
	s_nop 0
	v_fma_f32 v132, v78, v132, v138
	v_fma_f32 v133, v79, v133, v139
	s_nop 0
	v_fma_f32 v132, v126, v82, v132
	v_fma_f32 v133, v127, v83, v133
	s_nop 0
	v_mul_f32_e32 v138, 0x3d372713, v132
	v_mul_f32_e32 v139, 0x3d372713, v133
	v_mul_f32_e32 v138, v132, v138
	v_mul_f32_e32 v139, v133, v139
	v_fma_f32 v138, v132, v138, v132
	v_fma_f32 v139, v133, v139, v133
	v_mul_f32_e32 v138, 0xc0135761, v138
	v_mul_f32_e32 v139, 0xc0135761, v139
	v_exp_f32_e32 v138, v138
	v_exp_f32_e32 v139, v139
	v_add_f32_e32 v138, 1.0, v138
	v_add_f32_e32 v139, 1.0, v139
	v_rcp_f32_e32 v138, v138
	v_rcp_f32_e32 v139, v139
	s_nop 0
	v_mul_f32_e32 v132, v132, v138
	v_mul_f32_e32 v133, v133, v139
	v_mov_b32_e32 v138, v1
	v_mov_b32_e32 v139, v1
	v_mul_f32_e32 v132, v118, v132
	v_mul_f32_e32 v133, v119, v133
	v_mov_b32_e32 v118, v1
	v_mov_b32_dpp v138, v144 row_ror:2 row_mask:0xf bank_mask:0xf
	v_mov_b32_e32 v119, v1
	v_mov_b32_dpp v139, v145 row_ror:2 row_mask:0xf bank_mask:0xf
	v_mov_b32_dpp v118, v144 row_ror:1 row_mask:0xf bank_mask:0xf
	v_mov_b32_dpp v138, v128 row_shr:2 row_mask:0xf bank_mask:0xf
	v_mov_b32_dpp v119, v145 row_ror:1 row_mask:0xf bank_mask:0xf
	v_mov_b32_dpp v139, v129 row_shr:2 row_mask:0xf bank_mask:0xf
	v_mov_b32_dpp v118, v128 row_shr:1 row_mask:0xf bank_mask:0xf
	v_mov_b32_dpp v119, v129 row_shr:1 row_mask:0xf bank_mask:0xf
	v_fma_f32 v138, v76, v138, v88
	v_fma_f32 v139, v77, v139, v89
	s_nop 0
	v_fma_f32 v118, v80, v118, v138
	v_fma_f32 v119, v81, v119, v139
	s_nop 0
	v_fma_f32 v118, v128, v84, v118
	v_fma_f32 v119, v129, v85, v119
	s_nop 0
	v_mul_f32_e32 v138, 0x3d372713, v118
	v_mul_f32_e32 v139, 0x3d372713, v119
	v_mul_f32_e32 v138, v118, v138
	v_mul_f32_e32 v139, v119, v139
	v_fma_f32 v138, v118, v138, v118
	v_fma_f32 v139, v119, v139, v119
	v_mul_f32_e32 v138, 0xc0135761, v138
	v_mul_f32_e32 v139, 0xc0135761, v139
	v_exp_f32_e32 v138, v138
	v_exp_f32_e32 v139, v139
	v_add_f32_e32 v138, 1.0, v138
	v_add_f32_e32 v139, 1.0, v139
	v_rcp_f32_e32 v138, v138
	v_rcp_f32_e32 v139, v139
	s_nop 0
	v_mul_f32_e32 v118, v118, v138
	v_mul_f32_e32 v119, v119, v139
	s_nop 0
	v_mul_f32_e32 v138, v120, v118
	v_mul_f32_e32 v139, v121, v119
	v_mul_f32_e32 v118, v152, v124
	v_mul_f32_e32 v119, v152, v125
	v_mov_b32_e32 v124, v1
	v_mov_b32_e32 v125, v1
	v_mul_f32_e32 v120, v152, v122
	v_mul_f32_e32 v121, v152, v123
	v_mov_b32_e32 v122, v1
	v_mov_b32_dpp v124, v136 row_ror:2 row_mask:0xf bank_mask:0xf
	v_mov_b32_e32 v123, v1
	v_mov_b32_dpp v125, v137 row_ror:2 row_mask:0xf bank_mask:0xf
	v_mov_b32_dpp v122, v136 row_ror:1 row_mask:0xf bank_mask:0xf
	v_mov_b32_dpp v124, v120 row_shr:2 row_mask:0xf bank_mask:0xf
	v_mov_b32_dpp v123, v137 row_ror:1 row_mask:0xf bank_mask:0xf
	v_mov_b32_dpp v125, v121 row_shr:2 row_mask:0xf bank_mask:0xf
	v_mov_b32_dpp v122, v120 row_shr:1 row_mask:0xf bank_mask:0xf
	v_mov_b32_dpp v123, v121 row_shr:1 row_mask:0xf bank_mask:0xf
	v_fma_f32 v124, v46, v124, v62
	v_fma_f32 v125, v47, v125, v63
	s_nop 0
	v_fma_f32 v122, v50, v122, v124
	v_fma_f32 v123, v51, v123, v125
	s_nop 0
	v_fma_f32 v122, v120, v58, v122
	v_fma_f32 v123, v121, v59, v123
	s_nop 0
	v_mul_f32_e32 v124, 0x3d372713, v122
	v_mul_f32_e32 v125, 0x3d372713, v123
	v_mul_f32_e32 v124, v122, v124
	v_mul_f32_e32 v125, v123, v125
	v_fma_f32 v124, v122, v124, v122
	v_fma_f32 v125, v123, v125, v123
	v_mul_f32_e32 v124, 0xc0135761, v124
	v_mul_f32_e32 v125, 0xc0135761, v125
	v_exp_f32_e32 v124, v124
	v_exp_f32_e32 v125, v125
	v_add_f32_e32 v124, 1.0, v124
	v_add_f32_e32 v125, 1.0, v125
	v_rcp_f32_e32 v124, v124
	v_rcp_f32_e32 v125, v125
	s_nop 0
	v_mul_f32_e32 v122, v122, v124
	v_mul_f32_e32 v123, v123, v125
	v_mov_b32_e32 v124, v1
	v_mov_b32_e32 v125, v1
	v_mul_f32_e32 v122, v114, v122
	v_mul_f32_e32 v123, v115, v123
	v_mov_b32_e32 v114, v1
	v_mov_b32_dpp v124, v134 row_ror:2 row_mask:0xf bank_mask:0xf
	v_mov_b32_e32 v115, v1
	v_mov_b32_dpp v125, v135 row_ror:2 row_mask:0xf bank_mask:0xf
	v_mov_b32_dpp v114, v134 row_ror:1 row_mask:0xf bank_mask:0xf
	v_mov_b32_dpp v124, v118 row_shr:2 row_mask:0xf bank_mask:0xf
	v_mov_b32_dpp v115, v135 row_ror:1 row_mask:0xf bank_mask:0xf
	v_mov_b32_dpp v125, v119 row_shr:2 row_mask:0xf bank_mask:0xf
	v_mov_b32_dpp v114, v118 row_shr:1 row_mask:0xf bank_mask:0xf
	v_mov_b32_dpp v115, v119 row_shr:1 row_mask:0xf bank_mask:0xf
	v_fma_f32 v124, v48, v124, v64
	v_fma_f32 v125, v49, v125, v65
	s_nop 0
	v_fma_f32 v114, v52, v114, v124
	v_fma_f32 v115, v53, v115, v125
	s_nop 0
	v_fma_f32 v114, v118, v60, v114
	v_fma_f32 v115, v119, v61, v115
	s_nop 0
	v_mul_f32_e32 v124, 0x3d372713, v114
	v_mul_f32_e32 v125, 0x3d372713, v115
	v_mul_f32_e32 v124, v114, v124
	v_mul_f32_e32 v125, v115, v125
	v_fma_f32 v124, v114, v124, v114
	v_fma_f32 v125, v115, v125, v115
	v_mul_f32_e32 v124, 0xc0135761, v124
	v_mul_f32_e32 v125, 0xc0135761, v125
	v_exp_f32_e32 v124, v124
	v_exp_f32_e32 v125, v125
	v_add_f32_e32 v124, 1.0, v124
	v_add_f32_e32 v125, 1.0, v125
	v_rcp_f32_e32 v124, v124
	v_rcp_f32_e32 v125, v125
	s_nop 0
	v_mul_f32_e32 v114, v114, v124
	v_mul_f32_e32 v115, v115, v125
	s_nop 0
	v_mul_f32_e32 v124, v116, v114
	v_mul_f32_e32 v125, v117, v115
	v_cvt_pk_bf16_f32 v116, v122, v123
	v_or_b32_e32 v122, 32, v193
	v_mad_i64_i32 v[122:123], s[38:39], v122, s2, v[130:131]
	v_cvt_pk_bf16_f32 v114, v132, v133
	v_cvt_pk_bf16_f32 v115, v138, v139
	v_cvt_pk_bf16_f32 v117, v124, v125
	v_lshl_add_u64 v[122:123], v[122:123], 0, v[148:149]
	global_store_dwordx4 v[122:123], v[114:117], off
	s_nop 1
	v_mov_b32_e32 v116, v1
	v_mov_b32_e32 v117, v1
	v_mov_b32_e32 v114, v1
	v_mov_b32_dpp v116, v126 row_ror:2 row_mask:0xf bank_mask:0xf
	v_mov_b32_e32 v115, v1
	v_mov_b32_dpp v117, v127 row_ror:2 row_mask:0xf bank_mask:0xf
	v_mov_b32_dpp v114, v126 row_ror:1 row_mask:0xf bank_mask:0xf
	v_mov_b32_dpp v116, v110 row_shr:2 row_mask:0xf bank_mask:0xf
	v_mov_b32_dpp v115, v127 row_ror:1 row_mask:0xf bank_mask:0xf
	v_mov_b32_dpp v117, v111 row_shr:2 row_mask:0xf bank_mask:0xf
	v_mov_b32_dpp v114, v110 row_shr:1 row_mask:0xf bank_mask:0xf
	v_mov_b32_dpp v115, v111 row_shr:1 row_mask:0xf bank_mask:0xf
	v_fma_f32 v116, v74, v116, v86
	v_fma_f32 v117, v75, v117, v87
	s_nop 0
	v_fma_f32 v114, v78, v114, v116
	v_fma_f32 v115, v79, v115, v117
	s_nop 0
	v_fma_f32 v114, v110, v82, v114
	v_fma_f32 v115, v111, v83, v115
	s_nop 0
	v_mul_f32_e32 v116, 0x3d372713, v114
	v_mul_f32_e32 v117, 0x3d372713, v115
	v_mul_f32_e32 v116, v114, v116
	v_mul_f32_e32 v117, v115, v117
	v_fma_f32 v116, v114, v116, v114
	v_fma_f32 v117, v115, v117, v115
	v_mul_f32_e32 v116, 0xc0135761, v116
	v_mul_f32_e32 v117, 0xc0135761, v117
	v_exp_f32_e32 v116, v116
	v_exp_f32_e32 v117, v117
	v_add_f32_e32 v116, 1.0, v116
	v_add_f32_e32 v117, 1.0, v117
	v_rcp_f32_e32 v116, v116
	v_rcp_f32_e32 v117, v117
	s_nop 0
	v_mul_f32_e32 v114, v114, v116
	v_mul_f32_e32 v115, v115, v117
	v_mov_b32_e32 v116, v1
	v_mov_b32_e32 v117, v1
	v_mul_f32_e32 v114, v102, v114
	v_mul_f32_e32 v115, v103, v115
	v_mov_b32_e32 v102, v1
	v_mov_b32_dpp v116, v128 row_ror:2 row_mask:0xf bank_mask:0xf
	v_mov_b32_e32 v103, v1
	v_mov_b32_dpp v117, v129 row_ror:2 row_mask:0xf bank_mask:0xf
	v_mov_b32_dpp v102, v128 row_ror:1 row_mask:0xf bank_mask:0xf
	v_mov_b32_dpp v116, v112 row_shr:2 row_mask:0xf bank_mask:0xf
	v_mov_b32_dpp v103, v129 row_ror:1 row_mask:0xf bank_mask:0xf
	v_mov_b32_dpp v117, v113 row_shr:2 row_mask:0xf bank_mask:0xf
	v_mov_b32_dpp v102, v112 row_shr:1 row_mask:0xf bank_mask:0xf
	v_mov_b32_dpp v103, v113 row_shr:1 row_mask:0xf bank_mask:0xf
	v_fma_f32 v116, v76, v116, v88
	v_fma_f32 v117, v77, v117, v89
	s_nop 0
	v_fma_f32 v102, v80, v102, v116
	v_fma_f32 v103, v81, v103, v117
	s_nop 0
	v_fma_f32 v102, v112, v84, v102
	v_fma_f32 v103, v113, v85, v103
	s_nop 0
	v_mul_f32_e32 v116, 0x3d372713, v102
	v_mul_f32_e32 v117, 0x3d372713, v103
	v_mul_f32_e32 v116, v102, v116
	v_mul_f32_e32 v117, v103, v117
	v_fma_f32 v116, v102, v116, v102
	v_fma_f32 v117, v103, v117, v103
	v_mul_f32_e32 v116, 0xc0135761, v116
	v_mul_f32_e32 v117, 0xc0135761, v117
	v_exp_f32_e32 v116, v116
	v_exp_f32_e32 v117, v117
	v_add_f32_e32 v116, 1.0, v116
	v_add_f32_e32 v117, 1.0, v117
	v_rcp_f32_e32 v116, v116
	v_rcp_f32_e32 v117, v117
	s_nop 0
	v_mul_f32_e32 v102, v102, v116
	v_mul_f32_e32 v103, v103, v117
	s_nop 0
	v_mul_f32_e32 v116, v104, v102
	v_mul_f32_e32 v117, v105, v103
	v_mul_f32_e32 v102, v150, v108
	v_mul_f32_e32 v103, v150, v109
	v_mov_b32_e32 v108, v1
	v_mov_b32_e32 v109, v1
	v_mul_f32_e32 v104, v150, v106
	v_mul_f32_e32 v105, v150, v107
	v_mov_b32_e32 v106, v1
	v_mov_b32_dpp v108, v120 row_ror:2 row_mask:0xf bank_mask:0xf
	v_mov_b32_e32 v107, v1
	v_mov_b32_dpp v109, v121 row_ror:2 row_mask:0xf bank_mask:0xf
	v_mov_b32_dpp v106, v120 row_ror:1 row_mask:0xf bank_mask:0xf
	v_mov_b32_dpp v108, v104 row_shr:2 row_mask:0xf bank_mask:0xf
	v_mov_b32_dpp v107, v121 row_ror:1 row_mask:0xf bank_mask:0xf
	v_mov_b32_dpp v109, v105 row_shr:2 row_mask:0xf bank_mask:0xf
	v_mov_b32_dpp v106, v104 row_shr:1 row_mask:0xf bank_mask:0xf
	v_mov_b32_dpp v107, v105 row_shr:1 row_mask:0xf bank_mask:0xf
	v_fma_f32 v108, v46, v108, v62
	v_fma_f32 v109, v47, v109, v63
	s_nop 0
	v_fma_f32 v106, v50, v106, v108
	v_fma_f32 v107, v51, v107, v109
	s_nop 0
	v_fma_f32 v106, v104, v58, v106
	v_fma_f32 v107, v105, v59, v107
	s_nop 0
	v_mul_f32_e32 v108, 0x3d372713, v106
	v_mul_f32_e32 v109, 0x3d372713, v107
	v_mul_f32_e32 v108, v106, v108
	v_mul_f32_e32 v109, v107, v109
	v_fma_f32 v108, v106, v108, v106
	v_fma_f32 v109, v107, v109, v107
	v_mul_f32_e32 v108, 0xc0135761, v108
	v_mul_f32_e32 v109, 0xc0135761, v109
	v_exp_f32_e32 v108, v108
	v_exp_f32_e32 v109, v109
	v_add_f32_e32 v108, 1.0, v108
	v_add_f32_e32 v109, 1.0, v109
	v_rcp_f32_e32 v108, v108
	v_rcp_f32_e32 v109, v109
	s_nop 0
	v_mul_f32_e32 v106, v106, v108
	v_mul_f32_e32 v107, v107, v109
	v_mov_b32_e32 v108, v1
	v_mov_b32_e32 v109, v1
	v_mul_f32_e32 v106, v98, v106
	v_mul_f32_e32 v107, v99, v107
	v_mov_b32_e32 v98, v1
	v_mov_b32_dpp v108, v118 row_ror:2 row_mask:0xf bank_mask:0xf
	v_mov_b32_e32 v99, v1
	v_mov_b32_dpp v109, v119 row_ror:2 row_mask:0xf bank_mask:0xf
	v_mov_b32_dpp v98, v118 row_ror:1 row_mask:0xf bank_mask:0xf
	v_mov_b32_dpp v108, v102 row_shr:2 row_mask:0xf bank_mask:0xf
	v_mov_b32_dpp v99, v119 row_ror:1 row_mask:0xf bank_mask:0xf
	v_mov_b32_dpp v109, v103 row_shr:2 row_mask:0xf bank_mask:0xf
	v_mov_b32_dpp v98, v102 row_shr:1 row_mask:0xf bank_mask:0xf
	v_mov_b32_dpp v99, v103 row_shr:1 row_mask:0xf bank_mask:0xf
	v_fma_f32 v108, v48, v108, v64
	v_fma_f32 v109, v49, v109, v65
	s_nop 0
	v_fma_f32 v98, v52, v98, v108
	v_fma_f32 v99, v53, v99, v109
	s_nop 0
	v_fma_f32 v98, v102, v60, v98
	v_fma_f32 v99, v103, v61, v99
	s_nop 0
	v_mul_f32_e32 v108, 0x3d372713, v98
	v_mul_f32_e32 v109, 0x3d372713, v99
	v_mul_f32_e32 v108, v98, v108
	v_mul_f32_e32 v109, v99, v109
	v_fma_f32 v108, v98, v108, v98
	v_fma_f32 v109, v99, v109, v99
	v_mul_f32_e32 v108, 0xc0135761, v108
	v_mul_f32_e32 v109, 0xc0135761, v109
	v_exp_f32_e32 v108, v108
	v_exp_f32_e32 v109, v109
	v_add_f32_e32 v108, 1.0, v108
	v_add_f32_e32 v109, 1.0, v109
	v_rcp_f32_e32 v108, v108
	v_rcp_f32_e32 v109, v109
	s_nop 0
	v_mul_f32_e32 v98, v98, v108
	v_mul_f32_e32 v99, v99, v109
	s_nop 0
	v_mul_f32_e32 v108, v100, v98
	v_mul_f32_e32 v109, v101, v99
	v_cvt_pk_bf16_f32 v100, v106, v107
	v_or_b32_e32 v106, 48, v193
	v_mad_i64_i32 v[106:107], s[38:39], v106, s2, v[130:131]
	v_cvt_pk_bf16_f32 v98, v114, v115
	v_cvt_pk_bf16_f32 v99, v116, v117
	v_cvt_pk_bf16_f32 v101, v108, v109
	v_lshl_add_u64 v[106:107], v[106:107], 0, v[148:149]
	global_store_dwordx4 v[106:107], v[98:101], off
	s_mov_b64 s[38:39], exec
	s_and_b64 s[50:51], s[38:39], vcc
	v_mov_b32_e32 v228, v221
	s_mov_b64 exec, s[50:51]
	s_cbranch_execz .LBB0_366
	v_lshl_add_u64 v[106:107], v[146:147], 0, s[40:41]
	v_cvt_pk_bf16_f32 v101, v102, v103
	v_mov_b64_e32 v[102:103], s[42:43]
	v_mad_u64_u32 v[102:103], s[40:41], v106, s2, v[102:103]
	v_mad_i32_i24 v103, v107, s2, v103
	v_cvt_pk_bf16_f32 v98, v110, v111
	v_cvt_pk_bf16_f32 v99, v112, v113
	v_cvt_pk_bf16_f32 v100, v104, v105
	v_lshl_add_u64 v[102:103], v[182:183], 1, v[102:103]
	global_store_dwordx4 v[102:103], v[98:101], off
.LBB0_366:
	s_or_b64 exec, exec, s[38:39]
	s_nop 0
	v_ffbh_u32_e32 v98, v181
	v_min_u32_e32 v100, 32, v98
	v_lshlrev_b64 v[98:99], v100, v[180:181]
	v_min_u32_e32 v98, 1, v98
	v_or_b32_e32 v98, v99, v98
	v_cvt_f32_u32_e32 v101, v98
	v_ffbh_u32_e32 v98, v179
	v_min_u32_e32 v102, 32, v98
	v_lshlrev_b64 v[98:99], v102, v[178:179]
	v_min_u32_e32 v98, 1, v98
	v_or_b32_e32 v98, v99, v98
	v_cvt_f32_u32_e32 v98, v98
	v_sub_u32_e32 v99, 32, v100
	v_sub_u32_e32 v100, 32, v102
	v_ldexp_f32 v99, v101, v99
	v_ldexp_f32 v98, v98, v100
	s_mov_b32 s38, 0x32800000
	v_fma_f32 v102, v98, s38, v196
	v_fma_f32 v103, v99, s38, v196
	s_add_u32 s66, s66, 2
	v_mul_f32_e32 v98, 0x4b800000, v103
	v_cmp_gt_f32_e64 s[40:41], s96, v103
	v_cmp_gt_f32_e64 s[38:39], s96, v102
	s_addc_u32 s67, s67, 0
	v_cndmask_b32_e64 v98, v103, v98, s[40:41]
	v_rsq_f32_e32 v98, v98
	s_nop 0
	v_mul_f32_e32 v99, 0x45800000, v98
	v_cndmask_b32_e64 v104, v98, v99, s[40:41]
	v_mul_f32_e32 v98, v104, v96
	v_mul_f32_e32 v99, v104, v97
	v_mul_f32_e32 v100, v104, v94
	v_mul_f32_e32 v101, v104, v95
	v_mul_f32_e32 v94, v104, v92
	v_mul_f32_e32 v95, v104, v93
	v_mul_f32_e32 v96, v104, v90
	v_mul_f32_e32 v97, v104, v91
	v_mov_b32_dpp v106, v100 row_shr:1 row_mask:0xf bank_mask:0xf bound_ctrl:1
	v_mov_b32_dpp v108, v100 row_shr:2 row_mask:0xf bank_mask:0xf bound_ctrl:1
	v_mov_b32_dpp v107, v101 row_shr:1 row_mask:0xf bank_mask:0xf bound_ctrl:1
	v_mov_b32_dpp v109, v101 row_shr:2 row_mask:0xf bank_mask:0xf bound_ctrl:1
	v_mov_b32_dpp v112, v98 row_shr:1 row_mask:0xf bank_mask:0xf bound_ctrl:1
	v_mov_b32_dpp v114, v98 row_shr:2 row_mask:0xf bank_mask:0xf bound_ctrl:1
	v_mov_b32_dpp v113, v99 row_shr:1 row_mask:0xf bank_mask:0xf bound_ctrl:1
	v_mov_b32_dpp v115, v99 row_shr:2 row_mask:0xf bank_mask:0xf bound_ctrl:1
	v_mov_b32_dpp v116, v96 row_shr:1 row_mask:0xf bank_mask:0xf bound_ctrl:1
	v_mov_b32_dpp v118, v96 row_shr:2 row_mask:0xf bank_mask:0xf bound_ctrl:1
	v_mov_b32_dpp v117, v97 row_shr:1 row_mask:0xf bank_mask:0xf bound_ctrl:1
	v_mov_b32_dpp v119, v97 row_shr:2 row_mask:0xf bank_mask:0xf bound_ctrl:1
	v_mov_b32_dpp v120, v94 row_shr:1 row_mask:0xf bank_mask:0xf bound_ctrl:1
	v_mov_b32_dpp v122, v94 row_shr:2 row_mask:0xf bank_mask:0xf bound_ctrl:1
	v_mov_b32_dpp v121, v95 row_shr:1 row_mask:0xf bank_mask:0xf bound_ctrl:1
	v_mov_b32_dpp v123, v95 row_shr:2 row_mask:0xf bank_mask:0xf bound_ctrl:1
	s_and_saveexec_b64 s[40:41], s[36:37]
	s_xor_b64 s[36:37], exec, s[40:41]
	s_cbranch_execz .LBB0_368
	v_fma_f32 v90, v48, v122, v64
	v_fma_f32 v91, v49, v123, v65
	v_fma_f32 v118, v46, v118, v62
	v_fma_f32 v119, v47, v119, v63
	v_fma_f32 v90, v52, v120, v90
	v_fma_f32 v91, v53, v121, v91
	v_fma_f32 v116, v50, v116, v118
	v_fma_f32 v117, v51, v117, v119
	v_fma_f32 v90, v94, v60, v90
	v_fma_f32 v91, v95, v61, v91
	v_fma_f32 v116, v96, v58, v116
	v_fma_f32 v117, v97, v59, v117
	v_mul_f32_e32 v0, 0x3d372713, v90
	v_mul_f32_e32 v0, v90, v0
	v_mul_f32_e32 v92, 0x3d372713, v91
	v_fma_f32 v0, v90, v0, v90
	v_mul_f32_e32 v92, v91, v92
	v_mul_f32_e32 v0, 0xc0135761, v0
	v_fma_f32 v92, v91, v92, v91
	v_exp_f32_e32 v0, v0
	v_mul_f32_e32 v92, 0xc0135761, v92
	v_exp_f32_e32 v93, v92
	v_mul_f32_e32 v110, v104, v68
	v_mul_f32_e32 v111, v104, v69
	v_add_f32_e32 v0, 1.0, v0
	v_rcp_f32_e32 v92, v0
	v_add_f32_e32 v0, 1.0, v93
	v_mul_f32_e32 v93, 0x3d372713, v116
	v_mul_f32_e32 v93, v116, v93
	v_fma_f32 v93, v116, v93, v116
	v_mul_f32_e32 v93, 0xc0135761, v93
	v_exp_f32_e32 v103, v93
	v_mul_f32_e32 v93, 0x3d372713, v117
	v_mul_f32_e32 v93, v117, v93
	v_fma_f32 v93, v117, v93, v117
	v_mul_f32_e32 v93, 0xc0135761, v93
	v_exp_f32_e32 v105, v93
	v_rcp_f32_e32 v93, v0
	v_add_f32_e32 v0, 1.0, v103
	v_rcp_f32_e32 v118, v0
	v_add_f32_e32 v0, 1.0, v105
	v_rcp_f32_e32 v119, v0
	v_mul_f32_e32 v90, v90, v92
	v_mul_f32_e32 v91, v91, v93
	v_fma_f32 v108, v74, v108, v86
	v_fma_f32 v109, v75, v109, v87
	v_mul_f32_e32 v110, v110, v90
	v_mul_f32_e32 v111, v111, v91
	v_mul_f32_e32 v90, v104, v66
	v_mul_f32_e32 v91, v104, v67
	v_mul_f32_e32 v92, v116, v118
	v_mul_f32_e32 v93, v117, v119
	v_fma_f32 v106, v78, v106, v108
	v_fma_f32 v107, v79, v107, v109
	v_mul_f32_e32 v92, v90, v92
	v_mul_f32_e32 v93, v91, v93
	v_fma_f32 v90, v76, v114, v88
	v_fma_f32 v91, v77, v115, v89
	v_fma_f32 v106, v100, v82, v106
	v_fma_f32 v107, v101, v83, v107
	v_fma_f32 v90, v80, v112, v90
	v_fma_f32 v91, v81, v113, v91
	v_mul_f32_e32 v114, v104, v72
	v_mul_f32_e32 v115, v104, v73
	v_fma_f32 v90, v98, v84, v90
	v_fma_f32 v91, v99, v85, v91
	v_mul_f32_e32 v105, 0x3d372713, v107
	v_mul_f32_e32 v0, 0x3d372713, v90
	v_mul_f32_e32 v0, v90, v0
	v_mul_f32_e32 v103, 0x3d372713, v91
	v_fma_f32 v0, v90, v0, v90
	v_mul_f32_e32 v103, v91, v103
	v_mul_f32_e32 v0, 0xc0135761, v0
	v_fma_f32 v103, v91, v103, v91
	v_exp_f32_e32 v0, v0
	v_mul_f32_e32 v103, 0xc0135761, v103
	v_exp_f32_e32 v103, v103
	v_mul_f32_e32 v105, v107, v105
	v_add_f32_e32 v0, 1.0, v0
	v_rcp_f32_e32 v112, v0
	v_add_f32_e32 v0, 1.0, v103
	v_mul_f32_e32 v103, 0x3d372713, v106
	v_mul_f32_e32 v103, v106, v103
	v_fma_f32 v103, v106, v103, v106
	v_mul_f32_e32 v103, 0xc0135761, v103
	v_fma_f32 v105, v107, v105, v107
	v_exp_f32_e32 v103, v103
	v_mul_f32_e32 v105, 0xc0135761, v105
	v_exp_f32_e32 v105, v105
	v_rcp_f32_e32 v113, v0
	v_add_f32_e32 v0, 1.0, v103
	v_rcp_f32_e32 v108, v0
	v_add_f32_e32 v0, 1.0, v105
	v_rcp_f32_e32 v109, v0
	v_mul_f32_e32 v90, v90, v112
	v_mul_f32_e32 v91, v91, v113
	v_add_u32_e32 v0, 0x80, v193
	v_mul_f32_e32 v112, v114, v90
	v_mul_f32_e32 v113, v115, v91
	v_mul_f32_e32 v90, v104, v70
	v_mul_f32_e32 v91, v104, v71
	v_mul_f32_e32 v104, v106, v108
	v_mul_f32_e32 v105, v107, v109
	v_cvt_pk_bf16_f32 v92, v92, v93
	v_mul_f32_e32 v90, v90, v104
	v_mul_f32_e32 v91, v91, v105
	v_mov_b64_e32 v[104:105], s[16:17]
	v_cvt_pk_bf16_f32 v90, v90, v91
	v_cvt_pk_bf16_f32 v91, v112, v113
	v_cvt_pk_bf16_f32 v93, v110, v111
	v_mad_i64_i32 v[110:111], s[40:41], v0, s2, v[104:105]
.LBB0_368:
	s_or_saveexec_b64 s[36:37], s[36:37]
	s_lshl_b64 s[40:41], s[66:67], 2
	s_xor_b64 exec, exec, s[36:37]
	s_cbranch_execz .LBB0_370
	s_lshl_b64 s[50:51], s[66:67], 1
	v_or_b32_e32 v103, s50, v0
	v_or_b32_e32 v0, s40, v0
	v_mov_b64_e32 v[106:107], s[42:43]
	v_mad_u64_u32 v[106:107], s[66:67], v0, s2, v[106:107]
	v_mov_b32_e32 v105, v104
	v_mad_i32_i24 v107, s41, v232, v107
	v_cvt_pk_bf16_f32 v90, v100, v101
	v_cvt_pk_bf16_f32 v91, v98, v99
	v_cvt_pk_bf16_f32 v92, v96, v97
	v_cvt_pk_bf16_f32 v93, v94, v95
	v_lshl_add_u64 v[106:107], v[182:183], 1, v[106:107]
	v_mul_f32_e32 v66, v104, v66
	v_mul_f32_e32 v67, v105, v67
	global_store_dwordx4 v[106:107], v[90:93], off
	v_mul_f32_e32 v70, v104, v70
	v_mul_f32_e32 v71, v105, v71
	s_nop 0
	v_mov_b32_e32 v90, v104
	v_mov_b32_e32 v91, v104
	v_cvt_pk_bf16_f32 v92, v66, v67
	v_mov_b64_e32 v[66:67], s[44:45]
	v_mul_f32_e32 v72, v90, v72
	v_mul_f32_e32 v73, v91, v73
	v_mul_f32_e32 v68, v90, v68
	v_mul_f32_e32 v69, v91, v69
	v_mad_u64_u32 v[110:111], s[66:67], v103, s2, v[66:67]
	v_cvt_pk_bf16_f32 v90, v70, v71
	v_cvt_pk_bf16_f32 v91, v72, v73
	v_cvt_pk_bf16_f32 v93, v68, v69
	v_mad_i32_i24 v111, s51, v232, v111
.LBB0_370:
	s_or_b64 exec, exec, s[36:37]
	v_mul_f32_e32 v0, 0x4b800000, v102
	v_cndmask_b32_e64 v0, v102, v0, s[38:39]
	v_rsq_f32_e32 v0, v0
	s_mov_b32 s36, 0x32800000
	v_mov_b32_e32 v72, v1
	v_mov_b32_e32 v73, v1
	v_mul_f32_e32 v66, 0x45800000, v0
	v_cndmask_b32_e64 v68, v0, v66, s[38:39]
	v_ffbh_u32_e32 v0, v177
	v_min_u32_e32 v0, 32, v0
	v_lshlrev_b64 v[66:67], v0, v[176:177]
	v_min_u32_e32 v66, 1, v66
	v_or_b32_e32 v66, v67, v66
	v_cvt_f32_u32_e32 v66, v66
	v_sub_u32_e32 v0, 32, v0
	v_mul_f32_e32 v54, v68, v54
	v_mul_f32_e32 v55, v68, v55
	v_mov_b32_dpp v72, v100 row_ror:2 row_mask:0xf bank_mask:0xf
	v_ldexp_f32 v67, v66, v0
	v_ffbh_u32_e32 v0, v175
	v_min_u32_e32 v0, 32, v0
	v_lshlrev_b64 v[70:71], v0, v[174:175]
	v_min_u32_e32 v66, 1, v70
	v_or_b32_e32 v66, v71, v66
	v_cvt_f32_u32_e32 v66, v66
	v_sub_u32_e32 v0, 32, v0
	v_mov_b32_dpp v73, v101 row_ror:2 row_mask:0xf bank_mask:0xf
	v_mov_b32_dpp v72, v54 row_shr:2 row_mask:0xf bank_mask:0xf
	v_ldexp_f32 v66, v66, v0
	v_fma_f32 v70, v66, s36, v196
	v_fma_f32 v71, v67, s36, v196
	v_mov_b32_dpp v73, v55 row_shr:2 row_mask:0xf bank_mask:0xf
	v_mul_f32_e32 v0, 0x4b800000, v71
	v_cmp_gt_f32_e64 s[38:39], s96, v71
	v_cmp_gt_f32_e64 s[36:37], s96, v70
	v_fma_f32 v72, v74, v72, v86
	v_fma_f32 v73, v75, v73, v87
	v_cndmask_b32_e64 v0, v71, v0, s[38:39]
	v_rsq_f32_e32 v0, v0
	v_mul_f32_e32 v38, v68, v38
	v_mul_f32_e32 v39, v68, v39
	v_mul_f32_e32 v56, v68, v56
	v_mul_f32_e32 v57, v68, v57
	v_mul_f32_e32 v40, v68, v40
	v_mul_f32_e32 v41, v68, v41
	v_mul_f32_e32 v66, 0x45800000, v0
	v_cndmask_b32_e64 v66, v0, v66, s[38:39]
	v_mul_f32_e32 v0, 0x4b800000, v70
	v_cndmask_b32_e64 v0, v70, v0, s[36:37]
	v_lshl_add_u64 v[70:71], v[110:111], 0, v[148:149]
	v_rsq_f32_e32 v0, v0
	global_store_dwordx4 v[70:71], v[90:93], off
	v_mov_b32_e32 v70, v1
	v_mov_b32_e32 v71, v1
	v_mul_f32_e32 v67, 0x45800000, v0
	v_mov_b32_dpp v70, v100 row_ror:1 row_mask:0xf bank_mask:0xf
	v_mov_b32_dpp v71, v101 row_ror:1 row_mask:0xf bank_mask:0xf
	v_cndmask_b32_e64 v0, v0, v67, s[36:37]
	v_mov_b32_dpp v70, v54 row_shr:1 row_mask:0xf bank_mask:0xf
	v_mov_b32_dpp v71, v55 row_shr:1 row_mask:0xf bank_mask:0xf
	v_fma_f32 v70, v78, v70, v72
	v_fma_f32 v71, v79, v71, v73
	v_mul_f32_e32 v34, v68, v34
	v_mul_f32_e32 v35, v68, v35
	v_fma_f32 v70, v54, v82, v70
	v_fma_f32 v71, v55, v83, v71
	v_mul_f32_e32 v36, v68, v36
	v_mul_f32_e32 v37, v68, v37
	v_mul_f32_e32 v67, 0x3d372713, v70
	v_mul_f32_e32 v67, v70, v67
	v_fma_f32 v67, v70, v67, v70
	v_mul_f32_e32 v67, 0xc0135761, v67
	v_exp_f32_e32 v67, v67
	v_mul_f32_e32 v14, v0, v14
	v_mul_f32_e32 v15, v0, v15
	v_mul_f32_e32 v6, v0, v6
	v_mul_f32_e32 v7, v0, v7
	v_mul_f32_e32 v16, v0, v16
	v_mul_f32_e32 v17, v0, v17
	v_add_f32_e32 v67, 1.0, v67
	v_rcp_f32_e32 v72, v67
	v_mul_f32_e32 v67, 0x3d372713, v71
	v_mul_f32_e32 v67, v71, v67
	v_fma_f32 v67, v71, v67, v71
	v_mul_f32_e32 v67, 0xc0135761, v67
	v_exp_f32_e32 v67, v67
	v_mul_f32_e32 v8, v0, v8
	v_mul_f32_e32 v9, v0, v9
	v_mul_f32_e32 v2, v0, v2
	v_mul_f32_e32 v3, v0, v3
	v_mul_f32_e32 v4, v0, v4
	v_mul_f32_e32 v5, v0, v5
	v_add_f32_e32 v67, 1.0, v67
	v_rcp_f32_e32 v73, v67
	s_nop 0
	v_mul_f32_e32 v70, v70, v72
	v_mul_f32_e32 v71, v71, v73
	v_mov_b32_e32 v72, v1
	v_mov_b32_e32 v73, v1
	v_mul_f32_e32 v70, v38, v70
	v_mul_f32_e32 v71, v39, v71
	v_mov_b32_e32 v38, v1
	v_mov_b32_dpp v72, v98 row_ror:2 row_mask:0xf bank_mask:0xf
	v_mov_b32_e32 v39, v1
	v_mov_b32_dpp v73, v99 row_ror:2 row_mask:0xf bank_mask:0xf
	v_mov_b32_dpp v38, v98 row_ror:1 row_mask:0xf bank_mask:0xf
	v_mov_b32_dpp v72, v56 row_shr:2 row_mask:0xf bank_mask:0xf
	v_mov_b32_dpp v39, v99 row_ror:1 row_mask:0xf bank_mask:0xf
	v_mov_b32_dpp v73, v57 row_shr:2 row_mask:0xf bank_mask:0xf
	v_mov_b32_dpp v38, v56 row_shr:1 row_mask:0xf bank_mask:0xf
	v_mov_b32_dpp v39, v57 row_shr:1 row_mask:0xf bank_mask:0xf
	v_fma_f32 v72, v76, v72, v88
	v_fma_f32 v73, v77, v73, v89
	s_nop 0
	v_fma_f32 v38, v80, v38, v72
	v_fma_f32 v39, v81, v39, v73
	s_nop 0
	v_fma_f32 v38, v56, v84, v38
	v_fma_f32 v39, v57, v85, v39
	s_nop 0
	v_mul_f32_e32 v67, 0x3d372713, v38
	v_mul_f32_e32 v67, v38, v67
	v_fma_f32 v67, v38, v67, v38
	v_mul_f32_e32 v67, 0xc0135761, v67
	v_exp_f32_e32 v67, v67
	s_nop 0
	v_add_f32_e32 v67, 1.0, v67
	v_rcp_f32_e32 v72, v67
	v_mul_f32_e32 v67, 0x3d372713, v39
	v_mul_f32_e32 v67, v39, v67
	v_fma_f32 v67, v39, v67, v39
	v_mul_f32_e32 v67, 0xc0135761, v67
	v_exp_f32_e32 v67, v67
	s_nop 0
	v_add_f32_e32 v67, 1.0, v67
	v_rcp_f32_e32 v73, v67
	v_mul_f32_e32 v30, v66, v30
	v_mul_f32_e32 v31, v66, v31
	v_mul_f32_e32 v22, v66, v22
	v_mul_f32_e32 v23, v66, v23
	v_mul_f32_e32 v32, v66, v32
	v_mul_f32_e32 v33, v66, v33
	v_mul_f32_e32 v38, v38, v72
	v_mul_f32_e32 v39, v39, v73
	v_mul_f32_e32 v24, v66, v24
	v_mul_f32_e32 v25, v66, v25
	v_mul_f32_e32 v72, v40, v38
	v_mul_f32_e32 v73, v41, v39
	v_mul_f32_e32 v38, v68, v44
	v_mul_f32_e32 v39, v68, v45
	v_mov_b32_e32 v44, v1
	v_mov_b32_e32 v45, v1
	v_mul_f32_e32 v40, v68, v42
	v_mul_f32_e32 v41, v68, v43
	v_mov_b32_e32 v42, v1
	v_mov_b32_dpp v44, v96 row_ror:2 row_mask:0xf bank_mask:0xf
	v_mov_b32_e32 v43, v1
	v_mov_b32_dpp v45, v97 row_ror:2 row_mask:0xf bank_mask:0xf
	v_mov_b32_dpp v42, v96 row_ror:1 row_mask:0xf bank_mask:0xf
	v_mov_b32_dpp v44, v40 row_shr:2 row_mask:0xf bank_mask:0xf
	v_mov_b32_dpp v43, v97 row_ror:1 row_mask:0xf bank_mask:0xf
	v_mov_b32_dpp v45, v41 row_shr:2 row_mask:0xf bank_mask:0xf
	v_mov_b32_dpp v42, v40 row_shr:1 row_mask:0xf bank_mask:0xf
	v_mov_b32_dpp v43, v41 row_shr:1 row_mask:0xf bank_mask:0xf
	v_fma_f32 v44, v46, v44, v62
	v_fma_f32 v45, v47, v45, v63
	v_mul_f32_e32 v18, v66, v18
	v_mul_f32_e32 v19, v66, v19
	v_fma_f32 v42, v50, v42, v44
	v_fma_f32 v43, v51, v43, v45
	v_mul_f32_e32 v20, v66, v20
	v_mul_f32_e32 v21, v66, v21
	v_fma_f32 v42, v40, v58, v42
	v_fma_f32 v43, v41, v59, v43
	s_nop 0
	v_mul_f32_e32 v44, 0x3d372713, v42
	v_mul_f32_e32 v45, 0x3d372713, v43
	v_mul_f32_e32 v44, v42, v44
	v_mul_f32_e32 v45, v43, v45
	v_fma_f32 v44, v42, v44, v42
	v_fma_f32 v45, v43, v45, v43
	v_mul_f32_e32 v44, 0xc0135761, v44
	v_mul_f32_e32 v45, 0xc0135761, v45
	v_exp_f32_e32 v44, v44
	v_exp_f32_e32 v45, v45
	v_add_f32_e32 v44, 1.0, v44
	v_add_f32_e32 v45, 1.0, v45
	v_rcp_f32_e32 v44, v44
	v_rcp_f32_e32 v45, v45
	s_nop 0
	v_mul_f32_e32 v42, v42, v44
	v_mul_f32_e32 v43, v43, v45
	v_mov_b32_e32 v44, v1
	v_mov_b32_e32 v45, v1
	v_mul_f32_e32 v34, v34, v42
	v_mul_f32_e32 v35, v35, v43
	v_mov_b32_e32 v42, v1
	v_mov_b32_dpp v44, v94 row_ror:2 row_mask:0xf bank_mask:0xf
	v_mov_b32_e32 v43, v1
	v_mov_b32_dpp v45, v95 row_ror:2 row_mask:0xf bank_mask:0xf
	v_mov_b32_dpp v42, v94 row_ror:1 row_mask:0xf bank_mask:0xf
	v_mov_b32_dpp v44, v38 row_shr:2 row_mask:0xf bank_mask:0xf
	v_mov_b32_dpp v43, v95 row_ror:1 row_mask:0xf bank_mask:0xf
	v_mov_b32_dpp v45, v39 row_shr:2 row_mask:0xf bank_mask:0xf
	v_mov_b32_dpp v42, v38 row_shr:1 row_mask:0xf bank_mask:0xf
	v_mov_b32_dpp v43, v39 row_shr:1 row_mask:0xf bank_mask:0xf
	v_fma_f32 v44, v48, v44, v64
	v_fma_f32 v45, v49, v45, v65
	s_nop 0
	v_fma_f32 v42, v52, v42, v44
	v_fma_f32 v43, v53, v43, v45
	s_nop 0
	v_fma_f32 v42, v38, v60, v42
	v_fma_f32 v43, v39, v61, v43
	s_nop 0
	v_mul_f32_e32 v44, 0x3d372713, v42
	v_mul_f32_e32 v45, 0x3d372713, v43
	v_mul_f32_e32 v44, v42, v44
	v_mul_f32_e32 v45, v43, v45
	v_fma_f32 v44, v42, v44, v42
	v_fma_f32 v45, v43, v45, v43
	v_mul_f32_e32 v44, 0xc0135761, v44
	v_mul_f32_e32 v45, 0xc0135761, v45
	v_exp_f32_e32 v44, v44
	v_exp_f32_e32 v45, v45
	v_add_f32_e32 v44, 1.0, v44
	v_add_f32_e32 v45, 1.0, v45
	v_rcp_f32_e32 v44, v44
	v_rcp_f32_e32 v45, v45
	s_nop 0
	v_mul_f32_e32 v42, v42, v44
	v_mul_f32_e32 v43, v43, v45
	s_nop 0
	v_mul_f32_e32 v36, v36, v42
	v_mul_f32_e32 v37, v37, v43
	v_cvt_pk_bf16_f32 v44, v34, v35
	v_cvt_pk_bf16_f32 v45, v36, v37
	v_add_u32_e32 v36, 0x90, v193
	v_mov_b64_e32 v[34:35], s[16:17]
	v_mad_i64_i32 v[36:37], s[36:37], v36, s2, v[34:35]
	v_cvt_pk_bf16_f32 v42, v70, v71
	v_cvt_pk_bf16_f32 v43, v72, v73
	v_lshl_add_u64 v[36:37], v[36:37], 0, v[148:149]
	global_store_dwordx4 v[36:37], v[42:45], off
	v_mov_b32_e32 v36, v1
	v_mov_b32_e32 v37, v1
	v_mov_b32_e32 v42, v1
	v_mov_b32_e32 v43, v1
	v_mov_b32_dpp v36, v54 row_ror:1 row_mask:0xf bank_mask:0xf
	v_mov_b32_dpp v42, v54 row_ror:2 row_mask:0xf bank_mask:0xf
	v_mov_b32_dpp v43, v55 row_ror:2 row_mask:0xf bank_mask:0xf
	v_mov_b32_dpp v37, v55 row_ror:1 row_mask:0xf bank_mask:0xf
	v_mov_b32_dpp v42, v30 row_shr:2 row_mask:0xf bank_mask:0xf
	v_mov_b32_dpp v43, v31 row_shr:2 row_mask:0xf bank_mask:0xf
	v_mov_b32_dpp v36, v30 row_shr:1 row_mask:0xf bank_mask:0xf
	v_mov_b32_dpp v37, v31 row_shr:1 row_mask:0xf bank_mask:0xf
	v_fma_f32 v42, v74, v42, v86
	v_fma_f32 v43, v75, v43, v87
	s_nop 0
	v_fma_f32 v36, v78, v36, v42
	v_fma_f32 v37, v79, v37, v43
	s_nop 0
	v_fma_f32 v36, v30, v82, v36
	v_fma_f32 v37, v31, v83, v37
	s_nop 0
	v_mul_f32_e32 v42, 0x3d372713, v36
	v_mul_f32_e32 v43, 0x3d372713, v37
	v_mul_f32_e32 v42, v36, v42
	v_mul_f32_e32 v43, v37, v43
	v_fma_f32 v42, v36, v42, v36
	v_fma_f32 v43, v37, v43, v37
	v_mul_f32_e32 v42, 0xc0135761, v42
	v_mul_f32_e32 v43, 0xc0135761, v43
	v_exp_f32_e32 v42, v42
	v_exp_f32_e32 v43, v43
	v_add_f32_e32 v42, 1.0, v42
	v_add_f32_e32 v43, 1.0, v43
	v_rcp_f32_e32 v42, v42
	v_rcp_f32_e32 v43, v43
	s_nop 0
	v_mul_f32_e32 v36, v36, v42
	v_mul_f32_e32 v37, v37, v43
	v_mov_b32_e32 v42, v1
	v_mov_b32_e32 v43, v1
	v_mul_f32_e32 v36, v22, v36
	v_mul_f32_e32 v37, v23, v37
	v_mov_b32_e32 v22, v1
	v_mov_b32_dpp v42, v56 row_ror:2 row_mask:0xf bank_mask:0xf
	v_mov_b32_e32 v23, v1
	v_mov_b32_dpp v43, v57 row_ror:2 row_mask:0xf bank_mask:0xf
	v_mov_b32_dpp v22, v56 row_ror:1 row_mask:0xf bank_mask:0xf
	v_mov_b32_dpp v42, v32 row_shr:2 row_mask:0xf bank_mask:0xf
	v_mov_b32_dpp v23, v57 row_ror:1 row_mask:0xf bank_mask:0xf
	v_mov_b32_dpp v43, v33 row_shr:2 row_mask:0xf bank_mask:0xf
	v_mov_b32_dpp v22, v32 row_shr:1 row_mask:0xf bank_mask:0xf
	v_mov_b32_dpp v23, v33 row_shr:1 row_mask:0xf bank_mask:0xf
	v_fma_f32 v42, v76, v42, v88
	v_fma_f32 v43, v77, v43, v89
	s_nop 0
	v_fma_f32 v22, v80, v22, v42
	v_fma_f32 v23, v81, v23, v43
	s_nop 0
	v_fma_f32 v22, v32, v84, v22
	v_fma_f32 v23, v33, v85, v23
	s_nop 0
	v_mul_f32_e32 v42, 0x3d372713, v22
	v_mul_f32_e32 v43, 0x3d372713, v23
	v_mul_f32_e32 v42, v22, v42
	v_mul_f32_e32 v43, v23, v43
	v_fma_f32 v42, v22, v42, v22
	v_fma_f32 v43, v23, v43, v23
	v_mul_f32_e32 v42, 0xc0135761, v42
	v_mul_f32_e32 v43, 0xc0135761, v43
	v_exp_f32_e32 v42, v42
	v_exp_f32_e32 v43, v43
	v_add_f32_e32 v42, 1.0, v42
	v_add_f32_e32 v43, 1.0, v43
	v_rcp_f32_e32 v42, v42
	v_rcp_f32_e32 v43, v43
	s_nop 0
	v_mul_f32_e32 v22, v22, v42
	v_mul_f32_e32 v23, v23, v43
	s_nop 0
	v_mul_f32_e32 v42, v24, v22
	v_mul_f32_e32 v43, v25, v23
	v_mul_f32_e32 v22, v66, v28
	v_mul_f32_e32 v23, v66, v29
	v_mov_b32_e32 v28, v1
	v_mov_b32_e32 v29, v1
	v_mul_f32_e32 v24, v66, v26
	v_mul_f32_e32 v25, v66, v27
	v_mov_b32_e32 v26, v1
	v_mov_b32_dpp v28, v40 row_ror:2 row_mask:0xf bank_mask:0xf
	v_mov_b32_e32 v27, v1
	v_mov_b32_dpp v29, v41 row_ror:2 row_mask:0xf bank_mask:0xf
	v_mov_b32_dpp v26, v40 row_ror:1 row_mask:0xf bank_mask:0xf
	v_mov_b32_dpp v28, v24 row_shr:2 row_mask:0xf bank_mask:0xf
	v_mov_b32_dpp v27, v41 row_ror:1 row_mask:0xf bank_mask:0xf
	v_mov_b32_dpp v29, v25 row_shr:2 row_mask:0xf bank_mask:0xf
	v_mov_b32_dpp v26, v24 row_shr:1 row_mask:0xf bank_mask:0xf
	v_mov_b32_dpp v27, v25 row_shr:1 row_mask:0xf bank_mask:0xf
	v_fma_f32 v28, v46, v28, v62
	v_fma_f32 v29, v47, v29, v63
	s_nop 0
	v_fma_f32 v26, v50, v26, v28
	v_fma_f32 v27, v51, v27, v29
	s_nop 0
	v_fma_f32 v26, v24, v58, v26
	v_fma_f32 v27, v25, v59, v27
	s_nop 0
	v_mul_f32_e32 v28, 0x3d372713, v26
	v_mul_f32_e32 v29, 0x3d372713, v27
	v_mul_f32_e32 v28, v26, v28
	v_mul_f32_e32 v29, v27, v29
	v_fma_f32 v28, v26, v28, v26
	v_fma_f32 v29, v27, v29, v27
	v_mul_f32_e32 v28, 0xc0135761, v28
	v_mul_f32_e32 v29, 0xc0135761, v29
	v_exp_f32_e32 v28, v28
	v_exp_f32_e32 v29, v29
	v_add_f32_e32 v28, 1.0, v28
	v_add_f32_e32 v29, 1.0, v29
	v_rcp_f32_e32 v28, v28
	v_rcp_f32_e32 v29, v29
	s_nop 0
	v_mul_f32_e32 v26, v26, v28
	v_mul_f32_e32 v27, v27, v29
	v_mov_b32_e32 v28, v1
	v_mov_b32_e32 v29, v1
	v_mul_f32_e32 v26, v18, v26
	v_mul_f32_e32 v27, v19, v27
	v_mov_b32_e32 v18, v1
	v_mov_b32_dpp v28, v38 row_ror:2 row_mask:0xf bank_mask:0xf
	v_mov_b32_e32 v19, v1
	v_mov_b32_dpp v29, v39 row_ror:2 row_mask:0xf bank_mask:0xf
	v_mov_b32_dpp v18, v38 row_ror:1 row_mask:0xf bank_mask:0xf
	v_mov_b32_dpp v28, v22 row_shr:2 row_mask:0xf bank_mask:0xf
	v_mov_b32_dpp v19, v39 row_ror:1 row_mask:0xf bank_mask:0xf
	v_mov_b32_dpp v29, v23 row_shr:2 row_mask:0xf bank_mask:0xf
	v_mov_b32_dpp v18, v22 row_shr:1 row_mask:0xf bank_mask:0xf
	v_mov_b32_dpp v19, v23 row_shr:1 row_mask:0xf bank_mask:0xf
	v_fma_f32 v28, v48, v28, v64
	v_fma_f32 v29, v49, v29, v65
	s_nop 0
	v_fma_f32 v18, v52, v18, v28
	v_fma_f32 v19, v53, v19, v29
	s_nop 0
	v_fma_f32 v18, v22, v60, v18
	v_fma_f32 v19, v23, v61, v19
	s_nop 0
	v_mul_f32_e32 v28, 0x3d372713, v18
	v_mul_f32_e32 v29, 0x3d372713, v19
	v_mul_f32_e32 v28, v18, v28
	v_mul_f32_e32 v29, v19, v29
	v_fma_f32 v28, v18, v28, v18
	v_fma_f32 v29, v19, v29, v19
	v_mul_f32_e32 v28, 0xc0135761, v28
	v_mul_f32_e32 v29, 0xc0135761, v29
	v_exp_f32_e32 v28, v28
	v_exp_f32_e32 v29, v29
	v_add_f32_e32 v28, 1.0, v28
	v_add_f32_e32 v29, 1.0, v29
	v_rcp_f32_e32 v28, v28
	v_rcp_f32_e32 v29, v29
	s_nop 0
	v_mul_f32_e32 v18, v18, v28
	v_mul_f32_e32 v19, v19, v29
	s_nop 0
	v_mul_f32_e32 v28, v20, v18
	v_mul_f32_e32 v29, v21, v19
	v_cvt_pk_bf16_f32 v20, v26, v27
	v_add_u32_e32 v26, 0xa0, v193
	v_mad_i64_i32 v[26:27], s[36:37], v26, s2, v[34:35]
	v_cvt_pk_bf16_f32 v18, v36, v37
	v_cvt_pk_bf16_f32 v19, v42, v43
	v_cvt_pk_bf16_f32 v21, v28, v29
	v_lshl_add_u64 v[26:27], v[26:27], 0, v[148:149]
	global_store_dwordx4 v[26:27], v[18:21], off
	s_nop 1
	v_mov_b32_e32 v20, v1
	v_mov_b32_e32 v21, v1
	v_mov_b32_e32 v18, v1
	v_mov_b32_dpp v20, v30 row_ror:2 row_mask:0xf bank_mask:0xf
	v_mov_b32_e32 v19, v1
	v_mov_b32_dpp v21, v31 row_ror:2 row_mask:0xf bank_mask:0xf
	v_mov_b32_dpp v18, v30 row_ror:1 row_mask:0xf bank_mask:0xf
	v_mov_b32_dpp v20, v14 row_shr:2 row_mask:0xf bank_mask:0xf
	v_mov_b32_dpp v19, v31 row_ror:1 row_mask:0xf bank_mask:0xf
	v_mov_b32_dpp v21, v15 row_shr:2 row_mask:0xf bank_mask:0xf
	v_mov_b32_dpp v18, v14 row_shr:1 row_mask:0xf bank_mask:0xf
	v_mov_b32_dpp v19, v15 row_shr:1 row_mask:0xf bank_mask:0xf
	v_fma_f32 v20, v74, v20, v86
	v_fma_f32 v21, v75, v21, v87
	s_nop 0
	v_fma_f32 v18, v78, v18, v20
	v_fma_f32 v19, v79, v19, v21
	s_nop 0
	v_fma_f32 v18, v14, v82, v18
	v_fma_f32 v19, v15, v83, v19
	s_nop 0
	v_mul_f32_e32 v20, 0x3d372713, v18
	v_mul_f32_e32 v21, 0x3d372713, v19
	v_mul_f32_e32 v20, v18, v20
	v_mul_f32_e32 v21, v19, v21
	v_fma_f32 v20, v18, v20, v18
	v_fma_f32 v21, v19, v21, v19
	v_mul_f32_e32 v20, 0xc0135761, v20
	v_mul_f32_e32 v21, 0xc0135761, v21
	v_exp_f32_e32 v20, v20
	v_exp_f32_e32 v21, v21
	v_add_f32_e32 v20, 1.0, v20
	v_add_f32_e32 v21, 1.0, v21
	v_rcp_f32_e32 v20, v20
	v_rcp_f32_e32 v21, v21
	s_nop 0
	v_mul_f32_e32 v18, v18, v20
	v_mul_f32_e32 v19, v19, v21
	v_mov_b32_e32 v20, v1
	v_mov_b32_e32 v21, v1
	v_mul_f32_e32 v18, v6, v18
	v_mul_f32_e32 v19, v7, v19
	v_mov_b32_e32 v6, v1
	v_mov_b32_dpp v20, v32 row_ror:2 row_mask:0xf bank_mask:0xf
	v_mov_b32_e32 v7, v1
	v_mov_b32_dpp v21, v33 row_ror:2 row_mask:0xf bank_mask:0xf
	v_mov_b32_dpp v6, v32 row_ror:1 row_mask:0xf bank_mask:0xf
	v_mov_b32_dpp v20, v16 row_shr:2 row_mask:0xf bank_mask:0xf
	v_mov_b32_dpp v7, v33 row_ror:1 row_mask:0xf bank_mask:0xf
	v_mov_b32_dpp v21, v17 row_shr:2 row_mask:0xf bank_mask:0xf
	v_mov_b32_dpp v6, v16 row_shr:1 row_mask:0xf bank_mask:0xf
	v_mov_b32_dpp v7, v17 row_shr:1 row_mask:0xf bank_mask:0xf
	v_fma_f32 v20, v76, v20, v88
	v_fma_f32 v21, v77, v21, v89
	s_nop 0
	v_fma_f32 v6, v80, v6, v20
	v_fma_f32 v7, v81, v7, v21
	s_nop 0
	v_fma_f32 v6, v16, v84, v6
	v_fma_f32 v7, v17, v85, v7
	s_nop 0
	v_mul_f32_e32 v20, 0x3d372713, v6
	v_mul_f32_e32 v21, 0x3d372713, v7
	v_mul_f32_e32 v20, v6, v20
	v_mul_f32_e32 v21, v7, v21
	v_fma_f32 v20, v6, v20, v6
	v_fma_f32 v21, v7, v21, v7
	v_mul_f32_e32 v20, 0xc0135761, v20
	v_mul_f32_e32 v21, 0xc0135761, v21
	v_exp_f32_e32 v20, v20
	v_exp_f32_e32 v21, v21
	v_add_f32_e32 v20, 1.0, v20
	v_add_f32_e32 v21, 1.0, v21
	v_rcp_f32_e32 v20, v20
	v_rcp_f32_e32 v21, v21
	s_nop 0
	v_mul_f32_e32 v6, v6, v20
	v_mul_f32_e32 v7, v7, v21
	s_nop 0
	v_mul_f32_e32 v20, v8, v6
	v_mul_f32_e32 v21, v9, v7
	v_mul_f32_e32 v6, v0, v12
	v_mul_f32_e32 v7, v0, v13
	v_mov_b32_e32 v12, v1
	v_mov_b32_e32 v13, v1
	v_mul_f32_e32 v8, v0, v10
	v_mul_f32_e32 v9, v0, v11
	v_mov_b32_e32 v10, v1
	v_mov_b32_dpp v12, v24 row_ror:2 row_mask:0xf bank_mask:0xf
	v_mov_b32_e32 v11, v1
	v_mov_b32_dpp v13, v25 row_ror:2 row_mask:0xf bank_mask:0xf
	v_mov_b32_dpp v10, v24 row_ror:1 row_mask:0xf bank_mask:0xf
	v_mov_b32_dpp v12, v8 row_shr:2 row_mask:0xf bank_mask:0xf
	v_mov_b32_dpp v11, v25 row_ror:1 row_mask:0xf bank_mask:0xf
	v_mov_b32_dpp v13, v9 row_shr:2 row_mask:0xf bank_mask:0xf
	v_mov_b32_dpp v10, v8 row_shr:1 row_mask:0xf bank_mask:0xf
	v_mov_b32_dpp v11, v9 row_shr:1 row_mask:0xf bank_mask:0xf
	v_fma_f32 v12, v46, v12, v62
	v_fma_f32 v13, v47, v13, v63
	s_nop 0
	v_fma_f32 v10, v50, v10, v12
	v_fma_f32 v11, v51, v11, v13
	s_nop 0
	v_fma_f32 v10, v8, v58, v10
	v_fma_f32 v11, v9, v59, v11
	s_nop 0
	v_mul_f32_e32 v12, 0x3d372713, v10
	v_mul_f32_e32 v13, 0x3d372713, v11
	v_mul_f32_e32 v12, v10, v12
	v_mul_f32_e32 v13, v11, v13
	v_fma_f32 v12, v10, v12, v10
	v_fma_f32 v13, v11, v13, v11
	v_mul_f32_e32 v12, 0xc0135761, v12
	v_mul_f32_e32 v13, 0xc0135761, v13
	v_exp_f32_e32 v12, v12
	v_exp_f32_e32 v13, v13
	v_add_f32_e32 v12, 1.0, v12
	v_add_f32_e32 v13, 1.0, v13
	v_rcp_f32_e32 v12, v12
	v_rcp_f32_e32 v13, v13
	s_nop 0
	v_mul_f32_e32 v10, v10, v12
	v_mul_f32_e32 v11, v11, v13
	v_mov_b32_e32 v12, v1
	v_mov_b32_e32 v13, v1
	v_mul_f32_e32 v10, v2, v10
	v_mul_f32_e32 v11, v3, v11
	v_mov_b32_e32 v2, v1
	v_mov_b32_dpp v12, v22 row_ror:2 row_mask:0xf bank_mask:0xf
	v_mov_b32_e32 v3, v1
	v_mov_b32_dpp v13, v23 row_ror:2 row_mask:0xf bank_mask:0xf
	v_mov_b32_dpp v2, v22 row_ror:1 row_mask:0xf bank_mask:0xf
	v_mov_b32_dpp v12, v6 row_shr:2 row_mask:0xf bank_mask:0xf
	v_mov_b32_dpp v3, v23 row_ror:1 row_mask:0xf bank_mask:0xf
	v_mov_b32_dpp v13, v7 row_shr:2 row_mask:0xf bank_mask:0xf
	v_mov_b32_dpp v2, v6 row_shr:1 row_mask:0xf bank_mask:0xf
	v_mov_b32_dpp v3, v7 row_shr:1 row_mask:0xf bank_mask:0xf
	v_fma_f32 v12, v48, v12, v64
	v_fma_f32 v13, v49, v13, v65
	s_nop 0
	v_fma_f32 v2, v52, v2, v12
	v_fma_f32 v3, v53, v3, v13
	s_nop 0
	v_fma_f32 v2, v6, v60, v2
	v_fma_f32 v3, v7, v61, v3
	s_nop 0
	v_mul_f32_e32 v12, 0x3d372713, v2
	v_mul_f32_e32 v0, 0x3d372713, v3
	v_mul_f32_e32 v12, v2, v12
	v_mul_f32_e32 v0, v3, v0
	v_fma_f32 v12, v2, v12, v2
	v_fma_f32 v0, v3, v0, v3
	v_mul_f32_e32 v12, 0xc0135761, v12
	v_mul_f32_e32 v0, 0xc0135761, v0
	v_exp_f32_e32 v12, v12
	v_exp_f32_e32 v0, v0
	v_add_f32_e32 v12, 1.0, v12
	v_add_f32_e32 v0, 1.0, v0
	v_rcp_f32_e32 v12, v12
	v_rcp_f32_e32 v13, v0
	v_add_u32_e32 v0, 0xb0, v193
	v_mul_f32_e32 v2, v2, v12
	v_mul_f32_e32 v3, v3, v13
	s_nop 0
	v_mul_f32_e32 v12, v4, v2
	v_mul_f32_e32 v13, v5, v3
	v_cvt_pk_bf16_f32 v4, v10, v11
	v_mad_i64_i32 v[10:11], s[36:37], v0, s2, v[34:35]
	v_cvt_pk_bf16_f32 v2, v18, v19
	v_cvt_pk_bf16_f32 v3, v20, v21
	v_cvt_pk_bf16_f32 v5, v12, v13
	v_lshl_add_u64 v[10:11], v[10:11], 0, v[148:149]
	global_store_dwordx4 v[10:11], v[2:5], off
	s_and_saveexec_b64 s[36:37], vcc
	s_cbranch_execz .LBB0_372
	v_lshl_add_u64 v[10:11], v[146:147], 0, s[40:41]
	v_cvt_pk_bf16_f32 v5, v6, v7
	v_mov_b64_e32 v[6:7], s[42:43]
	v_mad_u64_u32 v[6:7], s[38:39], v10, s2, v[6:7]
	v_mad_i32_i24 v7, v11, s2, v7
	v_cvt_pk_bf16_f32 v2, v14, v15
	v_cvt_pk_bf16_f32 v3, v16, v17
	v_cvt_pk_bf16_f32 v4, v8, v9
	v_lshl_add_u64 v[6:7], v[182:183], 1, v[6:7]
	global_store_dwordx4 v[6:7], v[2:5], off

.LBB0_404:
	s_mov_b32 s0, -1
	s_add_u32 s14, s74, 0x2200000
	s_waitcnt vmcnt(0)
	s_barrier
	s_addc_u32 s15, s75, 0
	v_mbcnt_lo_u32_b32 v0, s0, 0
	v_mbcnt_hi_u32_b32 v166, s0, v0
	s_lshl_b32 s0, s88, 8
	v_and_b32_e32 v130, 15, v166
	s_add_i32 s17, s0, s63
	v_or_b32_e32 v156, s17, v130
	s_ashr_i32 s17, s16, 31
	s_lshl_b32 s1, s62, 5
	s_lshl_b64 s[16:17], s[16:17], 8
	v_lshrrev_b32_e32 v0, 1, v166
	s_or_b32 s16, s16, s1
	v_and_b32_e32 v0, 56, v0
	v_and_b32_e32 v131, 64, v231
	v_lshl_add_u64 v[154:155], s[16:17], 0, v[0:1]
	v_xor_b32_e32 v0, 16, v231
	v_add_u32_e32 v131, 64, v131
	v_cmp_lt_i32_e32 vcc, v0, v131
	v_lshlrev_b64 v[178:179], 1, v[154:155]
	s_mov_b64 s[16:17], 0x8800000
	v_cndmask_b32_e32 v0, v231, v0, vcc
	v_lshlrev_b32_e32 v168, 2, v0
	v_xor_b32_e32 v0, 32, v231
	v_cmp_lt_i32_e32 vcc, v0, v131
	v_ashrrev_i32_e32 v157, 31, v156
	v_lshlrev_b64 v[180:181], 11, v[156:157]
	v_cndmask_b32_e32 v0, v231, v0, vcc
	v_lshlrev_b32_e32 v167, 2, v0
	v_or_b32_e32 v0, s63, v130
	v_lshl_add_u64 v[130:131], s[74:75], 0, v[178:179]
	v_lshl_add_u64 v[158:159], v[130:131], 0, s[16:17]
	v_lshl_add_u64 v[130:131], v[158:159], 0, v[180:181]
	global_load_dwordx4 v[170:173], v[130:131], off
	global_load_dwordx4 v[174:177], v[130:131], off offset:256
	v_or_b32_e32 v130, 16, v156
	v_ashrrev_i32_e32 v131, 31, v130
	v_lshlrev_b64 v[164:165], 11, v[130:131]
	v_lshl_add_u64 v[130:131], v[158:159], 0, v[164:165]
	global_load_dwordx4 v[150:153], v[130:131], off
	global_load_dwordx4 v[146:149], v[130:131], off offset:256
	v_or_b32_e32 v130, 32, v156
	v_ashrrev_i32_e32 v131, 31, v130
	v_lshlrev_b64 v[162:163], 11, v[130:131]
	v_lshl_add_u64 v[130:131], v[158:159], 0, v[162:163]
	global_load_dwordx4 v[142:145], v[130:131], off
	global_load_dwordx4 v[138:141], v[130:131], off offset:256
	v_or_b32_e32 v130, 48, v156
	v_ashrrev_i32_e32 v131, 31, v130
	v_lshlrev_b64 v[160:161], 11, v[130:131]
	v_lshl_add_u64 v[130:131], v[158:159], 0, v[160:161]
	global_load_dwordx4 v[134:137], v[130:131], off
	s_nop 0
	global_load_dwordx4 v[130:133], v[130:131], off offset:256
	v_lshl_add_u64 v[180:181], s[14:15], 0, v[180:181]
	v_lshl_add_u64 v[178:179], v[180:181], 0, v[178:179]
	v_cmp_gt_u32_e32 vcc, 16, v166
	s_lshl_b32 s1, s62, 2
	s_waitcnt vmcnt(0)
	v_lshlrev_b32_e32 v182, 16, v170
	v_and_b32_e32 v183, 0xffff0000, v170
	v_lshlrev_b32_e32 v170, 16, v171
	v_and_b32_e32 v171, 0xffff0000, v171
	v_add_f32_e32 v128, v128, v170
	v_add_f32_e32 v129, v129, v171
	v_lshlrev_b32_e32 v170, 16, v172
	v_and_b32_e32 v171, 0xffff0000, v172
	v_add_f32_e32 v170, v122, v170
	v_add_f32_e32 v171, v123, v171
	v_lshlrev_b32_e32 v122, 16, v173
	v_and_b32_e32 v123, 0xffff0000, v173
	v_add_f32_e32 v126, v126, v182
	v_add_f32_e32 v127, v127, v183
	v_add_f32_e32 v172, v124, v122
	v_add_f32_e32 v173, v125, v123
	v_cvt_pk_bf16_f32 v122, v126, v127
	v_cvt_pk_bf16_f32 v123, v128, v129
	v_cvt_pk_bf16_f32 v124, v170, v171
	v_cvt_pk_bf16_f32 v125, v172, v173
	global_store_dwordx4 v[178:179], v[122:125], off
	s_nop 1
	v_mul_f32_e32 v122, v126, v126
	v_mul_f32_e32 v123, v127, v127
	v_mul_f32_e32 v126, v170, v170
	v_mul_f32_e32 v127, v171, v171
	v_lshlrev_b32_e32 v170, 16, v174
	v_and_b32_e32 v171, 0xffff0000, v174
	v_add_f32_e32 v118, v118, v170
	v_add_f32_e32 v119, v119, v171
	v_lshlrev_b32_e32 v170, 16, v175
	v_and_b32_e32 v171, 0xffff0000, v175
	v_add_f32_e32 v120, v120, v170
	v_add_f32_e32 v121, v121, v171
	v_lshlrev_b32_e32 v170, 16, v176
	v_and_b32_e32 v171, 0xffff0000, v176
	v_add_f32_e32 v170, v114, v170
	v_add_f32_e32 v171, v115, v171
	v_lshlrev_b32_e32 v114, 16, v177
	v_and_b32_e32 v115, 0xffff0000, v177
	v_mul_f32_e32 v124, v128, v128
	v_mul_f32_e32 v125, v129, v129
	v_mul_f32_e32 v128, v172, v172
	v_mul_f32_e32 v129, v173, v173
	v_add_f32_e32 v172, v116, v114
	v_add_f32_e32 v173, v117, v115
	v_cvt_pk_bf16_f32 v114, v118, v119
	v_cvt_pk_bf16_f32 v115, v120, v121
	v_cvt_pk_bf16_f32 v116, v170, v171
	v_cvt_pk_bf16_f32 v117, v172, v173
	global_store_dwordx4 v[178:179], v[114:117], off offset:256
	s_nop 1
	v_mul_f32_e32 v114, v118, v118
	v_mul_f32_e32 v115, v119, v119
	v_mul_f32_e32 v116, v120, v120
	v_mul_f32_e32 v117, v121, v121
	v_add_f32_e32 v114, v114, v115
	v_add_f32_e32 v116, v116, v117
	v_mul_f32_e32 v118, v170, v170
	v_mul_f32_e32 v119, v171, v171
	v_mul_f32_e32 v120, v172, v172
	v_mul_f32_e32 v121, v173, v173
	v_add_f32_e32 v114, v114, v116
	v_add_f32_e32 v115, v128, v129
	v_add_f32_e32 v116, v126, v127
	v_add_f32_e32 v120, v120, v121
	v_add_f32_e32 v118, v118, v119
	v_add_f32_e32 v115, v116, v115
	v_add_f32_e32 v116, v124, v125
	v_add_f32_e32 v117, v122, v123
	v_add_f32_e32 v118, v118, v120
	v_add_f32_e32 v116, v117, v116
	v_add_f32_e32 v114, v114, v118
	v_add_f32_e32 v115, v116, v115
	v_add_f32_e32 v114, v115, v114
	ds_bpermute_b32 v115, v168, v114
	s_waitcnt lgkmcnt(0)
	v_add_f32_e32 v114, v114, v115
	ds_bpermute_b32 v115, v167, v114
	s_and_saveexec_b64 s[16:17], vcc
	s_cbranch_execz .LBB0_406
	v_lshl_or_b32 v116, v0, 4, s1
	s_waitcnt lgkmcnt(0)
	v_add_f32_e32 v114, v114, v115
	ds_write_b32 v116, v114
.LBB0_406:
	s_or_b64 exec, exec, s[16:17]
	v_lshlrev_b32_e32 v114, 16, v150
	s_waitcnt lgkmcnt(0)
	v_and_b32_e32 v115, 0xffff0000, v150
	v_add_f32_e32 v110, v110, v114
	v_add_f32_e32 v111, v111, v115
	v_lshlrev_b32_e32 v114, 16, v151
	v_and_b32_e32 v115, 0xffff0000, v151
	v_add_f32_e32 v112, v112, v114
	v_add_f32_e32 v113, v113, v115
	v_lshlrev_b32_e32 v114, 16, v152
	v_and_b32_e32 v115, 0xffff0000, v152
	v_add_f32_e32 v114, v106, v114
	v_add_f32_e32 v115, v107, v115
	v_lshlrev_b32_e32 v106, 16, v153
	v_and_b32_e32 v107, 0xffff0000, v153
	v_add_f32_e32 v116, v108, v106
	v_add_f32_e32 v117, v109, v107
	v_lshl_add_u64 v[118:119], s[14:15], 0, v[164:165]
	v_cvt_pk_bf16_f32 v106, v110, v111
	v_cvt_pk_bf16_f32 v107, v112, v113
	v_cvt_pk_bf16_f32 v108, v114, v115
	v_cvt_pk_bf16_f32 v109, v116, v117
	v_lshl_add_u64 v[118:119], v[154:155], 1, v[118:119]
	global_store_dwordx4 v[118:119], v[106:109], off
	s_nop 1
	v_mul_f32_e32 v106, v110, v110
	v_mul_f32_e32 v107, v111, v111
	v_mul_f32_e32 v110, v114, v114
	v_mul_f32_e32 v111, v115, v115
	v_lshlrev_b32_e32 v114, 16, v146
	v_and_b32_e32 v115, 0xffff0000, v146
	v_add_f32_e32 v102, v102, v114
	v_add_f32_e32 v103, v103, v115
	v_lshlrev_b32_e32 v114, 16, v147
	v_and_b32_e32 v115, 0xffff0000, v147
	v_add_f32_e32 v104, v104, v114
	v_add_f32_e32 v105, v105, v115
	v_lshlrev_b32_e32 v114, 16, v148
	v_and_b32_e32 v115, 0xffff0000, v148
	v_add_f32_e32 v114, v98, v114
	v_add_f32_e32 v115, v99, v115
	v_lshlrev_b32_e32 v98, 16, v149
	v_and_b32_e32 v99, 0xffff0000, v149
	v_mul_f32_e32 v108, v112, v112
	v_mul_f32_e32 v109, v113, v113
	v_mul_f32_e32 v112, v116, v116
	v_mul_f32_e32 v113, v117, v117
	v_add_f32_e32 v116, v100, v98
	v_add_f32_e32 v117, v101, v99
	v_cvt_pk_bf16_f32 v98, v102, v103
	v_cvt_pk_bf16_f32 v99, v104, v105
	v_cvt_pk_bf16_f32 v100, v114, v115
	v_cvt_pk_bf16_f32 v101, v116, v117
	global_store_dwordx4 v[118:119], v[98:101], off offset:256
	s_nop 1
	v_mul_f32_e32 v98, v102, v102
	v_mul_f32_e32 v99, v103, v103
	v_mul_f32_e32 v100, v104, v104
	v_mul_f32_e32 v101, v105, v105
	v_add_f32_e32 v98, v98, v99
	v_add_f32_e32 v100, v100, v101
	v_mul_f32_e32 v102, v114, v114
	v_mul_f32_e32 v103, v115, v115
	v_mul_f32_e32 v104, v116, v116
	v_mul_f32_e32 v105, v117, v117
	v_add_f32_e32 v98, v98, v100
	v_add_f32_e32 v99, v112, v113
	v_add_f32_e32 v100, v110, v111
	v_add_f32_e32 v104, v104, v105
	v_add_f32_e32 v102, v102, v103
	v_add_f32_e32 v99, v100, v99
	v_add_f32_e32 v100, v108, v109
	v_add_f32_e32 v101, v106, v107
	v_add_f32_e32 v102, v102, v104
	v_add_f32_e32 v100, v101, v100
	v_add_f32_e32 v98, v98, v102
	v_add_f32_e32 v99, v100, v99
	v_add_f32_e32 v98, v99, v98
	ds_bpermute_b32 v99, v168, v98
	s_waitcnt lgkmcnt(0)
	v_add_f32_e32 v98, v98, v99
	ds_bpermute_b32 v99, v167, v98
	s_and_saveexec_b64 s[16:17], vcc
	s_mov_b32 s89, 0x2e8ba2e9
	s_mov_b32 s29, 0x47800000
	s_cbranch_execz .LBB0_408
	v_lshl_or_b32 v100, v0, 4, s1
	s_waitcnt lgkmcnt(0)
	v_add_f32_e32 v98, v98, v99
	ds_write_b32 v100, v98 offset:256
.LBB0_408:
	s_or_b64 exec, exec, s[16:17]
	v_lshlrev_b32_e32 v98, 16, v142
	s_waitcnt lgkmcnt(0)
	v_and_b32_e32 v99, 0xffff0000, v142
	v_add_f32_e32 v94, v94, v98
	v_add_f32_e32 v95, v95, v99
	v_lshlrev_b32_e32 v98, 16, v143
	v_and_b32_e32 v99, 0xffff0000, v143
	v_add_f32_e32 v96, v96, v98
	v_add_f32_e32 v97, v97, v99
	v_lshlrev_b32_e32 v98, 16, v144
	v_and_b32_e32 v99, 0xffff0000, v144
	v_add_f32_e32 v98, v90, v98
	v_add_f32_e32 v99, v91, v99
	v_lshlrev_b32_e32 v90, 16, v145
	v_and_b32_e32 v91, 0xffff0000, v145
	v_add_f32_e32 v100, v92, v90
	v_add_f32_e32 v101, v93, v91
	v_lshl_add_u64 v[102:103], s[14:15], 0, v[162:163]
	v_cvt_pk_bf16_f32 v90, v94, v95
	v_cvt_pk_bf16_f32 v91, v96, v97
	v_cvt_pk_bf16_f32 v92, v98, v99
	v_cvt_pk_bf16_f32 v93, v100, v101
	v_lshl_add_u64 v[102:103], v[154:155], 1, v[102:103]
	global_store_dwordx4 v[102:103], v[90:93], off
	s_nop 1
	v_mul_f32_e32 v90, v94, v94
	v_mul_f32_e32 v91, v95, v95
	v_mul_f32_e32 v94, v98, v98
	v_mul_f32_e32 v95, v99, v99
	v_lshlrev_b32_e32 v98, 16, v138
	v_and_b32_e32 v99, 0xffff0000, v138
	v_add_f32_e32 v86, v86, v98
	v_add_f32_e32 v87, v87, v99
	v_lshlrev_b32_e32 v98, 16, v139
	v_and_b32_e32 v99, 0xffff0000, v139
	v_add_f32_e32 v88, v88, v98
	v_add_f32_e32 v89, v89, v99
	v_lshlrev_b32_e32 v98, 16, v140
	v_and_b32_e32 v99, 0xffff0000, v140
	v_add_f32_e32 v98, v82, v98
	v_add_f32_e32 v99, v83, v99
	v_lshlrev_b32_e32 v82, 16, v141
	v_and_b32_e32 v83, 0xffff0000, v141
	v_mul_f32_e32 v92, v96, v96
	v_mul_f32_e32 v93, v97, v97
	v_mul_f32_e32 v96, v100, v100
	v_mul_f32_e32 v97, v101, v101
	v_add_f32_e32 v100, v84, v82
	v_add_f32_e32 v101, v85, v83
	v_cvt_pk_bf16_f32 v82, v86, v87
	v_cvt_pk_bf16_f32 v83, v88, v89
	v_cvt_pk_bf16_f32 v84, v98, v99
	v_cvt_pk_bf16_f32 v85, v100, v101
	global_store_dwordx4 v[102:103], v[82:85], off offset:256
	s_nop 1
	v_mul_f32_e32 v82, v86, v86
	v_mul_f32_e32 v83, v87, v87
	v_mul_f32_e32 v84, v88, v88
	v_mul_f32_e32 v85, v89, v89
	v_add_f32_e32 v82, v82, v83
	v_add_f32_e32 v84, v84, v85
	v_mul_f32_e32 v86, v98, v98
	v_mul_f32_e32 v87, v99, v99
	v_mul_f32_e32 v88, v100, v100
	v_mul_f32_e32 v89, v101, v101
	v_add_f32_e32 v82, v82, v84
	v_add_f32_e32 v83, v96, v97
	v_add_f32_e32 v84, v94, v95
	v_add_f32_e32 v88, v88, v89
	v_add_f32_e32 v86, v86, v87
	v_add_f32_e32 v83, v84, v83
	v_add_f32_e32 v84, v92, v93
	v_add_f32_e32 v85, v90, v91
	v_add_f32_e32 v86, v86, v88
	v_add_f32_e32 v84, v85, v84
	v_add_f32_e32 v82, v82, v86
	v_add_f32_e32 v83, v84, v83
	v_add_f32_e32 v82, v83, v82
	ds_bpermute_b32 v83, v168, v82
	s_waitcnt lgkmcnt(0)
	v_add_f32_e32 v82, v82, v83
	ds_bpermute_b32 v83, v167, v82
	s_and_saveexec_b64 s[16:17], vcc
	s_cbranch_execz .LBB0_410
	v_lshl_or_b32 v84, v0, 4, s1
	s_waitcnt lgkmcnt(0)
	v_add_f32_e32 v82, v82, v83
	ds_write_b32 v84, v82 offset:512
.LBB0_410:
	s_or_b64 exec, exec, s[16:17]
	v_lshlrev_b32_e32 v82, 16, v134
	s_waitcnt lgkmcnt(0)
	v_and_b32_e32 v83, 0xffff0000, v134
	v_add_f32_e32 v78, v78, v82
	v_add_f32_e32 v79, v79, v83
	v_lshlrev_b32_e32 v82, 16, v135
	v_and_b32_e32 v83, 0xffff0000, v135
	v_add_f32_e32 v80, v80, v82
	v_add_f32_e32 v81, v81, v83
	v_lshlrev_b32_e32 v82, 16, v136
	v_and_b32_e32 v83, 0xffff0000, v136
	v_add_f32_e32 v82, v74, v82
	v_add_f32_e32 v83, v75, v83
	v_lshlrev_b32_e32 v74, 16, v137
	v_and_b32_e32 v75, 0xffff0000, v137
	v_add_f32_e32 v84, v76, v74
	v_add_f32_e32 v85, v77, v75
	v_lshl_add_u64 v[86:87], s[14:15], 0, v[160:161]
	v_cvt_pk_bf16_f32 v74, v78, v79
	v_cvt_pk_bf16_f32 v75, v80, v81
	v_cvt_pk_bf16_f32 v76, v82, v83
	v_cvt_pk_bf16_f32 v77, v84, v85
	v_lshl_add_u64 v[86:87], v[154:155], 1, v[86:87]
	global_store_dwordx4 v[86:87], v[74:77], off
	s_nop 1
	v_mul_f32_e32 v74, v78, v78
	v_mul_f32_e32 v75, v79, v79
	v_mul_f32_e32 v78, v82, v82
	v_mul_f32_e32 v79, v83, v83
	v_lshlrev_b32_e32 v82, 16, v130
	v_and_b32_e32 v83, 0xffff0000, v130
	v_add_f32_e32 v70, v70, v82
	v_add_f32_e32 v71, v71, v83
	v_lshlrev_b32_e32 v82, 16, v131
	v_and_b32_e32 v83, 0xffff0000, v131
	v_add_f32_e32 v72, v72, v82
	v_add_f32_e32 v73, v73, v83
	v_lshlrev_b32_e32 v82, 16, v132
	v_and_b32_e32 v83, 0xffff0000, v132
	v_add_f32_e32 v82, v66, v82
	v_add_f32_e32 v83, v67, v83
	v_lshlrev_b32_e32 v66, 16, v133
	v_and_b32_e32 v67, 0xffff0000, v133
	v_mul_f32_e32 v76, v80, v80
	v_mul_f32_e32 v77, v81, v81
	v_mul_f32_e32 v80, v84, v84
	v_mul_f32_e32 v81, v85, v85
	v_add_f32_e32 v84, v68, v66
	v_add_f32_e32 v85, v69, v67
	v_cvt_pk_bf16_f32 v66, v70, v71
	v_cvt_pk_bf16_f32 v67, v72, v73
	v_cvt_pk_bf16_f32 v68, v82, v83
	v_cvt_pk_bf16_f32 v69, v84, v85
	global_store_dwordx4 v[86:87], v[66:69], off offset:256
	s_nop 1
	v_mul_f32_e32 v66, v70, v70
	v_mul_f32_e32 v67, v71, v71
	v_mul_f32_e32 v68, v72, v72
	v_mul_f32_e32 v69, v73, v73
	v_add_f32_e32 v66, v66, v67
	v_add_f32_e32 v68, v68, v69
	v_mul_f32_e32 v70, v82, v82
	v_mul_f32_e32 v71, v83, v83
	v_mul_f32_e32 v72, v84, v84
	v_mul_f32_e32 v73, v85, v85
	v_add_f32_e32 v66, v66, v68
	v_add_f32_e32 v67, v80, v81
	v_add_f32_e32 v68, v78, v79
	v_add_f32_e32 v72, v72, v73
	v_add_f32_e32 v70, v70, v71
	v_add_f32_e32 v67, v68, v67
	v_add_f32_e32 v68, v76, v77
	v_add_f32_e32 v69, v74, v75
	v_add_f32_e32 v70, v70, v72
	v_add_f32_e32 v68, v69, v68
	v_add_f32_e32 v66, v66, v70
	v_add_f32_e32 v67, v68, v67
	v_add_f32_e32 v66, v67, v66
	ds_bpermute_b32 v67, v168, v66
	s_waitcnt lgkmcnt(0)
	v_add_f32_e32 v66, v66, v67
	ds_bpermute_b32 v67, v167, v66
	s_and_saveexec_b64 s[16:17], vcc
	s_cbranch_execz .LBB0_412
	v_lshl_or_b32 v68, v0, 4, s1
	s_waitcnt lgkmcnt(0)
	v_add_f32_e32 v66, v66, v67
	ds_write_b32 v68, v66 offset:768
.LBB0_412:
	s_or_b64 exec, exec, s[16:17]
	s_waitcnt lgkmcnt(0)
	v_lshlrev_b64 v[66:67], 11, v[156:157]
	v_lshl_add_u64 v[104:105], v[66:67], 0, s[20:21]
	v_lshl_add_u64 v[68:69], v[158:159], 0, v[104:105]
	global_load_dwordx4 v[96:99], v[68:69], off
	global_load_dwordx4 v[100:103], v[68:69], off offset:256
	s_mov_b64 s[16:17], 0x48000
	v_lshl_add_u64 v[94:95], v[66:67], 0, s[16:17]
	s_mov_b64 s[16:17], 0x58000
	v_lshl_add_u64 v[68:69], v[158:159], 0, v[94:95]
	v_lshl_add_u64 v[92:93], v[66:67], 0, s[22:23]
	v_lshl_add_u64 v[90:91], v[66:67], 0, s[16:17]
	global_load_dwordx4 v[86:89], v[68:69], off
	global_load_dwordx4 v[82:85], v[68:69], off offset:256
	v_lshl_add_u64 v[68:69], v[158:159], 0, v[92:93]
	v_lshl_add_u64 v[66:67], v[158:159], 0, v[90:91]
	global_load_dwordx4 v[78:81], v[68:69], off
	global_load_dwordx4 v[74:77], v[68:69], off offset:256
	global_load_dwordx4 v[70:73], v[66:67], off
	s_nop 0
	global_load_dwordx4 v[66:69], v[66:67], off offset:256
	v_lshl_add_u64 v[104:105], s[14:15], 0, v[104:105]
	v_lshl_add_u64 v[104:105], v[154:155], 1, v[104:105]
	s_waitcnt vmcnt(7)
	v_lshlrev_b32_e32 v106, 16, v96
	v_and_b32_e32 v107, 0xffff0000, v96
	v_lshlrev_b32_e32 v96, 16, v97
	v_and_b32_e32 v97, 0xffff0000, v97
	v_add_f32_e32 v64, v64, v96
	v_add_f32_e32 v65, v65, v97
	v_lshlrev_b32_e32 v96, 16, v98
	v_and_b32_e32 v97, 0xffff0000, v98
	v_add_f32_e32 v96, v58, v96
	v_add_f32_e32 v97, v59, v97
	v_lshlrev_b32_e32 v58, 16, v99
	v_and_b32_e32 v59, 0xffff0000, v99
	v_add_f32_e32 v62, v62, v106
	v_add_f32_e32 v63, v63, v107
	v_add_f32_e32 v98, v60, v58
	v_add_f32_e32 v99, v61, v59
	v_cvt_pk_bf16_f32 v58, v62, v63
	v_cvt_pk_bf16_f32 v59, v64, v65
	v_cvt_pk_bf16_f32 v60, v96, v97
	v_cvt_pk_bf16_f32 v61, v98, v99
	global_store_dwordx4 v[104:105], v[58:61], off
	s_nop 1
	v_mul_f32_e32 v58, v62, v62
	v_mul_f32_e32 v59, v63, v63
	v_mul_f32_e32 v62, v96, v96
	v_mul_f32_e32 v63, v97, v97
	s_waitcnt vmcnt(7)
	v_lshlrev_b32_e32 v96, 16, v100
	v_and_b32_e32 v97, 0xffff0000, v100
	v_add_f32_e32 v54, v54, v96
	v_add_f32_e32 v55, v55, v97
	v_lshlrev_b32_e32 v96, 16, v101
	v_and_b32_e32 v97, 0xffff0000, v101
	v_add_f32_e32 v56, v56, v96
	v_add_f32_e32 v57, v57, v97
	v_lshlrev_b32_e32 v96, 16, v102
	v_and_b32_e32 v97, 0xffff0000, v102
	v_add_f32_e32 v96, v50, v96
	v_add_f32_e32 v97, v51, v97
	v_lshlrev_b32_e32 v50, 16, v103
	v_and_b32_e32 v51, 0xffff0000, v103
	v_mul_f32_e32 v60, v64, v64
	v_mul_f32_e32 v61, v65, v65
	v_mul_f32_e32 v64, v98, v98
	v_mul_f32_e32 v65, v99, v99
	v_add_f32_e32 v98, v52, v50
	v_add_f32_e32 v99, v53, v51
	v_cvt_pk_bf16_f32 v50, v54, v55
	v_cvt_pk_bf16_f32 v51, v56, v57
	v_cvt_pk_bf16_f32 v52, v96, v97
	v_cvt_pk_bf16_f32 v53, v98, v99
	global_store_dwordx4 v[104:105], v[50:53], off offset:256
	s_nop 1
	v_mul_f32_e32 v50, v54, v54
	v_mul_f32_e32 v51, v55, v55
	v_mul_f32_e32 v52, v56, v56
	v_mul_f32_e32 v53, v57, v57
	v_add_f32_e32 v50, v50, v51
	v_add_f32_e32 v52, v52, v53
	v_mul_f32_e32 v54, v96, v96
	v_mul_f32_e32 v55, v97, v97
	v_mul_f32_e32 v56, v98, v98
	v_mul_f32_e32 v57, v99, v99
	v_add_f32_e32 v50, v50, v52
	v_add_f32_e32 v51, v64, v65
	v_add_f32_e32 v52, v62, v63
	v_add_f32_e32 v56, v56, v57
	v_add_f32_e32 v54, v54, v55
	v_add_f32_e32 v51, v52, v51
	v_add_f32_e32 v52, v60, v61
	v_add_f32_e32 v53, v58, v59
	v_add_f32_e32 v54, v54, v56
	v_add_f32_e32 v52, v53, v52
	v_add_f32_e32 v50, v50, v54
	v_add_f32_e32 v51, v52, v51
	v_add_f32_e32 v50, v51, v50
	ds_bpermute_b32 v51, v168, v50
	s_waitcnt lgkmcnt(0)
	v_add_f32_e32 v50, v50, v51
	ds_bpermute_b32 v51, v167, v50
	s_and_saveexec_b64 s[16:17], vcc
	s_cbranch_execz .LBB0_414
	v_lshl_or_b32 v52, v0, 4, s1
	s_waitcnt lgkmcnt(0)
	v_add_f32_e32 v50, v50, v51
	ds_write_b32 v52, v50 offset:2048
.LBB0_414:
	s_or_b64 exec, exec, s[16:17]
	s_waitcnt vmcnt(7)
	v_lshlrev_b32_e32 v50, 16, v86
	s_waitcnt lgkmcnt(0)
	v_and_b32_e32 v51, 0xffff0000, v86
	v_add_f32_e32 v46, v46, v50
	v_add_f32_e32 v47, v47, v51
	v_lshlrev_b32_e32 v50, 16, v87
	v_and_b32_e32 v51, 0xffff0000, v87
	v_add_f32_e32 v48, v48, v50
	v_add_f32_e32 v49, v49, v51
	v_lshlrev_b32_e32 v50, 16, v88
	v_and_b32_e32 v51, 0xffff0000, v88
	v_add_f32_e32 v50, v42, v50
	v_add_f32_e32 v51, v43, v51
	v_lshlrev_b32_e32 v42, 16, v89
	v_and_b32_e32 v43, 0xffff0000, v89
	v_add_f32_e32 v52, v44, v42
	v_add_f32_e32 v53, v45, v43
	v_lshl_add_u64 v[54:55], s[14:15], 0, v[94:95]
	v_cvt_pk_bf16_f32 v42, v46, v47
	v_cvt_pk_bf16_f32 v43, v48, v49
	v_cvt_pk_bf16_f32 v44, v50, v51
	v_cvt_pk_bf16_f32 v45, v52, v53
	v_lshl_add_u64 v[54:55], v[154:155], 1, v[54:55]
	global_store_dwordx4 v[54:55], v[42:45], off
	s_nop 1
	v_mul_f32_e32 v42, v46, v46
	v_mul_f32_e32 v43, v47, v47
	v_mul_f32_e32 v46, v50, v50
	v_mul_f32_e32 v47, v51, v51
	s_waitcnt vmcnt(7)
	v_lshlrev_b32_e32 v50, 16, v82
	v_and_b32_e32 v51, 0xffff0000, v82
	v_add_f32_e32 v38, v38, v50
	v_add_f32_e32 v39, v39, v51
	v_lshlrev_b32_e32 v50, 16, v83
	v_and_b32_e32 v51, 0xffff0000, v83
	v_add_f32_e32 v40, v40, v50
	v_add_f32_e32 v41, v41, v51
	v_lshlrev_b32_e32 v50, 16, v84
	v_and_b32_e32 v51, 0xffff0000, v84
	v_add_f32_e32 v50, v34, v50
	v_add_f32_e32 v51, v35, v51
	v_lshlrev_b32_e32 v34, 16, v85
	v_and_b32_e32 v35, 0xffff0000, v85
	v_mul_f32_e32 v44, v48, v48
	v_mul_f32_e32 v45, v49, v49
	v_mul_f32_e32 v48, v52, v52
	v_mul_f32_e32 v49, v53, v53
	v_add_f32_e32 v52, v36, v34
	v_add_f32_e32 v53, v37, v35
	v_cvt_pk_bf16_f32 v34, v38, v39
	v_cvt_pk_bf16_f32 v35, v40, v41
	v_cvt_pk_bf16_f32 v36, v50, v51
	v_cvt_pk_bf16_f32 v37, v52, v53
	global_store_dwordx4 v[54:55], v[34:37], off offset:256
	s_nop 1
	v_mul_f32_e32 v34, v38, v38
	v_mul_f32_e32 v35, v39, v39
	v_mul_f32_e32 v36, v40, v40
	v_mul_f32_e32 v37, v41, v41
	v_add_f32_e32 v34, v34, v35
	v_add_f32_e32 v36, v36, v37
	v_mul_f32_e32 v38, v50, v50
	v_mul_f32_e32 v39, v51, v51
	v_mul_f32_e32 v40, v52, v52
	v_mul_f32_e32 v41, v53, v53
	v_add_f32_e32 v34, v34, v36
	v_add_f32_e32 v35, v48, v49
	v_add_f32_e32 v36, v46, v47
	v_add_f32_e32 v40, v40, v41
	v_add_f32_e32 v38, v38, v39
	v_add_f32_e32 v35, v36, v35
	v_add_f32_e32 v36, v44, v45
	v_add_f32_e32 v37, v42, v43
	v_add_f32_e32 v38, v38, v40
	v_add_f32_e32 v36, v37, v36
	v_add_f32_e32 v34, v34, v38
	v_add_f32_e32 v35, v36, v35
	v_add_f32_e32 v34, v35, v34
	ds_bpermute_b32 v35, v168, v34
	s_waitcnt lgkmcnt(0)
	v_add_f32_e32 v34, v34, v35
	ds_bpermute_b32 v35, v167, v34
	s_and_saveexec_b64 s[16:17], vcc
	s_cbranch_execz .LBB0_416
	v_lshl_or_b32 v36, v0, 4, s1
	s_waitcnt lgkmcnt(0)
	v_add_f32_e32 v34, v34, v35
	ds_write_b32 v36, v34 offset:2304
.LBB0_416:
	s_or_b64 exec, exec, s[16:17]
	s_waitcnt vmcnt(7)
	v_lshlrev_b32_e32 v34, 16, v78
	s_waitcnt lgkmcnt(0)
	v_and_b32_e32 v35, 0xffff0000, v78
	v_add_f32_e32 v30, v30, v34
	v_add_f32_e32 v31, v31, v35
	v_lshlrev_b32_e32 v34, 16, v79
	v_and_b32_e32 v35, 0xffff0000, v79
	v_add_f32_e32 v32, v32, v34
	v_add_f32_e32 v33, v33, v35
	v_lshlrev_b32_e32 v34, 16, v80
	v_and_b32_e32 v35, 0xffff0000, v80
	v_add_f32_e32 v34, v26, v34
	v_add_f32_e32 v35, v27, v35
	v_lshlrev_b32_e32 v26, 16, v81
	v_and_b32_e32 v27, 0xffff0000, v81
	v_add_f32_e32 v36, v28, v26
	v_add_f32_e32 v37, v29, v27
	v_lshl_add_u64 v[38:39], s[14:15], 0, v[92:93]
	v_cvt_pk_bf16_f32 v26, v30, v31
	v_cvt_pk_bf16_f32 v27, v32, v33
	v_cvt_pk_bf16_f32 v28, v34, v35
	v_cvt_pk_bf16_f32 v29, v36, v37
	v_lshl_add_u64 v[38:39], v[154:155], 1, v[38:39]
	global_store_dwordx4 v[38:39], v[26:29], off
	s_nop 1
	v_mul_f32_e32 v26, v30, v30
	v_mul_f32_e32 v27, v31, v31
	v_mul_f32_e32 v30, v34, v34
	v_mul_f32_e32 v31, v35, v35
	s_waitcnt vmcnt(7)
	v_lshlrev_b32_e32 v34, 16, v74
	v_and_b32_e32 v35, 0xffff0000, v74
	v_add_f32_e32 v22, v22, v34
	v_add_f32_e32 v23, v23, v35
	v_lshlrev_b32_e32 v34, 16, v75
	v_and_b32_e32 v35, 0xffff0000, v75
	v_add_f32_e32 v24, v24, v34
	v_add_f32_e32 v25, v25, v35
	v_lshlrev_b32_e32 v34, 16, v76
	v_and_b32_e32 v35, 0xffff0000, v76
	v_add_f32_e32 v34, v18, v34
	v_add_f32_e32 v35, v19, v35
	v_lshlrev_b32_e32 v18, 16, v77
	v_and_b32_e32 v19, 0xffff0000, v77
	v_mul_f32_e32 v28, v32, v32
	v_mul_f32_e32 v29, v33, v33
	v_mul_f32_e32 v32, v36, v36
	v_mul_f32_e32 v33, v37, v37
	v_add_f32_e32 v36, v20, v18
	v_add_f32_e32 v37, v21, v19
	v_cvt_pk_bf16_f32 v18, v22, v23
	v_cvt_pk_bf16_f32 v19, v24, v25
	v_cvt_pk_bf16_f32 v20, v34, v35
	v_cvt_pk_bf16_f32 v21, v36, v37
	global_store_dwordx4 v[38:39], v[18:21], off offset:256
	s_nop 1
	v_mul_f32_e32 v18, v22, v22
	v_mul_f32_e32 v19, v23, v23
	v_mul_f32_e32 v20, v24, v24
	v_mul_f32_e32 v21, v25, v25
	v_add_f32_e32 v18, v18, v19
	v_add_f32_e32 v20, v20, v21
	v_mul_f32_e32 v22, v34, v34
	v_mul_f32_e32 v23, v35, v35
	v_mul_f32_e32 v24, v36, v36
	v_mul_f32_e32 v25, v37, v37
	v_add_f32_e32 v18, v18, v20
	v_add_f32_e32 v19, v32, v33
	v_add_f32_e32 v20, v30, v31
	v_add_f32_e32 v24, v24, v25
	v_add_f32_e32 v22, v22, v23
	v_add_f32_e32 v19, v20, v19
	v_add_f32_e32 v20, v28, v29
	v_add_f32_e32 v21, v26, v27
	v_add_f32_e32 v22, v22, v24
	v_add_f32_e32 v20, v21, v20
	v_add_f32_e32 v18, v18, v22
	v_add_f32_e32 v19, v20, v19
	v_add_f32_e32 v18, v19, v18
	ds_bpermute_b32 v19, v168, v18
	s_waitcnt lgkmcnt(0)
	v_add_f32_e32 v18, v18, v19
	ds_bpermute_b32 v19, v167, v18
	s_and_saveexec_b64 s[16:17], vcc
	s_cbranch_execz .LBB0_418
	v_lshl_or_b32 v20, v0, 4, s1
	s_waitcnt lgkmcnt(0)
	v_add_f32_e32 v18, v18, v19
	ds_write_b32 v20, v18 offset:2560
.LBB0_418:
	s_or_b64 exec, exec, s[16:17]
	s_waitcnt vmcnt(7)
	v_lshlrev_b32_e32 v18, 16, v70
	s_waitcnt lgkmcnt(0)
	v_and_b32_e32 v19, 0xffff0000, v70
	v_add_f32_e32 v14, v14, v18
	v_add_f32_e32 v15, v15, v19
	v_lshlrev_b32_e32 v18, 16, v71
	v_and_b32_e32 v19, 0xffff0000, v71
	v_add_f32_e32 v16, v16, v18
	v_add_f32_e32 v17, v17, v19
	v_lshlrev_b32_e32 v18, 16, v72
	v_and_b32_e32 v19, 0xffff0000, v72
	v_add_f32_e32 v18, v10, v18
	v_add_f32_e32 v19, v11, v19
	v_lshlrev_b32_e32 v10, 16, v73
	v_and_b32_e32 v11, 0xffff0000, v73
	v_add_f32_e32 v20, v12, v10
	v_add_f32_e32 v21, v13, v11
	v_lshl_add_u64 v[22:23], s[14:15], 0, v[90:91]
	v_cvt_pk_bf16_f32 v10, v14, v15
	v_cvt_pk_bf16_f32 v11, v16, v17
	v_cvt_pk_bf16_f32 v12, v18, v19
	v_cvt_pk_bf16_f32 v13, v20, v21
	v_lshl_add_u64 v[22:23], v[154:155], 1, v[22:23]
	global_store_dwordx4 v[22:23], v[10:13], off
	s_nop 1
	v_mul_f32_e32 v10, v14, v14
	v_mul_f32_e32 v11, v15, v15
	v_mul_f32_e32 v14, v18, v18
	v_mul_f32_e32 v15, v19, v19
	s_waitcnt vmcnt(7)
	v_lshlrev_b32_e32 v18, 16, v66
	v_and_b32_e32 v19, 0xffff0000, v66
	v_add_f32_e32 v6, v6, v18
	v_add_f32_e32 v7, v7, v19
	v_lshlrev_b32_e32 v18, 16, v67
	v_and_b32_e32 v19, 0xffff0000, v67
	v_add_f32_e32 v8, v8, v18
	v_add_f32_e32 v9, v9, v19
	v_lshlrev_b32_e32 v18, 16, v68
	v_and_b32_e32 v19, 0xffff0000, v68
	v_add_f32_e32 v18, v2, v18
	v_add_f32_e32 v19, v3, v19
	v_lshlrev_b32_e32 v2, 16, v69
	v_and_b32_e32 v3, 0xffff0000, v69
	v_mul_f32_e32 v12, v16, v16
	v_mul_f32_e32 v13, v17, v17
	v_mul_f32_e32 v16, v20, v20
	v_mul_f32_e32 v17, v21, v21
	v_add_f32_e32 v20, v4, v2
	v_add_f32_e32 v21, v5, v3
	v_cvt_pk_bf16_f32 v2, v6, v7
	v_cvt_pk_bf16_f32 v3, v8, v9
	v_cvt_pk_bf16_f32 v4, v18, v19
	v_cvt_pk_bf16_f32 v5, v20, v21
	global_store_dwordx4 v[22:23], v[2:5], off offset:256
	s_nop 1
	v_mul_f32_e32 v2, v6, v6
	v_mul_f32_e32 v3, v7, v7
	v_mul_f32_e32 v4, v8, v8
	v_mul_f32_e32 v5, v9, v9
	v_add_f32_e32 v2, v2, v3
	v_add_f32_e32 v4, v4, v5
	v_mul_f32_e32 v6, v18, v18
	v_mul_f32_e32 v7, v19, v19
	v_mul_f32_e32 v8, v20, v20
	v_mul_f32_e32 v9, v21, v21
	v_add_f32_e32 v2, v2, v4
	v_add_f32_e32 v3, v16, v17
	v_add_f32_e32 v4, v14, v15
	v_add_f32_e32 v8, v8, v9
	v_add_f32_e32 v6, v6, v7
	v_add_f32_e32 v3, v4, v3
	v_add_f32_e32 v4, v12, v13
	v_add_f32_e32 v5, v10, v11
	v_add_f32_e32 v6, v6, v8
	v_add_f32_e32 v4, v5, v4
	v_add_f32_e32 v2, v2, v6
	v_add_f32_e32 v3, v4, v3
	v_add_f32_e32 v2, v3, v2
	ds_bpermute_b32 v3, v168, v2
	s_waitcnt lgkmcnt(0)
	v_add_f32_e32 v2, v2, v3
	ds_bpermute_b32 v3, v167, v2
	s_and_saveexec_b64 s[14:15], vcc
	s_cbranch_execz .LBB0_420
	v_lshl_or_b32 v0, v0, 4, s1
	s_waitcnt lgkmcnt(0)
	v_add_f32_e32 v2, v2, v3
	ds_write_b32 v0, v2 offset:2816

.LBB0_446:
	s_waitcnt vmcnt(0)
	v_ffbh_u32_e32 v142, v151
	v_min_u32_e32 v144, 32, v142
	v_lshlrev_b64 v[142:143], v144, v[150:151]
	v_min_u32_e32 v142, 1, v142
	v_or_b32_e32 v142, v143, v142
	v_cvt_f32_u32_e32 v145, v142
	v_ffbh_u32_e32 v142, v147
	v_min_u32_e32 v148, 32, v142
	v_lshlrev_b64 v[142:143], v148, v[146:147]
	v_min_u32_e32 v142, 1, v142
	v_or_b32_e32 v142, v143, v142
	v_cvt_f32_u32_e32 v142, v142
	v_sub_u32_e32 v143, 32, v144
	v_sub_u32_e32 v144, 32, v148
	v_ldexp_f32 v143, v145, v143
	v_ldexp_f32 v142, v142, v144
	s_mov_b32 s16, 0x32800000
	v_fma_f32 v142, v142, s16, v196
	v_fma_f32 v143, v143, s16, v196
	s_mov_b32 s14, -1
	v_mul_f32_e32 v144, 0x4b800000, v143
	v_cmp_gt_f32_e32 vcc, s96, v143
	s_barrier
	s_lshl_b32 s16, s31, 2
	v_cndmask_b32_e32 v143, v143, v144, vcc
	v_rsq_f32_e32 v143, v143
	v_mbcnt_lo_u32_b32 v0, s14, 0
	v_mbcnt_hi_u32_b32 v0, s14, v0
	v_and_b32_e32 v193, 15, v0
	v_mul_f32_e32 v144, 0x45800000, v143
	v_cndmask_b32_e32 v144, v143, v144, vcc
	v_mul_f32_e32 v182, v128, v144
	v_mul_f32_e32 v183, v129, v144
	v_mul_f32_e32 v128, v114, v144
	v_mul_f32_e32 v129, v115, v144
	v_and_b32_e32 v115, 64, v231
	v_xor_b32_e32 v114, 16, v231
	v_add_u32_e32 v115, 64, v115
	v_cmp_lt_i32_e32 vcc, v114, v115
	v_mul_f32_e32 v124, v124, v144
	v_mul_f32_e32 v125, v125, v144
	v_mul_f32_e32 v188, v126, v144
	v_mul_f32_e32 v189, v127, v144
	v_cndmask_b32_e32 v114, v231, v114, vcc
	v_mul_f32_e32 v122, v122, v144
	v_mul_f32_e32 v123, v123, v144
	v_mul_f32_e32 v154, v116, v144
	v_mul_f32_e32 v155, v117, v144
	v_lshlrev_b32_e32 v194, 2, v114
	v_max_f32_e32 v114, v182, v183
	v_max_f32_e32 v116, v124, v125
	v_mul_f32_e32 v126, v120, v144
	v_mul_f32_e32 v127, v121, v144
	v_max3_f32 v114, v188, v189, v114
	v_max3_f32 v116, v122, v123, v116
	v_mul_f32_e32 v172, v118, v144
	v_mul_f32_e32 v173, v119, v144
	v_max3_f32 v114, v114, s6, v116
	v_max_f32_e32 v116, v126, v127
	v_max_f32_e32 v117, v154, v155
	v_max3_f32 v116, v172, v173, v116
	v_max3_f32 v117, v128, v129, v117
	v_max3_f32 v114, v114, v116, v117
	ds_bpermute_b32 v116, v194, v114
	v_xor_b32_e32 v117, 32, v231
	v_cmp_lt_i32_e32 vcc, v117, v115
	v_or_b32_e32 v200, s1, v193
	v_cmp_gt_f32_e64 s[36:37], s96, v142
	v_cndmask_b32_e32 v115, v231, v117, vcc
	v_lshlrev_b32_e32 v195, 2, v115
	s_waitcnt lgkmcnt(0)
	v_max_f32_e32 v115, v116, v116
	v_max_f32_e32 v114, v114, v115
	ds_bpermute_b32 v115, v195, v114
	v_cmp_gt_u32_e32 vcc, 16, v0
	v_lshl_or_b32 v116, v200, 4, s16
	s_and_saveexec_b64 s[14:15], vcc
	s_cbranch_execz .LBB0_448
	s_waitcnt lgkmcnt(0)
	v_max_f32_e32 v115, v115, v115
	v_max_f32_e32 v114, v114, v114
	v_max_f32_e32 v114, v114, v115
	ds_write_b32 v116, v114
.LBB0_448:
	s_or_b64 exec, exec, s[14:15]
	v_mul_f32_e32 v114, 0x4b800000, v142
	v_cndmask_b32_e64 v114, v142, v114, s[36:37]
	v_rsq_f32_e32 v114, v114
	s_waitcnt lgkmcnt(0)
	v_mul_f32_e32 v115, 0x45800000, v114
	v_cndmask_b32_e64 v114, v114, v115, s[36:37]
	v_mul_f32_e32 v180, v112, v114
	v_mul_f32_e32 v181, v113, v114
	v_mul_f32_e32 v108, v108, v114
	v_mul_f32_e32 v109, v109, v114
	v_mul_f32_e32 v186, v110, v114
	v_mul_f32_e32 v187, v111, v114
	v_mul_f32_e32 v178, v106, v114
	v_mul_f32_e32 v179, v107, v114
	v_mul_f32_e32 v106, v98, v114
	v_mul_f32_e32 v107, v99, v114
	v_max_f32_e32 v98, v180, v181
	v_max_f32_e32 v99, v108, v109
	v_mul_f32_e32 v104, v104, v114
	v_mul_f32_e32 v105, v105, v114
	v_mul_f32_e32 v168, v102, v114
	v_mul_f32_e32 v169, v103, v114
	v_mul_f32_e32 v102, v100, v114
	v_mul_f32_e32 v103, v101, v114
	v_max3_f32 v98, v186, v187, v98
	v_max3_f32 v99, v178, v179, v99
	v_max3_f32 v98, v98, s6, v99
	v_max_f32_e32 v99, v104, v105
	v_max_f32_e32 v100, v102, v103
	v_max3_f32 v99, v168, v169, v99
	v_max3_f32 v100, v106, v107, v100
	v_max3_f32 v98, v98, v99, v100
	ds_bpermute_b32 v99, v194, v98
	s_waitcnt lgkmcnt(0)
	v_max_f32_e32 v99, v99, v99
	v_max_f32_e32 v98, v98, v99
	ds_bpermute_b32 v99, v195, v98
	s_and_saveexec_b64 s[14:15], vcc
	s_cbranch_execz .LBB0_450
	s_waitcnt lgkmcnt(0)
	v_max_f32_e32 v99, v99, v99
	v_max_f32_e32 v98, v98, v98
	v_max_f32_e32 v98, v98, v99
	ds_write_b32 v116, v98 offset:256
.LBB0_450:
	s_or_b64 exec, exec, s[14:15]
	v_ffbh_u32_e32 v98, v141
	v_min_u32_e32 v100, 32, v98
	s_waitcnt lgkmcnt(0)
	v_lshlrev_b64 v[98:99], v100, v[140:141]
	v_min_u32_e32 v98, 1, v98
	v_or_b32_e32 v98, v99, v98
	v_cvt_f32_u32_e32 v101, v98
	v_ffbh_u32_e32 v98, v139
	v_min_u32_e32 v110, 32, v98
	v_lshlrev_b64 v[98:99], v110, v[138:139]
	v_min_u32_e32 v98, 1, v98
	v_or_b32_e32 v98, v99, v98
	v_cvt_f32_u32_e32 v98, v98
	v_sub_u32_e32 v99, 32, v100
	v_sub_u32_e32 v100, 32, v110
	v_ldexp_f32 v99, v101, v99
	v_ldexp_f32 v98, v98, v100
	s_mov_b32 s14, 0x32800000
	v_fma_f32 v98, v98, s14, v196
	v_fma_f32 v99, v99, s14, v196
	s_nop 0
	v_mul_f32_e32 v100, 0x4b800000, v99
	v_cmp_gt_f32_e64 s[36:37], s96, v99
	s_nop 1
	v_cndmask_b32_e64 v99, v99, v100, s[36:37]
	v_rsq_f32_e32 v99, v99
	s_nop 0
	v_mul_f32_e32 v100, 0x45800000, v99
	v_cndmask_b32_e64 v100, v99, v100, s[36:37]
	v_mul_f32_e32 v184, v96, v100
	v_mul_f32_e32 v185, v97, v100
	v_mul_f32_e32 v174, v92, v100
	v_mul_f32_e32 v175, v93, v100
	v_mul_f32_e32 v190, v94, v100
	v_mul_f32_e32 v191, v95, v100
	v_mul_f32_e32 v96, v90, v100
	v_mul_f32_e32 v97, v91, v100
	v_mul_f32_e32 v112, v74, v100
	v_mul_f32_e32 v113, v75, v100
	v_max_f32_e32 v74, v184, v185
	v_max_f32_e32 v75, v174, v175
	v_mul_f32_e32 v110, v84, v100
	v_mul_f32_e32 v111, v85, v100
	v_mul_f32_e32 v114, v76, v100
	v_mul_f32_e32 v115, v77, v100
	v_max3_f32 v74, v190, v191, v74
	v_max3_f32 v75, v96, v97, v75
	v_mul_f32_e32 v176, v82, v100
	v_mul_f32_e32 v177, v83, v100
	v_max3_f32 v74, v74, s6, v75
	v_max_f32_e32 v75, v110, v111
	v_max_f32_e32 v76, v114, v115
	v_max3_f32 v75, v176, v177, v75
	v_max3_f32 v76, v112, v113, v76
	v_max3_f32 v74, v74, v75, v76
	ds_bpermute_b32 v75, v194, v74
	v_cmp_gt_f32_e64 s[36:37], s96, v98
	s_waitcnt lgkmcnt(0)
	v_max_f32_e32 v75, v75, v75
	v_max_f32_e32 v74, v74, v75
	ds_bpermute_b32 v75, v195, v74
	s_and_saveexec_b64 s[14:15], vcc
	s_cbranch_execz .LBB0_452
	s_waitcnt lgkmcnt(0)
	v_max_f32_e32 v75, v75, v75
	v_max_f32_e32 v74, v74, v74
	v_max_f32_e32 v74, v74, v75
	ds_write_b32 v116, v74 offset:512
.LBB0_452:
	s_or_b64 exec, exec, s[14:15]
	v_mul_f32_e32 v74, 0x4b800000, v98
	v_cndmask_b32_e64 v74, v98, v74, s[36:37]
	v_rsq_f32_e32 v74, v74
	s_waitcnt lgkmcnt(0)
	v_mul_f32_e32 v75, 0x45800000, v74
	v_cndmask_b32_e64 v82, v74, v75, s[36:37]
	v_mul_f32_e32 v164, v88, v82
	v_mul_f32_e32 v165, v89, v82
	v_mul_f32_e32 v76, v80, v82
	v_mul_f32_e32 v77, v81, v82
	v_mul_f32_e32 v170, v86, v82
	v_mul_f32_e32 v171, v87, v82
	v_mul_f32_e32 v162, v78, v82
	v_mul_f32_e32 v163, v79, v82
	v_mul_f32_e32 v150, v70, v82
	v_mul_f32_e32 v151, v71, v82
	v_mul_f32_e32 v70, v66, v82
	v_mul_f32_e32 v71, v67, v82
	v_max_f32_e32 v66, v164, v165
	v_max_f32_e32 v67, v76, v77
	v_mul_f32_e32 v74, v72, v82
	v_mul_f32_e32 v75, v73, v82
	v_mul_f32_e32 v72, v68, v82
	v_mul_f32_e32 v73, v69, v82
	v_max3_f32 v66, v170, v171, v66
	v_max3_f32 v67, v162, v163, v67
	v_max3_f32 v66, v66, s6, v67
	v_max_f32_e32 v67, v74, v75
	v_max_f32_e32 v68, v72, v73
	v_max3_f32 v67, v150, v151, v67
	v_max3_f32 v68, v70, v71, v68
	v_max3_f32 v66, v66, v67, v68
	ds_bpermute_b32 v67, v194, v66
	s_waitcnt lgkmcnt(0)
	v_max_f32_e32 v67, v67, v67
	v_max_f32_e32 v66, v66, v67
	ds_bpermute_b32 v67, v195, v66
	s_and_saveexec_b64 s[14:15], vcc
	s_cbranch_execz .LBB0_454
	s_waitcnt lgkmcnt(0)
	v_max_f32_e32 v67, v67, v67
	v_max_f32_e32 v66, v66, v66
	v_max_f32_e32 v66, v66, v67
	ds_write_b32 v116, v66 offset:768
.LBB0_454:
	s_or_b64 exec, exec, s[14:15]
	v_ffbh_u32_e32 v66, v137
	v_min_u32_e32 v68, 32, v66
	s_waitcnt lgkmcnt(0)
	v_lshlrev_b64 v[66:67], v68, v[136:137]
	v_min_u32_e32 v66, 1, v66
	v_or_b32_e32 v66, v67, v66
	v_cvt_f32_u32_e32 v69, v66
	v_ffbh_u32_e32 v66, v135
	v_min_u32_e32 v78, 32, v66
	v_lshlrev_b64 v[66:67], v78, v[134:135]
	v_min_u32_e32 v66, 1, v66
	v_or_b32_e32 v66, v67, v66
	v_cvt_f32_u32_e32 v66, v66
	v_sub_u32_e32 v67, 32, v68
	v_sub_u32_e32 v68, 32, v78
	v_ldexp_f32 v67, v69, v67
	v_ldexp_f32 v66, v66, v68
	s_mov_b32 s14, 0x32800000
	v_fma_f32 v66, v66, s14, v196
	v_fma_f32 v67, v67, s14, v196
	s_nop 0
	v_mul_f32_e32 v68, 0x4b800000, v67
	v_cmp_gt_f32_e64 s[36:37], s96, v67
	s_nop 1
	v_cndmask_b32_e64 v67, v67, v68, s[36:37]
	v_rsq_f32_e32 v67, v67
	s_nop 0
	v_mul_f32_e32 v68, 0x45800000, v67
	v_cndmask_b32_e64 v68, v67, v68, s[36:37]
	v_mul_f32_e32 v166, v64, v68
	v_mul_f32_e32 v167, v65, v68
	v_mul_f32_e32 v156, v60, v68
	v_mul_f32_e32 v157, v61, v68
	v_mul_f32_e32 v62, v62, v68
	v_mul_f32_e32 v63, v63, v68
	v_mul_f32_e32 v64, v58, v68
	v_mul_f32_e32 v65, v59, v68
	v_mul_f32_e32 v80, v42, v68
	v_mul_f32_e32 v81, v43, v68
	v_max_f32_e32 v42, v166, v167
	v_max_f32_e32 v43, v156, v157
	v_mul_f32_e32 v78, v52, v68
	v_mul_f32_e32 v79, v53, v68
	v_mul_f32_e32 v82, v44, v68
	v_mul_f32_e32 v83, v45, v68
	v_max3_f32 v42, v62, v63, v42
	v_max3_f32 v43, v64, v65, v43
	v_mul_f32_e32 v158, v50, v68
	v_mul_f32_e32 v159, v51, v68
	v_max3_f32 v42, v42, s6, v43
	v_max_f32_e32 v43, v78, v79
	v_max_f32_e32 v44, v82, v83
	v_max3_f32 v43, v158, v159, v43
	v_max3_f32 v44, v80, v81, v44
	v_max3_f32 v42, v42, v43, v44
	ds_bpermute_b32 v43, v194, v42
	v_cmp_gt_f32_e64 s[36:37], s96, v66
	s_waitcnt lgkmcnt(0)
	v_max_f32_e32 v43, v43, v43
	v_max_f32_e32 v42, v42, v43
	ds_bpermute_b32 v43, v195, v42
	s_and_saveexec_b64 s[14:15], vcc
	s_cbranch_execz .LBB0_456
	s_waitcnt lgkmcnt(0)
	v_max_f32_e32 v43, v43, v43
	v_max_f32_e32 v42, v42, v42
	v_max_f32_e32 v42, v42, v43
	ds_write_b32 v116, v42 offset:2048
.LBB0_456:
	s_or_b64 exec, exec, s[14:15]
	v_mul_f32_e32 v42, 0x4b800000, v66
	v_cndmask_b32_e64 v42, v66, v42, s[36:37]
	v_rsq_f32_e32 v42, v42
	s_waitcnt lgkmcnt(0)
	v_mul_f32_e32 v43, 0x45800000, v42
	v_cndmask_b32_e64 v50, v42, v43, s[36:37]
	v_mul_f32_e32 v146, v56, v50
	v_mul_f32_e32 v147, v57, v50
	v_mul_f32_e32 v44, v48, v50
	v_mul_f32_e32 v45, v49, v50
	v_mul_f32_e32 v152, v54, v50
	v_mul_f32_e32 v153, v55, v50
	v_mul_f32_e32 v144, v46, v50
	v_mul_f32_e32 v145, v47, v50
	v_mul_f32_e32 v136, v38, v50
	v_mul_f32_e32 v137, v39, v50
	v_mul_f32_e32 v38, v36, v50
	v_mul_f32_e32 v39, v37, v50
	v_mul_f32_e32 v36, v34, v50
	v_mul_f32_e32 v37, v35, v50
	v_max_f32_e32 v34, v146, v147
	v_max_f32_e32 v35, v44, v45
	v_mul_f32_e32 v42, v40, v50
	v_mul_f32_e32 v43, v41, v50
	v_max3_f32 v34, v152, v153, v34
	v_max3_f32 v35, v144, v145, v35
	v_max3_f32 v34, v34, s6, v35
	v_max_f32_e32 v35, v42, v43
	v_max_f32_e32 v40, v38, v39
	v_max3_f32 v35, v136, v137, v35
	v_max3_f32 v40, v36, v37, v40
	v_max3_f32 v34, v34, v35, v40
	ds_bpermute_b32 v35, v194, v34
	s_waitcnt lgkmcnt(0)
	v_max_f32_e32 v35, v35, v35
	v_max_f32_e32 v34, v34, v35
	ds_bpermute_b32 v35, v195, v34
	s_and_saveexec_b64 s[14:15], vcc
	s_cbranch_execz .LBB0_458
	s_waitcnt lgkmcnt(0)
	v_max_f32_e32 v35, v35, v35
	v_max_f32_e32 v34, v34, v34
	v_max_f32_e32 v34, v34, v35
	ds_write_b32 v116, v34 offset:2304
.LBB0_458:
	s_or_b64 exec, exec, s[14:15]
	v_ffbh_u32_e32 v34, v133
	v_min_u32_e32 v40, 32, v34
	s_waitcnt lgkmcnt(0)
	v_lshlrev_b64 v[34:35], v40, v[132:133]
	v_min_u32_e32 v34, 1, v34
	v_or_b32_e32 v34, v35, v34
	v_cvt_f32_u32_e32 v41, v34
	v_ffbh_u32_e32 v34, v131
	v_min_u32_e32 v46, 32, v34
	v_lshlrev_b64 v[34:35], v46, v[130:131]
	v_min_u32_e32 v34, 1, v34
	v_or_b32_e32 v34, v35, v34
	v_cvt_f32_u32_e32 v34, v34
	v_sub_u32_e32 v35, 32, v40
	v_sub_u32_e32 v40, 32, v46
	v_ldexp_f32 v35, v41, v35
	v_ldexp_f32 v34, v34, v40
	s_mov_b32 s14, 0x32800000
	v_fma_f32 v34, v34, s14, v196
	v_fma_f32 v35, v35, s14, v196
	s_nop 0
	v_mul_f32_e32 v40, 0x4b800000, v35
	v_cmp_gt_f32_e64 s[36:37], s96, v35
	s_nop 1
	v_cndmask_b32_e64 v35, v35, v40, s[36:37]
	v_rsq_f32_e32 v35, v35
	s_nop 0
	v_mul_f32_e32 v40, 0x45800000, v35
	v_cndmask_b32_e64 v40, v35, v40, s[36:37]
	v_mul_f32_e32 v148, v32, v40
	v_mul_f32_e32 v149, v33, v40
	v_mul_f32_e32 v140, v28, v40
	v_mul_f32_e32 v141, v29, v40
	v_mul_f32_e32 v160, v30, v40
	v_mul_f32_e32 v161, v31, v40
	v_mul_f32_e32 v32, v26, v40
	v_mul_f32_e32 v33, v27, v40
	v_mul_f32_e32 v48, v10, v40
	v_mul_f32_e32 v49, v11, v40
	v_max_f32_e32 v10, v148, v149
	v_max_f32_e32 v11, v140, v141
	v_mul_f32_e32 v46, v20, v40
	v_mul_f32_e32 v47, v21, v40
	v_mul_f32_e32 v50, v12, v40
	v_mul_f32_e32 v51, v13, v40
	v_max3_f32 v10, v160, v161, v10
	v_max3_f32 v11, v32, v33, v11
	v_mul_f32_e32 v142, v18, v40
	v_mul_f32_e32 v143, v19, v40
	v_max3_f32 v10, v10, s6, v11
	v_max_f32_e32 v11, v46, v47
	v_max_f32_e32 v12, v50, v51
	v_max3_f32 v11, v142, v143, v11
	v_max3_f32 v12, v48, v49, v12
	v_max3_f32 v10, v10, v11, v12
	ds_bpermute_b32 v11, v194, v10
	v_cmp_gt_f32_e64 s[36:37], s96, v34
	s_waitcnt lgkmcnt(0)
	v_max_f32_e32 v11, v11, v11
	v_max_f32_e32 v10, v10, v11
	ds_bpermute_b32 v11, v195, v10
	s_and_saveexec_b64 s[14:15], vcc
	s_cbranch_execz .LBB0_460
	s_waitcnt lgkmcnt(0)
	v_max_f32_e32 v11, v11, v11
	v_max_f32_e32 v10, v10, v10
	v_max_f32_e32 v10, v10, v11
	ds_write_b32 v116, v10 offset:2560
.LBB0_460:
	s_or_b64 exec, exec, s[14:15]
	v_mul_f32_e32 v10, 0x4b800000, v34
	v_cndmask_b32_e64 v10, v34, v10, s[36:37]
	v_rsq_f32_e32 v10, v10
	s_waitcnt lgkmcnt(0)
	v_mul_f32_e32 v11, 0x45800000, v10
	v_cndmask_b32_e64 v18, v10, v11, s[36:37]
	v_mul_f32_e32 v134, v24, v18
	v_mul_f32_e32 v135, v25, v18
	v_mul_f32_e32 v12, v16, v18
	v_mul_f32_e32 v13, v17, v18
	v_mul_f32_e32 v138, v22, v18
	v_mul_f32_e32 v139, v23, v18
	v_mul_f32_e32 v14, v14, v18
	v_mul_f32_e32 v15, v15, v18
	v_mul_f32_e32 v10, v8, v18
	v_mul_f32_e32 v11, v9, v18
	v_mul_f32_e32 v130, v6, v18
	v_mul_f32_e32 v131, v7, v18
	v_mul_f32_e32 v16, v4, v18
	v_mul_f32_e32 v17, v5, v18
	v_mul_f32_e32 v19, v3, v18
	v_mul_f32_e32 v18, v2, v18
	v_max_f32_e32 v2, v134, v135
	v_max_f32_e32 v3, v12, v13
	v_max3_f32 v2, v138, v139, v2
	v_max3_f32 v3, v14, v15, v3
	v_max3_f32 v2, v2, s6, v3
	v_max_f32_e32 v3, v10, v11
	v_max_f32_e32 v4, v16, v17
	v_max3_f32 v3, v130, v131, v3
	v_max3_f32 v4, v18, v19, v4
	v_max3_f32 v2, v2, v3, v4
	ds_bpermute_b32 v3, v194, v2
	s_waitcnt lgkmcnt(0)
	v_max_f32_e32 v3, v3, v3
	v_max_f32_e32 v2, v2, v3
	ds_bpermute_b32 v3, v195, v2
	s_and_saveexec_b64 s[14:15], vcc
	s_cbranch_execz .LBB0_462
	s_waitcnt lgkmcnt(0)
	v_max_f32_e32 v3, v3, v3
	v_max_f32_e32 v2, v2, v2
	v_max_f32_e32 v2, v2, v3
	ds_write_b32 v116, v2 offset:2816

.LBB0_478:
	s_or_b64 exec, exec, s[14:15]
	s_lshl_b32 s14, s34, 8
	s_add_i32 s14, s14, s1
	s_ashr_i32 s1, s0, 31
	s_waitcnt lgkmcnt(0)
	s_barrier
	s_lshl_b64 s[0:1], s[0:1], 9
	s_add_u32 s0, s74, s0
	ds_read_b128 v[136:139], v192 offset:4096
	v_or_b32_e32 v130, s14, v193
	s_addc_u32 s1, s75, s1
	s_lshl_b32 s14, s31, 6
	s_add_u32 s0, s0, s14
	s_addc_u32 s1, s1, 0
	v_and_b32_e32 v0, 0x70, v0
	s_waitcnt lgkmcnt(1)
	v_lshl_add_u64 v[18:19], s[0:1], 0, v[0:1]
	s_mov_b64 s[0:1], 0xa800000
	v_lshl_add_u64 v[134:135], v[18:19], 0, s[0:1]
	s_waitcnt lgkmcnt(0)
	v_mov_b32_e32 v18, v137
	v_mov_b32_e32 v19, v138
	v_mov_b32_e32 v137, v139
	v_add_f32_e32 v18, v18, v136
	v_add_f32_e32 v19, v19, v137
	s_nop 0
	v_add_f32_e32 v0, v18, v19
	v_div_scale_f32 v18, s[0:1], v0, v0, 1.0
	v_rcp_f32_e32 v19, v18
	s_nop 0
	v_fma_f32 v131, -v18, v19, 1.0
	v_fmac_f32_e32 v19, v131, v19
	v_div_scale_f32 v131, vcc, 1.0, v0, 1.0
	v_mul_f32_e32 v136, v131, v19
	v_fma_f32 v137, -v18, v136, v131
	v_fmac_f32_e32 v136, v137, v19
	v_fma_f32 v18, -v18, v136, v131
	v_div_fmas_f32 v18, v18, v19, v136
	v_div_fixup_f32 v0, v18, v0, 1.0
	v_ashrrev_i32_e32 v131, 31, v130
	v_lshlrev_b64 v[18:19], 11, v[130:131]
	v_mul_f32_e32 v118, v118, v0
	v_mul_f32_e32 v119, v119, v0
	v_mul_f32_e32 v116, v116, v0
	v_mul_f32_e32 v117, v117, v0
	v_mul_f32_e32 v122, v122, v0
	v_mul_f32_e32 v123, v123, v0
	v_mul_f32_e32 v120, v120, v0
	v_mul_f32_e32 v121, v121, v0
	v_lshl_add_u64 v[18:19], v[134:135], 0, v[18:19]
	v_cvt_pk_bf16_f32 v116, v116, v117
	v_cvt_pk_bf16_f32 v117, v118, v119
	v_cvt_pk_bf16_f32 v118, v120, v121
	v_cvt_pk_bf16_f32 v119, v122, v123
	global_store_dwordx4 v[18:19], v[116:119], off
	v_mul_f32_e32 v120, v132, v0
	v_mul_f32_e32 v121, v133, v0
	v_mul_f32_e32 v122, v128, v0
	v_mul_f32_e32 v123, v129, v0
	v_mul_f32_e32 v118, v126, v0
	v_mul_f32_e32 v119, v127, v0
	v_mul_f32_e32 v116, v124, v0
	v_mul_f32_e32 v117, v125, v0
	s_nop 0
	v_cvt_pk_bf16_f32 v116, v116, v117
	v_cvt_pk_bf16_f32 v117, v118, v119
	v_cvt_pk_bf16_f32 v118, v122, v123
	v_cvt_pk_bf16_f32 v119, v120, v121
	global_store_dwordx4 v[18:19], v[116:119], off offset:256
	ds_read_b128 v[116:119], v192 offset:4352
	s_waitcnt lgkmcnt(0)
	v_mov_b32_e32 v120, v117
	v_mov_b32_e32 v121, v118
	v_mov_b32_e32 v117, v119
	v_add_f32_e32 v116, v120, v116
	v_add_f32_e32 v117, v121, v117
	s_nop 0
	v_add_f32_e32 v0, v116, v117
	v_div_scale_f32 v116, s[0:1], v0, v0, 1.0
	v_rcp_f32_e32 v117, v116
	s_nop 0
	v_fma_f32 v118, -v116, v117, 1.0
	v_fmac_f32_e32 v117, v118, v117
	v_div_scale_f32 v118, vcc, 1.0, v0, 1.0
	v_mul_f32_e32 v119, v118, v117
	v_fma_f32 v120, -v116, v119, v118
	v_fmac_f32_e32 v119, v120, v117
	v_fma_f32 v116, -v116, v119, v118
	v_div_fmas_f32 v116, v116, v117, v119
	v_div_fixup_f32 v0, v116, v0, 1.0
	v_or_b32_e32 v116, 16, v130
	v_ashrrev_i32_e32 v117, 31, v116
	v_lshlrev_b64 v[116:117], 11, v[116:117]
	v_mul_f32_e32 v94, v94, v0
	v_mul_f32_e32 v95, v95, v0
	v_mul_f32_e32 v84, v84, v0
	v_mul_f32_e32 v85, v85, v0
	v_mul_f32_e32 v90, v90, v0
	v_mul_f32_e32 v91, v91, v0
	v_lshl_add_u64 v[120:121], v[134:135], 0, v[116:117]
	v_cvt_pk_bf16_f32 v116, v84, v85
	v_cvt_pk_bf16_f32 v117, v94, v95
	v_cvt_pk_bf16_f32 v118, v90, v91
	v_mul_f32_e32 v84, v98, v0
	v_mul_f32_e32 v85, v99, v0
	v_mul_f32_e32 v88, v88, v0
	v_mul_f32_e32 v89, v89, v0
	v_mul_f32_e32 v94, v108, v0
	v_mul_f32_e32 v95, v109, v0
	v_mul_f32_e32 v90, v104, v0
	v_mul_f32_e32 v91, v105, v0
	v_cvt_pk_bf16_f32 v88, v88, v89
	v_cvt_pk_bf16_f32 v89, v84, v85
	v_cvt_pk_bf16_f32 v90, v90, v91
	v_cvt_pk_bf16_f32 v91, v94, v95
	global_store_dwordx4 v[120:121], v[88:91], off offset:256
	ds_read_b128 v[88:91], v192 offset:4608
	v_mul_f32_e32 v100, v100, v0
	v_mul_f32_e32 v101, v101, v0
	s_waitcnt lgkmcnt(0)
	v_mov_b32_e32 v84, v89
	v_mov_b32_e32 v85, v90
	v_mov_b32_e32 v89, v91
	v_add_f32_e32 v84, v84, v88
	v_add_f32_e32 v85, v85, v89
	v_cvt_pk_bf16_f32 v119, v100, v101
	v_add_f32_e32 v0, v84, v85
	v_div_scale_f32 v84, s[0:1], v0, v0, 1.0
	v_rcp_f32_e32 v85, v84
	global_store_dwordx4 v[120:121], v[116:119], off
	v_fma_f32 v88, -v84, v85, 1.0
	v_fmac_f32_e32 v85, v88, v85
	v_div_scale_f32 v88, vcc, 1.0, v0, 1.0
	v_mul_f32_e32 v89, v88, v85
	v_fma_f32 v90, -v84, v89, v88
	v_fmac_f32_e32 v89, v90, v85
	v_fma_f32 v84, -v84, v89, v88
	v_div_fmas_f32 v84, v84, v85, v89
	v_div_fixup_f32 v0, v84, v0, 1.0
	v_or_b32_e32 v84, 32, v130
	v_ashrrev_i32_e32 v85, 31, v84
	v_lshlrev_b64 v[84:85], 11, v[84:85]
	v_lshl_add_u64 v[88:89], v[134:135], 0, v[84:85]
	v_mul_f32_e32 v90, v92, v0
	v_mul_f32_e32 v91, v93, v0
	v_mul_f32_e32 v84, v86, v0
	v_mul_f32_e32 v85, v87, v0
	v_mul_f32_e32 v92, v102, v0
	v_mul_f32_e32 v93, v103, v0
	v_mul_f32_e32 v86, v96, v0
	v_mul_f32_e32 v87, v97, v0
	v_cvt_pk_bf16_f32 v84, v84, v85
	v_cvt_pk_bf16_f32 v85, v90, v91
	v_cvt_pk_bf16_f32 v86, v86, v87
	v_cvt_pk_bf16_f32 v87, v92, v93
	global_store_dwordx4 v[88:89], v[84:87], off
	v_mul_f32_e32 v90, v114, v0
	v_mul_f32_e32 v91, v115, v0
	v_mul_f32_e32 v92, v112, v0
	v_mul_f32_e32 v93, v113, v0
	v_mul_f32_e32 v86, v110, v0
	v_mul_f32_e32 v87, v111, v0
	v_mul_f32_e32 v84, v106, v0
	v_mul_f32_e32 v85, v107, v0
	s_nop 0
	v_cvt_pk_bf16_f32 v84, v84, v85
	v_cvt_pk_bf16_f32 v85, v86, v87
	v_cvt_pk_bf16_f32 v86, v92, v93
	v_cvt_pk_bf16_f32 v87, v90, v91
	global_store_dwordx4 v[88:89], v[84:87], off offset:256
	ds_read_b128 v[84:87], v192 offset:4864
	s_waitcnt lgkmcnt(0)
	v_mov_b32_e32 v88, v85
	v_mov_b32_e32 v89, v86
	v_mov_b32_e32 v85, v87
	v_add_f32_e32 v84, v88, v84
	v_add_f32_e32 v85, v89, v85
	s_nop 0
	v_add_f32_e32 v0, v84, v85
	v_div_scale_f32 v84, s[0:1], v0, v0, 1.0
	v_rcp_f32_e32 v85, v84
	s_nop 0
	v_fma_f32 v86, -v84, v85, 1.0
	v_fmac_f32_e32 v85, v86, v85
	v_div_scale_f32 v86, vcc, 1.0, v0, 1.0
	v_mul_f32_e32 v87, v86, v85
	v_fma_f32 v88, -v84, v87, v86
	v_fmac_f32_e32 v87, v88, v85
	v_fma_f32 v84, -v84, v87, v86
	v_div_fmas_f32 v84, v84, v85, v87
	v_div_fixup_f32 v0, v84, v0, 1.0
	v_or_b32_e32 v84, 48, v130
	v_ashrrev_i32_e32 v85, 31, v84
	v_lshlrev_b64 v[84:85], 11, v[84:85]
	v_mul_f32_e32 v60, v60, v0
	v_mul_f32_e32 v61, v61, v0
	v_mul_f32_e32 v52, v52, v0
	v_mul_f32_e32 v53, v53, v0
	v_mul_f32_e32 v56, v56, v0
	v_mul_f32_e32 v57, v57, v0
	v_lshl_add_u64 v[88:89], v[134:135], 0, v[84:85]
	v_cvt_pk_bf16_f32 v84, v52, v53
	v_cvt_pk_bf16_f32 v85, v60, v61
	v_cvt_pk_bf16_f32 v86, v56, v57
	v_mul_f32_e32 v56, v66, v0
	v_mul_f32_e32 v57, v67, v0
	v_mul_f32_e32 v52, v54, v0
	v_mul_f32_e32 v53, v55, v0
	v_mul_f32_e32 v60, v76, v0
	v_mul_f32_e32 v61, v77, v0
	v_mul_f32_e32 v54, v70, v0
	v_mul_f32_e32 v55, v71, v0
	v_cvt_pk_bf16_f32 v52, v52, v53
	v_cvt_pk_bf16_f32 v53, v56, v57
	v_cvt_pk_bf16_f32 v54, v54, v55
	v_cvt_pk_bf16_f32 v55, v60, v61
	global_store_dwordx4 v[88:89], v[52:55], off offset:256
	ds_read_b128 v[52:55], v192 offset:6144
	v_mul_f32_e32 v68, v68, v0
	v_mul_f32_e32 v69, v69, v0
	s_waitcnt lgkmcnt(0)
	v_mov_b32_e32 v56, v53
	v_mov_b32_e32 v57, v54
	v_mov_b32_e32 v53, v55
	v_add_f32_e32 v52, v56, v52
	v_add_f32_e32 v53, v57, v53
	v_cvt_pk_bf16_f32 v87, v68, v69
	v_add_f32_e32 v0, v52, v53
	v_div_scale_f32 v52, s[0:1], v0, v0, 1.0
	v_rcp_f32_e32 v53, v52
	s_mov_b32 s0, 0x40000
	global_store_dwordx4 v[88:89], v[84:87], off
	v_fma_f32 v54, -v52, v53, 1.0
	v_fmac_f32_e32 v53, v54, v53
	v_div_scale_f32 v54, vcc, 1.0, v0, 1.0
	v_mul_f32_e32 v55, v54, v53
	v_fma_f32 v56, -v52, v55, v54
	v_fmac_f32_e32 v55, v56, v53
	v_fma_f32 v52, -v52, v55, v54
	v_div_fmas_f32 v52, v52, v53, v55
	v_div_fixup_f32 v0, v52, v0, 1.0
	v_mul_f32_e32 v54, v62, v0
	v_mul_f32_e32 v55, v63, v0
	v_mul_f32_e32 v52, v58, v0
	v_mul_f32_e32 v53, v59, v0
	v_mul_f32_e32 v58, v74, v0
	v_mul_f32_e32 v59, v75, v0
	v_mul_f32_e32 v60, v64, v0
	v_mul_f32_e32 v61, v65, v0
	v_cvt_pk_bf16_f32 v52, v52, v53
	v_cvt_pk_bf16_f32 v53, v54, v55
	v_cvt_pk_bf16_f32 v55, v58, v59
	v_add_co_u32_e32 v58, vcc, s0, v18
	v_cvt_pk_bf16_f32 v54, v60, v61
	s_nop 0
	v_addc_co_u32_e32 v59, vcc, 0, v19, vcc
	global_store_dwordx4 v[58:59], v[52:55], off
	v_mul_f32_e32 v58, v82, v0
	v_mul_f32_e32 v59, v83, v0
	v_mul_f32_e32 v60, v80, v0
	v_mul_f32_e32 v61, v81, v0
	v_mul_f32_e32 v54, v78, v0
	v_mul_f32_e32 v55, v79, v0
	v_mul_f32_e32 v52, v72, v0
	v_mul_f32_e32 v53, v73, v0
	v_lshl_add_u64 v[56:57], v[18:19], 0, s[20:21]
	v_cvt_pk_bf16_f32 v52, v52, v53
	v_cvt_pk_bf16_f32 v53, v54, v55
	v_cvt_pk_bf16_f32 v54, v60, v61
	v_cvt_pk_bf16_f32 v55, v58, v59
	global_store_dwordx4 v[56:57], v[52:55], off offset:256
	ds_read_b128 v[52:55], v192 offset:6400
	s_waitcnt lgkmcnt(0)
	v_mov_b32_e32 v56, v53
	v_mov_b32_e32 v57, v54
	v_mov_b32_e32 v53, v55
	v_add_f32_e32 v52, v56, v52
	v_add_f32_e32 v53, v57, v53
	s_nop 0
	v_add_f32_e32 v0, v52, v53
	v_div_scale_f32 v52, s[0:1], v0, v0, 1.0
	v_rcp_f32_e32 v53, v52
	s_mov_b64 s[0:1], 0x48000
	v_fma_f32 v54, -v52, v53, 1.0
	v_fmac_f32_e32 v53, v54, v53
	v_div_scale_f32 v54, vcc, 1.0, v0, 1.0
	v_mul_f32_e32 v55, v54, v53
	v_fma_f32 v56, -v52, v55, v54
	v_fmac_f32_e32 v55, v56, v53
	v_fma_f32 v52, -v52, v55, v54
	v_div_fmas_f32 v52, v52, v53, v55
	v_div_fixup_f32 v0, v52, v0, 1.0
	v_lshl_add_u64 v[52:53], v[18:19], 0, s[0:1]
	v_mul_f32_e32 v24, v24, v0
	v_mul_f32_e32 v25, v25, v0
	s_mov_b32 s0, 0x48000
	v_mul_f32_e32 v30, v30, v0
	v_mul_f32_e32 v31, v31, v0
	v_mul_f32_e32 v40, v40, v0
	v_mul_f32_e32 v41, v41, v0
	v_mul_f32_e32 v54, v28, v0
	v_mul_f32_e32 v55, v29, v0
	v_cvt_pk_bf16_f32 v28, v24, v25
	v_add_co_u32_e32 v24, vcc, s0, v18
	v_cvt_pk_bf16_f32 v29, v30, v31
	v_cvt_pk_bf16_f32 v30, v54, v55
	v_cvt_pk_bf16_f32 v31, v40, v41
	v_addc_co_u32_e32 v25, vcc, 0, v19, vcc
	global_store_dwordx4 v[24:25], v[28:31], off
	v_mul_f32_e32 v24, v34, v0
	v_mul_f32_e32 v25, v35, v0
	v_mul_f32_e32 v20, v20, v0
	v_mul_f32_e32 v21, v21, v0
	v_mul_f32_e32 v34, v44, v0
	v_mul_f32_e32 v35, v45, v0
	v_mul_f32_e32 v30, v36, v0
	v_mul_f32_e32 v31, v37, v0
	v_cvt_pk_bf16_f32 v28, v20, v21
	v_cvt_pk_bf16_f32 v29, v24, v25
	v_cvt_pk_bf16_f32 v30, v30, v31
	v_cvt_pk_bf16_f32 v31, v34, v35
	global_store_dwordx4 v[52:53], v[28:31], off offset:256
	ds_read_b128 v[28:31], v192 offset:6656
	s_waitcnt lgkmcnt(0)
	v_mov_b32_e32 v20, v29
	v_mov_b32_e32 v21, v30
	v_mov_b32_e32 v29, v31
	v_add_f32_e32 v20, v20, v28
	v_add_f32_e32 v21, v21, v29
	s_nop 0
	v_add_f32_e32 v0, v20, v21
	v_div_scale_f32 v20, s[0:1], v0, v0, 1.0
	v_rcp_f32_e32 v21, v20
	s_mov_b32 s0, 0x50000
	v_fma_f32 v24, -v20, v21, 1.0
	v_fmac_f32_e32 v21, v24, v21
	v_div_scale_f32 v24, vcc, 1.0, v0, 1.0
	v_mul_f32_e32 v25, v24, v21
	v_fma_f32 v28, -v20, v25, v24
	v_fmac_f32_e32 v25, v28, v21
	v_fma_f32 v20, -v20, v25, v24
	v_div_fmas_f32 v20, v20, v21, v25
	v_div_fixup_f32 v0, v20, v0, 1.0
	v_mul_f32_e32 v26, v26, v0
	v_mul_f32_e32 v27, v27, v0
	v_mul_f32_e32 v20, v22, v0
	v_mul_f32_e32 v21, v23, v0
	v_mul_f32_e32 v28, v42, v0
	v_mul_f32_e32 v29, v43, v0
	v_mul_f32_e32 v22, v32, v0
	v_mul_f32_e32 v23, v33, v0
	v_cvt_pk_bf16_f32 v20, v20, v21
	v_cvt_pk_bf16_f32 v21, v26, v27
	v_add_co_u32_e32 v26, vcc, s0, v18
	v_cvt_pk_bf16_f32 v22, v22, v23
	v_cvt_pk_bf16_f32 v23, v28, v29
	v_addc_co_u32_e32 v27, vcc, 0, v19, vcc
	global_store_dwordx4 v[26:27], v[20:23], off
	v_mul_f32_e32 v26, v50, v0
	v_mul_f32_e32 v27, v51, v0
	v_mul_f32_e32 v28, v48, v0
	v_mul_f32_e32 v29, v49, v0
	v_mul_f32_e32 v22, v46, v0
	v_mul_f32_e32 v23, v47, v0
	v_mul_f32_e32 v20, v38, v0
	v_mul_f32_e32 v21, v39, v0
	v_lshl_add_u64 v[24:25], v[18:19], 0, s[22:23]
	v_cvt_pk_bf16_f32 v20, v20, v21
	v_cvt_pk_bf16_f32 v21, v22, v23
	v_cvt_pk_bf16_f32 v22, v28, v29
	v_cvt_pk_bf16_f32 v23, v26, v27
	global_store_dwordx4 v[24:25], v[20:23], off offset:256
	ds_read_b128 v[20:23], v192 offset:6912
	s_waitcnt lgkmcnt(0)
	v_mov_b32_e32 v24, v21
	v_mov_b32_e32 v25, v22
	v_mov_b32_e32 v21, v23
	v_add_f32_e32 v20, v24, v20
	v_add_f32_e32 v21, v25, v21
	s_nop 0
	v_add_f32_e32 v0, v20, v21
	v_div_scale_f32 v20, s[0:1], v0, v0, 1.0
	v_rcp_f32_e32 v21, v20
	s_mov_b64 s[0:1], 0x58000
	v_fma_f32 v22, -v20, v21, 1.0
	v_fmac_f32_e32 v21, v22, v21
	v_div_scale_f32 v22, vcc, 1.0, v0, 1.0
	v_mul_f32_e32 v23, v22, v21
	v_fma_f32 v24, -v20, v23, v22
	v_fmac_f32_e32 v23, v24, v21
	v_fma_f32 v20, -v20, v23, v22
	v_div_fmas_f32 v20, v20, v21, v23
	v_div_fixup_f32 v0, v20, v0, 1.0
	v_lshl_add_u64 v[20:21], v[18:19], 0, s[0:1]
	v_mul_f32_e32 v8, v8, v0
	v_mul_f32_e32 v9, v9, v0
	v_mul_f32_e32 v4, v4, v0
	v_mul_f32_e32 v5, v5, v0
	s_mov_b32 s0, 0x58000
	v_mul_f32_e32 v14, v14, v0
	v_mul_f32_e32 v15, v15, v0
	v_mul_f32_e32 v6, v6, v0
	v_mul_f32_e32 v7, v7, v0
	v_cvt_pk_bf16_f32 v4, v4, v5
	v_cvt_pk_bf16_f32 v5, v8, v9
	v_add_co_u32_e32 v8, vcc, s0, v18
	v_cvt_pk_bf16_f32 v6, v6, v7
	v_cvt_pk_bf16_f32 v7, v14, v15
	v_addc_co_u32_e32 v9, vcc, 0, v19, vcc
	global_store_dwordx4 v[8:9], v[4:7], off
	v_mul_f32_e32 v2, v2, v0
	v_mul_f32_e32 v3, v3, v0
	v_mul_f32_e32 v8, v10, v0
	v_mul_f32_e32 v9, v11, v0
	v_mul_f32_e32 v4, v12, v0
	v_mul_f32_e32 v5, v13, v0
	v_mul_f32_e32 v6, v16, v0
	v_mul_f32_e32 v7, v17, v0
	v_cvt_pk_bf16_f32 v2, v2, v3
	v_cvt_pk_bf16_f32 v3, v4, v5
	v_cvt_pk_bf16_f32 v4, v8, v9
	v_cvt_pk_bf16_f32 v5, v6, v7
	global_store_dwordx4 v[20:21], v[2:5], off offset:256
	s_waitcnt lgkmcnt(0)
	s_barrier

.LBB0_503:
	s_mov_b32 s0, -1
	s_add_u32 s14, s74, 0x8800000
	s_waitcnt vmcnt(0)
	s_barrier
	s_addc_u32 s15, s75, 0
	v_mbcnt_lo_u32_b32 v0, s0, 0
	v_mbcnt_hi_u32_b32 v166, s0, v0
	s_lshl_b32 s0, s90, 8
	v_and_b32_e32 v130, 15, v166
	s_add_i32 s17, s0, s65
	v_or_b32_e32 v156, s17, v130
	s_ashr_i32 s17, s16, 31
	s_lshl_b32 s1, s64, 5
	s_lshl_b64 s[16:17], s[16:17], 8
	v_lshrrev_b32_e32 v0, 1, v166
	s_or_b32 s16, s16, s1
	v_and_b32_e32 v0, 56, v0
	v_and_b32_e32 v131, 64, v231
	v_lshl_add_u64 v[154:155], s[16:17], 0, v[0:1]
	v_xor_b32_e32 v0, 16, v231
	v_add_u32_e32 v131, 64, v131
	v_cmp_lt_i32_e32 vcc, v0, v131
	v_readlane_b32 s16, v253, 34
	v_lshlrev_b64 v[178:179], 1, v[154:155]
	v_cndmask_b32_e32 v0, v231, v0, vcc
	v_lshlrev_b32_e32 v168, 2, v0
	v_xor_b32_e32 v0, 32, v231
	v_cmp_lt_i32_e32 vcc, v0, v131
	v_readlane_b32 s17, v253, 35
	v_ashrrev_i32_e32 v157, 31, v156
	v_cndmask_b32_e32 v0, v231, v0, vcc
	v_lshl_add_u64 v[158:159], s[16:17], 0, v[178:179]
	v_lshlrev_b64 v[180:181], 11, v[156:157]
	v_lshlrev_b32_e32 v167, 2, v0
	v_or_b32_e32 v0, s65, v130
	v_lshl_add_u64 v[130:131], v[158:159], 0, v[180:181]
	global_load_dwordx4 v[170:173], v[130:131], off
	global_load_dwordx4 v[174:177], v[130:131], off offset:256
	v_or_b32_e32 v130, 16, v156
	v_ashrrev_i32_e32 v131, 31, v130
	v_lshlrev_b64 v[164:165], 11, v[130:131]
	v_lshl_add_u64 v[130:131], v[158:159], 0, v[164:165]
	global_load_dwordx4 v[150:153], v[130:131], off
	global_load_dwordx4 v[146:149], v[130:131], off offset:256
	v_or_b32_e32 v130, 32, v156
	v_ashrrev_i32_e32 v131, 31, v130
	v_lshlrev_b64 v[162:163], 11, v[130:131]
	v_lshl_add_u64 v[130:131], v[158:159], 0, v[162:163]
	global_load_dwordx4 v[142:145], v[130:131], off
	global_load_dwordx4 v[138:141], v[130:131], off offset:256
	v_or_b32_e32 v130, 48, v156
	v_ashrrev_i32_e32 v131, 31, v130
	v_lshlrev_b64 v[160:161], 11, v[130:131]
	v_lshl_add_u64 v[130:131], v[158:159], 0, v[160:161]
	global_load_dwordx4 v[134:137], v[130:131], off
	s_nop 0
	global_load_dwordx4 v[130:133], v[130:131], off offset:256
	v_lshl_add_u64 v[180:181], s[14:15], 0, v[180:181]
	v_lshl_add_u64 v[178:179], v[180:181], 0, v[178:179]
	v_cmp_gt_u32_e32 vcc, 16, v166
	s_lshl_b32 s1, s64, 2
	s_waitcnt vmcnt(0)
	v_lshlrev_b32_e32 v182, 16, v170
	v_and_b32_e32 v183, 0xffff0000, v170
	v_lshlrev_b32_e32 v170, 16, v171
	v_and_b32_e32 v171, 0xffff0000, v171
	v_add_f32_e32 v128, v128, v170
	v_add_f32_e32 v129, v129, v171
	v_lshlrev_b32_e32 v170, 16, v172
	v_and_b32_e32 v171, 0xffff0000, v172
	v_add_f32_e32 v170, v122, v170
	v_add_f32_e32 v171, v123, v171
	v_lshlrev_b32_e32 v122, 16, v173
	v_and_b32_e32 v123, 0xffff0000, v173
	v_add_f32_e32 v126, v126, v182
	v_add_f32_e32 v127, v127, v183
	v_add_f32_e32 v172, v124, v122
	v_add_f32_e32 v173, v125, v123
	v_cvt_pk_bf16_f32 v122, v126, v127
	v_cvt_pk_bf16_f32 v123, v128, v129
	v_cvt_pk_bf16_f32 v124, v170, v171
	v_cvt_pk_bf16_f32 v125, v172, v173
	global_store_dwordx4 v[178:179], v[122:125], off
	s_nop 1
	v_mul_f32_e32 v122, v126, v126
	v_mul_f32_e32 v123, v127, v127
	v_mul_f32_e32 v126, v170, v170
	v_mul_f32_e32 v127, v171, v171
	v_lshlrev_b32_e32 v170, 16, v174
	v_and_b32_e32 v171, 0xffff0000, v174
	v_add_f32_e32 v118, v118, v170
	v_add_f32_e32 v119, v119, v171
	v_lshlrev_b32_e32 v170, 16, v175
	v_and_b32_e32 v171, 0xffff0000, v175
	v_add_f32_e32 v120, v120, v170
	v_add_f32_e32 v121, v121, v171
	v_lshlrev_b32_e32 v170, 16, v176
	v_and_b32_e32 v171, 0xffff0000, v176
	v_add_f32_e32 v170, v114, v170
	v_add_f32_e32 v171, v115, v171
	v_lshlrev_b32_e32 v114, 16, v177
	v_and_b32_e32 v115, 0xffff0000, v177
	v_mul_f32_e32 v124, v128, v128
	v_mul_f32_e32 v125, v129, v129
	v_mul_f32_e32 v128, v172, v172
	v_mul_f32_e32 v129, v173, v173
	v_add_f32_e32 v172, v116, v114
	v_add_f32_e32 v173, v117, v115
	v_cvt_pk_bf16_f32 v114, v118, v119
	v_cvt_pk_bf16_f32 v115, v120, v121
	v_cvt_pk_bf16_f32 v116, v170, v171
	v_cvt_pk_bf16_f32 v117, v172, v173
	global_store_dwordx4 v[178:179], v[114:117], off offset:256
	s_nop 1
	v_mul_f32_e32 v114, v118, v118
	v_mul_f32_e32 v115, v119, v119
	v_mul_f32_e32 v116, v120, v120
	v_mul_f32_e32 v117, v121, v121
	v_add_f32_e32 v114, v114, v115
	v_add_f32_e32 v116, v116, v117
	v_mul_f32_e32 v118, v170, v170
	v_mul_f32_e32 v119, v171, v171
	v_mul_f32_e32 v120, v172, v172
	v_mul_f32_e32 v121, v173, v173
	v_add_f32_e32 v114, v114, v116
	v_add_f32_e32 v115, v128, v129
	v_add_f32_e32 v116, v126, v127
	v_add_f32_e32 v120, v120, v121
	v_add_f32_e32 v118, v118, v119
	v_add_f32_e32 v115, v116, v115
	v_add_f32_e32 v116, v124, v125
	v_add_f32_e32 v117, v122, v123
	v_add_f32_e32 v118, v118, v120
	v_add_f32_e32 v116, v117, v116
	v_add_f32_e32 v114, v114, v118
	v_add_f32_e32 v115, v116, v115
	v_add_f32_e32 v114, v115, v114
	ds_bpermute_b32 v115, v168, v114
	s_waitcnt lgkmcnt(0)
	v_add_f32_e32 v114, v114, v115
	ds_bpermute_b32 v115, v167, v114
	s_and_saveexec_b64 s[16:17], vcc
	s_cbranch_execz .LBB0_505
	v_lshl_or_b32 v116, v0, 4, s1
	s_waitcnt lgkmcnt(0)
	v_add_f32_e32 v114, v114, v115
	ds_write_b32 v116, v114
.LBB0_505:
	s_or_b64 exec, exec, s[16:17]
	v_lshlrev_b32_e32 v114, 16, v150
	s_waitcnt lgkmcnt(0)
	v_and_b32_e32 v115, 0xffff0000, v150
	v_add_f32_e32 v110, v110, v114
	v_add_f32_e32 v111, v111, v115
	v_lshlrev_b32_e32 v114, 16, v151
	v_and_b32_e32 v115, 0xffff0000, v151
	v_add_f32_e32 v112, v112, v114
	v_add_f32_e32 v113, v113, v115
	v_lshlrev_b32_e32 v114, 16, v152
	v_and_b32_e32 v115, 0xffff0000, v152
	v_add_f32_e32 v114, v106, v114
	v_add_f32_e32 v115, v107, v115
	v_lshlrev_b32_e32 v106, 16, v153
	v_and_b32_e32 v107, 0xffff0000, v153
	v_add_f32_e32 v116, v108, v106
	v_add_f32_e32 v117, v109, v107
	v_lshl_add_u64 v[118:119], s[14:15], 0, v[164:165]
	v_cvt_pk_bf16_f32 v106, v110, v111
	v_cvt_pk_bf16_f32 v107, v112, v113
	v_cvt_pk_bf16_f32 v108, v114, v115
	v_cvt_pk_bf16_f32 v109, v116, v117
	v_lshl_add_u64 v[118:119], v[154:155], 1, v[118:119]
	global_store_dwordx4 v[118:119], v[106:109], off
	s_nop 1
	v_mul_f32_e32 v106, v110, v110
	v_mul_f32_e32 v107, v111, v111
	v_mul_f32_e32 v110, v114, v114
	v_mul_f32_e32 v111, v115, v115
	v_lshlrev_b32_e32 v114, 16, v146
	v_and_b32_e32 v115, 0xffff0000, v146
	v_add_f32_e32 v102, v102, v114
	v_add_f32_e32 v103, v103, v115
	v_lshlrev_b32_e32 v114, 16, v147
	v_and_b32_e32 v115, 0xffff0000, v147
	v_add_f32_e32 v104, v104, v114
	v_add_f32_e32 v105, v105, v115
	v_lshlrev_b32_e32 v114, 16, v148
	v_and_b32_e32 v115, 0xffff0000, v148
	v_add_f32_e32 v114, v98, v114
	v_add_f32_e32 v115, v99, v115
	v_lshlrev_b32_e32 v98, 16, v149
	v_and_b32_e32 v99, 0xffff0000, v149
	v_mul_f32_e32 v108, v112, v112
	v_mul_f32_e32 v109, v113, v113
	v_mul_f32_e32 v112, v116, v116
	v_mul_f32_e32 v113, v117, v117
	v_add_f32_e32 v116, v100, v98
	v_add_f32_e32 v117, v101, v99
	v_cvt_pk_bf16_f32 v98, v102, v103
	v_cvt_pk_bf16_f32 v99, v104, v105
	v_cvt_pk_bf16_f32 v100, v114, v115
	v_cvt_pk_bf16_f32 v101, v116, v117
	global_store_dwordx4 v[118:119], v[98:101], off offset:256
	s_nop 1
	v_mul_f32_e32 v98, v102, v102
	v_mul_f32_e32 v99, v103, v103
	v_mul_f32_e32 v100, v104, v104
	v_mul_f32_e32 v101, v105, v105
	v_add_f32_e32 v98, v98, v99
	v_add_f32_e32 v100, v100, v101
	v_mul_f32_e32 v102, v114, v114
	v_mul_f32_e32 v103, v115, v115
	v_mul_f32_e32 v104, v116, v116
	v_mul_f32_e32 v105, v117, v117
	v_add_f32_e32 v98, v98, v100
	v_add_f32_e32 v99, v112, v113
	v_add_f32_e32 v100, v110, v111
	v_add_f32_e32 v104, v104, v105
	v_add_f32_e32 v102, v102, v103
	v_add_f32_e32 v99, v100, v99
	v_add_f32_e32 v100, v108, v109
	v_add_f32_e32 v101, v106, v107
	v_add_f32_e32 v102, v102, v104
	v_add_f32_e32 v100, v101, v100
	v_add_f32_e32 v98, v98, v102
	v_add_f32_e32 v99, v100, v99
	v_add_f32_e32 v98, v99, v98
	ds_bpermute_b32 v99, v168, v98
	s_waitcnt lgkmcnt(0)
	v_add_f32_e32 v98, v98, v99
	ds_bpermute_b32 v99, v167, v98
	s_and_saveexec_b64 s[16:17], vcc
	v_readlane_b32 s38, v253, 47
	v_readlane_b32 s91, v253, 27
	s_mov_b32 s89, 0x2e8ba2e9
	s_movk_i32 s90, 0xfea0
	s_mov_b32 s29, 0x47800000
	v_readlane_b32 s39, v253, 48
	s_cbranch_execz .LBB0_507
	v_lshl_or_b32 v100, v0, 4, s1
	s_waitcnt lgkmcnt(0)
	v_add_f32_e32 v98, v98, v99
	ds_write_b32 v100, v98 offset:256

.LBB0_545:
	s_mov_b32 s0, -1
	s_add_u32 s16, s74, 0x8800000
	s_waitcnt vmcnt(0)
	s_barrier
	s_addc_u32 s17, s75, 0
	v_mbcnt_lo_u32_b32 v0, s0, 0
	v_mbcnt_hi_u32_b32 v190, s0, v0
	s_lshl_b32 s14, s90, 8
	v_and_b32_e32 v193, 15, v190
	s_add_i32 s0, s14, s60
	s_ashr_i32 s37, s36, 31
	s_lshl_b32 s15, s61, 5
	v_or_b32_e32 v180, s0, v193
	s_lshl_b64 s[0:1], s[36:37], 8
	v_lshrrev_b32_e32 v0, 1, v190
	s_or_b32 s0, s0, s15
	v_and_b32_e32 v0, 56, v0
	v_lshl_add_u64 v[178:179], s[0:1], 0, v[0:1]
	v_readlane_b32 s0, v253, 47
	v_readlane_b32 s1, v253, 48
	v_ashrrev_i32_e32 v181, 31, v180
	v_lshlrev_b64 v[130:131], 12, v[180:181]
	v_lshl_add_u64 v[182:183], v[178:179], 2, s[0:1]
	v_lshl_add_u64 v[130:131], v[182:183], 0, v[130:131]
	global_load_dwordx4 v[200:203], v[130:131], off
	global_load_dwordx4 v[204:207], v[130:131], off offset:16
	global_load_dwordx4 v[208:211], v[130:131], off offset:512
	global_load_dwordx4 v[212:215], v[130:131], off offset:528
	v_or_b32_e32 v188, 16, v180
	v_or_b32_e32 v186, 32, v180
	v_or_b32_e32 v184, 48, v180
	v_ashrrev_i32_e32 v189, 31, v188
	v_ashrrev_i32_e32 v187, 31, v186
	v_ashrrev_i32_e32 v185, 31, v184
	v_lshlrev_b64 v[130:131], 12, v[188:189]
	v_lshlrev_b64 v[132:133], 12, v[186:187]
	v_lshlrev_b64 v[134:135], 12, v[184:185]
	v_lshl_add_u64 v[130:131], v[182:183], 0, v[130:131]
	v_lshl_add_u64 v[132:133], v[182:183], 0, v[132:133]
	v_lshl_add_u64 v[134:135], v[182:183], 0, v[134:135]
	global_load_dwordx4 v[170:173], v[130:131], off offset:16
	global_load_dwordx4 v[174:177], v[130:131], off
	global_load_dwordx4 v[162:165], v[130:131], off offset:528
	global_load_dwordx4 v[166:169], v[130:131], off offset:512
	global_load_dwordx4 v[154:157], v[132:133], off offset:16
	global_load_dwordx4 v[158:161], v[132:133], off
	global_load_dwordx4 v[146:149], v[132:133], off offset:528
	global_load_dwordx4 v[150:153], v[132:133], off offset:512
	global_load_dwordx4 v[138:141], v[134:135], off offset:16
	global_load_dwordx4 v[142:145], v[134:135], off
	s_nop 0
	global_load_dwordx4 v[130:133], v[134:135], off offset:528
	s_nop 0
	global_load_dwordx4 v[134:137], v[134:135], off offset:512
	v_and_b32_e32 v191, 64, v231
	v_xor_b32_e32 v0, 16, v231
	v_add_u32_e32 v191, 64, v191
	v_xor_b32_e32 v192, 32, v231
	v_cmp_lt_i32_e32 vcc, v0, v191
	v_lshlrev_b64 v[194:195], 11, v[180:181]
	s_lshl_b32 s15, s61, 2
	v_cndmask_b32_e32 v0, v231, v0, vcc
	v_cmp_lt_i32_e32 vcc, v192, v191
	s_waitcnt vmcnt(0)
	v_add_f32_e32 v128, v128, v202
	v_add_f32_e32 v129, v129, v203
	v_add_f32_e32 v126, v126, v200
	v_add_f32_e32 v127, v127, v201
	v_add_f32_e32 v124, v124, v206
	v_add_f32_e32 v125, v125, v207
	v_add_f32_e32 v122, v122, v204
	v_add_f32_e32 v123, v123, v205
	v_add_f32_e32 v200, v116, v214
	v_add_f32_e32 v201, v117, v215
	v_add_f32_e32 v202, v114, v212
	v_add_f32_e32 v203, v115, v213
	v_cvt_pk_bf16_f32 v114, v126, v127
	v_cvt_pk_bf16_f32 v115, v128, v129
	v_cvt_pk_bf16_f32 v116, v122, v123
	v_cvt_pk_bf16_f32 v117, v124, v125
	v_mul_f32_e32 v127, v127, v127
	v_mul_f32_e32 v129, v129, v129
	v_mul_f32_e32 v123, v123, v123
	v_mul_f32_e32 v125, v125, v125
	v_fmac_f32_e32 v127, v126, v126
	v_fmac_f32_e32 v129, v128, v128
	v_fmac_f32_e32 v123, v122, v122
	v_fmac_f32_e32 v125, v124, v124
	v_add_f32_e32 v120, v120, v210
	v_add_f32_e32 v121, v121, v211
	v_add_f32_e32 v118, v118, v208
	v_add_f32_e32 v119, v119, v209
	v_add_f32_e32 v122, v127, v129
	v_add_f32_e32 v123, v123, v125
	v_cndmask_b32_e32 v191, v231, v192, vcc
	v_lshlrev_b32_e32 v192, 2, v0
	v_or_b32_e32 v0, s60, v193
	v_mul_f32_e32 v181, v119, v119
	v_mul_f32_e32 v193, v121, v121
	v_mul_f32_e32 v204, v203, v203
	v_add_f32_e32 v122, v122, v123
	v_mul_f32_e32 v123, v201, v201
	v_fmac_f32_e32 v181, v118, v118
	v_fmac_f32_e32 v193, v120, v120
	v_fmac_f32_e32 v204, v202, v202
	v_fmac_f32_e32 v123, v200, v200
	v_add_f32_e32 v124, v181, v193
	v_add_f32_e32 v123, v204, v123
	v_add_f32_e32 v123, v124, v123
	v_add_f32_e32 v124, v122, v123
	ds_bpermute_b32 v125, v192, v124
	v_lshl_add_u64 v[122:123], s[16:17], 0, v[194:195]
	v_lshl_add_u64 v[122:123], v[178:179], 1, v[122:123]
	v_lshlrev_b32_e32 v191, 2, v191
	global_store_dwordx4 v[122:123], v[114:117], off
	v_cmp_gt_u32_e32 vcc, 16, v190
	s_waitcnt lgkmcnt(0)
	v_add_f32_e32 v114, v124, v125
	ds_bpermute_b32 v115, v191, v114
	v_cvt_pk_bf16_f32 v116, v118, v119
	v_cvt_pk_bf16_f32 v117, v120, v121
	v_cvt_pk_bf16_f32 v118, v202, v203
	v_cvt_pk_bf16_f32 v119, v200, v201
	global_store_dwordx4 v[122:123], v[116:119], off offset:256
	s_and_saveexec_b64 s[0:1], vcc
	s_cbranch_execz .LBB0_547
	v_lshl_or_b32 v116, v0, 4, s15
	s_waitcnt lgkmcnt(0)
	v_add_f32_e32 v114, v114, v115
	ds_write_b32 v116, v114
.LBB0_547:
	s_or_b64 exec, exec, s[0:1]
	v_add_f32_e32 v110, v110, v174
	v_add_f32_e32 v111, v111, v175
	v_add_f32_e32 v112, v112, v176
	v_add_f32_e32 v113, v113, v177
	v_add_f32_e32 v118, v106, v170
	v_add_f32_e32 v119, v107, v171
	v_cvt_pk_bf16_f32 v106, v110, v111
	v_mul_f32_e32 v111, v111, v111
	v_fmac_f32_e32 v111, v110, v110
	v_mul_f32_e32 v110, v113, v113
	v_add_f32_e32 v116, v108, v172
	v_add_f32_e32 v117, v109, v173
	v_fmac_f32_e32 v110, v112, v112
	v_cvt_pk_bf16_f32 v107, v112, v113
	v_add_f32_e32 v110, v111, v110
	v_mul_f32_e32 v111, v119, v119
	v_mul_f32_e32 v112, v117, v117
	v_fmac_f32_e32 v111, v118, v118
	v_fmac_f32_e32 v112, v116, v116
	v_add_f32_e32 v104, v104, v168
	v_add_f32_e32 v105, v105, v169
	v_add_f32_e32 v102, v102, v166
	v_add_f32_e32 v103, v103, v167
	v_add_f32_e32 v111, v111, v112
	v_add_f32_e32 v112, v98, v162
	v_add_f32_e32 v113, v99, v163
	v_mul_f32_e32 v98, v103, v103
	v_mul_f32_e32 v99, v105, v105
	v_cvt_pk_bf16_f32 v109, v116, v117
	v_add_f32_e32 v116, v110, v111
	v_add_f32_e32 v110, v100, v164
	v_add_f32_e32 v111, v101, v165
	v_fmac_f32_e32 v98, v102, v102
	v_fmac_f32_e32 v99, v104, v104
	v_add_f32_e32 v98, v98, v99
	v_mul_f32_e32 v99, v113, v113
	v_mul_f32_e32 v100, v111, v111
	v_fmac_f32_e32 v99, v112, v112
	v_fmac_f32_e32 v100, v110, v110
	v_add_f32_e32 v99, v99, v100
	v_add_f32_e32 v98, v98, v99
	v_add_f32_e32 v101, v116, v98
	ds_bpermute_b32 v116, v192, v101
	s_waitcnt lgkmcnt(1)
	v_lshlrev_b64 v[114:115], 11, v[188:189]
	v_lshl_add_u64 v[98:99], s[16:17], 0, v[114:115]
	v_lshl_add_u64 v[114:115], v[178:179], 1, v[98:99]
	v_cvt_pk_bf16_f32 v108, v118, v119
	s_waitcnt lgkmcnt(0)
	v_add_f32_e32 v98, v101, v116
	ds_bpermute_b32 v99, v191, v98
	v_cvt_pk_bf16_f32 v100, v102, v103
	v_cvt_pk_bf16_f32 v101, v104, v105
	v_cvt_pk_bf16_f32 v102, v112, v113
	v_cvt_pk_bf16_f32 v103, v110, v111
	global_store_dwordx4 v[114:115], v[106:109], off
	global_store_dwordx4 v[114:115], v[100:103], off offset:256
	s_and_saveexec_b64 s[0:1], vcc
	v_readlane_b32 s91, v253, 27
	s_mov_b32 s89, 0x2e8ba2e9
	s_movk_i32 s90, 0xfea0
	s_mov_b32 s29, 0x47800000
	s_cbranch_execz .LBB0_549
	v_lshl_or_b32 v100, v0, 4, s15
	s_waitcnt lgkmcnt(0)
	v_add_f32_e32 v98, v98, v99
	ds_write_b32 v100, v98 offset:256
.LBB0_549:
	s_or_b64 exec, exec, s[0:1]
	v_add_f32_e32 v94, v94, v158
	v_add_f32_e32 v95, v95, v159
	v_add_f32_e32 v96, v96, v160
	v_add_f32_e32 v97, v97, v161
	v_add_f32_e32 v102, v90, v154
	v_add_f32_e32 v103, v91, v155
	v_cvt_pk_bf16_f32 v90, v94, v95
	v_mul_f32_e32 v95, v95, v95
	v_fmac_f32_e32 v95, v94, v94
	v_mul_f32_e32 v94, v97, v97
	v_add_f32_e32 v100, v92, v156
	v_add_f32_e32 v101, v93, v157
	v_fmac_f32_e32 v94, v96, v96
	v_cvt_pk_bf16_f32 v91, v96, v97
	v_add_f32_e32 v94, v95, v94
	v_mul_f32_e32 v95, v103, v103
	v_mul_f32_e32 v96, v101, v101
	v_fmac_f32_e32 v95, v102, v102
	v_fmac_f32_e32 v96, v100, v100
	v_add_f32_e32 v88, v88, v152
	v_add_f32_e32 v89, v89, v153
	v_add_f32_e32 v86, v86, v150
	v_add_f32_e32 v87, v87, v151
	v_add_f32_e32 v95, v95, v96
	v_add_f32_e32 v96, v82, v146
	v_add_f32_e32 v97, v83, v147
	v_mul_f32_e32 v82, v87, v87
	v_mul_f32_e32 v83, v89, v89
	v_cvt_pk_bf16_f32 v93, v100, v101
	v_add_f32_e32 v100, v94, v95
	v_add_f32_e32 v94, v84, v148
	v_add_f32_e32 v95, v85, v149
	v_fmac_f32_e32 v82, v86, v86
	v_fmac_f32_e32 v83, v88, v88
	v_add_f32_e32 v82, v82, v83
	v_mul_f32_e32 v83, v97, v97
	v_mul_f32_e32 v84, v95, v95
	v_fmac_f32_e32 v83, v96, v96
	v_fmac_f32_e32 v84, v94, v94
	v_add_f32_e32 v83, v83, v84
	v_add_f32_e32 v82, v82, v83
	v_add_f32_e32 v85, v100, v82
	ds_bpermute_b32 v100, v192, v85
	s_waitcnt lgkmcnt(1)
	v_lshlrev_b64 v[98:99], 11, v[186:187]
	v_lshl_add_u64 v[82:83], s[16:17], 0, v[98:99]
	v_lshl_add_u64 v[98:99], v[178:179], 1, v[82:83]
	v_cvt_pk_bf16_f32 v92, v102, v103
	s_waitcnt lgkmcnt(0)
	v_add_f32_e32 v82, v85, v100
	ds_bpermute_b32 v83, v191, v82
	v_cvt_pk_bf16_f32 v84, v86, v87
	v_cvt_pk_bf16_f32 v85, v88, v89
	v_cvt_pk_bf16_f32 v86, v96, v97
	v_cvt_pk_bf16_f32 v87, v94, v95
	global_store_dwordx4 v[98:99], v[90:93], off
	global_store_dwordx4 v[98:99], v[84:87], off offset:256
	s_and_saveexec_b64 s[0:1], vcc
	s_cbranch_execz .LBB0_551
	v_lshl_or_b32 v84, v0, 4, s15
	s_waitcnt lgkmcnt(0)
	v_add_f32_e32 v82, v82, v83
	ds_write_b32 v84, v82 offset:512
.LBB0_551:
	s_or_b64 exec, exec, s[0:1]
	v_add_f32_e32 v78, v78, v142
	v_add_f32_e32 v79, v79, v143
	v_add_f32_e32 v80, v80, v144
	v_add_f32_e32 v81, v81, v145
	v_add_f32_e32 v86, v74, v138
	v_add_f32_e32 v87, v75, v139
	v_cvt_pk_bf16_f32 v74, v78, v79
	v_mul_f32_e32 v79, v79, v79
	v_fmac_f32_e32 v79, v78, v78
	v_mul_f32_e32 v78, v81, v81
	v_add_f32_e32 v84, v76, v140
	v_add_f32_e32 v85, v77, v141
	v_fmac_f32_e32 v78, v80, v80
	v_cvt_pk_bf16_f32 v75, v80, v81
	v_add_f32_e32 v78, v79, v78
	v_mul_f32_e32 v79, v87, v87
	v_mul_f32_e32 v80, v85, v85
	v_fmac_f32_e32 v79, v86, v86
	v_fmac_f32_e32 v80, v84, v84
	v_add_f32_e32 v72, v72, v136
	v_add_f32_e32 v73, v73, v137
	v_add_f32_e32 v70, v70, v134
	v_add_f32_e32 v71, v71, v135
	v_add_f32_e32 v79, v79, v80
	v_add_f32_e32 v80, v66, v130
	v_add_f32_e32 v81, v67, v131
	v_mul_f32_e32 v66, v71, v71
	v_mul_f32_e32 v67, v73, v73
	v_cvt_pk_bf16_f32 v77, v84, v85
	v_add_f32_e32 v84, v78, v79
	v_add_f32_e32 v78, v68, v132
	v_add_f32_e32 v79, v69, v133
	v_fmac_f32_e32 v66, v70, v70
	v_fmac_f32_e32 v67, v72, v72
	v_add_f32_e32 v66, v66, v67
	v_mul_f32_e32 v67, v81, v81
	v_mul_f32_e32 v68, v79, v79
	v_fmac_f32_e32 v67, v80, v80
	v_fmac_f32_e32 v68, v78, v78
	v_add_f32_e32 v67, v67, v68
	v_add_f32_e32 v66, v66, v67
	v_add_f32_e32 v69, v84, v66
	ds_bpermute_b32 v84, v192, v69
	s_waitcnt lgkmcnt(1)
	v_lshlrev_b64 v[82:83], 11, v[184:185]
	v_lshl_add_u64 v[66:67], s[16:17], 0, v[82:83]
	v_lshl_add_u64 v[82:83], v[178:179], 1, v[66:67]
	v_cvt_pk_bf16_f32 v76, v86, v87
	s_waitcnt lgkmcnt(0)
	v_add_f32_e32 v66, v69, v84
	ds_bpermute_b32 v67, v191, v66
	v_cvt_pk_bf16_f32 v68, v70, v71
	v_cvt_pk_bf16_f32 v69, v72, v73
	v_cvt_pk_bf16_f32 v70, v80, v81
	v_cvt_pk_bf16_f32 v71, v78, v79
	global_store_dwordx4 v[82:83], v[74:77], off
	global_store_dwordx4 v[82:83], v[68:71], off offset:256
	s_and_saveexec_b64 s[0:1], vcc
	s_cbranch_execz .LBB0_553
	v_lshl_or_b32 v68, v0, 4, s15
	s_waitcnt lgkmcnt(0)
	v_add_f32_e32 v66, v66, v67
	ds_write_b32 v68, v66 offset:768
.LBB0_553:
	s_or_b64 exec, exec, s[0:1]
	v_add_u32_e32 v136, 0x80, v180
	v_ashrrev_i32_e32 v137, 31, v136
	s_waitcnt lgkmcnt(0)
	v_lshlrev_b64 v[66:67], 12, v[136:137]
	v_lshl_add_u64 v[66:67], v[182:183], 0, v[66:67]
	global_load_dwordx4 v[120:123], v[66:67], off
	global_load_dwordx4 v[124:127], v[66:67], off offset:16
	global_load_dwordx4 v[128:131], v[66:67], off offset:512
	global_load_dwordx4 v[132:135], v[66:67], off offset:528
	v_add_u32_e32 v118, 0x90, v180
	v_add_u32_e32 v116, 0xa0, v180
	v_add_u32_e32 v114, 0xb0, v180
	v_ashrrev_i32_e32 v119, 31, v118
	v_ashrrev_i32_e32 v117, 31, v116
	v_ashrrev_i32_e32 v115, 31, v114
	v_lshlrev_b64 v[66:67], 12, v[118:119]
	v_lshlrev_b64 v[68:69], 12, v[116:117]
	v_lshlrev_b64 v[70:71], 12, v[114:115]
	v_lshl_add_u64 v[66:67], v[182:183], 0, v[66:67]
	v_lshl_add_u64 v[68:69], v[182:183], 0, v[68:69]
	v_lshl_add_u64 v[70:71], v[182:183], 0, v[70:71]
	global_load_dwordx4 v[106:109], v[66:67], off offset:16
	global_load_dwordx4 v[110:113], v[66:67], off
	global_load_dwordx4 v[98:101], v[66:67], off offset:528
	global_load_dwordx4 v[102:105], v[66:67], off offset:512
	global_load_dwordx4 v[90:93], v[68:69], off offset:16
	global_load_dwordx4 v[94:97], v[68:69], off
	global_load_dwordx4 v[82:85], v[68:69], off offset:528
	global_load_dwordx4 v[86:89], v[68:69], off offset:512
	global_load_dwordx4 v[74:77], v[70:71], off offset:16
	global_load_dwordx4 v[78:81], v[70:71], off
	s_nop 0
	global_load_dwordx4 v[66:69], v[70:71], off offset:528
	s_nop 0
	global_load_dwordx4 v[70:73], v[70:71], off offset:512
	v_lshlrev_b64 v[136:137], 11, v[136:137]
	s_waitcnt vmcnt(15)
	v_add_f32_e32 v64, v64, v122
	v_add_f32_e32 v65, v65, v123
	v_add_f32_e32 v62, v62, v120
	v_add_f32_e32 v63, v63, v121
	s_waitcnt vmcnt(14)
	v_add_f32_e32 v60, v60, v126
	v_add_f32_e32 v61, v61, v127
	v_add_f32_e32 v58, v58, v124
	v_add_f32_e32 v59, v59, v125
	s_waitcnt vmcnt(13)
	v_add_f32_e32 v56, v56, v130
	v_add_f32_e32 v57, v57, v131
	v_add_f32_e32 v54, v54, v128
	v_add_f32_e32 v55, v55, v129
	s_waitcnt vmcnt(12)
	v_add_f32_e32 v120, v52, v134
	v_add_f32_e32 v121, v53, v135
	v_add_f32_e32 v122, v50, v132
	v_add_f32_e32 v123, v51, v133
	v_cvt_pk_bf16_f32 v50, v62, v63
	v_cvt_pk_bf16_f32 v51, v64, v65
	v_cvt_pk_bf16_f32 v52, v58, v59
	v_cvt_pk_bf16_f32 v53, v60, v61
	v_mul_f32_e32 v63, v63, v63
	v_mul_f32_e32 v65, v65, v65
	v_mul_f32_e32 v59, v59, v59
	v_mul_f32_e32 v61, v61, v61
	v_mul_f32_e32 v124, v55, v55
	v_mul_f32_e32 v125, v57, v57
	v_mul_f32_e32 v126, v123, v123
	v_mul_f32_e32 v127, v121, v121
	v_fmac_f32_e32 v63, v62, v62
	v_fmac_f32_e32 v65, v64, v64
	v_fmac_f32_e32 v59, v58, v58
	v_fmac_f32_e32 v61, v60, v60
	v_fmac_f32_e32 v124, v54, v54
	v_fmac_f32_e32 v125, v56, v56
	v_fmac_f32_e32 v126, v122, v122
	v_fmac_f32_e32 v127, v120, v120
	v_add_f32_e32 v58, v63, v65
	v_add_f32_e32 v59, v59, v61
	v_add_f32_e32 v60, v124, v125
	v_add_f32_e32 v61, v126, v127
	v_add_f32_e32 v58, v58, v59
	v_add_f32_e32 v59, v60, v61
	v_add_f32_e32 v60, v58, v59
	ds_bpermute_b32 v61, v192, v60
	v_lshl_add_u64 v[58:59], s[16:17], 0, v[136:137]
	v_lshl_add_u64 v[58:59], v[178:179], 1, v[58:59]
	global_store_dwordx4 v[58:59], v[50:53], off
	s_waitcnt lgkmcnt(0)
	s_nop 0
	v_add_f32_e32 v50, v60, v61
	ds_bpermute_b32 v51, v191, v50
	v_cvt_pk_bf16_f32 v52, v54, v55
	v_cvt_pk_bf16_f32 v53, v56, v57
	v_cvt_pk_bf16_f32 v54, v122, v123
	v_cvt_pk_bf16_f32 v55, v120, v121
	global_store_dwordx4 v[58:59], v[52:55], off offset:256
	s_and_saveexec_b64 s[0:1], vcc
	s_cbranch_execz .LBB0_555
	v_lshl_or_b32 v52, v0, 4, s15
	s_waitcnt lgkmcnt(0)
	v_add_f32_e32 v50, v50, v51
	ds_write_b32 v52, v50 offset:2048
.LBB0_555:
	s_or_b64 exec, exec, s[0:1]
	s_waitcnt vmcnt(12)
	v_add_f32_e32 v46, v46, v110
	v_add_f32_e32 v47, v47, v111
	v_add_f32_e32 v48, v48, v112
	v_add_f32_e32 v49, v49, v113
	v_add_f32_e32 v54, v42, v106
	v_add_f32_e32 v55, v43, v107
	v_cvt_pk_bf16_f32 v42, v46, v47
	v_mul_f32_e32 v47, v47, v47
	v_fmac_f32_e32 v47, v46, v46
	v_mul_f32_e32 v46, v49, v49
	v_add_f32_e32 v52, v44, v108
	v_add_f32_e32 v53, v45, v109
	v_fmac_f32_e32 v46, v48, v48
	v_cvt_pk_bf16_f32 v43, v48, v49
	v_add_f32_e32 v46, v47, v46
	v_mul_f32_e32 v47, v55, v55
	v_mul_f32_e32 v48, v53, v53
	v_fmac_f32_e32 v47, v54, v54
	v_fmac_f32_e32 v48, v52, v52
	s_waitcnt vmcnt(10)
	v_add_f32_e32 v40, v40, v104
	v_add_f32_e32 v41, v41, v105
	v_add_f32_e32 v38, v38, v102
	v_add_f32_e32 v39, v39, v103
	v_add_f32_e32 v47, v47, v48
	v_add_f32_e32 v48, v34, v98
	v_add_f32_e32 v49, v35, v99
	v_mul_f32_e32 v34, v39, v39
	v_mul_f32_e32 v35, v41, v41
	v_cvt_pk_bf16_f32 v45, v52, v53
	v_add_f32_e32 v52, v46, v47
	v_add_f32_e32 v46, v36, v100
	v_add_f32_e32 v47, v37, v101
	v_fmac_f32_e32 v34, v38, v38
	v_fmac_f32_e32 v35, v40, v40
	v_add_f32_e32 v34, v34, v35
	v_mul_f32_e32 v35, v49, v49
	v_mul_f32_e32 v36, v47, v47
	v_fmac_f32_e32 v35, v48, v48
	v_fmac_f32_e32 v36, v46, v46
	v_add_f32_e32 v35, v35, v36
	v_add_f32_e32 v34, v34, v35
	v_add_f32_e32 v37, v52, v34
	ds_bpermute_b32 v52, v192, v37
	s_waitcnt lgkmcnt(1)
	v_lshlrev_b64 v[50:51], 11, v[118:119]
	v_lshl_add_u64 v[34:35], s[16:17], 0, v[50:51]
	v_lshl_add_u64 v[50:51], v[178:179], 1, v[34:35]
	v_cvt_pk_bf16_f32 v44, v54, v55
	s_waitcnt lgkmcnt(0)
	v_add_f32_e32 v34, v37, v52
	ds_bpermute_b32 v35, v191, v34
	v_cvt_pk_bf16_f32 v36, v38, v39
	v_cvt_pk_bf16_f32 v37, v40, v41
	v_cvt_pk_bf16_f32 v38, v48, v49
	v_cvt_pk_bf16_f32 v39, v46, v47
	global_store_dwordx4 v[50:51], v[42:45], off
	global_store_dwordx4 v[50:51], v[36:39], off offset:256
	s_and_saveexec_b64 s[0:1], vcc
	s_cbranch_execz .LBB0_557
	v_lshl_or_b32 v36, v0, 4, s15
	s_waitcnt lgkmcnt(0)
	v_add_f32_e32 v34, v34, v35
	ds_write_b32 v36, v34 offset:2304
.LBB0_557:
	s_or_b64 exec, exec, s[0:1]
	s_waitcnt vmcnt(10)
	v_add_f32_e32 v30, v30, v94
	v_add_f32_e32 v31, v31, v95
	v_add_f32_e32 v32, v32, v96
	v_add_f32_e32 v33, v33, v97
	v_add_f32_e32 v38, v26, v90
	v_add_f32_e32 v39, v27, v91
	v_cvt_pk_bf16_f32 v26, v30, v31
	v_mul_f32_e32 v31, v31, v31
	v_fmac_f32_e32 v31, v30, v30
	v_mul_f32_e32 v30, v33, v33
	v_add_f32_e32 v36, v28, v92
	v_add_f32_e32 v37, v29, v93
	v_fmac_f32_e32 v30, v32, v32
	v_cvt_pk_bf16_f32 v27, v32, v33
	v_add_f32_e32 v30, v31, v30
	v_mul_f32_e32 v31, v39, v39
	v_mul_f32_e32 v32, v37, v37
	v_fmac_f32_e32 v31, v38, v38
	v_fmac_f32_e32 v32, v36, v36
	s_waitcnt vmcnt(8)
	v_add_f32_e32 v24, v24, v88
	v_add_f32_e32 v25, v25, v89
	v_add_f32_e32 v22, v22, v86
	v_add_f32_e32 v23, v23, v87
	v_add_f32_e32 v31, v31, v32
	v_add_f32_e32 v32, v18, v82
	v_add_f32_e32 v33, v19, v83
	v_mul_f32_e32 v18, v23, v23
	v_mul_f32_e32 v19, v25, v25
	v_cvt_pk_bf16_f32 v29, v36, v37
	v_add_f32_e32 v36, v30, v31
	v_add_f32_e32 v30, v20, v84
	v_add_f32_e32 v31, v21, v85
	v_fmac_f32_e32 v18, v22, v22
	v_fmac_f32_e32 v19, v24, v24
	v_add_f32_e32 v18, v18, v19
	v_mul_f32_e32 v19, v33, v33
	v_mul_f32_e32 v20, v31, v31
	v_fmac_f32_e32 v19, v32, v32
	v_fmac_f32_e32 v20, v30, v30
	v_add_f32_e32 v19, v19, v20
	v_add_f32_e32 v18, v18, v19
	v_add_f32_e32 v21, v36, v18
	ds_bpermute_b32 v36, v192, v21
	s_waitcnt lgkmcnt(1)
	v_lshlrev_b64 v[34:35], 11, v[116:117]
	v_lshl_add_u64 v[18:19], s[16:17], 0, v[34:35]
	v_lshl_add_u64 v[34:35], v[178:179], 1, v[18:19]
	v_cvt_pk_bf16_f32 v28, v38, v39
	s_waitcnt lgkmcnt(0)
	v_add_f32_e32 v18, v21, v36
	ds_bpermute_b32 v19, v191, v18
	v_cvt_pk_bf16_f32 v20, v22, v23
	v_cvt_pk_bf16_f32 v21, v24, v25
	v_cvt_pk_bf16_f32 v22, v32, v33
	v_cvt_pk_bf16_f32 v23, v30, v31
	global_store_dwordx4 v[34:35], v[26:29], off
	global_store_dwordx4 v[34:35], v[20:23], off offset:256
	s_and_saveexec_b64 s[0:1], vcc
	s_cbranch_execz .LBB0_559
	v_lshl_or_b32 v20, v0, 4, s15
	s_waitcnt lgkmcnt(0)
	v_add_f32_e32 v18, v18, v19
	ds_write_b32 v20, v18 offset:2560
.LBB0_559:
	s_or_b64 exec, exec, s[0:1]
	s_waitcnt vmcnt(8)
	v_add_f32_e32 v14, v14, v78
	v_add_f32_e32 v15, v15, v79
	v_add_f32_e32 v16, v16, v80
	v_add_f32_e32 v17, v17, v81
	v_add_f32_e32 v22, v10, v74
	v_add_f32_e32 v23, v11, v75
	v_cvt_pk_bf16_f32 v10, v14, v15
	v_mul_f32_e32 v15, v15, v15
	v_fmac_f32_e32 v15, v14, v14
	v_mul_f32_e32 v14, v17, v17
	v_add_f32_e32 v20, v12, v76
	v_add_f32_e32 v21, v13, v77
	v_fmac_f32_e32 v14, v16, v16
	v_cvt_pk_bf16_f32 v11, v16, v17
	v_add_f32_e32 v14, v15, v14
	v_mul_f32_e32 v15, v23, v23
	v_mul_f32_e32 v16, v21, v21
	v_fmac_f32_e32 v15, v22, v22
	v_fmac_f32_e32 v16, v20, v20
	s_waitcnt vmcnt(6)
	v_add_f32_e32 v8, v8, v72
	v_add_f32_e32 v9, v9, v73
	v_add_f32_e32 v6, v6, v70
	v_add_f32_e32 v7, v7, v71
	v_add_f32_e32 v15, v15, v16
	v_add_f32_e32 v16, v2, v66
	v_add_f32_e32 v17, v3, v67
	v_mul_f32_e32 v2, v7, v7
	v_mul_f32_e32 v3, v9, v9
	v_cvt_pk_bf16_f32 v13, v20, v21
	v_add_f32_e32 v20, v14, v15
	v_add_f32_e32 v14, v4, v68
	v_add_f32_e32 v15, v5, v69
	v_fmac_f32_e32 v2, v6, v6
	v_fmac_f32_e32 v3, v8, v8
	v_add_f32_e32 v2, v2, v3
	v_mul_f32_e32 v3, v17, v17
	v_mul_f32_e32 v4, v15, v15
	v_fmac_f32_e32 v3, v16, v16
	v_fmac_f32_e32 v4, v14, v14
	v_add_f32_e32 v3, v3, v4
	v_add_f32_e32 v2, v2, v3
	v_add_f32_e32 v5, v20, v2
	ds_bpermute_b32 v20, v192, v5
	s_waitcnt lgkmcnt(1)
	v_lshlrev_b64 v[18:19], 11, v[114:115]
	v_lshl_add_u64 v[2:3], s[16:17], 0, v[18:19]
	v_lshl_add_u64 v[18:19], v[178:179], 1, v[2:3]
	v_cvt_pk_bf16_f32 v12, v22, v23
	s_waitcnt lgkmcnt(0)
	v_add_f32_e32 v2, v5, v20
	ds_bpermute_b32 v3, v191, v2
	v_cvt_pk_bf16_f32 v4, v6, v7
	v_cvt_pk_bf16_f32 v5, v8, v9
	v_cvt_pk_bf16_f32 v6, v16, v17
	v_cvt_pk_bf16_f32 v7, v14, v15
	global_store_dwordx4 v[18:19], v[10:13], off
	global_store_dwordx4 v[18:19], v[4:7], off offset:256
	s_and_saveexec_b64 s[0:1], vcc
	s_cbranch_execz .LBB0_561
	v_lshl_or_b32 v0, v0, 4, s15
	s_waitcnt lgkmcnt(0)
	v_add_f32_e32 v2, v2, v3
	ds_write_b32 v0, v2 offset:2816

.LBB0_582:
	v_lshrrev_b64 v[8:9], 8, v[6:7]
	v_and_b32_e32 v8, -4, v8
	v_lshl_add_u64 v[8:9], s[48:49], 0, v[8:9]
	global_load_dword v0, v[8:9], off
	s_nop 0
	global_load_dwordx4 v[8:11], v[2:3], off
	v_lshl_add_u64 v[6:7], v[6:7], 0, s[4:5]
	s_mov_b64 s[54:55], 0xfffff
	v_cmp_lt_u64_e32 vcc, s[54:55], v[6:7]
	v_lshl_add_u64 v[2:3], v[2:3], 0, s[68:69]
	s_or_b64 s[50:51], vcc, s[50:51]
	s_waitcnt vmcnt(0)
	v_mul_f32_e32 v8, v0, v8
	v_mul_f32_e32 v9, v0, v9
	v_mul_f32_e32 v10, v0, v10
	v_mul_f32_e32 v11, v0, v11
	v_cvt_pk_bf16_f32 v8, v8, v9
	v_cvt_pk_bf16_f32 v9, v10, v11
	global_store_dwordx2 v[4:5], v[8:9], off
	v_lshl_add_u64 v[4:5], v[4:5], 0, s[8:9]
	s_andn2_b64 exec, exec, s[50:51]
	s_cbranch_execnz .LBB0_582

.LBB0_591:
	global_load_dwordx4 v[2:5], v[36:37], off offset:-2048
	s_add_i32 s29, s29, s72
	s_cmpk_lt_i32 s29, 0x200
	s_waitcnt vmcnt(0)
	v_mul_f32_e32 v6, v4, v4
	v_mul_f32_e32 v7, v5, v5
	v_mul_f32_e32 v8, v2, v2
	v_mul_f32_e32 v9, v3, v3
	s_nop 0
	v_pk_mov_b32 v[10:11], v[8:9], v[6:7] op_sel:[1,0]
	v_mov_b32_e32 v9, v7
	v_add_f32_e32 v48, v10, v8
	v_add_f32_e32 v49, v11, v9
	global_load_dwordx4 v[10:13], v[36:37], off offset:-1024
	v_pk_add_f32 v[48:49], v[48:49], v[48:49] op_sel:[0,1] op_sel_hi:[1,0]
	s_waitcnt vmcnt(0)
	v_mul_f32_e32 v6, v12, v12
	v_mul_f32_e32 v7, v13, v13
	v_mul_f32_e32 v8, v10, v10
	v_mul_f32_e32 v9, v11, v11
	s_nop 0
	v_pk_mov_b32 v[14:15], v[8:9], v[6:7] op_sel:[1,0]
	v_mov_b32_e32 v9, v7
	v_add_f32_e32 v50, v14, v8
	v_add_f32_e32 v51, v15, v9
	global_load_dwordx4 v[14:17], v[36:37], off
	global_load_dwordx4 v[6:9], v[36:37], off offset:1024
	v_pk_add_f32 v[50:51], v[50:51], v[50:51] op_sel:[0,1] op_sel_hi:[1,0]
	v_lshl_add_u64 v[36:37], v[36:37], 0, s[76:77]
	s_waitcnt vmcnt(0)
	v_mul_f32_e32 v0, v6, v6
	v_mul_f32_e32 v52, v7, v7
	v_mov_b32_e32 v49, v0
	v_mov_b32_e32 v51, v52
	v_mul_f32_e32 v0, v15, v15
	v_mul_f32_e32 v53, v8, v8
	v_add_f32_e32 v48, v48, v50
	v_add_f32_e32 v49, v49, v51
	v_fma_f32 v50, v14, v14, v0
	v_fma_f32 v51, v15, v15, v0
	v_mul_f32_e32 v0, v17, v17
	v_mul_f32_e32 v54, v9, v9
	v_mov_b32_e32 v51, v53
	v_fma_f32 v52, v16, v16, v0
	v_fma_f32 v53, v17, v17, v0
	s_nop 0
	v_mov_b32_e32 v53, v54
	v_add_f32_e32 v50, v50, v52
	v_add_f32_e32 v51, v51, v53
	s_nop 0
	v_add_f32_e32 v48, v48, v50
	v_add_f32_e32 v49, v49, v51
	s_nop 0
	v_add_f32_e32 v0, v48, v49
	ds_bpermute_b32 v48, v42, v0
	s_waitcnt lgkmcnt(0)
	v_add_f32_e32 v0, v0, v48
	ds_bpermute_b32 v48, v43, v0
	s_waitcnt lgkmcnt(0)
	v_add_f32_e32 v0, v0, v48
	ds_bpermute_b32 v48, v44, v0
	s_waitcnt lgkmcnt(0)
	v_add_f32_e32 v0, v0, v48
	ds_bpermute_b32 v48, v45, v0
	s_waitcnt lgkmcnt(0)
	v_add_f32_e32 v0, v0, v48
	ds_bpermute_b32 v48, v46, v0
	s_waitcnt lgkmcnt(0)
	v_add_f32_e32 v0, v0, v48
	ds_bpermute_b32 v48, v47, v0
	s_waitcnt lgkmcnt(0)
	v_add_f32_e32 v0, v0, v48
	v_fmamk_f32 v0, v0, 0x3a800000, v196
	v_cmp_gt_f32_e32 vcc, s96, v0
	v_mul_f32_e32 v48, 0x4b800000, v0
	s_nop 0
	v_cndmask_b32_e32 v0, v0, v48, vcc
	v_rsq_f32_e32 v0, v0
	s_nop 0
	v_mul_f32_e32 v48, 0x45800000, v0
	v_cndmask_b32_e32 v0, v0, v48, vcc
	global_load_dwordx4 v[48:51], v[34:35], off
	v_mul_f32_e32 v2, v2, v0
	v_mul_f32_e32 v3, v3, v0
	v_mul_f32_e32 v4, v4, v0
	v_mul_f32_e32 v5, v5, v0
	v_mul_f32_e32 v10, v10, v0
	v_mul_f32_e32 v11, v11, v0
	v_mul_f32_e32 v6, v6, v0
	v_mul_f32_e32 v7, v7, v0
	s_waitcnt vmcnt(0)
	v_mul_f32_e32 v2, v48, v2
	v_mul_f32_e32 v3, v49, v3
	v_mul_f32_e32 v4, v50, v4
	v_mul_f32_e32 v5, v51, v5
	v_cvt_pk_bf16_f32 v2, v2, v3
	v_cvt_pk_bf16_f32 v3, v4, v5
	global_store_dwordx2 v[38:39], v[2:3], off offset:-1024
	global_load_dwordx4 v[2:5], v[34:35], off offset:1024
	s_waitcnt vmcnt(0)
	v_mul_f32_e32 v2, v2, v10
	v_mul_f32_e32 v3, v3, v11
	v_mul_f32_e32 v10, v12, v0
	v_mul_f32_e32 v11, v13, v0
	v_cvt_pk_bf16_f32 v2, v2, v3
	v_mul_f32_e32 v4, v4, v10
	v_mul_f32_e32 v5, v5, v11
	v_mul_f32_e32 v10, v14, v0
	v_mul_f32_e32 v11, v15, v0
	v_cvt_pk_bf16_f32 v3, v4, v5
	global_store_dwordx2 v[38:39], v[2:3], off offset:-512
	global_load_dwordx4 v[2:5], v[34:35], off offset:2048
	s_waitcnt vmcnt(0)
	v_mul_f32_e32 v2, v2, v10
	v_mul_f32_e32 v3, v3, v11
	v_mul_f32_e32 v10, v16, v0
	v_mul_f32_e32 v11, v17, v0
	v_cvt_pk_bf16_f32 v2, v2, v3
	v_mul_f32_e32 v4, v4, v10
	v_mul_f32_e32 v5, v5, v11
	s_nop 0
	v_cvt_pk_bf16_f32 v3, v4, v5
	global_store_dwordx2 v[38:39], v[2:3], off
	global_load_dwordx4 v[2:5], v[34:35], off offset:3072
	s_waitcnt vmcnt(0)
	v_mul_f32_e32 v2, v2, v6
	v_mul_f32_e32 v3, v3, v7
	v_mul_f32_e32 v6, v8, v0
	v_mul_f32_e32 v7, v9, v0
	v_cvt_pk_bf16_f32 v2, v2, v3
	v_mul_f32_e32 v4, v4, v6
	v_mul_f32_e32 v5, v5, v7
	s_nop 0
	v_cvt_pk_bf16_f32 v3, v4, v5
	global_store_dwordx2 v[38:39], v[2:3], off offset:512
	v_lshl_add_u64 v[38:39], v[38:39], 0, s[78:79]
	s_cbranch_scc1 .LBB0_591
	s_branch .LBB0_579

.LBB0_622:
	v_or_b32_e32 v110, 8, v102
	v_or_b32_e32 v108, 16, v102
	s_andn2_b64 vcc, exec, s[46:47]
	v_or_b32_e32 v106, 24, v102
	s_cbranch_vccnz .LBB0_626
	s_and_b64 vcc, exec, s[36:37]
	s_cbranch_vccnz .LBB0_625
	v_and_b32_e32 v0, 7, v235
	v_lshlrev_b32_e32 v112, 4, v0
	v_add3_u32 v67, s34, v112, v71
	s_waitcnt vmcnt(7)
	v_mul_f32_e32 v30, v30, v68
	v_mul_f32_e32 v31, v31, v68
	ds_write2_b32 v67, v30, v31 offset1:1
	v_mul_f32_e32 v30, v32, v68
	v_mul_f32_e32 v31, v33, v68
	ds_write2_b32 v67, v30, v31 offset0:2 offset1:3
	v_add_u32_e32 v32, 0x420, v67
	s_waitcnt vmcnt(6)
	v_mul_f32_e32 v30, v38, v66
	v_mul_f32_e32 v31, v39, v66
	ds_write2_b32 v32, v30, v31 offset1:1
	v_add_u32_e32 v32, 0x428, v67
	v_mul_f32_e32 v30, v40, v66
	v_mul_f32_e32 v31, v41, v66
	ds_write2_b32 v32, v30, v31 offset1:1
	v_add_u32_e32 v32, 0x840, v67
	s_waitcnt vmcnt(5)
	v_mul_f32_e32 v30, v34, v76
	v_mul_f32_e32 v31, v35, v76
	ds_write2_b32 v32, v30, v31 offset1:1
	v_add_u32_e32 v32, 0x848, v67
	v_mul_f32_e32 v30, v36, v76
	v_mul_f32_e32 v31, v37, v76
	ds_write2_b32 v32, v30, v31 offset1:1
	v_add_u32_e32 v32, 0xc60, v67
	s_waitcnt vmcnt(4)
	v_mul_f32_e32 v30, v46, v74
	v_mul_f32_e32 v31, v47, v74
	ds_write2_b32 v32, v30, v31 offset1:1
	v_add_u32_e32 v32, 0xc68, v67
	v_mul_f32_e32 v30, v48, v74
	v_mul_f32_e32 v31, v49, v74
	ds_write2_b32 v32, v30, v31 offset1:1
	v_add_u32_e32 v32, 0x1080, v67
	s_waitcnt vmcnt(3)
	v_mul_f32_e32 v30, v42, v84
	v_mul_f32_e32 v31, v43, v84
	ds_write2_b32 v32, v30, v31 offset1:1
	v_add_u32_e32 v32, 0x1088, v67
	v_mul_f32_e32 v30, v44, v84
	v_mul_f32_e32 v31, v45, v84
	ds_write2_b32 v32, v30, v31 offset1:1
	v_add_u32_e32 v32, 0x14a0, v67
	s_waitcnt vmcnt(2)
	v_mul_f32_e32 v30, v54, v82
	v_mul_f32_e32 v31, v55, v82
	ds_write2_b32 v32, v30, v31 offset1:1
	v_add_u32_e32 v32, 0x14a8, v67
	v_mul_f32_e32 v30, v56, v82
	v_mul_f32_e32 v31, v57, v82
	ds_write2_b32 v32, v30, v31 offset1:1
	v_add_u32_e32 v32, 0x18c0, v67
	s_waitcnt vmcnt(1)
	v_mul_f32_e32 v30, v50, v92
	v_mul_f32_e32 v31, v51, v92
	ds_write2_b32 v32, v30, v31 offset1:1
	v_add_u32_e32 v32, 0x18c8, v67
	v_mul_f32_e32 v30, v52, v92
	v_mul_f32_e32 v31, v53, v92
	ds_write2_b32 v32, v30, v31 offset1:1
	v_add_u32_e32 v32, 0x1ce0, v67
	s_waitcnt vmcnt(0)
	v_mul_f32_e32 v30, v58, v90
	v_mul_f32_e32 v31, v59, v90
	ds_write2_b32 v32, v30, v31 offset1:1
	v_add_u32_e32 v32, 0x1ce8, v67
	v_mul_f32_e32 v30, v60, v90
	v_mul_f32_e32 v31, v61, v90
	ds_write2_b32 v32, v30, v31 offset1:1
	s_waitcnt lgkmcnt(0)
	v_mul_u32_u24_e32 v0, 0x420, v0
	v_add3_u32 v52, s34, v0, v73
	ds_read2_b32 v[34:35], v52 offset0:33 offset1:41
	ds_read2_b32 v[36:37], v52 offset1:8
	ds_read2_b32 v[38:39], v52 offset0:66 offset1:74
	ds_read2_b32 v[40:41], v52 offset0:99 offset1:107
	ds_read2_b32 v[42:43], v52 offset0:132 offset1:140
	ds_read2_b32 v[44:45], v52 offset0:165 offset1:173
	ds_read2_b32 v[46:47], v52 offset0:198 offset1:206
	ds_read2_b32 v[48:49], v52 offset0:231 offset1:239
	v_lshlrev_b32_e32 v0, 11, v102
	v_lshl_add_u64 v[50:51], s[16:17], 0, v[0:1]
	v_mov_b32_e32 v113, v1
	s_waitcnt lgkmcnt(0)
	v_cvt_pk_bf16_f32 v30, v36, v34
	v_cvt_pk_bf16_f32 v31, v38, v40
	v_cvt_pk_bf16_f32 v32, v42, v44
	v_cvt_pk_bf16_f32 v33, v46, v48
	v_lshl_add_u64 v[50:51], v[50:51], 0, v[112:113]
	global_store_dwordx4 v[50:51], v[30:33], off
	v_lshlrev_b32_e32 v0, 11, v110
	s_nop 0
	v_cvt_pk_bf16_f32 v30, v37, v35
	v_cvt_pk_bf16_f32 v31, v39, v41
	v_cvt_pk_bf16_f32 v32, v43, v45
	v_cvt_pk_bf16_f32 v33, v47, v49
	ds_read2_b32 v[36:37], v52 offset0:49 offset1:57
	ds_read2_b32 v[38:39], v52 offset0:16 offset1:24
	ds_read2_b32 v[40:41], v52 offset0:82 offset1:90
	ds_read2_b32 v[42:43], v52 offset0:115 offset1:123
	ds_read2_b32 v[44:45], v52 offset0:148 offset1:156
	ds_read2_b32 v[46:47], v52 offset0:181 offset1:189
	ds_read2_b32 v[48:49], v52 offset0:214 offset1:222
	ds_read2_b32 v[50:51], v52 offset0:247 offset1:255
	v_lshl_add_u64 v[34:35], s[16:17], 0, v[0:1]
	v_lshl_add_u64 v[34:35], v[34:35], 0, v[112:113]
	v_lshlrev_b32_e32 v0, 11, v108
	global_store_dwordx4 v[34:35], v[30:33], off
	v_lshl_add_u64 v[34:35], s[16:17], 0, v[0:1]
	v_lshl_add_u64 v[34:35], v[34:35], 0, v[112:113]
	s_waitcnt lgkmcnt(6)
	v_cvt_pk_bf16_f32 v30, v38, v36
	s_waitcnt lgkmcnt(4)
	v_cvt_pk_bf16_f32 v31, v40, v42
	s_waitcnt lgkmcnt(2)
	v_cvt_pk_bf16_f32 v32, v44, v46
	s_waitcnt lgkmcnt(0)
	v_cvt_pk_bf16_f32 v33, v48, v50
	v_lshlrev_b32_e32 v0, 11, v106
	global_store_dwordx4 v[34:35], v[30:33], off
	v_lshl_add_u64 v[34:35], s[16:17], 0, v[0:1]
	v_lshl_add_u64 v[34:35], v[34:35], 0, v[112:113]
	v_cvt_pk_bf16_f32 v30, v39, v37
	v_cvt_pk_bf16_f32 v31, v41, v43
	v_cvt_pk_bf16_f32 v32, v45, v47
	v_cvt_pk_bf16_f32 v33, v49, v51
	global_store_dwordx4 v[34:35], v[30:33], off
	s_waitcnt lgkmcnt(0)

.LBB0_641:
	s_andn2_b64 vcc, exec, s[38:39]
	s_cbranch_vccnz .LBB0_645
	s_cmp_eq_u32 s31, 0
	s_cbranch_scc1 .LBB0_644
	v_and_b32_e32 v0, 7, v235
	s_waitcnt vmcnt(7)
	v_lshlrev_b32_e32 v30, 4, v0
	v_add3_u32 v31, s34, v30, v71
	v_mul_f32_e32 v2, v2, v72
	v_mul_f32_e32 v3, v3, v72
	ds_write2_b32 v31, v2, v3 offset1:1
	v_mul_f32_e32 v2, v4, v72
	v_mul_f32_e32 v3, v5, v72
	ds_write2_b32 v31, v2, v3 offset0:2 offset1:3
	v_add_u32_e32 v4, 0x420, v31
	s_waitcnt vmcnt(6)
	v_mul_f32_e32 v2, v10, v70
	v_mul_f32_e32 v3, v11, v70
	ds_write2_b32 v4, v2, v3 offset1:1
	v_add_u32_e32 v4, 0x428, v31
	v_mul_f32_e32 v2, v12, v70
	v_mul_f32_e32 v3, v13, v70
	ds_write2_b32 v4, v2, v3 offset1:1
	v_add_u32_e32 v4, 0x840, v31
	s_waitcnt vmcnt(5)
	v_mul_f32_e32 v2, v6, v80
	v_mul_f32_e32 v3, v7, v80
	ds_write2_b32 v4, v2, v3 offset1:1
	v_add_u32_e32 v4, 0x848, v31
	v_mul_f32_e32 v2, v8, v80
	v_mul_f32_e32 v3, v9, v80
	ds_write2_b32 v4, v2, v3 offset1:1
	v_add_u32_e32 v4, 0xc60, v31
	s_waitcnt vmcnt(4)
	v_mul_f32_e32 v2, v18, v78
	v_mul_f32_e32 v3, v19, v78
	ds_write2_b32 v4, v2, v3 offset1:1
	v_add_u32_e32 v4, 0xc68, v31
	v_mul_f32_e32 v2, v20, v78
	v_mul_f32_e32 v3, v21, v78
	ds_write2_b32 v4, v2, v3 offset1:1
	v_add_u32_e32 v4, 0x1080, v31
	s_waitcnt vmcnt(3)
	v_mul_f32_e32 v2, v14, v88
	v_mul_f32_e32 v3, v15, v88
	ds_write2_b32 v4, v2, v3 offset1:1
	v_add_u32_e32 v4, 0x1088, v31
	v_mul_f32_e32 v2, v16, v88
	v_mul_f32_e32 v3, v17, v88
	ds_write2_b32 v4, v2, v3 offset1:1
	v_add_u32_e32 v4, 0x14a0, v31
	s_waitcnt vmcnt(2)
	v_mul_f32_e32 v2, v26, v86
	v_mul_f32_e32 v3, v27, v86
	ds_write2_b32 v4, v2, v3 offset1:1
	v_add_u32_e32 v4, 0x14a8, v31
	v_mul_f32_e32 v2, v28, v86
	v_mul_f32_e32 v3, v29, v86
	ds_write2_b32 v4, v2, v3 offset1:1
	v_add_u32_e32 v4, 0x18c0, v31
	s_waitcnt vmcnt(1)
	v_mul_f32_e32 v2, v22, v96
	v_mul_f32_e32 v3, v23, v96
	ds_write2_b32 v4, v2, v3 offset1:1
	v_add_u32_e32 v4, 0x18c8, v31
	v_mul_f32_e32 v2, v24, v96
	v_mul_f32_e32 v3, v25, v96
	ds_write2_b32 v4, v2, v3 offset1:1
	v_add_u32_e32 v4, 0x1ce0, v31
	s_waitcnt vmcnt(0)
	v_mul_f32_e32 v2, v62, v94
	v_mul_f32_e32 v3, v63, v94
	ds_write2_b32 v4, v2, v3 offset1:1
	v_add_u32_e32 v4, 0x1ce8, v31
	v_mul_f32_e32 v2, v64, v94
	v_mul_f32_e32 v3, v65, v94
	ds_write2_b32 v4, v2, v3 offset1:1
	s_waitcnt lgkmcnt(0)
	v_mul_u32_u24_e32 v0, 0x420, v0
	v_add3_u32 v24, s34, v0, v73
	ds_read2_b32 v[6:7], v24 offset0:33 offset1:41
	ds_read2_b32 v[8:9], v24 offset1:8
	ds_read2_b32 v[10:11], v24 offset0:66 offset1:74
	ds_read2_b32 v[12:13], v24 offset0:99 offset1:107
	ds_read2_b32 v[14:15], v24 offset0:132 offset1:140
	ds_read2_b32 v[16:17], v24 offset0:165 offset1:173
	ds_read2_b32 v[18:19], v24 offset0:198 offset1:206
	ds_read2_b32 v[20:21], v24 offset0:231 offset1:239
	v_lshlrev_b32_e32 v0, 11, v102
	v_lshl_add_u64 v[22:23], s[14:15], 0, v[0:1]
	v_mov_b32_e32 v31, v1
	s_waitcnt lgkmcnt(0)
	v_cvt_pk_bf16_f32 v2, v8, v6
	v_cvt_pk_bf16_f32 v3, v10, v12
	v_cvt_pk_bf16_f32 v4, v14, v16
	v_cvt_pk_bf16_f32 v5, v18, v20
	v_lshl_add_u64 v[22:23], v[22:23], 0, v[30:31]
	global_store_dwordx4 v[22:23], v[2:5], off
	v_lshlrev_b32_e32 v0, 11, v110
	s_nop 0
	v_cvt_pk_bf16_f32 v2, v9, v7
	v_cvt_pk_bf16_f32 v3, v11, v13
	v_cvt_pk_bf16_f32 v4, v15, v17
	v_cvt_pk_bf16_f32 v5, v19, v21
	ds_read2_b32 v[8:9], v24 offset0:49 offset1:57
	ds_read2_b32 v[10:11], v24 offset0:16 offset1:24
	ds_read2_b32 v[12:13], v24 offset0:82 offset1:90
	ds_read2_b32 v[14:15], v24 offset0:115 offset1:123
	ds_read2_b32 v[16:17], v24 offset0:148 offset1:156
	ds_read2_b32 v[18:19], v24 offset0:181 offset1:189
	ds_read2_b32 v[20:21], v24 offset0:214 offset1:222
	ds_read2_b32 v[22:23], v24 offset0:247 offset1:255
	v_lshl_add_u64 v[6:7], s[14:15], 0, v[0:1]
	v_lshl_add_u64 v[6:7], v[6:7], 0, v[30:31]
	v_lshlrev_b32_e32 v0, 11, v108
	global_store_dwordx4 v[6:7], v[2:5], off
	v_lshl_add_u64 v[6:7], s[14:15], 0, v[0:1]
	v_lshl_add_u64 v[6:7], v[6:7], 0, v[30:31]
	s_waitcnt lgkmcnt(6)
	v_cvt_pk_bf16_f32 v2, v10, v8
	s_waitcnt lgkmcnt(4)
	v_cvt_pk_bf16_f32 v3, v12, v14
	s_waitcnt lgkmcnt(2)
	v_cvt_pk_bf16_f32 v4, v16, v18
	s_waitcnt lgkmcnt(0)
	v_cvt_pk_bf16_f32 v5, v20, v22
	v_lshlrev_b32_e32 v0, 11, v106
	global_store_dwordx4 v[6:7], v[2:5], off
	v_lshl_add_u64 v[6:7], s[14:15], 0, v[0:1]
	v_lshl_add_u64 v[6:7], v[6:7], 0, v[30:31]
	v_cvt_pk_bf16_f32 v2, v11, v9
	v_cvt_pk_bf16_f32 v3, v13, v15
	v_cvt_pk_bf16_f32 v4, v17, v19
	v_cvt_pk_bf16_f32 v5, v21, v23
	global_store_dwordx4 v[6:7], v[2:5], off
	s_waitcnt lgkmcnt(0)

.LBB0_660:
	s_andn2_b64 vcc, exec, s[38:39]
	s_cbranch_vccnz .LBB0_664
	s_cmp_eq_u32 s31, 0
	s_cbranch_scc1 .LBB0_663
	v_and_b32_e32 v0, 7, v235
	s_waitcnt vmcnt(0)
	v_lshlrev_b32_e32 v62, 4, v0
	v_add3_u32 v63, s34, v62, v71
	v_mul_f32_e32 v34, v34, v76
	v_mul_f32_e32 v35, v35, v76
	ds_write2_b32 v63, v34, v35 offset1:1
	v_mul_f32_e32 v34, v36, v76
	v_mul_f32_e32 v35, v37, v76
	ds_write2_b32 v63, v34, v35 offset0:2 offset1:3
	v_add_u32_e32 v36, 0x420, v63
	v_mul_f32_e32 v34, v42, v74
	v_mul_f32_e32 v35, v43, v74
	ds_write2_b32 v36, v34, v35 offset1:1
	v_add_u32_e32 v36, 0x428, v63
	v_mul_f32_e32 v34, v44, v74
	v_mul_f32_e32 v35, v45, v74
	ds_write2_b32 v36, v34, v35 offset1:1
	v_add_u32_e32 v36, 0x840, v63
	v_mul_f32_e32 v34, v38, v84
	v_mul_f32_e32 v35, v39, v84
	ds_write2_b32 v36, v34, v35 offset1:1
	v_add_u32_e32 v36, 0x848, v63
	v_mul_f32_e32 v34, v40, v84
	v_mul_f32_e32 v35, v41, v84
	ds_write2_b32 v36, v34, v35 offset1:1
	v_add_u32_e32 v36, 0xc60, v63
	v_mul_f32_e32 v34, v50, v82
	v_mul_f32_e32 v35, v51, v82
	ds_write2_b32 v36, v34, v35 offset1:1
	v_add_u32_e32 v36, 0xc68, v63
	v_mul_f32_e32 v34, v52, v82
	v_mul_f32_e32 v35, v53, v82
	ds_write2_b32 v36, v34, v35 offset1:1
	v_add_u32_e32 v36, 0x1080, v63
	v_mul_f32_e32 v34, v46, v92
	v_mul_f32_e32 v35, v47, v92
	ds_write2_b32 v36, v34, v35 offset1:1
	v_add_u32_e32 v36, 0x1088, v63
	v_mul_f32_e32 v34, v48, v92
	v_mul_f32_e32 v35, v49, v92
	ds_write2_b32 v36, v34, v35 offset1:1
	v_add_u32_e32 v36, 0x14a0, v63
	v_mul_f32_e32 v34, v58, v90
	v_mul_f32_e32 v35, v59, v90
	ds_write2_b32 v36, v34, v35 offset1:1
	v_add_u32_e32 v36, 0x14a8, v63
	v_mul_f32_e32 v34, v60, v90
	v_mul_f32_e32 v35, v61, v90
	ds_write2_b32 v36, v34, v35 offset1:1
	v_add_u32_e32 v36, 0x18c0, v63
	v_mul_f32_e32 v34, v54, v114
	v_mul_f32_e32 v35, v55, v114
	ds_write2_b32 v36, v34, v35 offset1:1
	v_add_u32_e32 v36, 0x18c8, v63
	v_mul_f32_e32 v34, v56, v114
	v_mul_f32_e32 v35, v57, v114
	ds_write2_b32 v36, v34, v35 offset1:1
	v_add_u32_e32 v36, 0x1ce0, v63
	v_mul_f32_e32 v34, v66, v112
	v_mul_f32_e32 v35, v67, v112
	ds_write2_b32 v36, v34, v35 offset1:1
	v_add_u32_e32 v36, 0x1ce8, v63
	v_mul_f32_e32 v34, v68, v112
	v_mul_f32_e32 v35, v69, v112
	ds_write2_b32 v36, v34, v35 offset1:1
	s_waitcnt lgkmcnt(0)
	v_mul_u32_u24_e32 v0, 0x420, v0
	v_add3_u32 v56, s34, v0, v73
	ds_read2_b32 v[38:39], v56 offset0:33 offset1:41
	ds_read2_b32 v[40:41], v56 offset1:8
	ds_read2_b32 v[42:43], v56 offset0:66 offset1:74
	ds_read2_b32 v[44:45], v56 offset0:99 offset1:107
	ds_read2_b32 v[46:47], v56 offset0:132 offset1:140
	ds_read2_b32 v[48:49], v56 offset0:165 offset1:173
	ds_read2_b32 v[50:51], v56 offset0:198 offset1:206
	ds_read2_b32 v[52:53], v56 offset0:231 offset1:239
	v_lshlrev_b32_e32 v0, 11, v102
	v_lshl_add_u64 v[54:55], s[16:17], 0, v[0:1]
	v_mov_b32_e32 v63, v1
	s_waitcnt lgkmcnt(0)
	v_cvt_pk_bf16_f32 v34, v40, v38
	v_cvt_pk_bf16_f32 v35, v42, v44
	v_cvt_pk_bf16_f32 v36, v46, v48
	v_cvt_pk_bf16_f32 v37, v50, v52
	v_lshl_add_u64 v[54:55], v[54:55], 0, v[62:63]
	global_store_dwordx4 v[54:55], v[34:37], off
	v_lshlrev_b32_e32 v0, 11, v110
	s_nop 0
	v_cvt_pk_bf16_f32 v34, v41, v39
	v_cvt_pk_bf16_f32 v35, v43, v45
	v_cvt_pk_bf16_f32 v36, v47, v49
	v_cvt_pk_bf16_f32 v37, v51, v53
	ds_read2_b32 v[40:41], v56 offset0:49 offset1:57
	ds_read2_b32 v[42:43], v56 offset0:16 offset1:24
	ds_read2_b32 v[44:45], v56 offset0:82 offset1:90
	ds_read2_b32 v[46:47], v56 offset0:115 offset1:123
	ds_read2_b32 v[48:49], v56 offset0:148 offset1:156
	ds_read2_b32 v[50:51], v56 offset0:181 offset1:189
	ds_read2_b32 v[52:53], v56 offset0:214 offset1:222
	ds_read2_b32 v[54:55], v56 offset0:247 offset1:255
	v_lshl_add_u64 v[38:39], s[16:17], 0, v[0:1]
	v_lshl_add_u64 v[38:39], v[38:39], 0, v[62:63]
	v_lshlrev_b32_e32 v0, 11, v108
	global_store_dwordx4 v[38:39], v[34:37], off
	v_lshl_add_u64 v[38:39], s[16:17], 0, v[0:1]
	v_lshl_add_u64 v[38:39], v[38:39], 0, v[62:63]
	s_waitcnt lgkmcnt(6)
	v_cvt_pk_bf16_f32 v34, v42, v40
	s_waitcnt lgkmcnt(4)
	v_cvt_pk_bf16_f32 v35, v44, v46
	s_waitcnt lgkmcnt(2)
	v_cvt_pk_bf16_f32 v36, v48, v50
	s_waitcnt lgkmcnt(0)
	v_cvt_pk_bf16_f32 v37, v52, v54
	v_lshlrev_b32_e32 v0, 11, v106
	global_store_dwordx4 v[38:39], v[34:37], off
	v_lshl_add_u64 v[38:39], s[16:17], 0, v[0:1]
	v_lshl_add_u64 v[38:39], v[38:39], 0, v[62:63]
	v_cvt_pk_bf16_f32 v34, v43, v41
	v_cvt_pk_bf16_f32 v35, v45, v47
	v_cvt_pk_bf16_f32 v36, v49, v51
	v_cvt_pk_bf16_f32 v37, v53, v55
	global_store_dwordx4 v[38:39], v[34:37], off
	s_waitcnt lgkmcnt(0)

.LBB0_682:
	s_andn2_b64 vcc, exec, s[50:51]
	s_cbranch_vccnz .LBB0_686
	s_cmp_eq_u32 s31, 0
	s_cbranch_scc1 .LBB0_685
	s_waitcnt vmcnt(6)
	v_mul_f32_e32 v2, v126, v2
	v_mul_f32_e32 v3, v126, v3
	ds_write2_b32 v103, v2, v3 offset1:1
	v_mul_f32_e32 v2, v126, v4
	v_mul_f32_e32 v3, v126, v5
	ds_write2_b32 v103, v2, v3 offset0:2 offset1:3
	s_waitcnt vmcnt(5)
	v_mul_f32_e32 v2, v120, v14
	v_mul_f32_e32 v3, v120, v15
	v_add_u32_e32 v0, 0x420, v103
	ds_write2_b32 v0, v2, v3 offset1:1
	v_mul_f32_e32 v2, v120, v16
	v_mul_f32_e32 v3, v120, v17
	v_add_u32_e32 v0, 0x428, v103
	ds_write2_b32 v0, v2, v3 offset1:1
	s_waitcnt vmcnt(3)
	v_mul_f32_e32 v2, v132, v6
	v_mul_f32_e32 v3, v132, v7
	v_add_u32_e32 v0, 0x840, v103
	ds_write2_b32 v0, v2, v3 offset1:1
	v_mul_f32_e32 v2, v132, v8
	v_mul_f32_e32 v3, v132, v9
	v_add_u32_e32 v0, 0x848, v103
	ds_write2_b32 v0, v2, v3 offset1:1
	s_waitcnt vmcnt(5)
	v_mul_f32_e32 v2, v128, v22
	v_mul_f32_e32 v3, v128, v23
	v_add_u32_e32 v0, 0xc60, v103
	ds_write2_b32 v0, v2, v3 offset1:1
	v_mul_f32_e32 v2, v128, v24
	v_mul_f32_e32 v3, v128, v25
	v_add_u32_e32 v0, 0xc68, v103
	ds_write2_b32 v0, v2, v3 offset1:1
	s_waitcnt vmcnt(3)
	v_mul_f32_e32 v2, v136, v10
	v_mul_f32_e32 v3, v136, v11
	v_add_u32_e32 v0, 0x1080, v103
	ds_write2_b32 v0, v2, v3 offset1:1
	v_mul_f32_e32 v2, v136, v12
	v_mul_f32_e32 v3, v136, v13
	v_add_u32_e32 v0, 0x1088, v103
	ds_write2_b32 v0, v2, v3 offset1:1
	v_mul_f32_e32 v2, v130, v26
	v_mul_f32_e32 v3, v130, v27
	v_add_u32_e32 v0, 0x14a0, v103
	ds_write2_b32 v0, v2, v3 offset1:1
	v_mul_f32_e32 v2, v130, v28
	v_mul_f32_e32 v3, v130, v29
	v_add_u32_e32 v0, 0x14a8, v103
	ds_write2_b32 v0, v2, v3 offset1:1
	s_waitcnt vmcnt(2)
	v_mul_f32_e32 v2, v138, v18
	v_mul_f32_e32 v3, v138, v19
	v_add_u32_e32 v0, 0x18c0, v103
	ds_write2_b32 v0, v2, v3 offset1:1
	v_mul_f32_e32 v2, v138, v20
	v_mul_f32_e32 v3, v138, v21
	v_add_u32_e32 v0, 0x18c8, v103
	ds_write2_b32 v0, v2, v3 offset1:1
	s_waitcnt vmcnt(0)
	v_mul_f32_e32 v2, v134, v30
	v_mul_f32_e32 v3, v134, v31
	v_add_u32_e32 v0, 0x1ce0, v103
	ds_write2_b32 v0, v2, v3 offset1:1
	v_mul_f32_e32 v2, v134, v32
	v_mul_f32_e32 v3, v134, v33
	v_add_u32_e32 v0, 0x1ce8, v103
	ds_write2_b32 v0, v2, v3 offset1:1
	s_waitcnt lgkmcnt(0)
	ds_read2_b32 v[6:7], v99 offset0:33 offset1:41
	ds_read2_b32 v[8:9], v99 offset1:8
	ds_read2_b32 v[10:11], v99 offset0:66 offset1:74
	ds_read2_b32 v[12:13], v99 offset0:99 offset1:107
	ds_read2_b32 v[14:15], v99 offset0:132 offset1:140
	ds_read2_b32 v[16:17], v99 offset0:165 offset1:173
	ds_read2_b32 v[18:19], v99 offset0:198 offset1:206
	ds_read2_b32 v[20:21], v99 offset0:231 offset1:239
	v_lshl_add_u64 v[22:23], s[14:15], 0, v[124:125]
	v_lshlrev_b32_e32 v0, 1, v112
	s_waitcnt lgkmcnt(6)
	v_cvt_pk_bf16_f32 v2, v8, v6
	s_waitcnt lgkmcnt(4)
	v_cvt_pk_bf16_f32 v3, v10, v12
	s_waitcnt lgkmcnt(2)
	v_cvt_pk_bf16_f32 v4, v14, v16
	s_waitcnt lgkmcnt(0)
	v_cvt_pk_bf16_f32 v5, v18, v20
	v_lshl_add_u64 v[22:23], v[22:23], 0, v[0:1]
	global_store_dwordx4 v[22:23], v[2:5], off
	s_nop 1
	v_cvt_pk_bf16_f32 v2, v9, v7
	v_cvt_pk_bf16_f32 v3, v11, v13
	v_cvt_pk_bf16_f32 v4, v15, v17
	v_cvt_pk_bf16_f32 v5, v19, v21
	ds_read2_b32 v[8:9], v99 offset0:49 offset1:57
	ds_read2_b32 v[10:11], v99 offset0:16 offset1:24
	ds_read2_b32 v[12:13], v99 offset0:82 offset1:90
	ds_read2_b32 v[14:15], v99 offset0:115 offset1:123
	ds_read2_b32 v[16:17], v99 offset0:148 offset1:156
	ds_read2_b32 v[18:19], v99 offset0:181 offset1:189
	ds_read2_b32 v[20:21], v99 offset0:214 offset1:222
	ds_read2_b32 v[22:23], v99 offset0:247 offset1:255
	v_lshl_add_u64 v[6:7], s[14:15], 0, v[122:123]
	v_lshl_add_u64 v[6:7], v[6:7], 0, v[0:1]
	global_store_dwordx4 v[6:7], v[2:5], off
	v_lshl_add_u64 v[6:7], s[14:15], 0, v[118:119]
	v_lshl_add_u64 v[6:7], v[6:7], 0, v[0:1]
	s_waitcnt lgkmcnt(6)
	v_cvt_pk_bf16_f32 v2, v10, v8
	s_waitcnt lgkmcnt(4)
	v_cvt_pk_bf16_f32 v3, v12, v14
	s_waitcnt lgkmcnt(2)
	v_cvt_pk_bf16_f32 v4, v16, v18
	s_waitcnt lgkmcnt(0)
	v_cvt_pk_bf16_f32 v5, v20, v22
	global_store_dwordx4 v[6:7], v[2:5], off
	v_lshl_add_u64 v[6:7], s[14:15], 0, v[116:117]
	v_lshl_add_u64 v[6:7], v[6:7], 0, v[0:1]
	v_cvt_pk_bf16_f32 v2, v11, v9
	v_cvt_pk_bf16_f32 v3, v13, v15
	v_cvt_pk_bf16_f32 v4, v17, v19
	v_cvt_pk_bf16_f32 v5, v21, v23
	global_store_dwordx4 v[6:7], v[2:5], off
	s_waitcnt lgkmcnt(0)

.LBB0_700:
	s_andn2_b64 vcc, exec, s[50:51]
	s_cbranch_vccnz .LBB0_667
	s_cmp_eq_u32 s31, 0
	s_cbranch_scc1 .LBB0_666
	s_waitcnt vmcnt(6)
	v_mul_f32_e32 v2, v2, v126
	v_mul_f32_e32 v3, v3, v126
	ds_write2_b32 v103, v2, v3 offset1:1
	v_mul_f32_e32 v2, v4, v126
	v_mul_f32_e32 v3, v5, v126
	ds_write2_b32 v103, v2, v3 offset0:2 offset1:3
	s_waitcnt vmcnt(5)
	v_mul_f32_e32 v2, v14, v120
	v_mul_f32_e32 v3, v15, v120
	v_add_u32_e32 v0, 0x420, v103
	ds_write2_b32 v0, v2, v3 offset1:1
	v_mul_f32_e32 v2, v16, v120
	v_mul_f32_e32 v3, v17, v120
	v_add_u32_e32 v0, 0x428, v103
	ds_write2_b32 v0, v2, v3 offset1:1
	s_waitcnt vmcnt(3)
	v_mul_f32_e32 v2, v6, v132
	v_mul_f32_e32 v3, v7, v132
	v_add_u32_e32 v0, 0x840, v103
	ds_write2_b32 v0, v2, v3 offset1:1
	v_mul_f32_e32 v2, v8, v132
	v_mul_f32_e32 v3, v9, v132
	v_add_u32_e32 v0, 0x848, v103
	ds_write2_b32 v0, v2, v3 offset1:1
	v_mul_f32_e32 v2, v22, v128
	v_mul_f32_e32 v3, v23, v128
	v_add_u32_e32 v0, 0xc60, v103
	ds_write2_b32 v0, v2, v3 offset1:1
	v_mul_f32_e32 v2, v24, v128
	v_mul_f32_e32 v3, v25, v128
	v_add_u32_e32 v0, 0xc68, v103
	ds_write2_b32 v0, v2, v3 offset1:1
	v_mul_f32_e32 v2, v10, v136
	v_mul_f32_e32 v3, v11, v136
	v_add_u32_e32 v0, 0x1080, v103
	ds_write2_b32 v0, v2, v3 offset1:1
	v_mul_f32_e32 v2, v12, v136
	v_mul_f32_e32 v3, v13, v136
	v_add_u32_e32 v0, 0x1088, v103
	ds_write2_b32 v0, v2, v3 offset1:1
	v_mul_f32_e32 v2, v26, v130
	v_mul_f32_e32 v3, v27, v130
	v_add_u32_e32 v0, 0x14a0, v103
	ds_write2_b32 v0, v2, v3 offset1:1
	v_mul_f32_e32 v2, v28, v130
	v_mul_f32_e32 v3, v29, v130
	v_add_u32_e32 v0, 0x14a8, v103
	ds_write2_b32 v0, v2, v3 offset1:1
	s_waitcnt vmcnt(2)
	v_mul_f32_e32 v2, v18, v138
	v_mul_f32_e32 v3, v19, v138
	v_add_u32_e32 v0, 0x18c0, v103
	ds_write2_b32 v0, v2, v3 offset1:1
	v_mul_f32_e32 v2, v20, v138
	v_mul_f32_e32 v3, v21, v138
	v_add_u32_e32 v0, 0x18c8, v103
	ds_write2_b32 v0, v2, v3 offset1:1
	s_waitcnt vmcnt(0)
	v_mul_f32_e32 v2, v30, v134
	v_mul_f32_e32 v3, v31, v134
	v_add_u32_e32 v0, 0x1ce0, v103
	ds_write2_b32 v0, v2, v3 offset1:1
	v_mul_f32_e32 v2, v32, v134
	v_mul_f32_e32 v3, v33, v134
	v_add_u32_e32 v0, 0x1ce8, v103
	ds_write2_b32 v0, v2, v3 offset1:1
	s_waitcnt lgkmcnt(0)
	ds_read2_b32 v[6:7], v99 offset0:33 offset1:41
	ds_read2_b32 v[8:9], v99 offset1:8
	ds_read2_b32 v[10:11], v99 offset0:66 offset1:74
	ds_read2_b32 v[12:13], v99 offset0:99 offset1:107
	ds_read2_b32 v[14:15], v99 offset0:132 offset1:140
	ds_read2_b32 v[16:17], v99 offset0:165 offset1:173
	ds_read2_b32 v[18:19], v99 offset0:198 offset1:206
	ds_read2_b32 v[20:21], v99 offset0:231 offset1:239
	v_lshl_add_u64 v[22:23], s[14:15], 0, v[124:125]
	v_lshlrev_b32_e32 v0, 1, v112
	s_waitcnt lgkmcnt(6)
	v_cvt_pk_bf16_f32 v2, v8, v6
	s_waitcnt lgkmcnt(4)
	v_cvt_pk_bf16_f32 v3, v10, v12
	s_waitcnt lgkmcnt(2)
	v_cvt_pk_bf16_f32 v4, v14, v16
	s_waitcnt lgkmcnt(0)
	v_cvt_pk_bf16_f32 v5, v18, v20
	v_lshl_add_u64 v[22:23], v[22:23], 0, v[0:1]
	global_store_dwordx4 v[22:23], v[2:5], off
	s_nop 1
	v_cvt_pk_bf16_f32 v2, v9, v7
	v_cvt_pk_bf16_f32 v3, v11, v13
	v_cvt_pk_bf16_f32 v4, v15, v17
	v_cvt_pk_bf16_f32 v5, v19, v21
	ds_read2_b32 v[8:9], v99 offset0:49 offset1:57
	ds_read2_b32 v[10:11], v99 offset0:16 offset1:24
	ds_read2_b32 v[12:13], v99 offset0:82 offset1:90
	ds_read2_b32 v[14:15], v99 offset0:115 offset1:123
	ds_read2_b32 v[16:17], v99 offset0:148 offset1:156
	ds_read2_b32 v[18:19], v99 offset0:181 offset1:189
	ds_read2_b32 v[20:21], v99 offset0:214 offset1:222
	ds_read2_b32 v[22:23], v99 offset0:247 offset1:255
	v_lshl_add_u64 v[6:7], s[14:15], 0, v[122:123]
	v_lshl_add_u64 v[6:7], v[6:7], 0, v[0:1]
	global_store_dwordx4 v[6:7], v[2:5], off
	v_lshl_add_u64 v[6:7], s[14:15], 0, v[118:119]
	v_lshl_add_u64 v[6:7], v[6:7], 0, v[0:1]
	s_waitcnt lgkmcnt(6)
	v_cvt_pk_bf16_f32 v2, v10, v8
	s_waitcnt lgkmcnt(4)
	v_cvt_pk_bf16_f32 v3, v12, v14
	s_waitcnt lgkmcnt(2)
	v_cvt_pk_bf16_f32 v4, v16, v18
	s_waitcnt lgkmcnt(0)
	v_cvt_pk_bf16_f32 v5, v20, v22
	global_store_dwordx4 v[6:7], v[2:5], off
	v_lshl_add_u64 v[6:7], s[14:15], 0, v[116:117]
	v_lshl_add_u64 v[6:7], v[6:7], 0, v[0:1]
	v_cvt_pk_bf16_f32 v2, v11, v9
	v_cvt_pk_bf16_f32 v3, v13, v15
	v_cvt_pk_bf16_f32 v4, v17, v19
	v_cvt_pk_bf16_f32 v5, v21, v23
	global_store_dwordx4 v[6:7], v[2:5], off
	s_waitcnt lgkmcnt(0)
	s_branch .LBB0_666

.LBB0_725:
	s_and_b64 vcc, exec, s[46:47]
	s_cbranch_vccz .LBB0_729
	s_cmp_eq_u32 s31, 0
	s_cbranch_scc1 .LBB0_728
	s_waitcnt vmcnt(6)
	v_mul_f32_e32 v2, v2, v126
	v_mul_f32_e32 v3, v3, v126
	ds_write2_b32 v103, v2, v3 offset1:1
	v_mul_f32_e32 v2, v4, v126
	v_mul_f32_e32 v3, v5, v126
	ds_write2_b32 v103, v2, v3 offset0:2 offset1:3
	s_waitcnt vmcnt(5)
	v_mul_f32_e32 v2, v14, v120
	v_mul_f32_e32 v3, v15, v120
	v_add_u32_e32 v0, 0x420, v103
	ds_write2_b32 v0, v2, v3 offset1:1
	v_mul_f32_e32 v2, v16, v120
	v_mul_f32_e32 v3, v17, v120
	v_add_u32_e32 v0, 0x428, v103
	ds_write2_b32 v0, v2, v3 offset1:1
	s_waitcnt vmcnt(3)
	v_mul_f32_e32 v2, v6, v132
	v_mul_f32_e32 v3, v7, v132
	v_add_u32_e32 v0, 0x840, v103
	ds_write2_b32 v0, v2, v3 offset1:1
	v_mul_f32_e32 v2, v8, v132
	v_mul_f32_e32 v3, v9, v132
	v_add_u32_e32 v0, 0x848, v103
	ds_write2_b32 v0, v2, v3 offset1:1
	v_mul_f32_e32 v2, v22, v128
	v_mul_f32_e32 v3, v23, v128
	v_add_u32_e32 v0, 0xc60, v103
	ds_write2_b32 v0, v2, v3 offset1:1
	v_mul_f32_e32 v2, v24, v128
	v_mul_f32_e32 v3, v25, v128
	v_add_u32_e32 v0, 0xc68, v103
	ds_write2_b32 v0, v2, v3 offset1:1
	v_mul_f32_e32 v2, v10, v136
	v_mul_f32_e32 v3, v11, v136
	v_add_u32_e32 v0, 0x1080, v103
	ds_write2_b32 v0, v2, v3 offset1:1
	v_mul_f32_e32 v2, v12, v136
	v_mul_f32_e32 v3, v13, v136
	v_add_u32_e32 v0, 0x1088, v103
	ds_write2_b32 v0, v2, v3 offset1:1
	v_mul_f32_e32 v2, v26, v130
	v_mul_f32_e32 v3, v27, v130
	v_add_u32_e32 v0, 0x14a0, v103
	ds_write2_b32 v0, v2, v3 offset1:1
	v_mul_f32_e32 v2, v28, v130
	v_mul_f32_e32 v3, v29, v130
	v_add_u32_e32 v0, 0x14a8, v103
	ds_write2_b32 v0, v2, v3 offset1:1
	s_waitcnt vmcnt(2)
	v_mul_f32_e32 v2, v18, v138
	v_mul_f32_e32 v3, v19, v138
	v_add_u32_e32 v0, 0x18c0, v103
	ds_write2_b32 v0, v2, v3 offset1:1
	v_mul_f32_e32 v2, v20, v138
	v_mul_f32_e32 v3, v21, v138
	v_add_u32_e32 v0, 0x18c8, v103
	ds_write2_b32 v0, v2, v3 offset1:1
	s_waitcnt vmcnt(0)
	v_mul_f32_e32 v2, v30, v134
	v_mul_f32_e32 v3, v31, v134
	v_add_u32_e32 v0, 0x1ce0, v103
	ds_write2_b32 v0, v2, v3 offset1:1
	v_mul_f32_e32 v2, v32, v134
	v_mul_f32_e32 v3, v33, v134
	v_add_u32_e32 v0, 0x1ce8, v103
	ds_write2_b32 v0, v2, v3 offset1:1
	s_waitcnt lgkmcnt(0)
	ds_read2_b32 v[6:7], v99 offset0:33 offset1:41
	ds_read2_b32 v[8:9], v99 offset1:8
	ds_read2_b32 v[10:11], v99 offset0:66 offset1:74
	ds_read2_b32 v[12:13], v99 offset0:99 offset1:107
	ds_read2_b32 v[14:15], v99 offset0:132 offset1:140
	ds_read2_b32 v[16:17], v99 offset0:165 offset1:173
	ds_read2_b32 v[18:19], v99 offset0:198 offset1:206
	ds_read2_b32 v[20:21], v99 offset0:231 offset1:239
	v_lshl_add_u64 v[22:23], s[14:15], 0, v[124:125]
	v_lshlrev_b32_e32 v0, 1, v112
	s_waitcnt lgkmcnt(6)
	v_cvt_pk_bf16_f32 v2, v8, v6
	s_waitcnt lgkmcnt(4)
	v_cvt_pk_bf16_f32 v3, v10, v12
	s_waitcnt lgkmcnt(2)
	v_cvt_pk_bf16_f32 v4, v14, v16
	s_waitcnt lgkmcnt(0)
	v_cvt_pk_bf16_f32 v5, v18, v20
	v_lshl_add_u64 v[22:23], v[22:23], 0, v[0:1]
	global_store_dwordx4 v[22:23], v[2:5], off
	s_nop 1
	v_cvt_pk_bf16_f32 v2, v9, v7
	v_cvt_pk_bf16_f32 v3, v11, v13
	v_cvt_pk_bf16_f32 v4, v15, v17
	v_cvt_pk_bf16_f32 v5, v19, v21
	ds_read2_b32 v[8:9], v99 offset0:49 offset1:57
	ds_read2_b32 v[10:11], v99 offset0:16 offset1:24
	ds_read2_b32 v[12:13], v99 offset0:82 offset1:90
	ds_read2_b32 v[14:15], v99 offset0:115 offset1:123
	ds_read2_b32 v[16:17], v99 offset0:148 offset1:156
	ds_read2_b32 v[18:19], v99 offset0:181 offset1:189
	ds_read2_b32 v[20:21], v99 offset0:214 offset1:222
	ds_read2_b32 v[22:23], v99 offset0:247 offset1:255
	v_lshl_add_u64 v[6:7], s[14:15], 0, v[122:123]
	v_lshl_add_u64 v[6:7], v[6:7], 0, v[0:1]
	global_store_dwordx4 v[6:7], v[2:5], off
	v_lshl_add_u64 v[6:7], s[14:15], 0, v[118:119]
	v_lshl_add_u64 v[6:7], v[6:7], 0, v[0:1]
	s_waitcnt lgkmcnt(6)
	v_cvt_pk_bf16_f32 v2, v10, v8
	s_waitcnt lgkmcnt(4)
	v_cvt_pk_bf16_f32 v3, v12, v14
	s_waitcnt lgkmcnt(2)
	v_cvt_pk_bf16_f32 v4, v16, v18
	s_waitcnt lgkmcnt(0)
	v_cvt_pk_bf16_f32 v5, v20, v22
	global_store_dwordx4 v[6:7], v[2:5], off
	v_lshl_add_u64 v[6:7], s[14:15], 0, v[116:117]
	v_lshl_add_u64 v[6:7], v[6:7], 0, v[0:1]
	v_cvt_pk_bf16_f32 v2, v11, v9
	v_cvt_pk_bf16_f32 v3, v13, v15
	v_cvt_pk_bf16_f32 v4, v17, v19
	v_cvt_pk_bf16_f32 v5, v21, v23
	global_store_dwordx4 v[6:7], v[2:5], off
	s_waitcnt lgkmcnt(0)

.LBB0_744:
	s_andn2_b64 vcc, exec, s[46:47]
	s_cbranch_vccnz .LBB0_748
	s_cmp_eq_u32 s31, 0
	s_cbranch_scc1 .LBB0_747
	s_waitcnt vmcnt(0)
	v_mul_f32_e32 v2, v62, v140
	v_mul_f32_e32 v3, v63, v140
	ds_write2_b32 v103, v2, v3 offset1:1
	v_mul_f32_e32 v2, v64, v140
	v_mul_f32_e32 v3, v65, v140
	ds_write2_b32 v103, v2, v3 offset0:2 offset1:3
	v_mul_f32_e32 v2, v74, v142
	v_mul_f32_e32 v3, v75, v142
	v_add_u32_e32 v0, 0x420, v103
	ds_write2_b32 v0, v2, v3 offset1:1
	v_mul_f32_e32 v2, v76, v142
	v_mul_f32_e32 v3, v77, v142
	v_add_u32_e32 v0, 0x428, v103
	ds_write2_b32 v0, v2, v3 offset1:1
	v_mul_f32_e32 v2, v70, v146
	v_mul_f32_e32 v3, v71, v146
	v_add_u32_e32 v0, 0x840, v103
	ds_write2_b32 v0, v2, v3 offset1:1
	v_mul_f32_e32 v2, v72, v146
	v_mul_f32_e32 v3, v73, v146
	v_add_u32_e32 v0, 0x848, v103
	ds_write2_b32 v0, v2, v3 offset1:1
	v_mul_f32_e32 v2, v82, v144
	v_mul_f32_e32 v3, v83, v144
	v_add_u32_e32 v0, 0xc60, v103
	ds_write2_b32 v0, v2, v3 offset1:1
	v_mul_f32_e32 v2, v84, v144
	v_mul_f32_e32 v3, v85, v144
	v_add_u32_e32 v0, 0xc68, v103
	ds_write2_b32 v0, v2, v3 offset1:1
	v_mul_f32_e32 v2, v78, v150
	v_mul_f32_e32 v3, v79, v150
	v_add_u32_e32 v0, 0x1080, v103
	ds_write2_b32 v0, v2, v3 offset1:1
	v_mul_f32_e32 v2, v80, v150
	v_mul_f32_e32 v3, v81, v150
	v_add_u32_e32 v0, 0x1088, v103
	ds_write2_b32 v0, v2, v3 offset1:1
	v_mul_f32_e32 v2, v90, v148
	v_mul_f32_e32 v3, v91, v148
	v_add_u32_e32 v0, 0x14a0, v103
	ds_write2_b32 v0, v2, v3 offset1:1
	v_mul_f32_e32 v2, v92, v148
	v_mul_f32_e32 v3, v93, v148
	v_add_u32_e32 v0, 0x14a8, v103
	ds_write2_b32 v0, v2, v3 offset1:1
	v_mul_f32_e32 v2, v86, v154
	v_mul_f32_e32 v3, v87, v154
	v_add_u32_e32 v0, 0x18c0, v103
	ds_write2_b32 v0, v2, v3 offset1:1
	v_mul_f32_e32 v2, v88, v154
	v_mul_f32_e32 v3, v89, v154
	v_add_u32_e32 v0, 0x18c8, v103
	ds_write2_b32 v0, v2, v3 offset1:1
	v_mul_f32_e32 v2, v94, v152
	v_mul_f32_e32 v3, v95, v152
	v_add_u32_e32 v0, 0x1ce0, v103
	ds_write2_b32 v0, v2, v3 offset1:1
	v_mul_f32_e32 v2, v96, v152
	v_mul_f32_e32 v3, v97, v152
	v_add_u32_e32 v0, 0x1ce8, v103
	ds_write2_b32 v0, v2, v3 offset1:1
	s_waitcnt lgkmcnt(0)
	ds_read2_b32 v[6:7], v99 offset0:33 offset1:41
	ds_read2_b32 v[8:9], v99 offset1:8
	ds_read2_b32 v[10:11], v99 offset0:66 offset1:74
	ds_read2_b32 v[12:13], v99 offset0:99 offset1:107
	ds_read2_b32 v[14:15], v99 offset0:132 offset1:140
	ds_read2_b32 v[16:17], v99 offset0:165 offset1:173
	ds_read2_b32 v[18:19], v99 offset0:198 offset1:206
	ds_read2_b32 v[20:21], v99 offset0:231 offset1:239
	v_lshl_add_u64 v[22:23], s[38:39], 0, v[124:125]
	v_lshlrev_b32_e32 v0, 1, v112
	s_waitcnt lgkmcnt(6)
	v_cvt_pk_bf16_f32 v2, v8, v6
	s_waitcnt lgkmcnt(4)
	v_cvt_pk_bf16_f32 v3, v10, v12
	s_waitcnt lgkmcnt(2)
	v_cvt_pk_bf16_f32 v4, v14, v16
	s_waitcnt lgkmcnt(0)
	v_cvt_pk_bf16_f32 v5, v18, v20
	v_lshl_add_u64 v[22:23], v[22:23], 0, v[0:1]
	global_store_dwordx4 v[22:23], v[2:5], off
	s_nop 1
	v_cvt_pk_bf16_f32 v2, v9, v7
	v_cvt_pk_bf16_f32 v3, v11, v13
	v_cvt_pk_bf16_f32 v4, v15, v17
	v_cvt_pk_bf16_f32 v5, v19, v21
	ds_read2_b32 v[8:9], v99 offset0:49 offset1:57
	ds_read2_b32 v[10:11], v99 offset0:16 offset1:24
	ds_read2_b32 v[12:13], v99 offset0:82 offset1:90
	ds_read2_b32 v[14:15], v99 offset0:115 offset1:123
	ds_read2_b32 v[16:17], v99 offset0:148 offset1:156
	ds_read2_b32 v[18:19], v99 offset0:181 offset1:189
	ds_read2_b32 v[20:21], v99 offset0:214 offset1:222
	ds_read2_b32 v[22:23], v99 offset0:247 offset1:255
	v_lshl_add_u64 v[6:7], s[38:39], 0, v[122:123]
	v_lshl_add_u64 v[6:7], v[6:7], 0, v[0:1]
	global_store_dwordx4 v[6:7], v[2:5], off
	v_lshl_add_u64 v[6:7], s[38:39], 0, v[118:119]
	v_lshl_add_u64 v[6:7], v[6:7], 0, v[0:1]
	s_waitcnt lgkmcnt(6)
	v_cvt_pk_bf16_f32 v2, v10, v8
	s_waitcnt lgkmcnt(4)
	v_cvt_pk_bf16_f32 v3, v12, v14
	s_waitcnt lgkmcnt(2)
	v_cvt_pk_bf16_f32 v4, v16, v18
	s_waitcnt lgkmcnt(0)
	v_cvt_pk_bf16_f32 v5, v20, v22
	global_store_dwordx4 v[6:7], v[2:5], off
	v_lshl_add_u64 v[6:7], s[38:39], 0, v[116:117]
	v_lshl_add_u64 v[6:7], v[6:7], 0, v[0:1]
	v_cvt_pk_bf16_f32 v2, v11, v9
	v_cvt_pk_bf16_f32 v3, v13, v15
	v_cvt_pk_bf16_f32 v4, v17, v19
	v_cvt_pk_bf16_f32 v5, v21, v23
	global_store_dwordx4 v[6:7], v[2:5], off
	s_waitcnt lgkmcnt(0)

.LBB0_754:
	s_andn2_b64 vcc, exec, s[36:37]
	s_cbranch_vccnz .LBB0_751
	s_cmp_eq_u32 s31, 0
	s_cbranch_scc1 .LBB0_750
	s_waitcnt vmcnt(3)
	v_mul_f32_e32 v34, v136, v34
	v_mul_f32_e32 v35, v136, v35
	ds_write2_b32 v103, v34, v35 offset1:1
	v_mul_f32_e32 v34, v136, v36
	v_mul_f32_e32 v35, v136, v37
	ds_write2_b32 v103, v34, v35 offset0:2 offset1:3
	v_mul_f32_e32 v34, v134, v42
	v_mul_f32_e32 v35, v134, v43
	v_add_u32_e32 v0, 0x420, v103
	ds_write2_b32 v0, v34, v35 offset1:1
	v_mul_f32_e32 v34, v134, v44
	v_mul_f32_e32 v35, v134, v45
	v_add_u32_e32 v0, 0x428, v103
	ds_write2_b32 v0, v34, v35 offset1:1
	s_waitcnt vmcnt(2)
	v_mul_f32_e32 v34, v138, v38
	v_mul_f32_e32 v35, v138, v39
	v_add_u32_e32 v0, 0x840, v103
	ds_write2_b32 v0, v34, v35 offset1:1
	v_mul_f32_e32 v34, v138, v40
	v_mul_f32_e32 v35, v138, v41
	v_add_u32_e32 v0, 0x848, v103
	ds_write2_b32 v0, v34, v35 offset1:1
	v_mul_f32_e32 v34, v130, v50
	v_mul_f32_e32 v35, v130, v51
	v_add_u32_e32 v0, 0xc60, v103
	ds_write2_b32 v0, v34, v35 offset1:1
	v_mul_f32_e32 v34, v130, v52
	v_mul_f32_e32 v35, v130, v53
	v_add_u32_e32 v0, 0xc68, v103
	ds_write2_b32 v0, v34, v35 offset1:1
	v_mul_f32_e32 v34, v132, v46
	v_mul_f32_e32 v35, v132, v47
	v_add_u32_e32 v0, 0x1080, v103
	ds_write2_b32 v0, v34, v35 offset1:1
	v_mul_f32_e32 v34, v132, v48
	v_mul_f32_e32 v35, v132, v49
	v_add_u32_e32 v0, 0x1088, v103
	ds_write2_b32 v0, v34, v35 offset1:1
	s_waitcnt vmcnt(0)
	v_mul_f32_e32 v34, v126, v58
	v_mul_f32_e32 v35, v126, v59
	v_add_u32_e32 v0, 0x14a0, v103
	ds_write2_b32 v0, v34, v35 offset1:1
	v_mul_f32_e32 v34, v126, v60
	v_mul_f32_e32 v35, v126, v61
	v_add_u32_e32 v0, 0x14a8, v103
	ds_write2_b32 v0, v34, v35 offset1:1
	v_mul_f32_e32 v34, v128, v54
	v_mul_f32_e32 v35, v128, v55
	v_add_u32_e32 v0, 0x18c0, v103
	ds_write2_b32 v0, v34, v35 offset1:1
	v_mul_f32_e32 v34, v128, v56
	v_mul_f32_e32 v35, v128, v57
	v_add_u32_e32 v0, 0x18c8, v103
	ds_write2_b32 v0, v34, v35 offset1:1
	v_mul_f32_e32 v34, v120, v66
	v_mul_f32_e32 v35, v120, v67
	v_add_u32_e32 v0, 0x1ce0, v103
	ds_write2_b32 v0, v34, v35 offset1:1
	v_mul_f32_e32 v34, v120, v68
	v_mul_f32_e32 v35, v120, v69
	v_add_u32_e32 v0, 0x1ce8, v103
	ds_write2_b32 v0, v34, v35 offset1:1
	s_waitcnt lgkmcnt(0)
	ds_read2_b32 v[38:39], v99 offset0:33 offset1:41
	ds_read2_b32 v[40:41], v99 offset1:8
	ds_read2_b32 v[42:43], v99 offset0:66 offset1:74
	ds_read2_b32 v[44:45], v99 offset0:99 offset1:107
	ds_read2_b32 v[46:47], v99 offset0:132 offset1:140
	ds_read2_b32 v[48:49], v99 offset0:165 offset1:173
	ds_read2_b32 v[50:51], v99 offset0:198 offset1:206
	ds_read2_b32 v[52:53], v99 offset0:231 offset1:239
	v_mad_u64_u32 v[54:55], s[36:37], s34, v102, 0
	v_lshl_add_u64 v[54:55], v[54:55], 1, s[14:15]
	v_lshlrev_b32_e32 v0, 1, v112
	s_waitcnt lgkmcnt(6)
	v_cvt_pk_bf16_f32 v34, v40, v38
	s_waitcnt lgkmcnt(4)
	v_cvt_pk_bf16_f32 v35, v42, v44
	s_waitcnt lgkmcnt(2)
	v_cvt_pk_bf16_f32 v36, v46, v48
	s_waitcnt lgkmcnt(0)
	v_cvt_pk_bf16_f32 v37, v50, v52
	v_lshl_add_u64 v[54:55], v[54:55], 0, v[0:1]
	global_store_dwordx4 v[54:55], v[34:37], off
	s_nop 1
	v_cvt_pk_bf16_f32 v34, v41, v39
	v_cvt_pk_bf16_f32 v35, v43, v45
	v_cvt_pk_bf16_f32 v36, v47, v49
	v_cvt_pk_bf16_f32 v37, v51, v53
	v_mad_u64_u32 v[38:39], s[36:37], s34, v110, 0
	ds_read2_b32 v[40:41], v99 offset0:16 offset1:24
	ds_read2_b32 v[42:43], v99 offset0:49 offset1:57
	ds_read2_b32 v[44:45], v99 offset0:82 offset1:90
	ds_read2_b32 v[46:47], v99 offset0:115 offset1:123
	ds_read2_b32 v[48:49], v99 offset0:148 offset1:156
	ds_read2_b32 v[50:51], v99 offset0:181 offset1:189
	ds_read2_b32 v[52:53], v99 offset0:214 offset1:222
	ds_read2_b32 v[54:55], v99 offset0:247 offset1:255
	v_lshl_add_u64 v[38:39], v[38:39], 1, s[14:15]
	v_lshl_add_u64 v[38:39], v[38:39], 0, v[0:1]
	global_store_dwordx4 v[38:39], v[34:37], off
	v_mad_u64_u32 v[38:39], s[36:37], s34, v108, 0
	v_lshl_add_u64 v[38:39], v[38:39], 1, s[14:15]
	s_waitcnt lgkmcnt(6)
	v_cvt_pk_bf16_f32 v34, v40, v42
	s_waitcnt lgkmcnt(4)
	v_cvt_pk_bf16_f32 v35, v44, v46
	s_waitcnt lgkmcnt(2)
	v_cvt_pk_bf16_f32 v36, v48, v50
	s_waitcnt lgkmcnt(0)
	v_cvt_pk_bf16_f32 v37, v52, v54
	v_lshl_add_u64 v[38:39], v[38:39], 0, v[0:1]
	global_store_dwordx4 v[38:39], v[34:37], off
	v_mad_u64_u32 v[38:39], s[36:37], s34, v106, 0
	v_lshl_add_u64 v[38:39], v[38:39], 1, s[14:15]
	v_cvt_pk_bf16_f32 v34, v41, v43
	v_cvt_pk_bf16_f32 v35, v45, v47
	v_cvt_pk_bf16_f32 v36, v49, v51
	v_cvt_pk_bf16_f32 v37, v53, v55
	v_lshl_add_u64 v[38:39], v[38:39], 0, v[0:1]
	global_store_dwordx4 v[38:39], v[34:37], off
	s_waitcnt lgkmcnt(0)
	s_branch .LBB0_750

.LBB0_759:
	s_and_b64 vcc, exec, s[16:17]
	s_cbranch_vccz .LBB0_763
	s_cmp_eq_u32 s31, 0
	s_cbranch_scc1 .LBB0_762
	s_waitcnt vmcnt(3)
	v_mul_f32_e32 v34, v34, v136
	v_mul_f32_e32 v35, v35, v136
	ds_write2_b32 v103, v34, v35 offset1:1
	v_mul_f32_e32 v34, v36, v136
	v_mul_f32_e32 v35, v37, v136
	ds_write2_b32 v103, v34, v35 offset0:2 offset1:3
	v_mul_f32_e32 v34, v42, v134
	v_mul_f32_e32 v35, v43, v134
	v_add_u32_e32 v0, 0x420, v103
	ds_write2_b32 v0, v34, v35 offset1:1
	v_mul_f32_e32 v34, v44, v134
	v_mul_f32_e32 v35, v45, v134
	v_add_u32_e32 v0, 0x428, v103
	ds_write2_b32 v0, v34, v35 offset1:1
	s_waitcnt vmcnt(2)
	v_mul_f32_e32 v34, v38, v138
	v_mul_f32_e32 v35, v39, v138
	v_add_u32_e32 v0, 0x840, v103
	ds_write2_b32 v0, v34, v35 offset1:1
	v_mul_f32_e32 v34, v40, v138
	v_mul_f32_e32 v35, v41, v138
	v_add_u32_e32 v0, 0x848, v103
	ds_write2_b32 v0, v34, v35 offset1:1
	v_mul_f32_e32 v34, v50, v130
	v_mul_f32_e32 v35, v51, v130
	v_add_u32_e32 v0, 0xc60, v103
	ds_write2_b32 v0, v34, v35 offset1:1
	v_mul_f32_e32 v34, v52, v130
	v_mul_f32_e32 v35, v53, v130
	v_add_u32_e32 v0, 0xc68, v103
	ds_write2_b32 v0, v34, v35 offset1:1
	v_mul_f32_e32 v34, v46, v132
	v_mul_f32_e32 v35, v47, v132
	v_add_u32_e32 v0, 0x1080, v103
	ds_write2_b32 v0, v34, v35 offset1:1
	v_mul_f32_e32 v34, v48, v132
	v_mul_f32_e32 v35, v49, v132
	v_add_u32_e32 v0, 0x1088, v103
	ds_write2_b32 v0, v34, v35 offset1:1
	s_waitcnt vmcnt(0)
	v_mul_f32_e32 v34, v58, v126
	v_mul_f32_e32 v35, v59, v126
	v_add_u32_e32 v0, 0x14a0, v103
	ds_write2_b32 v0, v34, v35 offset1:1
	v_mul_f32_e32 v34, v60, v126
	v_mul_f32_e32 v35, v61, v126
	v_add_u32_e32 v0, 0x14a8, v103
	ds_write2_b32 v0, v34, v35 offset1:1
	v_mul_f32_e32 v34, v54, v128
	v_mul_f32_e32 v35, v55, v128
	v_add_u32_e32 v0, 0x18c0, v103
	ds_write2_b32 v0, v34, v35 offset1:1
	v_mul_f32_e32 v34, v56, v128
	v_mul_f32_e32 v35, v57, v128
	v_add_u32_e32 v0, 0x18c8, v103
	ds_write2_b32 v0, v34, v35 offset1:1
	v_mul_f32_e32 v34, v66, v120
	v_mul_f32_e32 v35, v67, v120
	v_add_u32_e32 v0, 0x1ce0, v103
	ds_write2_b32 v0, v34, v35 offset1:1
	v_mul_f32_e32 v34, v68, v120
	v_mul_f32_e32 v35, v69, v120
	v_add_u32_e32 v0, 0x1ce8, v103
	ds_write2_b32 v0, v34, v35 offset1:1
	s_waitcnt lgkmcnt(0)
	ds_read2_b32 v[38:39], v99 offset0:33 offset1:41
	ds_read2_b32 v[40:41], v99 offset1:8
	ds_read2_b32 v[42:43], v99 offset0:66 offset1:74
	ds_read2_b32 v[44:45], v99 offset0:99 offset1:107
	ds_read2_b32 v[46:47], v99 offset0:132 offset1:140
	ds_read2_b32 v[48:49], v99 offset0:165 offset1:173
	ds_read2_b32 v[50:51], v99 offset0:198 offset1:206
	ds_read2_b32 v[52:53], v99 offset0:231 offset1:239
	v_mul_u32_u24_e32 v0, s34, v102
	v_lshlrev_b32_e32 v0, 1, v0
	v_lshl_add_u64 v[54:55], s[14:15], 0, v[0:1]
	v_lshlrev_b32_e32 v0, 1, v112
	s_lshl_b32 s14, s34, 3
	s_waitcnt lgkmcnt(6)
	v_cvt_pk_bf16_f32 v34, v40, v38
	s_waitcnt lgkmcnt(4)
	v_cvt_pk_bf16_f32 v35, v42, v44
	s_waitcnt lgkmcnt(2)
	v_cvt_pk_bf16_f32 v36, v46, v48
	s_waitcnt lgkmcnt(0)
	v_cvt_pk_bf16_f32 v37, v50, v52
	v_lshl_add_u64 v[56:57], v[54:55], 0, v[0:1]
	s_ashr_i32 s15, s14, 31
	global_store_dwordx4 v[56:57], v[34:37], off
	s_lshl_b64 s[14:15], s[14:15], 1
	s_nop 0
	v_cvt_pk_bf16_f32 v34, v41, v39
	v_cvt_pk_bf16_f32 v35, v43, v45
	v_cvt_pk_bf16_f32 v36, v47, v49
	v_cvt_pk_bf16_f32 v37, v51, v53
	v_lshl_add_u64 v[38:39], v[54:55], 0, s[14:15]
	ds_read2_b32 v[42:43], v99 offset0:16 offset1:24
	ds_read2_b32 v[44:45], v99 offset0:49 offset1:57
	ds_read2_b32 v[46:47], v99 offset0:82 offset1:90
	ds_read2_b32 v[48:49], v99 offset0:115 offset1:123
	ds_read2_b32 v[50:51], v99 offset0:148 offset1:156
	ds_read2_b32 v[52:53], v99 offset0:181 offset1:189
	ds_read2_b32 v[54:55], v99 offset0:214 offset1:222
	ds_read2_b32 v[56:57], v99 offset0:247 offset1:255
	v_lshl_add_u64 v[40:41], v[38:39], 0, v[0:1]
	v_lshl_add_u64 v[38:39], v[38:39], 0, s[14:15]
	global_store_dwordx4 v[40:41], v[34:37], off
	v_lshl_add_u64 v[40:41], v[38:39], 0, v[0:1]
	v_lshl_add_u64 v[38:39], v[38:39], 0, s[14:15]
	s_waitcnt lgkmcnt(6)
	v_cvt_pk_bf16_f32 v34, v42, v44
	s_waitcnt lgkmcnt(4)
	v_cvt_pk_bf16_f32 v35, v46, v48
	s_waitcnt lgkmcnt(2)
	v_cvt_pk_bf16_f32 v36, v50, v52
	s_waitcnt lgkmcnt(0)
	v_cvt_pk_bf16_f32 v37, v54, v56
	global_store_dwordx4 v[40:41], v[34:37], off
	v_lshl_add_u64 v[38:39], v[38:39], 0, v[0:1]
	s_nop 0
	v_cvt_pk_bf16_f32 v34, v43, v45
	v_cvt_pk_bf16_f32 v35, v47, v49
	v_cvt_pk_bf16_f32 v36, v51, v53
	v_cvt_pk_bf16_f32 v37, v55, v57
	global_store_dwordx4 v[38:39], v[34:37], off
	s_waitcnt lgkmcnt(0)

.LBB0_781:
	s_andn2_b64 vcc, exec, s[46:47]
	s_cbranch_vccnz .LBB0_785
	s_cmp_eq_u32 s31, 0
	s_cbranch_scc1 .LBB0_784
	v_mul_f32_e32 v26, v134, v26
	v_mul_f32_e32 v27, v134, v27
	v_add_u32_e32 v0, 0x420, v103
	ds_write2_b32 v0, v26, v27 offset1:1
	v_mul_f32_e32 v26, v134, v28
	v_mul_f32_e32 v27, v134, v29
	v_add_u32_e32 v0, 0x428, v103
	ds_write2_b32 v0, v26, v27 offset1:1
	v_mul_f32_e32 v22, v138, v22
	v_mul_f32_e32 v23, v138, v23
	v_add_u32_e32 v0, 0x840, v103
	ds_write2_b32 v0, v22, v23 offset1:1
	v_mul_f32_e32 v22, v138, v24
	v_mul_f32_e32 v23, v138, v25
	v_add_u32_e32 v0, 0x848, v103
	ds_write2_b32 v0, v22, v23 offset1:1
	v_mul_f32_e32 v18, v130, v18
	v_mul_f32_e32 v19, v130, v19
	v_add_u32_e32 v0, 0xc60, v103
	ds_write2_b32 v0, v18, v19 offset1:1
	v_mul_f32_e32 v18, v130, v20
	v_mul_f32_e32 v19, v130, v21
	v_add_u32_e32 v0, 0xc68, v103
	ds_write2_b32 v0, v18, v19 offset1:1
	v_mul_f32_e32 v14, v132, v14
	v_mul_f32_e32 v15, v132, v15
	v_add_u32_e32 v0, 0x1080, v103
	ds_write2_b32 v0, v14, v15 offset1:1
	v_mul_f32_e32 v14, v132, v16
	v_mul_f32_e32 v15, v132, v17
	v_add_u32_e32 v0, 0x1088, v103
	ds_write2_b32 v0, v14, v15 offset1:1
	s_waitcnt vmcnt(2)
	v_mul_f32_e32 v10, v126, v10
	v_mul_f32_e32 v11, v126, v11
	v_add_u32_e32 v0, 0x14a0, v103
	ds_write2_b32 v0, v10, v11 offset1:1
	v_mul_f32_e32 v10, v126, v12
	v_mul_f32_e32 v11, v126, v13
	v_add_u32_e32 v0, 0x14a8, v103
	ds_write2_b32 v0, v10, v11 offset1:1
	s_waitcnt vmcnt(1)
	v_mul_f32_e32 v6, v128, v6
	v_mul_f32_e32 v7, v128, v7
	v_add_u32_e32 v0, 0x18c0, v103
	ds_write2_b32 v0, v6, v7 offset1:1
	v_mul_f32_e32 v6, v128, v8
	v_mul_f32_e32 v7, v128, v9
	v_add_u32_e32 v0, 0x18c8, v103
	s_waitcnt vmcnt(0)
	v_mul_f32_e32 v30, v136, v30
	v_mul_f32_e32 v31, v136, v31
	ds_write2_b32 v0, v6, v7 offset1:1
	v_mul_f32_e32 v2, v120, v2
	v_mul_f32_e32 v3, v120, v3
	v_add_u32_e32 v0, 0x1ce0, v103
	ds_write2_b32 v103, v30, v31 offset1:1
	v_mul_f32_e32 v30, v136, v32
	v_mul_f32_e32 v31, v136, v33
	ds_write2_b32 v0, v2, v3 offset1:1
	v_mul_f32_e32 v2, v120, v4
	v_mul_f32_e32 v3, v120, v5
	v_add_u32_e32 v0, 0x1ce8, v103
	ds_write2_b32 v103, v30, v31 offset0:2 offset1:3
	ds_write2_b32 v0, v2, v3 offset1:1
	s_waitcnt lgkmcnt(0)
	ds_read2_b32 v[6:7], v99 offset0:33 offset1:41
	ds_read2_b32 v[8:9], v99 offset1:8
	ds_read2_b32 v[10:11], v99 offset0:66 offset1:74
	ds_read2_b32 v[12:13], v99 offset0:99 offset1:107
	ds_read2_b32 v[14:15], v99 offset0:132 offset1:140
	ds_read2_b32 v[16:17], v99 offset0:165 offset1:173
	ds_read2_b32 v[18:19], v99 offset0:198 offset1:206
	ds_read2_b32 v[20:21], v99 offset0:231 offset1:239
	v_mad_u64_u32 v[22:23], s[36:37], s34, v102, 0
	v_lshl_add_u64 v[22:23], v[22:23], 1, s[0:1]
	v_lshlrev_b32_e32 v0, 1, v112
	s_waitcnt lgkmcnt(6)
	v_cvt_pk_bf16_f32 v2, v8, v6
	s_waitcnt lgkmcnt(4)
	v_cvt_pk_bf16_f32 v3, v10, v12
	s_waitcnt lgkmcnt(2)
	v_cvt_pk_bf16_f32 v4, v14, v16
	s_waitcnt lgkmcnt(0)
	v_cvt_pk_bf16_f32 v5, v18, v20
	v_lshl_add_u64 v[22:23], v[22:23], 0, v[0:1]
	global_store_dwordx4 v[22:23], v[2:5], off
	s_nop 1
	v_cvt_pk_bf16_f32 v2, v9, v7
	v_cvt_pk_bf16_f32 v3, v11, v13
	v_cvt_pk_bf16_f32 v4, v15, v17
	v_cvt_pk_bf16_f32 v5, v19, v21
	v_mad_u64_u32 v[6:7], s[36:37], s34, v110, 0
	ds_read2_b32 v[8:9], v99 offset0:16 offset1:24
	ds_read2_b32 v[10:11], v99 offset0:49 offset1:57
	ds_read2_b32 v[12:13], v99 offset0:82 offset1:90
	ds_read2_b32 v[14:15], v99 offset0:115 offset1:123
	ds_read2_b32 v[16:17], v99 offset0:148 offset1:156
	ds_read2_b32 v[18:19], v99 offset0:181 offset1:189
	ds_read2_b32 v[20:21], v99 offset0:214 offset1:222
	ds_read2_b32 v[22:23], v99 offset0:247 offset1:255
	v_lshl_add_u64 v[6:7], v[6:7], 1, s[0:1]
	v_lshl_add_u64 v[6:7], v[6:7], 0, v[0:1]
	global_store_dwordx4 v[6:7], v[2:5], off
	v_mad_u64_u32 v[6:7], s[36:37], s34, v108, 0
	v_lshl_add_u64 v[6:7], v[6:7], 1, s[0:1]
	s_waitcnt lgkmcnt(6)
	v_cvt_pk_bf16_f32 v2, v8, v10
	s_waitcnt lgkmcnt(4)
	v_cvt_pk_bf16_f32 v3, v12, v14
	s_waitcnt lgkmcnt(2)
	v_cvt_pk_bf16_f32 v4, v16, v18
	s_waitcnt lgkmcnt(0)
	v_cvt_pk_bf16_f32 v5, v20, v22
	v_lshl_add_u64 v[6:7], v[6:7], 0, v[0:1]
	global_store_dwordx4 v[6:7], v[2:5], off
	v_mad_u64_u32 v[6:7], s[36:37], s34, v106, 0
	v_lshl_add_u64 v[6:7], v[6:7], 1, s[0:1]
	v_cvt_pk_bf16_f32 v2, v9, v11
	v_cvt_pk_bf16_f32 v3, v13, v15
	v_cvt_pk_bf16_f32 v4, v17, v19
	v_cvt_pk_bf16_f32 v5, v21, v23
	v_lshl_add_u64 v[6:7], v[6:7], 0, v[0:1]
	global_store_dwordx4 v[6:7], v[2:5], off
	s_waitcnt lgkmcnt(0)

.LBB0_799:
	s_andn2_b64 vcc, exec, s[46:47]
	s_cbranch_vccnz .LBB0_766
	s_cmp_eq_u32 s31, 0
	s_cbranch_scc1 .LBB0_765
	v_mul_f32_e32 v26, v26, v134
	v_mul_f32_e32 v27, v27, v134
	v_add_u32_e32 v0, 0x420, v103
	ds_write2_b32 v0, v26, v27 offset1:1
	v_mul_f32_e32 v26, v28, v134
	v_mul_f32_e32 v27, v29, v134
	v_add_u32_e32 v0, 0x428, v103
	ds_write2_b32 v0, v26, v27 offset1:1
	v_mul_f32_e32 v22, v22, v138
	v_mul_f32_e32 v23, v23, v138
	v_add_u32_e32 v0, 0x840, v103
	ds_write2_b32 v0, v22, v23 offset1:1
	v_mul_f32_e32 v22, v24, v138
	v_mul_f32_e32 v23, v25, v138
	v_add_u32_e32 v0, 0x848, v103
	ds_write2_b32 v0, v22, v23 offset1:1
	v_mul_f32_e32 v18, v18, v130
	v_mul_f32_e32 v19, v19, v130
	v_add_u32_e32 v0, 0xc60, v103
	ds_write2_b32 v0, v18, v19 offset1:1
	v_mul_f32_e32 v18, v20, v130
	v_mul_f32_e32 v19, v21, v130
	v_add_u32_e32 v0, 0xc68, v103
	ds_write2_b32 v0, v18, v19 offset1:1
	v_mul_f32_e32 v14, v14, v132
	v_mul_f32_e32 v15, v15, v132
	v_add_u32_e32 v0, 0x1080, v103
	ds_write2_b32 v0, v14, v15 offset1:1
	v_mul_f32_e32 v14, v16, v132
	v_mul_f32_e32 v15, v17, v132
	v_add_u32_e32 v0, 0x1088, v103
	ds_write2_b32 v0, v14, v15 offset1:1
	s_waitcnt vmcnt(2)
	v_mul_f32_e32 v10, v10, v126
	v_mul_f32_e32 v11, v11, v126
	v_add_u32_e32 v0, 0x14a0, v103
	ds_write2_b32 v0, v10, v11 offset1:1
	v_mul_f32_e32 v10, v12, v126
	v_mul_f32_e32 v11, v13, v126
	v_add_u32_e32 v0, 0x14a8, v103
	ds_write2_b32 v0, v10, v11 offset1:1
	s_waitcnt vmcnt(1)
	v_mul_f32_e32 v6, v6, v128
	v_mul_f32_e32 v7, v7, v128
	v_add_u32_e32 v0, 0x18c0, v103
	ds_write2_b32 v0, v6, v7 offset1:1
	v_mul_f32_e32 v6, v8, v128
	v_mul_f32_e32 v7, v9, v128
	v_add_u32_e32 v0, 0x18c8, v103
	s_waitcnt vmcnt(0)
	v_mul_f32_e32 v30, v30, v136
	v_mul_f32_e32 v31, v31, v136
	ds_write2_b32 v0, v6, v7 offset1:1
	v_mul_f32_e32 v2, v2, v120
	v_mul_f32_e32 v3, v3, v120
	v_add_u32_e32 v0, 0x1ce0, v103
	ds_write2_b32 v103, v30, v31 offset1:1
	v_mul_f32_e32 v30, v32, v136
	v_mul_f32_e32 v31, v33, v136
	ds_write2_b32 v0, v2, v3 offset1:1
	v_mul_f32_e32 v2, v4, v120
	v_mul_f32_e32 v3, v5, v120
	v_add_u32_e32 v0, 0x1ce8, v103
	ds_write2_b32 v103, v30, v31 offset0:2 offset1:3
	ds_write2_b32 v0, v2, v3 offset1:1
	s_waitcnt lgkmcnt(0)
	ds_read2_b32 v[6:7], v99 offset0:33 offset1:41
	ds_read2_b32 v[8:9], v99 offset1:8
	ds_read2_b32 v[10:11], v99 offset0:66 offset1:74
	ds_read2_b32 v[12:13], v99 offset0:99 offset1:107
	ds_read2_b32 v[14:15], v99 offset0:132 offset1:140
	ds_read2_b32 v[16:17], v99 offset0:165 offset1:173
	ds_read2_b32 v[18:19], v99 offset0:198 offset1:206
	ds_read2_b32 v[20:21], v99 offset0:231 offset1:239
	v_mad_u64_u32 v[22:23], s[36:37], s34, v102, 0
	v_lshl_add_u64 v[22:23], v[22:23], 1, s[0:1]
	v_lshlrev_b32_e32 v0, 1, v112
	s_waitcnt lgkmcnt(6)
	v_cvt_pk_bf16_f32 v2, v8, v6
	s_waitcnt lgkmcnt(4)
	v_cvt_pk_bf16_f32 v3, v10, v12
	s_waitcnt lgkmcnt(2)
	v_cvt_pk_bf16_f32 v4, v14, v16
	s_waitcnt lgkmcnt(0)
	v_cvt_pk_bf16_f32 v5, v18, v20
	v_lshl_add_u64 v[22:23], v[22:23], 0, v[0:1]
	global_store_dwordx4 v[22:23], v[2:5], off
	s_nop 1
	v_cvt_pk_bf16_f32 v2, v9, v7
	v_cvt_pk_bf16_f32 v3, v11, v13
	v_cvt_pk_bf16_f32 v4, v15, v17
	v_cvt_pk_bf16_f32 v5, v19, v21
	v_mad_u64_u32 v[6:7], s[36:37], s34, v110, 0
	ds_read2_b32 v[8:9], v99 offset0:16 offset1:24
	ds_read2_b32 v[10:11], v99 offset0:49 offset1:57
	ds_read2_b32 v[12:13], v99 offset0:82 offset1:90
	ds_read2_b32 v[14:15], v99 offset0:115 offset1:123
	ds_read2_b32 v[16:17], v99 offset0:148 offset1:156
	ds_read2_b32 v[18:19], v99 offset0:181 offset1:189
	ds_read2_b32 v[20:21], v99 offset0:214 offset1:222
	ds_read2_b32 v[22:23], v99 offset0:247 offset1:255
	v_lshl_add_u64 v[6:7], v[6:7], 1, s[0:1]
	v_lshl_add_u64 v[6:7], v[6:7], 0, v[0:1]
	global_store_dwordx4 v[6:7], v[2:5], off
	v_mad_u64_u32 v[6:7], s[36:37], s34, v108, 0
	v_lshl_add_u64 v[6:7], v[6:7], 1, s[0:1]
	s_waitcnt lgkmcnt(6)
	v_cvt_pk_bf16_f32 v2, v8, v10
	s_waitcnt lgkmcnt(4)
	v_cvt_pk_bf16_f32 v3, v12, v14
	s_waitcnt lgkmcnt(2)
	v_cvt_pk_bf16_f32 v4, v16, v18
	s_waitcnt lgkmcnt(0)
	v_cvt_pk_bf16_f32 v5, v20, v22
	v_lshl_add_u64 v[6:7], v[6:7], 0, v[0:1]
	global_store_dwordx4 v[6:7], v[2:5], off
	v_mad_u64_u32 v[6:7], s[36:37], s34, v106, 0
	v_lshl_add_u64 v[6:7], v[6:7], 1, s[0:1]
	v_cvt_pk_bf16_f32 v2, v9, v11
	v_cvt_pk_bf16_f32 v3, v13, v15
	v_cvt_pk_bf16_f32 v4, v17, v19
	v_cvt_pk_bf16_f32 v5, v21, v23
	v_lshl_add_u64 v[6:7], v[6:7], 0, v[0:1]
	global_store_dwordx4 v[6:7], v[2:5], off
	s_waitcnt lgkmcnt(0)
	s_branch .LBB0_765

.LBB0_812:
	s_andn2_b64 vcc, exec, s[16:17]
	s_cbranch_vccnz .LBB0_816
	s_cmp_eq_u32 s31, 0
	s_cbranch_scc1 .LBB0_815
	v_mul_f32_e32 v26, v26, v134
	v_mul_f32_e32 v27, v27, v134
	v_add_u32_e32 v0, 0x420, v103
	ds_write2_b32 v0, v26, v27 offset1:1
	v_mul_f32_e32 v26, v28, v134
	v_mul_f32_e32 v27, v29, v134
	v_add_u32_e32 v0, 0x428, v103
	ds_write2_b32 v0, v26, v27 offset1:1
	v_mul_f32_e32 v22, v22, v138
	v_mul_f32_e32 v23, v23, v138
	v_add_u32_e32 v0, 0x840, v103
	ds_write2_b32 v0, v22, v23 offset1:1
	v_mul_f32_e32 v22, v24, v138
	v_mul_f32_e32 v23, v25, v138
	v_add_u32_e32 v0, 0x848, v103
	ds_write2_b32 v0, v22, v23 offset1:1
	v_mul_f32_e32 v18, v18, v130
	v_mul_f32_e32 v19, v19, v130
	v_add_u32_e32 v0, 0xc60, v103
	ds_write2_b32 v0, v18, v19 offset1:1
	v_mul_f32_e32 v18, v20, v130
	v_mul_f32_e32 v19, v21, v130
	v_add_u32_e32 v0, 0xc68, v103
	ds_write2_b32 v0, v18, v19 offset1:1
	v_mul_f32_e32 v14, v14, v132
	v_mul_f32_e32 v15, v15, v132
	v_add_u32_e32 v0, 0x1080, v103
	ds_write2_b32 v0, v14, v15 offset1:1
	v_mul_f32_e32 v14, v16, v132
	v_mul_f32_e32 v15, v17, v132
	v_add_u32_e32 v0, 0x1088, v103
	ds_write2_b32 v0, v14, v15 offset1:1
	s_waitcnt vmcnt(2)
	v_mul_f32_e32 v10, v10, v126
	v_mul_f32_e32 v11, v11, v126
	v_add_u32_e32 v0, 0x14a0, v103
	ds_write2_b32 v0, v10, v11 offset1:1
	v_mul_f32_e32 v10, v12, v126
	v_mul_f32_e32 v11, v13, v126
	v_add_u32_e32 v0, 0x14a8, v103
	ds_write2_b32 v0, v10, v11 offset1:1
	s_waitcnt vmcnt(1)
	v_mul_f32_e32 v6, v6, v128
	v_mul_f32_e32 v7, v7, v128
	v_add_u32_e32 v0, 0x18c0, v103
	ds_write2_b32 v0, v6, v7 offset1:1
	v_mul_f32_e32 v6, v8, v128
	v_mul_f32_e32 v7, v9, v128
	v_add_u32_e32 v0, 0x18c8, v103
	s_waitcnt vmcnt(0)
	v_mul_f32_e32 v30, v30, v136
	v_mul_f32_e32 v31, v31, v136
	ds_write2_b32 v0, v6, v7 offset1:1
	v_mul_f32_e32 v2, v2, v120
	v_mul_f32_e32 v3, v3, v120
	v_add_u32_e32 v0, 0x1ce0, v103
	ds_write2_b32 v103, v30, v31 offset1:1
	v_mul_f32_e32 v30, v32, v136
	v_mul_f32_e32 v31, v33, v136
	ds_write2_b32 v0, v2, v3 offset1:1
	v_mul_f32_e32 v2, v4, v120
	v_mul_f32_e32 v3, v5, v120
	v_add_u32_e32 v0, 0x1ce8, v103
	ds_write2_b32 v103, v30, v31 offset0:2 offset1:3
	ds_write2_b32 v0, v2, v3 offset1:1
	s_waitcnt lgkmcnt(0)
	ds_read2_b32 v[6:7], v99 offset0:33 offset1:41
	ds_read2_b32 v[8:9], v99 offset1:8
	ds_read2_b32 v[10:11], v99 offset0:66 offset1:74
	ds_read2_b32 v[12:13], v99 offset0:99 offset1:107
	ds_read2_b32 v[14:15], v99 offset0:132 offset1:140
	ds_read2_b32 v[16:17], v99 offset0:165 offset1:173
	ds_read2_b32 v[18:19], v99 offset0:198 offset1:206
	ds_read2_b32 v[20:21], v99 offset0:231 offset1:239
	v_mad_u64_u32 v[22:23], s[16:17], s34, v102, 0
	v_lshl_add_u64 v[22:23], v[22:23], 1, s[0:1]
	v_lshlrev_b32_e32 v0, 1, v112
	s_waitcnt lgkmcnt(6)
	v_cvt_pk_bf16_f32 v2, v8, v6
	s_waitcnt lgkmcnt(4)
	v_cvt_pk_bf16_f32 v3, v10, v12
	s_waitcnt lgkmcnt(2)
	v_cvt_pk_bf16_f32 v4, v14, v16
	s_waitcnt lgkmcnt(0)
	v_cvt_pk_bf16_f32 v5, v18, v20
	v_lshl_add_u64 v[22:23], v[22:23], 0, v[0:1]
	global_store_dwordx4 v[22:23], v[2:5], off
	s_nop 1
	v_cvt_pk_bf16_f32 v2, v9, v7
	v_cvt_pk_bf16_f32 v3, v11, v13
	v_cvt_pk_bf16_f32 v4, v15, v17
	v_cvt_pk_bf16_f32 v5, v19, v21
	v_mad_u64_u32 v[6:7], s[16:17], s34, v110, 0
	ds_read2_b32 v[8:9], v99 offset0:16 offset1:24
	ds_read2_b32 v[10:11], v99 offset0:49 offset1:57
	ds_read2_b32 v[12:13], v99 offset0:82 offset1:90
	ds_read2_b32 v[14:15], v99 offset0:115 offset1:123
	ds_read2_b32 v[16:17], v99 offset0:148 offset1:156
	ds_read2_b32 v[18:19], v99 offset0:181 offset1:189
	ds_read2_b32 v[20:21], v99 offset0:214 offset1:222
	ds_read2_b32 v[22:23], v99 offset0:247 offset1:255
	v_lshl_add_u64 v[6:7], v[6:7], 1, s[0:1]
	v_lshl_add_u64 v[6:7], v[6:7], 0, v[0:1]
	global_store_dwordx4 v[6:7], v[2:5], off
	v_mad_u64_u32 v[6:7], s[16:17], s34, v108, 0
	v_lshl_add_u64 v[6:7], v[6:7], 1, s[0:1]
	s_waitcnt lgkmcnt(6)
	v_cvt_pk_bf16_f32 v2, v8, v10
	s_waitcnt lgkmcnt(4)
	v_cvt_pk_bf16_f32 v3, v12, v14
	s_waitcnt lgkmcnt(2)
	v_cvt_pk_bf16_f32 v4, v16, v18
	s_waitcnt lgkmcnt(0)
	v_cvt_pk_bf16_f32 v5, v20, v22
	v_lshl_add_u64 v[6:7], v[6:7], 0, v[0:1]
	global_store_dwordx4 v[6:7], v[2:5], off
	v_mad_u64_u32 v[6:7], s[16:17], s34, v106, 0
	v_lshl_add_u64 v[6:7], v[6:7], 1, s[0:1]
	v_cvt_pk_bf16_f32 v2, v9, v11
	v_cvt_pk_bf16_f32 v3, v13, v15
	v_cvt_pk_bf16_f32 v4, v17, v19
	v_cvt_pk_bf16_f32 v5, v21, v23
	v_lshl_add_u64 v[6:7], v[6:7], 0, v[0:1]
	global_store_dwordx4 v[6:7], v[2:5], off
	s_waitcnt lgkmcnt(0)

.LBB0_817:
	s_waitcnt vmcnt(0)
	v_mul_f32_e32 v2, v62, v136
	v_mul_f32_e32 v3, v63, v136
	ds_write2_b32 v103, v2, v3 offset1:1
	v_mul_f32_e32 v2, v64, v136
	v_mul_f32_e32 v3, v65, v136
	ds_write2_b32 v103, v2, v3 offset0:2 offset1:3
	v_mul_f32_e32 v2, v50, v134
	v_mul_f32_e32 v3, v51, v134
	v_add_u32_e32 v0, 0x420, v103
	ds_write2_b32 v0, v2, v3 offset1:1
	v_mul_f32_e32 v2, v52, v134
	v_mul_f32_e32 v3, v53, v134
	v_add_u32_e32 v0, 0x428, v103
	ds_write2_b32 v0, v2, v3 offset1:1
	v_mul_f32_e32 v2, v58, v138
	v_mul_f32_e32 v3, v59, v138
	v_add_u32_e32 v0, 0x840, v103
	ds_write2_b32 v0, v2, v3 offset1:1
	v_mul_f32_e32 v2, v60, v138
	v_mul_f32_e32 v3, v61, v138
	v_add_u32_e32 v0, 0x848, v103
	ds_write2_b32 v0, v2, v3 offset1:1
	v_mul_f32_e32 v2, v42, v130
	v_mul_f32_e32 v3, v43, v130
	v_add_u32_e32 v0, 0xc60, v103
	ds_write2_b32 v0, v2, v3 offset1:1
	v_mul_f32_e32 v2, v44, v130
	v_mul_f32_e32 v3, v45, v130
	v_add_u32_e32 v0, 0xc68, v103
	ds_write2_b32 v0, v2, v3 offset1:1
	v_mul_f32_e32 v2, v54, v132
	v_mul_f32_e32 v3, v55, v132
	v_add_u32_e32 v0, 0x1080, v103
	ds_write2_b32 v0, v2, v3 offset1:1
	v_mul_f32_e32 v2, v56, v132
	v_mul_f32_e32 v3, v57, v132
	v_add_u32_e32 v0, 0x1088, v103
	ds_write2_b32 v0, v2, v3 offset1:1
	v_mul_f32_e32 v2, v38, v126
	v_mul_f32_e32 v3, v39, v126
	v_add_u32_e32 v0, 0x14a0, v103
	ds_write2_b32 v0, v2, v3 offset1:1
	v_mul_f32_e32 v2, v40, v126
	v_mul_f32_e32 v3, v41, v126
	v_add_u32_e32 v0, 0x14a8, v103
	ds_write2_b32 v0, v2, v3 offset1:1
	v_mul_f32_e32 v2, v46, v128
	v_mul_f32_e32 v3, v47, v128
	v_add_u32_e32 v0, 0x18c0, v103
	ds_write2_b32 v0, v2, v3 offset1:1
	v_mul_f32_e32 v2, v48, v128
	v_mul_f32_e32 v3, v49, v128
	v_add_u32_e32 v0, 0x18c8, v103
	ds_write2_b32 v0, v2, v3 offset1:1
	v_mul_f32_e32 v2, v34, v120
	v_mul_f32_e32 v3, v35, v120
	v_add_u32_e32 v0, 0x1ce0, v103
	ds_write2_b32 v0, v2, v3 offset1:1
	v_mul_f32_e32 v2, v36, v120
	v_mul_f32_e32 v3, v37, v120
	v_add_u32_e32 v0, 0x1ce8, v103
	ds_write2_b32 v0, v2, v3 offset1:1
	s_waitcnt lgkmcnt(0)
	ds_read2_b32 v[6:7], v99 offset0:33 offset1:41
	ds_read2_b32 v[8:9], v99 offset1:8
	ds_read2_b32 v[10:11], v99 offset0:66 offset1:74
	ds_read2_b32 v[12:13], v99 offset0:99 offset1:107
	ds_read2_b32 v[14:15], v99 offset0:132 offset1:140
	ds_read2_b32 v[16:17], v99 offset0:165 offset1:173
	ds_read2_b32 v[18:19], v99 offset0:198 offset1:206
	ds_read2_b32 v[20:21], v99 offset0:231 offset1:239
	v_mad_u64_u32 v[22:23], s[0:1], s34, v102, 0
	v_lshl_add_u64 v[22:23], v[22:23], 1, s[14:15]
	v_lshlrev_b32_e32 v0, 1, v112
	s_waitcnt lgkmcnt(6)
	v_cvt_pk_bf16_f32 v2, v8, v6
	s_waitcnt lgkmcnt(4)
	v_cvt_pk_bf16_f32 v3, v10, v12
	s_waitcnt lgkmcnt(2)
	v_cvt_pk_bf16_f32 v4, v14, v16
	s_waitcnt lgkmcnt(0)
	v_cvt_pk_bf16_f32 v5, v18, v20
	v_lshl_add_u64 v[22:23], v[22:23], 0, v[0:1]
	global_store_dwordx4 v[22:23], v[2:5], off
	s_nop 1
	v_cvt_pk_bf16_f32 v2, v9, v7
	v_cvt_pk_bf16_f32 v3, v11, v13
	v_cvt_pk_bf16_f32 v4, v15, v17
	v_cvt_pk_bf16_f32 v5, v19, v21
	v_mad_u64_u32 v[6:7], s[0:1], s34, v110, 0
	ds_read2_b32 v[8:9], v99 offset0:16 offset1:24
	ds_read2_b32 v[10:11], v99 offset0:49 offset1:57
	ds_read2_b32 v[12:13], v99 offset0:82 offset1:90
	ds_read2_b32 v[14:15], v99 offset0:115 offset1:123
	ds_read2_b32 v[16:17], v99 offset0:148 offset1:156
	ds_read2_b32 v[18:19], v99 offset0:181 offset1:189
	ds_read2_b32 v[20:21], v99 offset0:214 offset1:222
	ds_read2_b32 v[22:23], v99 offset0:247 offset1:255
	v_lshl_add_u64 v[6:7], v[6:7], 1, s[14:15]
	v_lshl_add_u64 v[6:7], v[6:7], 0, v[0:1]
	global_store_dwordx4 v[6:7], v[2:5], off
	v_mad_u64_u32 v[6:7], s[0:1], s34, v108, 0
	v_lshl_add_u64 v[6:7], v[6:7], 1, s[14:15]
	s_waitcnt lgkmcnt(6)
	v_cvt_pk_bf16_f32 v2, v8, v10
	s_waitcnt lgkmcnt(4)
	v_cvt_pk_bf16_f32 v3, v12, v14
	s_waitcnt lgkmcnt(2)
	v_cvt_pk_bf16_f32 v4, v16, v18
	s_waitcnt lgkmcnt(0)
	v_cvt_pk_bf16_f32 v5, v20, v22
	v_lshl_add_u64 v[6:7], v[6:7], 0, v[0:1]
	global_store_dwordx4 v[6:7], v[2:5], off
	v_mad_u64_u32 v[6:7], s[0:1], s34, v106, 0
	v_lshl_add_u64 v[6:7], v[6:7], 1, s[14:15]
	v_cvt_pk_bf16_f32 v2, v9, v11
	v_cvt_pk_bf16_f32 v3, v13, v15
	v_cvt_pk_bf16_f32 v4, v17, v19
	v_cvt_pk_bf16_f32 v5, v21, v23
	v_lshl_add_u64 v[6:7], v[6:7], 0, v[0:1]
	global_store_dwordx4 v[6:7], v[2:5], off
	s_waitcnt lgkmcnt(0)

.LBB0_870:
	s_waitcnt vmcnt(0)
	v_lshlrev_b32_e32 v0, 16, v190
	v_max_f32_e32 v0, v0, v0
	v_max_f32_e32 v220, 0x2b800000, v0
	v_and_b32_e32 v0, 0xffff0000, v190
	v_max_f32_e32 v0, v0, v0
	v_max_f32_e32 v221, 0x2b800000, v0
	v_lshlrev_b32_e32 v0, 16, v191
	v_max_f32_e32 v0, v0, v0
	v_max_f32_e32 v222, 0x2b800000, v0
	v_and_b32_e32 v0, 0xffff0000, v191
	v_max_f32_e32 v0, v0, v0
	v_max_f32_e32 v223, 0x2b800000, v0
	v_lshlrev_b32_e32 v0, 16, v192
	v_max_f32_e32 v0, v0, v0
	v_max_f32_e32 v190, 0x2b800000, v0
	v_and_b32_e32 v0, 0xffff0000, v192
	v_max_f32_e32 v0, v0, v0
	v_max_f32_e32 v191, 0x2b800000, v0
	v_lshlrev_b32_e32 v0, 16, v193
	v_max_f32_e32 v0, v0, v0
	v_max_f32_e32 v192, 0x2b800000, v0
	v_and_b32_e32 v0, 0xffff0000, v193
	v_max_f32_e32 v0, v0, v0
	s_and_b64 vcc, exec, s[38:39]
	v_max_f32_e32 v193, 0x2b800000, v0
	s_cbranch_vccnz .LBB0_872
	v_lshlrev_b32_e32 v0, 16, v158
	v_max_f32_e32 v0, v0, v0
	v_max_f32_e32 v0, 0x2b800000, v0
	v_rcp_f32_e32 v226, v0
	v_and_b32_e32 v0, 0xffff0000, v158
	v_max_f32_e32 v0, v0, v0
	v_max_f32_e32 v0, 0x2b800000, v0
	v_rcp_f32_e32 v227, v0
	v_lshlrev_b32_e32 v0, 16, v159
	v_max_f32_e32 v0, v0, v0
	v_max_f32_e32 v0, 0x2b800000, v0
	v_rcp_f32_e32 v238, v0
	v_and_b32_e32 v0, 0xffff0000, v159
	v_max_f32_e32 v0, v0, v0
	v_max_f32_e32 v0, 0x2b800000, v0
	v_rcp_f32_e32 v239, v0
	v_lshlrev_b32_e32 v0, 16, v160
	v_max_f32_e32 v0, v0, v0
	v_max_f32_e32 v0, 0x2b800000, v0
	v_mul_f32_e32 v220, v220, v226
	v_mul_f32_e32 v221, v221, v227
	v_rcp_f32_e32 v226, v0
	v_and_b32_e32 v0, 0xffff0000, v160
	v_max_f32_e32 v0, v0, v0
	v_max_f32_e32 v0, 0x2b800000, v0
	v_rcp_f32_e32 v227, v0
	v_lshlrev_b32_e32 v0, 16, v161
	v_max_f32_e32 v0, v0, v0
	v_max_f32_e32 v0, 0x2b800000, v0
	v_mul_f32_e32 v222, v222, v238
	v_mul_f32_e32 v223, v223, v239
	v_rcp_f32_e32 v238, v0
	v_and_b32_e32 v0, 0xffff0000, v161
	v_max_f32_e32 v0, v0, v0
	v_max_f32_e32 v0, 0x2b800000, v0
	v_rcp_f32_e32 v239, v0
	v_mul_f32_e32 v190, v190, v226
	v_mul_f32_e32 v191, v191, v227
	v_mul_f32_e32 v192, v192, v238
	v_mul_f32_e32 v193, v193, v239
.LBB0_872:
	v_lshlrev_b64 v[226:227], 11, v[212:213]
	v_mul_f32_e32 v122, v122, v190
	v_mul_f32_e32 v123, v123, v191
	v_cndmask_b32_e64 v0, 0, 1, s[56:57]
	v_lshl_add_u64 v[190:191], s[14:15], 0, v[226:227]
	v_mul_f32_e32 v128, v128, v222
	v_mul_f32_e32 v129, v129, v223
	v_mul_f32_e32 v126, v126, v220
	v_mul_f32_e32 v127, v127, v221
	v_mul_f32_e32 v124, v124, v192
	v_mul_f32_e32 v125, v125, v193
	v_cmp_ne_u32_e64 s[40:41], 1, v0
	s_andn2_b64 vcc, exec, s[56:57]
	v_lshl_add_u64 v[190:191], v[210:211], 1, v[190:191]
	s_cbranch_vccnz .LBB0_874
	v_cvt_pk_bf16_f32 v220, v126, v127
	v_cvt_pk_bf16_f32 v221, v128, v129
	v_cvt_pk_bf16_f32 v222, v122, v123
	v_cvt_pk_bf16_f32 v223, v124, v125
	global_store_dwordx4 v[190:191], v[220:223], off
.LBB0_874:
	v_lshlrev_b32_e32 v0, 16, v186
	v_max_f32_e32 v0, v0, v0
	v_max_f32_e32 v192, 0x2b800000, v0
	v_and_b32_e32 v0, 0xffff0000, v186
	v_max_f32_e32 v0, v0, v0
	v_max_f32_e32 v193, 0x2b800000, v0
	v_lshlrev_b32_e32 v0, 16, v187
	v_max_f32_e32 v0, v0, v0
	v_max_f32_e32 v220, 0x2b800000, v0
	v_and_b32_e32 v0, 0xffff0000, v187
	v_max_f32_e32 v0, v0, v0
	v_max_f32_e32 v221, 0x2b800000, v0
	v_lshlrev_b32_e32 v0, 16, v188
	v_max_f32_e32 v0, v0, v0
	v_max_f32_e32 v186, 0x2b800000, v0
	v_and_b32_e32 v0, 0xffff0000, v188
	v_max_f32_e32 v0, v0, v0
	v_max_f32_e32 v187, 0x2b800000, v0
	v_lshlrev_b32_e32 v0, 16, v189
	v_max_f32_e32 v0, v0, v0
	v_max_f32_e32 v188, 0x2b800000, v0
	v_and_b32_e32 v0, 0xffff0000, v189
	v_max_f32_e32 v0, v0, v0
	s_and_b64 vcc, exec, s[38:39]
	v_max_f32_e32 v189, 0x2b800000, v0
	s_cbranch_vccnz .LBB0_876
	v_lshlrev_b32_e32 v0, 16, v154
	v_max_f32_e32 v0, v0, v0
	v_max_f32_e32 v0, 0x2b800000, v0
	v_rcp_f32_e32 v222, v0
	v_and_b32_e32 v0, 0xffff0000, v154
	v_max_f32_e32 v0, v0, v0
	v_max_f32_e32 v0, 0x2b800000, v0
	v_rcp_f32_e32 v223, v0
	v_lshlrev_b32_e32 v0, 16, v155
	v_max_f32_e32 v0, v0, v0
	v_max_f32_e32 v0, 0x2b800000, v0
	v_rcp_f32_e32 v226, v0
	v_and_b32_e32 v0, 0xffff0000, v155
	v_max_f32_e32 v0, v0, v0
	v_max_f32_e32 v0, 0x2b800000, v0
	v_rcp_f32_e32 v227, v0
	v_lshlrev_b32_e32 v0, 16, v156
	v_max_f32_e32 v0, v0, v0
	v_max_f32_e32 v0, 0x2b800000, v0
	v_mul_f32_e32 v192, v192, v222
	v_mul_f32_e32 v193, v193, v223
	v_rcp_f32_e32 v222, v0
	v_and_b32_e32 v0, 0xffff0000, v156
	v_max_f32_e32 v0, v0, v0
	v_max_f32_e32 v0, 0x2b800000, v0
	v_rcp_f32_e32 v223, v0
	v_lshlrev_b32_e32 v0, 16, v157
	v_max_f32_e32 v0, v0, v0
	v_max_f32_e32 v0, 0x2b800000, v0
	v_mul_f32_e32 v220, v220, v226
	v_mul_f32_e32 v221, v221, v227
	v_rcp_f32_e32 v226, v0
	v_and_b32_e32 v0, 0xffff0000, v157
	v_max_f32_e32 v0, v0, v0
	v_max_f32_e32 v0, 0x2b800000, v0
	v_rcp_f32_e32 v227, v0
	v_mul_f32_e32 v186, v186, v222
	v_mul_f32_e32 v187, v187, v223
	v_mul_f32_e32 v188, v188, v226
	v_mul_f32_e32 v189, v189, v227
.LBB0_876:
	v_mul_f32_e32 v96, v96, v220
	v_mul_f32_e32 v97, v97, v221
	v_mul_f32_e32 v94, v94, v192
	v_mul_f32_e32 v95, v95, v193
	v_mul_f32_e32 v92, v92, v188
	v_mul_f32_e32 v93, v93, v189
	s_and_b64 vcc, exec, s[40:41]
	v_mul_f32_e32 v90, v90, v186
	v_mul_f32_e32 v91, v91, v187
	s_cbranch_vccnz .LBB0_878
	v_cvt_pk_bf16_f32 v186, v94, v95
	v_cvt_pk_bf16_f32 v187, v96, v97
	v_cvt_pk_bf16_f32 v188, v90, v91
	v_cvt_pk_bf16_f32 v189, v92, v93
	global_store_dwordx4 v[190:191], v[186:189], off offset:256
.LBB0_878:
	v_lshlrev_b32_e32 v0, 16, v182
	v_max_f32_e32 v0, v0, v0
	v_max_f32_e32 v186, 0x2b800000, v0
	v_and_b32_e32 v0, 0xffff0000, v182
	v_max_f32_e32 v0, v0, v0
	v_max_f32_e32 v187, 0x2b800000, v0
	v_lshlrev_b32_e32 v0, 16, v183
	v_max_f32_e32 v0, v0, v0
	v_max_f32_e32 v188, 0x2b800000, v0
	v_and_b32_e32 v0, 0xffff0000, v183
	v_max_f32_e32 v0, v0, v0
	v_max_f32_e32 v189, 0x2b800000, v0
	v_lshlrev_b32_e32 v0, 16, v184
	v_max_f32_e32 v0, v0, v0
	v_max_f32_e32 v182, 0x2b800000, v0
	v_and_b32_e32 v0, 0xffff0000, v184
	v_max_f32_e32 v0, v0, v0
	v_max_f32_e32 v183, 0x2b800000, v0
	v_lshlrev_b32_e32 v0, 16, v185
	v_max_f32_e32 v0, v0, v0
	v_max_f32_e32 v184, 0x2b800000, v0
	v_and_b32_e32 v0, 0xffff0000, v185
	v_max_f32_e32 v0, v0, v0
	s_and_b64 vcc, exec, s[38:39]
	v_max_f32_e32 v185, 0x2b800000, v0
	s_cbranch_vccnz .LBB0_880
	v_lshlrev_b32_e32 v0, 16, v150
	v_max_f32_e32 v0, v0, v0
	v_max_f32_e32 v0, 0x2b800000, v0
	v_rcp_f32_e32 v190, v0
	v_and_b32_e32 v0, 0xffff0000, v150
	v_max_f32_e32 v0, v0, v0
	v_max_f32_e32 v0, 0x2b800000, v0
	v_rcp_f32_e32 v191, v0
	v_lshlrev_b32_e32 v0, 16, v151
	v_max_f32_e32 v0, v0, v0
	v_max_f32_e32 v0, 0x2b800000, v0
	v_rcp_f32_e32 v192, v0
	v_and_b32_e32 v0, 0xffff0000, v151
	v_max_f32_e32 v0, v0, v0
	v_max_f32_e32 v0, 0x2b800000, v0
	v_rcp_f32_e32 v193, v0
	v_lshlrev_b32_e32 v0, 16, v152
	v_max_f32_e32 v0, v0, v0
	v_max_f32_e32 v0, 0x2b800000, v0
	v_mul_f32_e32 v186, v186, v190
	v_mul_f32_e32 v187, v187, v191
	v_rcp_f32_e32 v190, v0
	v_and_b32_e32 v0, 0xffff0000, v152
	v_max_f32_e32 v0, v0, v0
	v_max_f32_e32 v0, 0x2b800000, v0
	v_rcp_f32_e32 v191, v0
	v_lshlrev_b32_e32 v0, 16, v153
	v_max_f32_e32 v0, v0, v0
	v_max_f32_e32 v0, 0x2b800000, v0
	v_mul_f32_e32 v188, v188, v192
	v_mul_f32_e32 v189, v189, v193
	v_rcp_f32_e32 v192, v0
	v_and_b32_e32 v0, 0xffff0000, v153
	v_max_f32_e32 v0, v0, v0
	v_max_f32_e32 v0, 0x2b800000, v0
	v_rcp_f32_e32 v193, v0
	v_mul_f32_e32 v182, v182, v190
	v_mul_f32_e32 v183, v183, v191
	v_mul_f32_e32 v184, v184, v192
	v_mul_f32_e32 v185, v185, v193
.LBB0_880:
	v_lshlrev_b64 v[190:191], 11, v[218:219]
	v_mul_f32_e32 v114, v114, v182
	v_mul_f32_e32 v115, v115, v183
	v_lshl_add_u64 v[182:183], s[14:15], 0, v[190:191]
	v_mul_f32_e32 v120, v120, v188
	v_mul_f32_e32 v121, v121, v189
	v_mul_f32_e32 v118, v118, v186
	v_mul_f32_e32 v119, v119, v187
	v_mul_f32_e32 v116, v116, v184
	v_mul_f32_e32 v117, v117, v185
	s_and_b64 vcc, exec, s[40:41]
	v_lshl_add_u64 v[182:183], v[210:211], 1, v[182:183]
	s_cbranch_vccnz .LBB0_882
	v_cvt_pk_bf16_f32 v184, v118, v119
	v_cvt_pk_bf16_f32 v185, v120, v121
	v_cvt_pk_bf16_f32 v186, v114, v115
	v_cvt_pk_bf16_f32 v187, v116, v117
	global_store_dwordx4 v[182:183], v[184:187], off
.LBB0_882:
	v_lshlrev_b32_e32 v0, 16, v178
	v_max_f32_e32 v0, v0, v0
	v_max_f32_e32 v184, 0x2b800000, v0
	v_and_b32_e32 v0, 0xffff0000, v178
	v_max_f32_e32 v0, v0, v0
	v_max_f32_e32 v185, 0x2b800000, v0
	v_lshlrev_b32_e32 v0, 16, v179
	v_max_f32_e32 v0, v0, v0
	v_max_f32_e32 v186, 0x2b800000, v0
	v_and_b32_e32 v0, 0xffff0000, v179
	v_max_f32_e32 v0, v0, v0
	v_max_f32_e32 v187, 0x2b800000, v0
	v_lshlrev_b32_e32 v0, 16, v180
	v_max_f32_e32 v0, v0, v0
	v_max_f32_e32 v178, 0x2b800000, v0
	v_and_b32_e32 v0, 0xffff0000, v180
	v_max_f32_e32 v0, v0, v0
	v_max_f32_e32 v179, 0x2b800000, v0
	v_lshlrev_b32_e32 v0, 16, v181
	v_max_f32_e32 v0, v0, v0
	v_max_f32_e32 v180, 0x2b800000, v0
	v_and_b32_e32 v0, 0xffff0000, v181
	v_max_f32_e32 v0, v0, v0
	s_and_b64 vcc, exec, s[38:39]
	v_max_f32_e32 v181, 0x2b800000, v0
	s_cbranch_vccnz .LBB0_884
	v_lshlrev_b32_e32 v0, 16, v146
	v_max_f32_e32 v0, v0, v0
	v_max_f32_e32 v0, 0x2b800000, v0
	v_rcp_f32_e32 v188, v0
	v_and_b32_e32 v0, 0xffff0000, v146
	v_max_f32_e32 v0, v0, v0
	v_max_f32_e32 v0, 0x2b800000, v0
	v_rcp_f32_e32 v189, v0
	v_lshlrev_b32_e32 v0, 16, v147
	v_max_f32_e32 v0, v0, v0
	v_max_f32_e32 v0, 0x2b800000, v0
	v_rcp_f32_e32 v190, v0
	v_and_b32_e32 v0, 0xffff0000, v147
	v_max_f32_e32 v0, v0, v0
	v_max_f32_e32 v0, 0x2b800000, v0
	v_rcp_f32_e32 v191, v0
	v_lshlrev_b32_e32 v0, 16, v148
	v_max_f32_e32 v0, v0, v0
	v_max_f32_e32 v0, 0x2b800000, v0
	v_mul_f32_e32 v184, v184, v188
	v_mul_f32_e32 v185, v185, v189
	v_rcp_f32_e32 v188, v0
	v_and_b32_e32 v0, 0xffff0000, v148
	v_max_f32_e32 v0, v0, v0
	v_max_f32_e32 v0, 0x2b800000, v0
	v_rcp_f32_e32 v189, v0
	v_lshlrev_b32_e32 v0, 16, v149
	v_max_f32_e32 v0, v0, v0
	v_max_f32_e32 v0, 0x2b800000, v0
	v_mul_f32_e32 v186, v186, v190
	v_mul_f32_e32 v187, v187, v191
	v_rcp_f32_e32 v190, v0
	v_and_b32_e32 v0, 0xffff0000, v149
	v_max_f32_e32 v0, v0, v0
	v_max_f32_e32 v0, 0x2b800000, v0
	v_rcp_f32_e32 v191, v0
	v_mul_f32_e32 v178, v178, v188
	v_mul_f32_e32 v179, v179, v189
	v_mul_f32_e32 v180, v180, v190
	v_mul_f32_e32 v181, v181, v191
.LBB0_884:
	v_mul_f32_e32 v88, v88, v186
	v_mul_f32_e32 v89, v89, v187
	v_mul_f32_e32 v86, v86, v184
	v_mul_f32_e32 v87, v87, v185
	v_mul_f32_e32 v84, v84, v180
	v_mul_f32_e32 v85, v85, v181
	s_and_b64 vcc, exec, s[40:41]
	v_mul_f32_e32 v82, v82, v178
	v_mul_f32_e32 v83, v83, v179
	s_cbranch_vccnz .LBB0_886
	v_cvt_pk_bf16_f32 v178, v86, v87
	v_cvt_pk_bf16_f32 v179, v88, v89
	v_cvt_pk_bf16_f32 v180, v82, v83
	v_cvt_pk_bf16_f32 v181, v84, v85
	global_store_dwordx4 v[182:183], v[178:181], off offset:256
.LBB0_886:
	v_lshlrev_b32_e32 v0, 16, v174
	v_max_f32_e32 v0, v0, v0
	v_max_f32_e32 v178, 0x2b800000, v0
	v_and_b32_e32 v0, 0xffff0000, v174
	v_max_f32_e32 v0, v0, v0
	v_max_f32_e32 v179, 0x2b800000, v0
	v_lshlrev_b32_e32 v0, 16, v175
	v_max_f32_e32 v0, v0, v0
	v_max_f32_e32 v180, 0x2b800000, v0
	v_and_b32_e32 v0, 0xffff0000, v175
	v_max_f32_e32 v0, v0, v0
	v_max_f32_e32 v181, 0x2b800000, v0
	v_lshlrev_b32_e32 v0, 16, v176
	v_max_f32_e32 v0, v0, v0
	v_max_f32_e32 v174, 0x2b800000, v0
	v_and_b32_e32 v0, 0xffff0000, v176
	v_max_f32_e32 v0, v0, v0
	v_max_f32_e32 v175, 0x2b800000, v0
	v_lshlrev_b32_e32 v0, 16, v177
	v_max_f32_e32 v0, v0, v0
	v_max_f32_e32 v176, 0x2b800000, v0
	v_and_b32_e32 v0, 0xffff0000, v177
	v_max_f32_e32 v0, v0, v0
	s_and_b64 vcc, exec, s[38:39]
	v_max_f32_e32 v177, 0x2b800000, v0
	s_cbranch_vccnz .LBB0_888
	v_lshlrev_b32_e32 v0, 16, v142
	v_max_f32_e32 v0, v0, v0
	v_max_f32_e32 v0, 0x2b800000, v0
	v_rcp_f32_e32 v182, v0
	v_and_b32_e32 v0, 0xffff0000, v142
	v_max_f32_e32 v0, v0, v0
	v_max_f32_e32 v0, 0x2b800000, v0
	v_rcp_f32_e32 v183, v0
	v_lshlrev_b32_e32 v0, 16, v143
	v_max_f32_e32 v0, v0, v0
	v_max_f32_e32 v0, 0x2b800000, v0
	v_rcp_f32_e32 v184, v0
	v_and_b32_e32 v0, 0xffff0000, v143
	v_max_f32_e32 v0, v0, v0
	v_max_f32_e32 v0, 0x2b800000, v0
	v_rcp_f32_e32 v185, v0
	v_lshlrev_b32_e32 v0, 16, v144
	v_max_f32_e32 v0, v0, v0
	v_max_f32_e32 v0, 0x2b800000, v0
	v_mul_f32_e32 v178, v178, v182
	v_mul_f32_e32 v179, v179, v183
	v_rcp_f32_e32 v182, v0
	v_and_b32_e32 v0, 0xffff0000, v144
	v_max_f32_e32 v0, v0, v0
	v_max_f32_e32 v0, 0x2b800000, v0
	v_rcp_f32_e32 v183, v0
	v_lshlrev_b32_e32 v0, 16, v145
	v_max_f32_e32 v0, v0, v0
	v_max_f32_e32 v0, 0x2b800000, v0
	v_mul_f32_e32 v180, v180, v184
	v_mul_f32_e32 v181, v181, v185
	v_rcp_f32_e32 v184, v0
	v_and_b32_e32 v0, 0xffff0000, v145
	v_max_f32_e32 v0, v0, v0
	v_max_f32_e32 v0, 0x2b800000, v0
	v_rcp_f32_e32 v185, v0
	v_mul_f32_e32 v174, v174, v182
	v_mul_f32_e32 v175, v175, v183
	v_mul_f32_e32 v176, v176, v184
	v_mul_f32_e32 v177, v177, v185
.LBB0_888:
	v_lshlrev_b64 v[182:183], 11, v[216:217]
	v_mul_f32_e32 v106, v106, v174
	v_mul_f32_e32 v107, v107, v175
	v_lshl_add_u64 v[174:175], s[14:15], 0, v[182:183]
	v_mul_f32_e32 v112, v112, v180
	v_mul_f32_e32 v113, v113, v181
	v_mul_f32_e32 v110, v110, v178
	v_mul_f32_e32 v111, v111, v179
	v_mul_f32_e32 v108, v108, v176
	v_mul_f32_e32 v109, v109, v177
	s_and_b64 vcc, exec, s[40:41]
	v_lshl_add_u64 v[174:175], v[210:211], 1, v[174:175]
	s_cbranch_vccnz .LBB0_890
	v_cvt_pk_bf16_f32 v176, v110, v111
	v_cvt_pk_bf16_f32 v177, v112, v113
	v_cvt_pk_bf16_f32 v178, v106, v107
	v_cvt_pk_bf16_f32 v179, v108, v109
	global_store_dwordx4 v[174:175], v[176:179], off
.LBB0_890:
	v_lshlrev_b32_e32 v0, 16, v170
	v_max_f32_e32 v0, v0, v0
	v_max_f32_e32 v176, 0x2b800000, v0
	v_and_b32_e32 v0, 0xffff0000, v170
	v_max_f32_e32 v0, v0, v0
	v_max_f32_e32 v177, 0x2b800000, v0
	v_lshlrev_b32_e32 v0, 16, v171
	v_max_f32_e32 v0, v0, v0
	v_max_f32_e32 v178, 0x2b800000, v0
	v_and_b32_e32 v0, 0xffff0000, v171
	v_max_f32_e32 v0, v0, v0
	v_max_f32_e32 v179, 0x2b800000, v0
	v_lshlrev_b32_e32 v0, 16, v172
	v_max_f32_e32 v0, v0, v0
	v_max_f32_e32 v170, 0x2b800000, v0
	v_and_b32_e32 v0, 0xffff0000, v172
	v_max_f32_e32 v0, v0, v0
	v_max_f32_e32 v171, 0x2b800000, v0
	v_lshlrev_b32_e32 v0, 16, v173
	v_max_f32_e32 v0, v0, v0
	v_max_f32_e32 v172, 0x2b800000, v0
	v_and_b32_e32 v0, 0xffff0000, v173
	v_max_f32_e32 v0, v0, v0
	s_and_b64 vcc, exec, s[38:39]
	v_max_f32_e32 v173, 0x2b800000, v0
	s_cbranch_vccnz .LBB0_892
	v_lshlrev_b32_e32 v0, 16, v138
	v_max_f32_e32 v0, v0, v0
	v_max_f32_e32 v0, 0x2b800000, v0
	v_rcp_f32_e32 v180, v0
	v_and_b32_e32 v0, 0xffff0000, v138
	v_max_f32_e32 v0, v0, v0
	v_max_f32_e32 v0, 0x2b800000, v0
	v_rcp_f32_e32 v181, v0
	v_lshlrev_b32_e32 v0, 16, v139
	v_max_f32_e32 v0, v0, v0
	v_max_f32_e32 v0, 0x2b800000, v0
	v_rcp_f32_e32 v182, v0
	v_and_b32_e32 v0, 0xffff0000, v139
	v_max_f32_e32 v0, v0, v0
	v_max_f32_e32 v0, 0x2b800000, v0
	v_rcp_f32_e32 v183, v0
	v_lshlrev_b32_e32 v0, 16, v140
	v_max_f32_e32 v0, v0, v0
	v_max_f32_e32 v0, 0x2b800000, v0
	v_mul_f32_e32 v176, v176, v180
	v_mul_f32_e32 v177, v177, v181
	v_rcp_f32_e32 v180, v0
	v_and_b32_e32 v0, 0xffff0000, v140
	v_max_f32_e32 v0, v0, v0
	v_max_f32_e32 v0, 0x2b800000, v0
	v_rcp_f32_e32 v181, v0
	v_lshlrev_b32_e32 v0, 16, v141
	v_max_f32_e32 v0, v0, v0
	v_max_f32_e32 v0, 0x2b800000, v0
	v_mul_f32_e32 v178, v178, v182
	v_mul_f32_e32 v179, v179, v183
	v_rcp_f32_e32 v182, v0
	v_and_b32_e32 v0, 0xffff0000, v141
	v_max_f32_e32 v0, v0, v0
	v_max_f32_e32 v0, 0x2b800000, v0
	v_rcp_f32_e32 v183, v0
	v_mul_f32_e32 v170, v170, v180
	v_mul_f32_e32 v171, v171, v181
	v_mul_f32_e32 v172, v172, v182
	v_mul_f32_e32 v173, v173, v183
.LBB0_892:
	v_mul_f32_e32 v80, v80, v178
	v_mul_f32_e32 v81, v81, v179
	v_mul_f32_e32 v78, v78, v176
	v_mul_f32_e32 v79, v79, v177
	v_mul_f32_e32 v76, v76, v172
	v_mul_f32_e32 v77, v77, v173
	s_and_b64 vcc, exec, s[40:41]
	v_mul_f32_e32 v74, v74, v170
	v_mul_f32_e32 v75, v75, v171
	s_cbranch_vccnz .LBB0_894
	v_cvt_pk_bf16_f32 v170, v78, v79
	v_cvt_pk_bf16_f32 v171, v80, v81
	v_cvt_pk_bf16_f32 v172, v74, v75
	v_cvt_pk_bf16_f32 v173, v76, v77
	global_store_dwordx4 v[174:175], v[170:173], off offset:256
.LBB0_894:
	v_lshlrev_b32_e32 v0, 16, v166
	v_max_f32_e32 v0, v0, v0
	v_max_f32_e32 v170, 0x2b800000, v0
	v_and_b32_e32 v0, 0xffff0000, v166
	v_max_f32_e32 v0, v0, v0
	v_max_f32_e32 v171, 0x2b800000, v0
	v_lshlrev_b32_e32 v0, 16, v167
	v_max_f32_e32 v0, v0, v0
	v_max_f32_e32 v172, 0x2b800000, v0
	v_and_b32_e32 v0, 0xffff0000, v167
	v_max_f32_e32 v0, v0, v0
	v_max_f32_e32 v173, 0x2b800000, v0
	v_lshlrev_b32_e32 v0, 16, v168
	v_max_f32_e32 v0, v0, v0
	v_max_f32_e32 v166, 0x2b800000, v0
	v_and_b32_e32 v0, 0xffff0000, v168
	v_max_f32_e32 v0, v0, v0
	v_max_f32_e32 v167, 0x2b800000, v0
	v_lshlrev_b32_e32 v0, 16, v169
	v_max_f32_e32 v0, v0, v0
	v_max_f32_e32 v168, 0x2b800000, v0
	v_and_b32_e32 v0, 0xffff0000, v169
	v_max_f32_e32 v0, v0, v0
	s_and_b64 vcc, exec, s[38:39]
	v_max_f32_e32 v169, 0x2b800000, v0
	s_cbranch_vccnz .LBB0_896
	v_lshlrev_b32_e32 v0, 16, v134
	v_max_f32_e32 v0, v0, v0
	v_max_f32_e32 v0, 0x2b800000, v0
	v_rcp_f32_e32 v174, v0
	v_and_b32_e32 v0, 0xffff0000, v134
	v_max_f32_e32 v0, v0, v0
	v_max_f32_e32 v0, 0x2b800000, v0
	v_rcp_f32_e32 v175, v0
	v_lshlrev_b32_e32 v0, 16, v135
	v_max_f32_e32 v0, v0, v0
	v_max_f32_e32 v0, 0x2b800000, v0
	v_rcp_f32_e32 v176, v0
	v_and_b32_e32 v0, 0xffff0000, v135
	v_max_f32_e32 v0, v0, v0
	v_max_f32_e32 v0, 0x2b800000, v0
	v_rcp_f32_e32 v177, v0
	v_lshlrev_b32_e32 v0, 16, v136
	v_max_f32_e32 v0, v0, v0
	v_max_f32_e32 v0, 0x2b800000, v0
	v_mul_f32_e32 v170, v170, v174
	v_mul_f32_e32 v171, v171, v175
	v_rcp_f32_e32 v174, v0
	v_and_b32_e32 v0, 0xffff0000, v136
	v_max_f32_e32 v0, v0, v0
	v_max_f32_e32 v0, 0x2b800000, v0
	v_rcp_f32_e32 v175, v0
	v_lshlrev_b32_e32 v0, 16, v137
	v_max_f32_e32 v0, v0, v0
	v_max_f32_e32 v0, 0x2b800000, v0
	v_mul_f32_e32 v172, v172, v176
	v_mul_f32_e32 v173, v173, v177
	v_rcp_f32_e32 v176, v0
	v_and_b32_e32 v0, 0xffff0000, v137
	v_max_f32_e32 v0, v0, v0
	v_max_f32_e32 v0, 0x2b800000, v0
	v_rcp_f32_e32 v177, v0
	v_mul_f32_e32 v166, v166, v174
	v_mul_f32_e32 v167, v167, v175
	v_mul_f32_e32 v168, v168, v176
	v_mul_f32_e32 v169, v169, v177
.LBB0_896:
	v_lshlrev_b64 v[174:175], 11, v[214:215]
	v_mul_f32_e32 v98, v98, v166
	v_mul_f32_e32 v99, v99, v167
	v_lshl_add_u64 v[166:167], s[14:15], 0, v[174:175]
	v_mul_f32_e32 v104, v104, v172
	v_mul_f32_e32 v105, v105, v173
	v_mul_f32_e32 v102, v102, v170
	v_mul_f32_e32 v103, v103, v171
	v_mul_f32_e32 v100, v100, v168
	v_mul_f32_e32 v101, v101, v169
	s_and_b64 vcc, exec, s[40:41]
	v_lshl_add_u64 v[166:167], v[210:211], 1, v[166:167]
	s_cbranch_vccnz .LBB0_898
	v_cvt_pk_bf16_f32 v168, v102, v103
	v_cvt_pk_bf16_f32 v169, v104, v105
	v_cvt_pk_bf16_f32 v170, v98, v99
	v_cvt_pk_bf16_f32 v171, v100, v101
	global_store_dwordx4 v[166:167], v[168:171], off
.LBB0_898:
	v_lshlrev_b32_e32 v0, 16, v162
	v_max_f32_e32 v0, v0, v0
	v_max_f32_e32 v168, 0x2b800000, v0
	v_and_b32_e32 v0, 0xffff0000, v162
	v_max_f32_e32 v0, v0, v0
	v_max_f32_e32 v169, 0x2b800000, v0
	v_lshlrev_b32_e32 v0, 16, v163
	v_max_f32_e32 v0, v0, v0
	v_max_f32_e32 v170, 0x2b800000, v0
	v_and_b32_e32 v0, 0xffff0000, v163
	v_max_f32_e32 v0, v0, v0
	v_max_f32_e32 v171, 0x2b800000, v0
	v_lshlrev_b32_e32 v0, 16, v164
	v_max_f32_e32 v0, v0, v0
	v_max_f32_e32 v162, 0x2b800000, v0
	v_and_b32_e32 v0, 0xffff0000, v164
	v_max_f32_e32 v0, v0, v0
	v_max_f32_e32 v163, 0x2b800000, v0
	v_lshlrev_b32_e32 v0, 16, v165
	v_max_f32_e32 v0, v0, v0
	v_max_f32_e32 v164, 0x2b800000, v0
	v_and_b32_e32 v0, 0xffff0000, v165
	v_max_f32_e32 v0, v0, v0
	s_and_b64 vcc, exec, s[38:39]
	v_max_f32_e32 v165, 0x2b800000, v0
	s_cbranch_vccnz .LBB0_900
	v_lshlrev_b32_e32 v0, 16, v130
	v_max_f32_e32 v0, v0, v0
	v_max_f32_e32 v0, 0x2b800000, v0
	v_rcp_f32_e32 v172, v0
	v_and_b32_e32 v0, 0xffff0000, v130
	v_max_f32_e32 v0, v0, v0
	v_max_f32_e32 v0, 0x2b800000, v0
	v_rcp_f32_e32 v173, v0
	v_lshlrev_b32_e32 v0, 16, v131
	v_max_f32_e32 v0, v0, v0
	v_max_f32_e32 v0, 0x2b800000, v0
	v_rcp_f32_e32 v174, v0
	v_and_b32_e32 v0, 0xffff0000, v131
	v_max_f32_e32 v0, v0, v0
	v_max_f32_e32 v0, 0x2b800000, v0
	v_rcp_f32_e32 v175, v0
	v_lshlrev_b32_e32 v0, 16, v132
	v_max_f32_e32 v0, v0, v0
	v_max_f32_e32 v0, 0x2b800000, v0
	v_mul_f32_e32 v168, v168, v172
	v_mul_f32_e32 v169, v169, v173
	v_rcp_f32_e32 v172, v0
	v_and_b32_e32 v0, 0xffff0000, v132
	v_max_f32_e32 v0, v0, v0
	v_max_f32_e32 v0, 0x2b800000, v0
	v_rcp_f32_e32 v173, v0
	v_lshlrev_b32_e32 v0, 16, v133
	v_max_f32_e32 v0, v0, v0
	v_max_f32_e32 v0, 0x2b800000, v0
	v_mul_f32_e32 v170, v170, v174
	v_mul_f32_e32 v171, v171, v175
	v_rcp_f32_e32 v174, v0
	v_and_b32_e32 v0, 0xffff0000, v133
	v_max_f32_e32 v0, v0, v0
	v_max_f32_e32 v0, 0x2b800000, v0
	v_rcp_f32_e32 v175, v0
	v_mul_f32_e32 v162, v162, v172
	v_mul_f32_e32 v163, v163, v173
	v_mul_f32_e32 v164, v164, v174
	v_mul_f32_e32 v165, v165, v175
.LBB0_900:
	v_mul_f32_e32 v72, v72, v170
	v_mul_f32_e32 v73, v73, v171
	v_mul_f32_e32 v70, v70, v168
	v_mul_f32_e32 v71, v71, v169
	v_mul_f32_e32 v68, v68, v164
	v_mul_f32_e32 v69, v69, v165
	s_and_b64 vcc, exec, s[40:41]
	v_mul_f32_e32 v66, v66, v162
	v_mul_f32_e32 v67, v67, v163
	s_cbranch_vccnz .LBB0_902
	v_cvt_pk_bf16_f32 v162, v70, v71
	v_cvt_pk_bf16_f32 v163, v72, v73
	v_cvt_pk_bf16_f32 v164, v66, v67
	v_cvt_pk_bf16_f32 v165, v68, v69
	global_store_dwordx4 v[166:167], v[162:165], off offset:256

.LBB0_918:
	s_waitcnt vmcnt(7)
	v_lshlrev_b32_e32 v0, 16, v190
	v_max_f32_e32 v0, v0, v0
	v_max_f32_e32 v220, 0x2b800000, v0
	v_and_b32_e32 v0, 0xffff0000, v190
	v_max_f32_e32 v0, v0, v0
	v_max_f32_e32 v221, 0x2b800000, v0
	v_lshlrev_b32_e32 v0, 16, v191
	v_max_f32_e32 v0, v0, v0
	v_max_f32_e32 v222, 0x2b800000, v0
	v_and_b32_e32 v0, 0xffff0000, v191
	v_max_f32_e32 v0, v0, v0
	v_max_f32_e32 v223, 0x2b800000, v0
	v_lshlrev_b32_e32 v0, 16, v192
	v_max_f32_e32 v0, v0, v0
	v_max_f32_e32 v190, 0x2b800000, v0
	v_and_b32_e32 v0, 0xffff0000, v192
	v_max_f32_e32 v0, v0, v0
	v_max_f32_e32 v191, 0x2b800000, v0
	v_lshlrev_b32_e32 v0, 16, v193
	v_max_f32_e32 v0, v0, v0
	v_max_f32_e32 v192, 0x2b800000, v0
	v_and_b32_e32 v0, 0xffff0000, v193
	v_max_f32_e32 v0, v0, v0
	s_and_b64 vcc, exec, s[38:39]
	v_max_f32_e32 v193, 0x2b800000, v0
	s_cbranch_vccnz .LBB0_920
	v_lshlrev_b32_e32 v0, 16, v158
	v_max_f32_e32 v0, v0, v0
	v_max_f32_e32 v0, 0x2b800000, v0
	v_rcp_f32_e32 v226, v0
	v_and_b32_e32 v0, 0xffff0000, v158
	v_max_f32_e32 v0, v0, v0
	v_max_f32_e32 v0, 0x2b800000, v0
	v_rcp_f32_e32 v227, v0
	v_lshlrev_b32_e32 v0, 16, v159
	v_max_f32_e32 v0, v0, v0
	v_max_f32_e32 v0, 0x2b800000, v0
	v_rcp_f32_e32 v158, v0
	v_and_b32_e32 v0, 0xffff0000, v159
	v_max_f32_e32 v0, v0, v0
	v_max_f32_e32 v0, 0x2b800000, v0
	v_rcp_f32_e32 v159, v0
	v_lshlrev_b32_e32 v0, 16, v160
	v_max_f32_e32 v0, v0, v0
	v_max_f32_e32 v0, 0x2b800000, v0
	v_mul_f32_e32 v222, v222, v158
	v_mul_f32_e32 v223, v223, v159
	v_rcp_f32_e32 v158, v0
	v_and_b32_e32 v0, 0xffff0000, v160
	v_max_f32_e32 v0, v0, v0
	v_max_f32_e32 v0, 0x2b800000, v0
	v_rcp_f32_e32 v159, v0
	v_lshlrev_b32_e32 v0, 16, v161
	v_max_f32_e32 v0, v0, v0
	v_max_f32_e32 v0, 0x2b800000, v0
	v_rcp_f32_e32 v160, v0
	v_and_b32_e32 v0, 0xffff0000, v161
	v_max_f32_e32 v0, v0, v0
	v_max_f32_e32 v0, 0x2b800000, v0
	v_rcp_f32_e32 v161, v0
	v_mul_f32_e32 v220, v220, v226
	v_mul_f32_e32 v221, v221, v227
	v_mul_f32_e32 v190, v190, v158
	v_mul_f32_e32 v191, v191, v159
	v_mul_f32_e32 v192, v192, v160
	v_mul_f32_e32 v193, v193, v161
.LBB0_920:
	v_lshlrev_b64 v[158:159], 11, v[218:219]
	v_lshl_add_u64 v[158:159], s[14:15], 0, v[158:159]
	v_mul_f32_e32 v64, v64, v222
	v_mul_f32_e32 v65, v65, v223
	v_mul_f32_e32 v62, v62, v220
	v_mul_f32_e32 v63, v63, v221
	v_mul_f32_e32 v60, v60, v192
	v_mul_f32_e32 v61, v61, v193
	v_mul_f32_e32 v58, v58, v190
	v_mul_f32_e32 v59, v59, v191
	s_and_b64 vcc, exec, s[40:41]
	v_lshl_add_u64 v[158:159], v[210:211], 1, v[158:159]
	s_cbranch_vccnz .LBB0_922
	v_cvt_pk_bf16_f32 v190, v62, v63
	v_cvt_pk_bf16_f32 v191, v64, v65
	v_cvt_pk_bf16_f32 v192, v58, v59
	v_cvt_pk_bf16_f32 v193, v60, v61
	global_store_dwordx4 v[158:159], v[190:193], off
.LBB0_922:
	s_waitcnt vmcnt(6)
	v_lshlrev_b32_e32 v0, 16, v186
	v_max_f32_e32 v0, v0, v0
	v_max_f32_e32 v160, 0x2b800000, v0
	v_and_b32_e32 v0, 0xffff0000, v186
	v_max_f32_e32 v0, v0, v0
	v_max_f32_e32 v161, 0x2b800000, v0
	v_lshlrev_b32_e32 v0, 16, v187
	v_max_f32_e32 v0, v0, v0
	v_max_f32_e32 v190, 0x2b800000, v0
	v_and_b32_e32 v0, 0xffff0000, v187
	v_max_f32_e32 v0, v0, v0
	v_max_f32_e32 v191, 0x2b800000, v0
	v_lshlrev_b32_e32 v0, 16, v188
	v_max_f32_e32 v0, v0, v0
	v_max_f32_e32 v186, 0x2b800000, v0
	v_and_b32_e32 v0, 0xffff0000, v188
	v_max_f32_e32 v0, v0, v0
	v_max_f32_e32 v187, 0x2b800000, v0
	v_lshlrev_b32_e32 v0, 16, v189
	v_max_f32_e32 v0, v0, v0
	v_max_f32_e32 v188, 0x2b800000, v0
	v_and_b32_e32 v0, 0xffff0000, v189
	v_max_f32_e32 v0, v0, v0
	s_and_b64 vcc, exec, s[38:39]
	v_max_f32_e32 v189, 0x2b800000, v0
	s_cbranch_vccnz .LBB0_924
	v_lshlrev_b32_e32 v0, 16, v154
	v_max_f32_e32 v0, v0, v0
	v_max_f32_e32 v0, 0x2b800000, v0
	v_rcp_f32_e32 v192, v0
	v_and_b32_e32 v0, 0xffff0000, v154
	v_max_f32_e32 v0, v0, v0
	v_max_f32_e32 v0, 0x2b800000, v0
	v_rcp_f32_e32 v193, v0
	v_lshlrev_b32_e32 v0, 16, v155
	v_max_f32_e32 v0, v0, v0
	v_max_f32_e32 v0, 0x2b800000, v0
	v_rcp_f32_e32 v154, v0
	v_and_b32_e32 v0, 0xffff0000, v155
	v_max_f32_e32 v0, v0, v0
	v_max_f32_e32 v0, 0x2b800000, v0
	v_rcp_f32_e32 v155, v0
	v_lshlrev_b32_e32 v0, 16, v156
	v_max_f32_e32 v0, v0, v0
	v_max_f32_e32 v0, 0x2b800000, v0
	v_mul_f32_e32 v190, v190, v154
	v_mul_f32_e32 v191, v191, v155
	v_rcp_f32_e32 v154, v0
	v_and_b32_e32 v0, 0xffff0000, v156
	v_max_f32_e32 v0, v0, v0
	v_max_f32_e32 v0, 0x2b800000, v0
	v_rcp_f32_e32 v155, v0
	v_lshlrev_b32_e32 v0, 16, v157
	v_max_f32_e32 v0, v0, v0
	v_max_f32_e32 v0, 0x2b800000, v0
	v_rcp_f32_e32 v156, v0
	v_and_b32_e32 v0, 0xffff0000, v157
	v_max_f32_e32 v0, v0, v0
	v_max_f32_e32 v0, 0x2b800000, v0
	v_rcp_f32_e32 v157, v0
	v_mul_f32_e32 v160, v160, v192
	v_mul_f32_e32 v161, v161, v193
	v_mul_f32_e32 v186, v186, v154
	v_mul_f32_e32 v187, v187, v155
	v_mul_f32_e32 v188, v188, v156
	v_mul_f32_e32 v189, v189, v157
.LBB0_924:
	v_mul_f32_e32 v32, v32, v190
	v_mul_f32_e32 v33, v33, v191
	v_mul_f32_e32 v30, v30, v160
	v_mul_f32_e32 v31, v31, v161
	v_mul_f32_e32 v28, v28, v188
	v_mul_f32_e32 v29, v29, v189
	s_and_b64 vcc, exec, s[40:41]
	v_mul_f32_e32 v26, v26, v186
	v_mul_f32_e32 v27, v27, v187
	s_cbranch_vccnz .LBB0_926
	v_cvt_pk_bf16_f32 v154, v30, v31
	v_cvt_pk_bf16_f32 v155, v32, v33
	v_cvt_pk_bf16_f32 v156, v26, v27
	v_cvt_pk_bf16_f32 v157, v28, v29
	global_store_dwordx4 v[158:159], v[154:157], off offset:256
.LBB0_926:
	s_waitcnt vmcnt(5)
	v_lshlrev_b32_e32 v0, 16, v182
	v_max_f32_e32 v0, v0, v0
	v_max_f32_e32 v154, 0x2b800000, v0
	v_and_b32_e32 v0, 0xffff0000, v182
	v_max_f32_e32 v0, v0, v0
	v_max_f32_e32 v155, 0x2b800000, v0
	v_lshlrev_b32_e32 v0, 16, v183
	v_max_f32_e32 v0, v0, v0
	v_max_f32_e32 v158, 0x2b800000, v0
	v_and_b32_e32 v0, 0xffff0000, v183
	v_max_f32_e32 v0, v0, v0
	v_max_f32_e32 v159, 0x2b800000, v0
	v_lshlrev_b32_e32 v0, 16, v184
	v_max_f32_e32 v0, v0, v0
	v_max_f32_e32 v156, 0x2b800000, v0
	v_and_b32_e32 v0, 0xffff0000, v184
	v_max_f32_e32 v0, v0, v0
	v_max_f32_e32 v157, 0x2b800000, v0
	v_lshlrev_b32_e32 v0, 16, v185
	v_max_f32_e32 v0, v0, v0
	v_max_f32_e32 v160, 0x2b800000, v0
	v_and_b32_e32 v0, 0xffff0000, v185
	v_max_f32_e32 v0, v0, v0
	s_and_b64 vcc, exec, s[38:39]
	v_max_f32_e32 v161, 0x2b800000, v0
	s_cbranch_vccnz .LBB0_928
	v_lshlrev_b32_e32 v0, 16, v150
	v_max_f32_e32 v0, v0, v0
	v_max_f32_e32 v0, 0x2b800000, v0
	v_rcp_f32_e32 v182, v0
	v_and_b32_e32 v0, 0xffff0000, v150
	v_max_f32_e32 v0, v0, v0
	v_max_f32_e32 v0, 0x2b800000, v0
	v_rcp_f32_e32 v183, v0
	v_lshlrev_b32_e32 v0, 16, v151
	v_max_f32_e32 v0, v0, v0
	v_max_f32_e32 v0, 0x2b800000, v0
	v_rcp_f32_e32 v150, v0
	v_and_b32_e32 v0, 0xffff0000, v151
	v_max_f32_e32 v0, v0, v0
	v_max_f32_e32 v0, 0x2b800000, v0
	v_rcp_f32_e32 v151, v0
	v_lshlrev_b32_e32 v0, 16, v152
	v_max_f32_e32 v0, v0, v0
	v_max_f32_e32 v0, 0x2b800000, v0
	v_mul_f32_e32 v158, v158, v150
	v_mul_f32_e32 v159, v159, v151
	v_rcp_f32_e32 v150, v0
	v_and_b32_e32 v0, 0xffff0000, v152
	v_max_f32_e32 v0, v0, v0
	v_max_f32_e32 v0, 0x2b800000, v0
	v_rcp_f32_e32 v151, v0
	v_lshlrev_b32_e32 v0, 16, v153
	v_max_f32_e32 v0, v0, v0
	v_max_f32_e32 v0, 0x2b800000, v0
	v_rcp_f32_e32 v152, v0
	v_and_b32_e32 v0, 0xffff0000, v153
	v_max_f32_e32 v0, v0, v0
	v_max_f32_e32 v0, 0x2b800000, v0
	v_rcp_f32_e32 v153, v0
	v_mul_f32_e32 v154, v154, v182
	v_mul_f32_e32 v155, v155, v183
	v_mul_f32_e32 v156, v156, v150
	v_mul_f32_e32 v157, v157, v151
	v_mul_f32_e32 v160, v160, v152
	v_mul_f32_e32 v161, v161, v153
.LBB0_928:
	v_lshlrev_b64 v[150:151], 11, v[216:217]
	v_lshl_add_u64 v[150:151], s[14:15], 0, v[150:151]
	v_mul_f32_e32 v56, v56, v158
	v_mul_f32_e32 v57, v57, v159
	v_mul_f32_e32 v54, v54, v154
	v_mul_f32_e32 v55, v55, v155
	v_mul_f32_e32 v52, v52, v160
	v_mul_f32_e32 v53, v53, v161
	v_mul_f32_e32 v50, v50, v156
	v_mul_f32_e32 v51, v51, v157
	s_and_b64 vcc, exec, s[40:41]
	v_lshl_add_u64 v[150:151], v[210:211], 1, v[150:151]
	s_cbranch_vccnz .LBB0_930
	v_cvt_pk_bf16_f32 v152, v54, v55
	v_cvt_pk_bf16_f32 v153, v56, v57
	v_cvt_pk_bf16_f32 v154, v50, v51
	v_cvt_pk_bf16_f32 v155, v52, v53
	global_store_dwordx4 v[150:151], v[152:155], off
.LBB0_930:
	s_waitcnt vmcnt(4)
	v_lshlrev_b32_e32 v0, 16, v178
	v_max_f32_e32 v0, v0, v0
	v_max_f32_e32 v152, 0x2b800000, v0
	v_and_b32_e32 v0, 0xffff0000, v178
	v_max_f32_e32 v0, v0, v0
	v_max_f32_e32 v153, 0x2b800000, v0
	v_lshlrev_b32_e32 v0, 16, v179
	v_max_f32_e32 v0, v0, v0
	v_max_f32_e32 v156, 0x2b800000, v0
	v_and_b32_e32 v0, 0xffff0000, v179
	v_max_f32_e32 v0, v0, v0
	v_max_f32_e32 v157, 0x2b800000, v0
	v_lshlrev_b32_e32 v0, 16, v180
	v_max_f32_e32 v0, v0, v0
	v_max_f32_e32 v154, 0x2b800000, v0
	v_and_b32_e32 v0, 0xffff0000, v180
	v_max_f32_e32 v0, v0, v0
	v_max_f32_e32 v155, 0x2b800000, v0
	v_lshlrev_b32_e32 v0, 16, v181
	v_max_f32_e32 v0, v0, v0
	v_max_f32_e32 v158, 0x2b800000, v0
	v_and_b32_e32 v0, 0xffff0000, v181
	v_max_f32_e32 v0, v0, v0
	s_and_b64 vcc, exec, s[38:39]
	v_max_f32_e32 v159, 0x2b800000, v0
	s_cbranch_vccnz .LBB0_932
	v_lshlrev_b32_e32 v0, 16, v146
	v_max_f32_e32 v0, v0, v0
	v_max_f32_e32 v0, 0x2b800000, v0
	v_rcp_f32_e32 v160, v0
	v_and_b32_e32 v0, 0xffff0000, v146
	v_max_f32_e32 v0, v0, v0
	v_max_f32_e32 v0, 0x2b800000, v0
	v_rcp_f32_e32 v161, v0
	v_lshlrev_b32_e32 v0, 16, v147
	v_max_f32_e32 v0, v0, v0
	v_max_f32_e32 v0, 0x2b800000, v0
	v_rcp_f32_e32 v146, v0
	v_and_b32_e32 v0, 0xffff0000, v147
	v_max_f32_e32 v0, v0, v0
	v_max_f32_e32 v0, 0x2b800000, v0
	v_rcp_f32_e32 v147, v0
	v_lshlrev_b32_e32 v0, 16, v148
	v_max_f32_e32 v0, v0, v0
	v_max_f32_e32 v0, 0x2b800000, v0
	v_mul_f32_e32 v156, v156, v146
	v_mul_f32_e32 v157, v157, v147
	v_rcp_f32_e32 v146, v0
	v_and_b32_e32 v0, 0xffff0000, v148
	v_max_f32_e32 v0, v0, v0
	v_max_f32_e32 v0, 0x2b800000, v0
	v_rcp_f32_e32 v147, v0
	v_lshlrev_b32_e32 v0, 16, v149
	v_max_f32_e32 v0, v0, v0
	v_max_f32_e32 v0, 0x2b800000, v0
	v_rcp_f32_e32 v148, v0
	v_and_b32_e32 v0, 0xffff0000, v149
	v_max_f32_e32 v0, v0, v0
	v_max_f32_e32 v0, 0x2b800000, v0
	v_rcp_f32_e32 v149, v0
	v_mul_f32_e32 v152, v152, v160
	v_mul_f32_e32 v153, v153, v161
	v_mul_f32_e32 v154, v154, v146
	v_mul_f32_e32 v155, v155, v147
	v_mul_f32_e32 v158, v158, v148
	v_mul_f32_e32 v159, v159, v149
.LBB0_932:
	v_mul_f32_e32 v24, v24, v156
	v_mul_f32_e32 v25, v25, v157
	v_mul_f32_e32 v22, v22, v152
	v_mul_f32_e32 v23, v23, v153
	v_mul_f32_e32 v20, v20, v158
	v_mul_f32_e32 v21, v21, v159
	s_and_b64 vcc, exec, s[40:41]
	v_mul_f32_e32 v18, v18, v154
	v_mul_f32_e32 v19, v19, v155
	s_cbranch_vccnz .LBB0_934
	v_cvt_pk_bf16_f32 v146, v22, v23
	v_cvt_pk_bf16_f32 v147, v24, v25
	v_cvt_pk_bf16_f32 v148, v18, v19
	v_cvt_pk_bf16_f32 v149, v20, v21
	global_store_dwordx4 v[150:151], v[146:149], off offset:256
.LBB0_934:
	s_waitcnt vmcnt(3)
	v_lshlrev_b32_e32 v0, 16, v174
	v_max_f32_e32 v0, v0, v0
	v_max_f32_e32 v146, 0x2b800000, v0
	v_and_b32_e32 v0, 0xffff0000, v174
	v_max_f32_e32 v0, v0, v0
	v_max_f32_e32 v147, 0x2b800000, v0
	v_lshlrev_b32_e32 v0, 16, v175
	v_max_f32_e32 v0, v0, v0
	v_max_f32_e32 v150, 0x2b800000, v0
	v_and_b32_e32 v0, 0xffff0000, v175
	v_max_f32_e32 v0, v0, v0
	v_max_f32_e32 v151, 0x2b800000, v0
	v_lshlrev_b32_e32 v0, 16, v176
	v_max_f32_e32 v0, v0, v0
	v_max_f32_e32 v148, 0x2b800000, v0
	v_and_b32_e32 v0, 0xffff0000, v176
	v_max_f32_e32 v0, v0, v0
	v_max_f32_e32 v149, 0x2b800000, v0
	v_lshlrev_b32_e32 v0, 16, v177
	v_max_f32_e32 v0, v0, v0
	v_max_f32_e32 v152, 0x2b800000, v0
	v_and_b32_e32 v0, 0xffff0000, v177
	v_max_f32_e32 v0, v0, v0
	s_and_b64 vcc, exec, s[38:39]
	v_max_f32_e32 v153, 0x2b800000, v0
	s_cbranch_vccnz .LBB0_936
	v_lshlrev_b32_e32 v0, 16, v142
	v_max_f32_e32 v0, v0, v0
	v_max_f32_e32 v0, 0x2b800000, v0
	v_rcp_f32_e32 v154, v0
	v_and_b32_e32 v0, 0xffff0000, v142
	v_max_f32_e32 v0, v0, v0
	v_max_f32_e32 v0, 0x2b800000, v0
	v_rcp_f32_e32 v155, v0
	v_lshlrev_b32_e32 v0, 16, v143
	v_max_f32_e32 v0, v0, v0
	v_max_f32_e32 v0, 0x2b800000, v0
	v_rcp_f32_e32 v142, v0
	v_and_b32_e32 v0, 0xffff0000, v143
	v_max_f32_e32 v0, v0, v0
	v_max_f32_e32 v0, 0x2b800000, v0
	v_rcp_f32_e32 v143, v0
	v_lshlrev_b32_e32 v0, 16, v144
	v_max_f32_e32 v0, v0, v0
	v_max_f32_e32 v0, 0x2b800000, v0
	v_mul_f32_e32 v150, v150, v142
	v_mul_f32_e32 v151, v151, v143
	v_rcp_f32_e32 v142, v0
	v_and_b32_e32 v0, 0xffff0000, v144
	v_max_f32_e32 v0, v0, v0
	v_max_f32_e32 v0, 0x2b800000, v0
	v_rcp_f32_e32 v143, v0
	v_lshlrev_b32_e32 v0, 16, v145
	v_max_f32_e32 v0, v0, v0
	v_max_f32_e32 v0, 0x2b800000, v0
	v_rcp_f32_e32 v144, v0
	v_and_b32_e32 v0, 0xffff0000, v145
	v_max_f32_e32 v0, v0, v0
	v_max_f32_e32 v0, 0x2b800000, v0
	v_rcp_f32_e32 v145, v0
	v_mul_f32_e32 v146, v146, v154
	v_mul_f32_e32 v147, v147, v155
	v_mul_f32_e32 v148, v148, v142
	v_mul_f32_e32 v149, v149, v143
	v_mul_f32_e32 v152, v152, v144
	v_mul_f32_e32 v153, v153, v145
.LBB0_936:
	v_lshlrev_b64 v[142:143], 11, v[214:215]
	v_lshl_add_u64 v[142:143], s[14:15], 0, v[142:143]
	v_mul_f32_e32 v48, v48, v150
	v_mul_f32_e32 v49, v49, v151
	v_mul_f32_e32 v46, v46, v146
	v_mul_f32_e32 v47, v47, v147
	v_mul_f32_e32 v44, v44, v152
	v_mul_f32_e32 v45, v45, v153
	v_mul_f32_e32 v42, v42, v148
	v_mul_f32_e32 v43, v43, v149
	s_and_b64 vcc, exec, s[40:41]
	v_lshl_add_u64 v[142:143], v[210:211], 1, v[142:143]
	s_cbranch_vccnz .LBB0_938
	v_cvt_pk_bf16_f32 v144, v46, v47
	v_cvt_pk_bf16_f32 v145, v48, v49
	v_cvt_pk_bf16_f32 v146, v42, v43
	v_cvt_pk_bf16_f32 v147, v44, v45
	global_store_dwordx4 v[142:143], v[144:147], off
.LBB0_938:
	s_waitcnt vmcnt(2)
	v_lshlrev_b32_e32 v0, 16, v170
	v_max_f32_e32 v0, v0, v0
	v_max_f32_e32 v144, 0x2b800000, v0
	v_and_b32_e32 v0, 0xffff0000, v170
	v_max_f32_e32 v0, v0, v0
	v_max_f32_e32 v145, 0x2b800000, v0
	v_lshlrev_b32_e32 v0, 16, v171
	v_max_f32_e32 v0, v0, v0
	v_max_f32_e32 v148, 0x2b800000, v0
	v_and_b32_e32 v0, 0xffff0000, v171
	v_max_f32_e32 v0, v0, v0
	v_max_f32_e32 v149, 0x2b800000, v0
	v_lshlrev_b32_e32 v0, 16, v172
	v_max_f32_e32 v0, v0, v0
	v_max_f32_e32 v146, 0x2b800000, v0
	v_and_b32_e32 v0, 0xffff0000, v172
	v_max_f32_e32 v0, v0, v0
	v_max_f32_e32 v147, 0x2b800000, v0
	v_lshlrev_b32_e32 v0, 16, v173
	v_max_f32_e32 v0, v0, v0
	v_max_f32_e32 v150, 0x2b800000, v0
	v_and_b32_e32 v0, 0xffff0000, v173
	v_max_f32_e32 v0, v0, v0
	s_and_b64 vcc, exec, s[38:39]
	v_max_f32_e32 v151, 0x2b800000, v0
	s_cbranch_vccnz .LBB0_940
	v_lshlrev_b32_e32 v0, 16, v138
	v_max_f32_e32 v0, v0, v0
	v_max_f32_e32 v0, 0x2b800000, v0
	v_rcp_f32_e32 v152, v0
	v_and_b32_e32 v0, 0xffff0000, v138
	v_max_f32_e32 v0, v0, v0
	v_max_f32_e32 v0, 0x2b800000, v0
	v_rcp_f32_e32 v153, v0
	v_lshlrev_b32_e32 v0, 16, v139
	v_max_f32_e32 v0, v0, v0
	v_max_f32_e32 v0, 0x2b800000, v0
	v_rcp_f32_e32 v138, v0
	v_and_b32_e32 v0, 0xffff0000, v139
	v_max_f32_e32 v0, v0, v0
	v_max_f32_e32 v0, 0x2b800000, v0
	v_rcp_f32_e32 v139, v0
	v_lshlrev_b32_e32 v0, 16, v140
	v_max_f32_e32 v0, v0, v0
	v_max_f32_e32 v0, 0x2b800000, v0
	v_mul_f32_e32 v148, v148, v138
	v_mul_f32_e32 v149, v149, v139
	v_rcp_f32_e32 v138, v0
	v_and_b32_e32 v0, 0xffff0000, v140
	v_max_f32_e32 v0, v0, v0
	v_max_f32_e32 v0, 0x2b800000, v0
	v_rcp_f32_e32 v139, v0
	v_lshlrev_b32_e32 v0, 16, v141
	v_max_f32_e32 v0, v0, v0
	v_max_f32_e32 v0, 0x2b800000, v0
	v_rcp_f32_e32 v140, v0
	v_and_b32_e32 v0, 0xffff0000, v141
	v_max_f32_e32 v0, v0, v0
	v_max_f32_e32 v0, 0x2b800000, v0
	v_rcp_f32_e32 v141, v0
	v_mul_f32_e32 v144, v144, v152
	v_mul_f32_e32 v145, v145, v153
	v_mul_f32_e32 v146, v146, v138
	v_mul_f32_e32 v147, v147, v139
	v_mul_f32_e32 v150, v150, v140
	v_mul_f32_e32 v151, v151, v141
.LBB0_940:
	v_mul_f32_e32 v16, v16, v148
	v_mul_f32_e32 v17, v17, v149
	v_mul_f32_e32 v14, v14, v144
	v_mul_f32_e32 v15, v15, v145
	v_mul_f32_e32 v12, v12, v150
	v_mul_f32_e32 v13, v13, v151
	s_and_b64 vcc, exec, s[40:41]
	v_mul_f32_e32 v10, v10, v146
	v_mul_f32_e32 v11, v11, v147
	s_cbranch_vccnz .LBB0_942
	v_cvt_pk_bf16_f32 v138, v14, v15
	v_cvt_pk_bf16_f32 v139, v16, v17
	v_cvt_pk_bf16_f32 v140, v10, v11
	v_cvt_pk_bf16_f32 v141, v12, v13
	global_store_dwordx4 v[142:143], v[138:141], off offset:256
.LBB0_942:
	s_waitcnt vmcnt(1)
	v_lshlrev_b32_e32 v0, 16, v166
	v_max_f32_e32 v0, v0, v0
	v_max_f32_e32 v138, 0x2b800000, v0
	v_and_b32_e32 v0, 0xffff0000, v166
	v_max_f32_e32 v0, v0, v0
	v_max_f32_e32 v139, 0x2b800000, v0
	v_lshlrev_b32_e32 v0, 16, v167
	v_max_f32_e32 v0, v0, v0
	v_max_f32_e32 v142, 0x2b800000, v0
	v_and_b32_e32 v0, 0xffff0000, v167
	v_max_f32_e32 v0, v0, v0
	v_max_f32_e32 v143, 0x2b800000, v0
	v_lshlrev_b32_e32 v0, 16, v168
	v_max_f32_e32 v0, v0, v0
	v_max_f32_e32 v140, 0x2b800000, v0
	v_and_b32_e32 v0, 0xffff0000, v168
	v_max_f32_e32 v0, v0, v0
	v_max_f32_e32 v141, 0x2b800000, v0
	v_lshlrev_b32_e32 v0, 16, v169
	v_max_f32_e32 v0, v0, v0
	v_max_f32_e32 v144, 0x2b800000, v0
	v_and_b32_e32 v0, 0xffff0000, v169
	v_max_f32_e32 v0, v0, v0
	s_and_b64 vcc, exec, s[38:39]
	v_max_f32_e32 v145, 0x2b800000, v0
	s_cbranch_vccnz .LBB0_944
	v_lshlrev_b32_e32 v0, 16, v134
	v_max_f32_e32 v0, v0, v0
	v_max_f32_e32 v0, 0x2b800000, v0
	v_rcp_f32_e32 v146, v0
	v_and_b32_e32 v0, 0xffff0000, v134
	v_max_f32_e32 v0, v0, v0
	v_max_f32_e32 v0, 0x2b800000, v0
	v_rcp_f32_e32 v147, v0
	v_lshlrev_b32_e32 v0, 16, v135
	v_max_f32_e32 v0, v0, v0
	v_max_f32_e32 v0, 0x2b800000, v0
	v_rcp_f32_e32 v134, v0
	v_and_b32_e32 v0, 0xffff0000, v135
	v_max_f32_e32 v0, v0, v0
	v_max_f32_e32 v0, 0x2b800000, v0
	v_rcp_f32_e32 v135, v0
	v_lshlrev_b32_e32 v0, 16, v136
	v_max_f32_e32 v0, v0, v0
	v_max_f32_e32 v0, 0x2b800000, v0
	v_mul_f32_e32 v142, v142, v134
	v_mul_f32_e32 v143, v143, v135
	v_rcp_f32_e32 v134, v0
	v_and_b32_e32 v0, 0xffff0000, v136
	v_max_f32_e32 v0, v0, v0
	v_max_f32_e32 v0, 0x2b800000, v0
	v_rcp_f32_e32 v135, v0
	v_lshlrev_b32_e32 v0, 16, v137
	v_max_f32_e32 v0, v0, v0
	v_max_f32_e32 v0, 0x2b800000, v0
	v_rcp_f32_e32 v136, v0
	v_and_b32_e32 v0, 0xffff0000, v137
	v_max_f32_e32 v0, v0, v0
	v_max_f32_e32 v0, 0x2b800000, v0
	v_rcp_f32_e32 v137, v0
	v_mul_f32_e32 v138, v138, v146
	v_mul_f32_e32 v139, v139, v147
	v_mul_f32_e32 v140, v140, v134
	v_mul_f32_e32 v141, v141, v135
	v_mul_f32_e32 v144, v144, v136
	v_mul_f32_e32 v145, v145, v137
.LBB0_944:
	v_lshlrev_b64 v[134:135], 11, v[212:213]
	v_lshl_add_u64 v[134:135], s[14:15], 0, v[134:135]
	v_mul_f32_e32 v40, v40, v142
	v_mul_f32_e32 v41, v41, v143
	v_mul_f32_e32 v38, v38, v138
	v_mul_f32_e32 v39, v39, v139
	v_mul_f32_e32 v36, v36, v144
	v_mul_f32_e32 v37, v37, v145
	v_mul_f32_e32 v34, v34, v140
	v_mul_f32_e32 v35, v35, v141
	s_and_b64 vcc, exec, s[40:41]
	v_lshl_add_u64 v[134:135], v[210:211], 1, v[134:135]
	s_cbranch_vccnz .LBB0_946
	v_cvt_pk_bf16_f32 v136, v38, v39
	v_cvt_pk_bf16_f32 v137, v40, v41
	v_cvt_pk_bf16_f32 v138, v34, v35
	v_cvt_pk_bf16_f32 v139, v36, v37
	global_store_dwordx4 v[134:135], v[136:139], off
.LBB0_946:
	s_waitcnt vmcnt(0)
	v_lshlrev_b32_e32 v0, 16, v162
	v_max_f32_e32 v0, v0, v0
	v_max_f32_e32 v136, 0x2b800000, v0
	v_and_b32_e32 v0, 0xffff0000, v162
	v_max_f32_e32 v0, v0, v0
	v_max_f32_e32 v137, 0x2b800000, v0
	v_lshlrev_b32_e32 v0, 16, v163
	v_max_f32_e32 v0, v0, v0
	v_max_f32_e32 v140, 0x2b800000, v0
	v_and_b32_e32 v0, 0xffff0000, v163
	v_max_f32_e32 v0, v0, v0
	v_max_f32_e32 v141, 0x2b800000, v0
	v_lshlrev_b32_e32 v0, 16, v164
	v_max_f32_e32 v0, v0, v0
	v_max_f32_e32 v138, 0x2b800000, v0
	v_and_b32_e32 v0, 0xffff0000, v164
	v_max_f32_e32 v0, v0, v0
	v_max_f32_e32 v139, 0x2b800000, v0
	v_lshlrev_b32_e32 v0, 16, v165
	v_max_f32_e32 v0, v0, v0
	v_max_f32_e32 v142, 0x2b800000, v0
	v_and_b32_e32 v0, 0xffff0000, v165
	v_max_f32_e32 v0, v0, v0
	s_and_b64 vcc, exec, s[38:39]
	v_max_f32_e32 v143, 0x2b800000, v0
	s_cbranch_vccnz .LBB0_948
	v_lshlrev_b32_e32 v0, 16, v130
	v_max_f32_e32 v0, v0, v0
	v_max_f32_e32 v0, 0x2b800000, v0
	v_rcp_f32_e32 v144, v0
	v_and_b32_e32 v0, 0xffff0000, v130
	v_max_f32_e32 v0, v0, v0
	v_max_f32_e32 v0, 0x2b800000, v0
	v_rcp_f32_e32 v145, v0
	v_lshlrev_b32_e32 v0, 16, v131
	v_max_f32_e32 v0, v0, v0
	v_max_f32_e32 v0, 0x2b800000, v0
	v_rcp_f32_e32 v130, v0
	v_and_b32_e32 v0, 0xffff0000, v131
	v_max_f32_e32 v0, v0, v0
	v_max_f32_e32 v0, 0x2b800000, v0
	v_rcp_f32_e32 v131, v0
	v_lshlrev_b32_e32 v0, 16, v132
	v_max_f32_e32 v0, v0, v0
	v_max_f32_e32 v0, 0x2b800000, v0
	v_mul_f32_e32 v140, v140, v130
	v_mul_f32_e32 v141, v141, v131
	v_rcp_f32_e32 v130, v0
	v_and_b32_e32 v0, 0xffff0000, v132
	v_max_f32_e32 v0, v0, v0
	v_max_f32_e32 v0, 0x2b800000, v0
	v_rcp_f32_e32 v131, v0
	v_lshlrev_b32_e32 v0, 16, v133
	v_max_f32_e32 v0, v0, v0
	v_max_f32_e32 v0, 0x2b800000, v0
	v_rcp_f32_e32 v132, v0
	v_and_b32_e32 v0, 0xffff0000, v133
	v_max_f32_e32 v0, v0, v0
	v_max_f32_e32 v0, 0x2b800000, v0
	v_rcp_f32_e32 v133, v0
	v_mul_f32_e32 v136, v136, v144
	v_mul_f32_e32 v137, v137, v145
	v_mul_f32_e32 v138, v138, v130
	v_mul_f32_e32 v139, v139, v131
	v_mul_f32_e32 v142, v142, v132
	v_mul_f32_e32 v143, v143, v133
.LBB0_948:
	v_mul_f32_e32 v8, v8, v140
	v_mul_f32_e32 v9, v9, v141
	v_mul_f32_e32 v6, v6, v136
	v_mul_f32_e32 v7, v7, v137
	v_mul_f32_e32 v4, v4, v142
	v_mul_f32_e32 v5, v5, v143
	s_and_b64 vcc, exec, s[40:41]
	v_mul_f32_e32 v2, v2, v138
	v_mul_f32_e32 v3, v3, v139
	s_cbranch_vccnz .LBB0_950
	v_cvt_pk_bf16_f32 v130, v6, v7
	v_cvt_pk_bf16_f32 v131, v8, v9
	v_cvt_pk_bf16_f32 v132, v2, v3
	v_cvt_pk_bf16_f32 v133, v4, v5
	global_store_dwordx4 v[134:135], v[130:133], off offset:256

.LBB0_1061:
	s_waitcnt vmcnt(0)
	v_ffbh_u32_e32 v159, v157
	v_min_u32_e32 v159, 32, v159
	v_lshlrev_b64 v[156:157], v159, v[156:157]
	v_min_u32_e32 v156, 1, v156
	v_or_b32_e32 v156, v157, v156
	v_cvt_f32_u32_e32 v156, v156
	v_sub_u32_e32 v157, 32, v159
	s_mov_b32 s36, 0x358637bd
	v_mov_b64_e32 v[164:165], s[36:37]
	v_ldexp_f32 v157, v156, v157
	v_ffbh_u32_e32 v156, v155
	v_min_u32_e32 v156, 32, v156
	v_lshlrev_b64 v[154:155], v156, v[154:155]
	v_min_u32_e32 v154, 1, v154
	v_or_b32_e32 v154, v155, v154
	v_cvt_f32_u32_e32 v154, v154
	v_sub_u32_e32 v155, 32, v156
	s_mov_b32 s48, 0x32800000
	s_mov_b32 s29, -1
	v_ldexp_f32 v156, v154, v155
	v_fma_f32 v154, v156, s48, v164
	v_fma_f32 v155, v157, s48, v164
	v_readlane_b32 s92, v253, 28
	v_mul_f32_e32 v156, 0x4b800000, v155
	v_cmp_gt_f32_e64 s[36:37], s96, v155
	v_cmp_gt_f32_e32 vcc, s96, v154
	v_mbcnt_lo_u32_b32 v0, s29, 0
	v_cndmask_b32_e64 v155, v155, v156, s[36:37]
	v_rsq_f32_e32 v155, v155
	v_mbcnt_hi_u32_b32 v0, s29, v0
	s_lshl_b32 s29, s84, 8
	s_add_i32 s29, s29, s52
	v_mul_f32_e32 v156, 0x45800000, v155
	v_cndmask_b32_e64 v155, v155, v156, s[36:37]
	v_mul_f32_e32 v156, 0x4b800000, v154
	v_cndmask_b32_e32 v154, v154, v156, vcc
	v_rsq_f32_e32 v154, v154
	v_and_or_b32 v158, v0, 15, s29
	v_and_b32_e32 v0, 0x70, v0
	v_ashrrev_i32_e32 v159, 31, v158
	v_mul_f32_e32 v156, 0x45800000, v154
	v_cndmask_b32_e32 v154, v154, v156, vcc
	v_ffbh_u32_e32 v156, v153
	v_min_u32_e32 v156, 32, v156
	v_lshlrev_b64 v[152:153], v156, v[152:153]
	v_min_u32_e32 v152, 1, v152
	v_or_b32_e32 v152, v153, v152
	v_cvt_f32_u32_e32 v152, v152
	v_sub_u32_e32 v153, 32, v156
	s_mov_b32 s89, 0x2e8ba2e9
	s_movk_i32 s90, 0xfea0
	v_ldexp_f32 v153, v152, v153
	v_ffbh_u32_e32 v152, v151
	v_min_u32_e32 v152, 32, v152
	v_lshlrev_b64 v[150:151], v152, v[150:151]
	v_min_u32_e32 v150, 1, v150
	v_or_b32_e32 v150, v151, v150
	v_cvt_f32_u32_e32 v150, v150
	v_sub_u32_e32 v151, 32, v152
	v_readlane_b32 s93, v253, 29
	v_ldexp_f32 v152, v150, v151
	v_fma_f32 v150, v152, s48, v164
	v_fma_f32 v151, v153, s48, v164
	s_nop 0
	v_mul_f32_e32 v152, 0x4b800000, v151
	v_cmp_gt_f32_e64 s[36:37], s96, v151
	v_cmp_gt_f32_e32 vcc, s96, v150
	s_nop 0
	v_cndmask_b32_e64 v151, v151, v152, s[36:37]
	v_rsq_f32_e32 v151, v151
	s_nop 0
	v_mul_f32_e32 v152, 0x45800000, v151
	v_cndmask_b32_e64 v151, v151, v152, s[36:37]
	v_mul_f32_e32 v152, 0x4b800000, v150
	v_cndmask_b32_e32 v150, v150, v152, vcc
	v_rsq_f32_e32 v150, v150
	s_nop 0
	v_mul_f32_e32 v152, 0x45800000, v150
	v_cndmask_b32_e32 v150, v150, v152, vcc
	v_ffbh_u32_e32 v152, v149
	v_min_u32_e32 v152, 32, v152
	v_lshlrev_b64 v[148:149], v152, v[148:149]
	v_min_u32_e32 v148, 1, v148
	v_or_b32_e32 v148, v149, v148
	v_cvt_f32_u32_e32 v148, v148
	v_sub_u32_e32 v149, 32, v152
	v_ldexp_f32 v149, v148, v149
	v_ffbh_u32_e32 v148, v147
	v_min_u32_e32 v148, 32, v148
	v_lshlrev_b64 v[146:147], v148, v[146:147]
	v_min_u32_e32 v146, 1, v146
	v_or_b32_e32 v146, v147, v146
	v_cvt_f32_u32_e32 v146, v146
	v_sub_u32_e32 v147, 32, v148
	v_ldexp_f32 v148, v146, v147
	v_fma_f32 v146, v148, s48, v164
	v_fma_f32 v147, v149, s48, v164
	s_nop 0
	v_mul_f32_e32 v148, 0x4b800000, v147
	v_cmp_gt_f32_e64 s[36:37], s96, v147
	v_cmp_gt_f32_e32 vcc, s96, v146
	s_nop 0
	v_cndmask_b32_e64 v147, v147, v148, s[36:37]
	v_rsq_f32_e32 v147, v147
	s_nop 0
	v_mul_f32_e32 v148, 0x45800000, v147
	v_cndmask_b32_e64 v149, v147, v148, s[36:37]
	v_mul_f32_e32 v147, 0x4b800000, v146
	v_cndmask_b32_e32 v146, v146, v147, vcc
	v_rsq_f32_e32 v146, v146
	s_nop 0
	v_mul_f32_e32 v147, 0x45800000, v146
	v_cndmask_b32_e32 v148, v146, v147, vcc
	v_ffbh_u32_e32 v146, v145
	v_min_u32_e32 v146, 32, v146
	v_lshlrev_b64 v[144:145], v146, v[144:145]
	v_min_u32_e32 v144, 1, v144
	v_or_b32_e32 v144, v145, v144
	v_cvt_f32_u32_e32 v144, v144
	v_sub_u32_e32 v145, 32, v146
	v_ldexp_f32 v145, v144, v145
	v_ffbh_u32_e32 v144, v143
	v_min_u32_e32 v144, 32, v144
	v_lshlrev_b64 v[142:143], v144, v[142:143]
	v_min_u32_e32 v142, 1, v142
	v_or_b32_e32 v142, v143, v142
	v_cvt_f32_u32_e32 v142, v142
	v_sub_u32_e32 v143, 32, v144
	v_ldexp_f32 v144, v142, v143
	v_fma_f32 v142, v144, s48, v164
	v_fma_f32 v143, v145, s48, v164
	s_nop 0
	v_mul_f32_e32 v144, 0x4b800000, v143
	v_cmp_gt_f32_e64 s[36:37], s96, v143
	v_cmp_gt_f32_e32 vcc, s96, v142
	s_nop 0
	v_cndmask_b32_e64 v143, v143, v144, s[36:37]
	v_rsq_f32_e32 v143, v143
	s_nop 0
	v_mul_f32_e32 v144, 0x45800000, v143
	v_cndmask_b32_e64 v147, v143, v144, s[36:37]
	s_ashr_i32 s36, s83, 2
	s_ashr_i32 s37, s36, 31
	s_lshl_b64 s[36:37], s[36:37], 25
	s_add_u32 s29, s60, s36
	s_addc_u32 s36, s61, s37
	s_lshl_b32 s37, s83, 9
	s_and_b32 s37, s37, 0x600
	s_add_u32 s29, s29, s37
	s_addc_u32 s37, s36, 0
	s_add_u32 s36, s29, s82
	s_addc_u32 s37, s37, 0
	v_lshl_add_u64 v[144:145], s[36:37], 0, v[0:1]
	v_mul_f32_e32 v0, 0xbfb8aa3b, v155
	v_mul_f32_e32 v122, v0, v122
	v_mul_f32_e32 v123, v0, v123
	v_exp_f32_e32 v122, v122
	v_mul_f32_e32 v124, v0, v124
	v_mul_f32_e32 v125, v0, v125
	v_mul_f32_e32 v128, v0, v128
	v_mul_f32_e32 v129, v0, v129
	v_mul_f32_e32 v126, v0, v126
	v_mul_f32_e32 v127, v0, v127
	v_add_f32_e32 v122, 1.0, v122
	v_rcp_f32_e32 v152, v122
	v_exp_f32_e32 v122, v123
	v_exp_f32_e32 v126, v126
	v_exp_f32_e32 v127, v127
	v_exp_f32_e32 v128, v128
	v_add_f32_e32 v122, 1.0, v122
	v_rcp_f32_e32 v153, v122
	v_exp_f32_e32 v122, v124
	v_exp_f32_e32 v129, v129
	v_mul_f32_e32 v143, 0x4b800000, v142
	v_cndmask_b32_e32 v142, v142, v143, vcc
	v_add_f32_e32 v122, 1.0, v122
	v_rcp_f32_e32 v155, v122
	v_exp_f32_e32 v122, v125
	v_rsq_f32_e32 v142, v142
	v_add_f32_e32 v126, 1.0, v126
	v_add_f32_e32 v127, 1.0, v127
	v_add_f32_e32 v128, 1.0, v128
	v_add_f32_e32 v129, 1.0, v129
	v_add_f32_e32 v122, 1.0, v122
	v_mul_f32_e32 v114, v0, v114
	v_mul_f32_e32 v115, v0, v115
	v_rcp_f32_e32 v126, v126
	v_rcp_f32_e32 v127, v127
	v_rcp_f32_e32 v128, v128
	v_rcp_f32_e32 v129, v129
	v_rcp_f32_e32 v125, v122
	v_mul_f32_e32 v120, v0, v120
	v_mul_f32_e32 v121, v0, v121
	v_mul_f32_e32 v118, v0, v118
	v_mul_f32_e32 v119, v0, v119
	v_mul_f32_e32 v116, v0, v116
	v_mul_f32_e32 v117, v0, v117
	v_exp_f32_e32 v0, v114
	v_exp_f32_e32 v114, v115
	v_mul_f32_e32 v143, 0x45800000, v142
	v_cndmask_b32_e32 v146, v142, v143, vcc
	v_lshlrev_b64 v[142:143], 11, v[158:159]
	v_lshl_add_u64 v[142:143], v[144:145], 0, v[142:143]
	v_cvt_pk_bf16_f32 v122, v126, v127
	v_cvt_pk_bf16_f32 v123, v128, v129
	v_cvt_pk_bf16_f32 v124, v152, v153
	v_cvt_pk_bf16_f32 v125, v155, v125
	v_add_f32_e32 v114, 1.0, v114
	global_store_dwordx4 v[142:143], v[122:125], off
	v_add_f32_e32 v0, 1.0, v0
	v_rcp_f32_e32 v0, v0
	v_rcp_f32_e32 v122, v114
	v_exp_f32_e32 v114, v116
	v_exp_f32_e32 v118, v118
	v_exp_f32_e32 v119, v119
	v_exp_f32_e32 v120, v120
	v_add_f32_e32 v114, 1.0, v114
	v_exp_f32_e32 v121, v121
	v_rcp_f32_e32 v123, v114
	v_exp_f32_e32 v114, v117
	v_cvt_pk_bf16_f32 v116, v0, v122
	v_mul_f32_e32 v0, 0xbfb8aa3b, v154
	v_add_f32_e32 v118, 1.0, v118
	v_add_f32_e32 v119, 1.0, v119
	v_add_f32_e32 v120, 1.0, v120
	v_add_f32_e32 v121, 1.0, v121
	v_add_f32_e32 v114, 1.0, v114
	v_mul_f32_e32 v106, v0, v106
	v_mul_f32_e32 v107, v0, v107
	v_rcp_f32_e32 v118, v118
	v_rcp_f32_e32 v119, v119
	v_rcp_f32_e32 v120, v120
	v_rcp_f32_e32 v121, v121
	v_rcp_f32_e32 v117, v114
	v_exp_f32_e32 v106, v106
	v_cvt_pk_bf16_f32 v114, v118, v119
	v_cvt_pk_bf16_f32 v115, v120, v121
	v_cvt_pk_bf16_f32 v117, v123, v117
	v_add_f32_e32 v106, 1.0, v106
	global_store_dwordx4 v[142:143], v[114:117], off offset:256
	v_mul_f32_e32 v108, v0, v108
	v_mul_f32_e32 v109, v0, v109
	v_mul_f32_e32 v112, v0, v112
	v_mul_f32_e32 v113, v0, v113
	v_rcp_f32_e32 v116, v106
	v_exp_f32_e32 v106, v107
	v_mul_f32_e32 v110, v0, v110
	v_mul_f32_e32 v111, v0, v111
	v_exp_f32_e32 v110, v110
	v_exp_f32_e32 v111, v111
	v_add_f32_e32 v106, 1.0, v106
	v_rcp_f32_e32 v117, v106
	v_exp_f32_e32 v106, v108
	v_exp_f32_e32 v112, v112
	v_exp_f32_e32 v113, v113
	v_add_f32_e32 v110, 1.0, v110
	v_add_f32_e32 v106, 1.0, v106
	v_rcp_f32_e32 v118, v106
	v_exp_f32_e32 v106, v109
	v_add_f32_e32 v111, 1.0, v111
	v_add_f32_e32 v112, 1.0, v112
	v_add_f32_e32 v113, 1.0, v113
	v_add_f32_e32 v106, 1.0, v106
	v_mul_f32_e32 v98, v0, v98
	v_mul_f32_e32 v99, v0, v99
	v_rcp_f32_e32 v110, v110
	v_rcp_f32_e32 v111, v111
	v_rcp_f32_e32 v112, v112
	v_rcp_f32_e32 v113, v113
	v_rcp_f32_e32 v109, v106
	v_mul_f32_e32 v104, v0, v104
	v_mul_f32_e32 v105, v0, v105
	v_mul_f32_e32 v102, v0, v102
	v_mul_f32_e32 v103, v0, v103
	v_mul_f32_e32 v100, v0, v100
	v_mul_f32_e32 v101, v0, v101
	v_exp_f32_e32 v0, v98
	v_exp_f32_e32 v98, v99
	v_or_b32_e32 v114, 16, v158
	v_ashrrev_i32_e32 v115, 31, v114
	v_lshlrev_b64 v[114:115], 11, v[114:115]
	v_lshl_add_u64 v[114:115], v[144:145], 0, v[114:115]
	v_cvt_pk_bf16_f32 v106, v110, v111
	v_cvt_pk_bf16_f32 v107, v112, v113
	v_cvt_pk_bf16_f32 v108, v116, v117
	v_cvt_pk_bf16_f32 v109, v118, v109
	v_add_f32_e32 v98, 1.0, v98
	global_store_dwordx4 v[114:115], v[106:109], off
	v_add_f32_e32 v0, 1.0, v0
	v_rcp_f32_e32 v0, v0
	v_rcp_f32_e32 v106, v98
	v_exp_f32_e32 v98, v100
	v_exp_f32_e32 v102, v102
	v_exp_f32_e32 v103, v103
	v_exp_f32_e32 v104, v104
	v_add_f32_e32 v98, 1.0, v98
	v_exp_f32_e32 v105, v105
	v_rcp_f32_e32 v107, v98
	v_exp_f32_e32 v98, v101
	v_cvt_pk_bf16_f32 v100, v0, v106
	v_mul_f32_e32 v0, 0xbfb8aa3b, v151
	v_add_f32_e32 v102, 1.0, v102
	v_add_f32_e32 v103, 1.0, v103
	v_add_f32_e32 v104, 1.0, v104
	v_add_f32_e32 v105, 1.0, v105
	v_add_f32_e32 v98, 1.0, v98
	v_mul_f32_e32 v90, v0, v90
	v_mul_f32_e32 v91, v0, v91
	v_rcp_f32_e32 v102, v102
	v_rcp_f32_e32 v103, v103
	v_rcp_f32_e32 v104, v104
	v_rcp_f32_e32 v105, v105
	v_rcp_f32_e32 v101, v98
	v_exp_f32_e32 v90, v90
	v_cvt_pk_bf16_f32 v98, v102, v103
	v_cvt_pk_bf16_f32 v99, v104, v105
	v_cvt_pk_bf16_f32 v101, v107, v101
	v_add_f32_e32 v90, 1.0, v90
	global_store_dwordx4 v[114:115], v[98:101], off offset:256
	v_mul_f32_e32 v92, v0, v92
	v_mul_f32_e32 v93, v0, v93
	v_mul_f32_e32 v96, v0, v96
	v_mul_f32_e32 v97, v0, v97
	v_rcp_f32_e32 v100, v90
	v_exp_f32_e32 v90, v91
	v_mul_f32_e32 v94, v0, v94
	v_mul_f32_e32 v95, v0, v95
	v_exp_f32_e32 v94, v94
	v_exp_f32_e32 v95, v95
	v_add_f32_e32 v90, 1.0, v90
	v_rcp_f32_e32 v101, v90
	v_exp_f32_e32 v90, v92
	v_exp_f32_e32 v96, v96
	v_exp_f32_e32 v97, v97
	v_add_f32_e32 v94, 1.0, v94
	v_add_f32_e32 v90, 1.0, v90
	v_rcp_f32_e32 v102, v90
	v_exp_f32_e32 v90, v93
	v_add_f32_e32 v95, 1.0, v95
	v_add_f32_e32 v96, 1.0, v96
	v_add_f32_e32 v97, 1.0, v97
	v_add_f32_e32 v90, 1.0, v90
	v_mul_f32_e32 v82, v0, v82
	v_mul_f32_e32 v83, v0, v83
	v_rcp_f32_e32 v94, v94
	v_rcp_f32_e32 v95, v95
	v_rcp_f32_e32 v96, v96
	v_rcp_f32_e32 v97, v97
	v_rcp_f32_e32 v93, v90
	v_mul_f32_e32 v88, v0, v88
	v_mul_f32_e32 v89, v0, v89
	v_mul_f32_e32 v86, v0, v86
	v_mul_f32_e32 v87, v0, v87
	v_mul_f32_e32 v84, v0, v84
	v_mul_f32_e32 v85, v0, v85
	v_exp_f32_e32 v0, v82
	v_exp_f32_e32 v82, v83
	v_or_b32_e32 v98, 32, v158
	v_ashrrev_i32_e32 v99, 31, v98
	v_lshlrev_b64 v[98:99], 11, v[98:99]
	v_lshl_add_u64 v[98:99], v[144:145], 0, v[98:99]
	v_cvt_pk_bf16_f32 v90, v94, v95
	v_cvt_pk_bf16_f32 v91, v96, v97
	v_cvt_pk_bf16_f32 v92, v100, v101
	v_cvt_pk_bf16_f32 v93, v102, v93
	v_add_f32_e32 v82, 1.0, v82
	global_store_dwordx4 v[98:99], v[90:93], off
	v_add_f32_e32 v0, 1.0, v0
	v_rcp_f32_e32 v0, v0
	v_rcp_f32_e32 v90, v82
	v_exp_f32_e32 v82, v84
	v_exp_f32_e32 v86, v86
	v_exp_f32_e32 v87, v87
	v_exp_f32_e32 v88, v88
	v_add_f32_e32 v82, 1.0, v82
	v_exp_f32_e32 v89, v89
	v_rcp_f32_e32 v91, v82
	v_exp_f32_e32 v82, v85
	v_cvt_pk_bf16_f32 v84, v0, v90
	v_mul_f32_e32 v0, 0xbfb8aa3b, v150
	v_add_f32_e32 v86, 1.0, v86
	v_add_f32_e32 v87, 1.0, v87
	v_add_f32_e32 v88, 1.0, v88
	v_add_f32_e32 v89, 1.0, v89
	v_add_f32_e32 v82, 1.0, v82
	v_mul_f32_e32 v74, v0, v74
	v_mul_f32_e32 v75, v0, v75
	v_rcp_f32_e32 v86, v86
	v_rcp_f32_e32 v87, v87
	v_rcp_f32_e32 v88, v88
	v_rcp_f32_e32 v89, v89
	v_rcp_f32_e32 v85, v82
	v_exp_f32_e32 v74, v74
	v_cvt_pk_bf16_f32 v82, v86, v87
	v_cvt_pk_bf16_f32 v83, v88, v89
	v_cvt_pk_bf16_f32 v85, v91, v85
	v_add_f32_e32 v74, 1.0, v74
	global_store_dwordx4 v[98:99], v[82:85], off offset:256
	v_mul_f32_e32 v76, v0, v76
	v_mul_f32_e32 v77, v0, v77
	v_mul_f32_e32 v80, v0, v80
	v_mul_f32_e32 v81, v0, v81
	v_rcp_f32_e32 v84, v74
	v_exp_f32_e32 v74, v75
	v_mul_f32_e32 v78, v0, v78
	v_mul_f32_e32 v79, v0, v79
	v_exp_f32_e32 v78, v78
	v_exp_f32_e32 v79, v79
	v_add_f32_e32 v74, 1.0, v74
	v_rcp_f32_e32 v85, v74
	v_exp_f32_e32 v74, v76
	v_exp_f32_e32 v80, v80
	v_exp_f32_e32 v81, v81
	v_add_f32_e32 v78, 1.0, v78
	v_add_f32_e32 v74, 1.0, v74
	v_rcp_f32_e32 v86, v74
	v_exp_f32_e32 v74, v77
	v_add_f32_e32 v79, 1.0, v79
	v_add_f32_e32 v80, 1.0, v80
	v_add_f32_e32 v81, 1.0, v81
	v_add_f32_e32 v74, 1.0, v74
	v_mul_f32_e32 v66, v0, v66
	v_mul_f32_e32 v67, v0, v67
	v_rcp_f32_e32 v78, v78
	v_rcp_f32_e32 v79, v79
	v_rcp_f32_e32 v80, v80
	v_rcp_f32_e32 v81, v81
	v_rcp_f32_e32 v77, v74
	v_mul_f32_e32 v72, v0, v72
	v_mul_f32_e32 v73, v0, v73
	v_mul_f32_e32 v70, v0, v70
	v_mul_f32_e32 v71, v0, v71
	v_mul_f32_e32 v68, v0, v68
	v_mul_f32_e32 v69, v0, v69
	v_exp_f32_e32 v0, v66
	v_exp_f32_e32 v66, v67
	v_or_b32_e32 v82, 48, v158
	v_ashrrev_i32_e32 v83, 31, v82
	v_lshlrev_b64 v[82:83], 11, v[82:83]
	v_lshl_add_u64 v[82:83], v[144:145], 0, v[82:83]
	v_cvt_pk_bf16_f32 v74, v78, v79
	v_cvt_pk_bf16_f32 v75, v80, v81
	v_cvt_pk_bf16_f32 v76, v84, v85
	v_cvt_pk_bf16_f32 v77, v86, v77
	v_add_f32_e32 v66, 1.0, v66
	global_store_dwordx4 v[82:83], v[74:77], off
	v_add_f32_e32 v0, 1.0, v0
	v_rcp_f32_e32 v0, v0
	v_rcp_f32_e32 v74, v66
	v_exp_f32_e32 v66, v68
	v_exp_f32_e32 v70, v70
	v_exp_f32_e32 v71, v71
	v_exp_f32_e32 v72, v72
	v_add_f32_e32 v66, 1.0, v66
	v_exp_f32_e32 v73, v73
	v_rcp_f32_e32 v75, v66
	v_exp_f32_e32 v66, v69
	v_cvt_pk_bf16_f32 v68, v0, v74
	v_mul_f32_e32 v0, 0xbfb8aa3b, v149
	v_add_f32_e32 v70, 1.0, v70
	v_add_f32_e32 v71, 1.0, v71
	v_add_f32_e32 v72, 1.0, v72
	v_add_f32_e32 v73, 1.0, v73
	v_add_f32_e32 v66, 1.0, v66
	v_mul_f32_e32 v58, v0, v58
	v_mul_f32_e32 v59, v0, v59
	v_rcp_f32_e32 v70, v70
	v_rcp_f32_e32 v71, v71
	v_rcp_f32_e32 v72, v72
	v_rcp_f32_e32 v73, v73
	v_rcp_f32_e32 v69, v66
	v_exp_f32_e32 v58, v58
	v_cvt_pk_bf16_f32 v66, v70, v71
	v_cvt_pk_bf16_f32 v67, v72, v73
	v_cvt_pk_bf16_f32 v69, v75, v69
	v_add_f32_e32 v58, 1.0, v58
	global_store_dwordx4 v[82:83], v[66:69], off offset:256
	v_mul_f32_e32 v60, v0, v60
	v_mul_f32_e32 v61, v0, v61
	v_mul_f32_e32 v62, v0, v62
	v_mul_f32_e32 v63, v0, v63
	v_rcp_f32_e32 v68, v58
	v_exp_f32_e32 v58, v59
	v_mul_f32_e32 v64, v0, v64
	v_mul_f32_e32 v65, v0, v65
	v_exp_f32_e32 v62, v62
	v_exp_f32_e32 v63, v63
	v_add_f32_e32 v58, 1.0, v58
	v_rcp_f32_e32 v69, v58
	v_exp_f32_e32 v58, v60
	v_exp_f32_e32 v64, v64
	v_exp_f32_e32 v65, v65
	v_add_f32_e32 v62, 1.0, v62
	v_add_f32_e32 v58, 1.0, v58
	v_rcp_f32_e32 v70, v58
	v_exp_f32_e32 v58, v61
	v_add_f32_e32 v63, 1.0, v63
	v_rcp_f32_e32 v62, v62
	v_rcp_f32_e32 v63, v63
	v_add_f32_e32 v64, 1.0, v64
	v_add_f32_e32 v65, 1.0, v65
	v_add_f32_e32 v58, 1.0, v58
	v_mul_f32_e32 v50, v0, v50
	v_mul_f32_e32 v51, v0, v51
	v_rcp_f32_e32 v64, v64
	v_rcp_f32_e32 v65, v65
	v_rcp_f32_e32 v61, v58
	v_mul_f32_e32 v56, v0, v56
	v_mul_f32_e32 v57, v0, v57
	v_mul_f32_e32 v54, v0, v54
	v_mul_f32_e32 v55, v0, v55
	v_mul_f32_e32 v52, v0, v52
	v_mul_f32_e32 v53, v0, v53
	v_exp_f32_e32 v0, v50
	v_exp_f32_e32 v50, v51
	s_mov_b32 s29, 0x40000
	v_cvt_pk_bf16_f32 v58, v62, v63
	v_add_co_u32_e32 v62, vcc, s29, v142
	v_cvt_pk_bf16_f32 v59, v64, v65
	v_cvt_pk_bf16_f32 v60, v68, v69
	v_cvt_pk_bf16_f32 v61, v70, v61
	v_addc_co_u32_e32 v63, vcc, 0, v143, vcc
	v_add_f32_e32 v50, 1.0, v50
	global_store_dwordx4 v[62:63], v[58:61], off
	v_add_f32_e32 v0, 1.0, v0
	v_rcp_f32_e32 v0, v0
	v_rcp_f32_e32 v58, v50
	v_exp_f32_e32 v50, v52
	v_exp_f32_e32 v54, v54
	v_exp_f32_e32 v55, v55
	v_exp_f32_e32 v56, v56
	v_add_f32_e32 v50, 1.0, v50
	v_exp_f32_e32 v57, v57
	v_rcp_f32_e32 v59, v50
	v_exp_f32_e32 v50, v53
	v_cvt_pk_bf16_f32 v52, v0, v58
	v_mul_f32_e32 v0, 0xbfb8aa3b, v148
	v_add_f32_e32 v54, 1.0, v54
	v_add_f32_e32 v55, 1.0, v55
	v_add_f32_e32 v56, 1.0, v56
	v_add_f32_e32 v57, 1.0, v57
	v_add_f32_e32 v50, 1.0, v50
	v_mul_f32_e32 v42, v0, v42
	v_mul_f32_e32 v43, v0, v43
	v_rcp_f32_e32 v54, v54
	v_rcp_f32_e32 v55, v55
	v_rcp_f32_e32 v56, v56
	v_rcp_f32_e32 v57, v57
	v_rcp_f32_e32 v53, v50
	v_exp_f32_e32 v42, v42
	v_lshl_add_u64 v[66:67], v[142:143], 0, s[20:21]
	v_cvt_pk_bf16_f32 v50, v54, v55
	v_cvt_pk_bf16_f32 v51, v56, v57
	v_cvt_pk_bf16_f32 v53, v59, v53
	v_add_f32_e32 v42, 1.0, v42
	global_store_dwordx4 v[66:67], v[50:53], off offset:256
	v_mul_f32_e32 v44, v0, v44
	v_mul_f32_e32 v45, v0, v45
	v_mul_f32_e32 v46, v0, v46
	v_mul_f32_e32 v47, v0, v47
	v_rcp_f32_e32 v52, v42
	v_exp_f32_e32 v42, v43
	v_mul_f32_e32 v48, v0, v48
	v_mul_f32_e32 v49, v0, v49
	v_exp_f32_e32 v46, v46
	v_exp_f32_e32 v47, v47
	v_add_f32_e32 v42, 1.0, v42
	v_rcp_f32_e32 v53, v42
	v_exp_f32_e32 v42, v44
	v_exp_f32_e32 v48, v48
	v_exp_f32_e32 v49, v49
	v_add_f32_e32 v46, 1.0, v46
	v_add_f32_e32 v42, 1.0, v42
	v_rcp_f32_e32 v54, v42
	v_exp_f32_e32 v42, v45
	v_add_f32_e32 v47, 1.0, v47
	v_rcp_f32_e32 v46, v46
	v_rcp_f32_e32 v47, v47
	v_add_f32_e32 v48, 1.0, v48
	v_add_f32_e32 v49, 1.0, v49
	v_add_f32_e32 v42, 1.0, v42
	v_mul_f32_e32 v34, v0, v34
	v_mul_f32_e32 v35, v0, v35
	v_rcp_f32_e32 v48, v48
	v_rcp_f32_e32 v49, v49
	v_rcp_f32_e32 v45, v42
	v_mul_f32_e32 v40, v0, v40
	v_mul_f32_e32 v41, v0, v41
	v_mul_f32_e32 v38, v0, v38
	v_mul_f32_e32 v39, v0, v39
	v_mul_f32_e32 v36, v0, v36
	v_mul_f32_e32 v37, v0, v37
	v_exp_f32_e32 v0, v34
	v_exp_f32_e32 v34, v35
	s_mov_b32 s29, 0x48000
	v_cvt_pk_bf16_f32 v42, v46, v47
	v_add_co_u32_e32 v46, vcc, s29, v142
	v_cvt_pk_bf16_f32 v43, v48, v49
	v_cvt_pk_bf16_f32 v44, v52, v53
	v_cvt_pk_bf16_f32 v45, v54, v45
	v_addc_co_u32_e32 v47, vcc, 0, v143, vcc
	v_add_f32_e32 v34, 1.0, v34
	global_store_dwordx4 v[46:47], v[42:45], off
	v_add_f32_e32 v0, 1.0, v0
	v_rcp_f32_e32 v0, v0
	v_rcp_f32_e32 v42, v34
	v_exp_f32_e32 v34, v36
	v_exp_f32_e32 v38, v38
	v_exp_f32_e32 v39, v39
	v_exp_f32_e32 v40, v40
	v_add_f32_e32 v34, 1.0, v34
	v_exp_f32_e32 v41, v41
	v_rcp_f32_e32 v43, v34
	v_exp_f32_e32 v34, v37
	v_cvt_pk_bf16_f32 v36, v0, v42
	v_mul_f32_e32 v0, 0xbfb8aa3b, v147
	v_add_f32_e32 v38, 1.0, v38
	v_add_f32_e32 v39, 1.0, v39
	v_add_f32_e32 v40, 1.0, v40
	v_add_f32_e32 v41, 1.0, v41
	v_add_f32_e32 v34, 1.0, v34
	v_mul_f32_e32 v26, v0, v26
	v_mul_f32_e32 v27, v0, v27
	v_rcp_f32_e32 v38, v38
	v_rcp_f32_e32 v39, v39
	v_rcp_f32_e32 v40, v40
	v_rcp_f32_e32 v41, v41
	v_rcp_f32_e32 v37, v34
	v_exp_f32_e32 v26, v26
	s_mov_b64 s[36:37], 0x48000
	v_lshl_add_u64 v[50:51], v[142:143], 0, s[36:37]
	v_cvt_pk_bf16_f32 v34, v38, v39
	v_cvt_pk_bf16_f32 v35, v40, v41
	v_cvt_pk_bf16_f32 v37, v43, v37
	v_add_f32_e32 v26, 1.0, v26
	global_store_dwordx4 v[50:51], v[34:37], off offset:256
	v_mul_f32_e32 v28, v0, v28
	v_mul_f32_e32 v29, v0, v29
	v_mul_f32_e32 v30, v0, v30
	v_mul_f32_e32 v31, v0, v31
	v_rcp_f32_e32 v36, v26
	v_exp_f32_e32 v26, v27
	v_mul_f32_e32 v32, v0, v32
	v_mul_f32_e32 v33, v0, v33
	v_exp_f32_e32 v30, v30
	v_exp_f32_e32 v31, v31
	v_add_f32_e32 v26, 1.0, v26
	v_rcp_f32_e32 v37, v26
	v_exp_f32_e32 v26, v28
	v_exp_f32_e32 v32, v32
	v_exp_f32_e32 v33, v33
	v_add_f32_e32 v30, 1.0, v30
	v_add_f32_e32 v26, 1.0, v26
	v_rcp_f32_e32 v38, v26
	v_exp_f32_e32 v26, v29
	v_add_f32_e32 v31, 1.0, v31
	v_rcp_f32_e32 v30, v30
	v_rcp_f32_e32 v31, v31
	v_add_f32_e32 v32, 1.0, v32
	v_add_f32_e32 v33, 1.0, v33
	v_add_f32_e32 v26, 1.0, v26
	v_mul_f32_e32 v18, v0, v18
	v_mul_f32_e32 v19, v0, v19
	v_rcp_f32_e32 v32, v32
	v_rcp_f32_e32 v33, v33
	v_rcp_f32_e32 v29, v26
	v_mul_f32_e32 v24, v0, v24
	v_mul_f32_e32 v25, v0, v25
	v_mul_f32_e32 v22, v0, v22
	v_mul_f32_e32 v23, v0, v23
	v_mul_f32_e32 v20, v0, v20
	v_mul_f32_e32 v21, v0, v21
	v_exp_f32_e32 v0, v18
	v_exp_f32_e32 v18, v19
	s_mov_b32 s29, 0x50000
	v_cvt_pk_bf16_f32 v26, v30, v31
	v_add_co_u32_e32 v30, vcc, s29, v142
	v_cvt_pk_bf16_f32 v27, v32, v33
	v_cvt_pk_bf16_f32 v28, v36, v37
	v_cvt_pk_bf16_f32 v29, v38, v29
	v_addc_co_u32_e32 v31, vcc, 0, v143, vcc
	v_add_f32_e32 v18, 1.0, v18
	global_store_dwordx4 v[30:31], v[26:29], off
	v_add_f32_e32 v0, 1.0, v0
	v_rcp_f32_e32 v0, v0
	v_rcp_f32_e32 v26, v18
	v_exp_f32_e32 v18, v20
	v_exp_f32_e32 v22, v22
	v_exp_f32_e32 v23, v23
	v_exp_f32_e32 v24, v24
	v_add_f32_e32 v18, 1.0, v18
	v_exp_f32_e32 v25, v25
	v_rcp_f32_e32 v27, v18
	v_exp_f32_e32 v18, v21
	v_cvt_pk_bf16_f32 v20, v0, v26
	v_mul_f32_e32 v0, 0xbfb8aa3b, v146
	v_add_f32_e32 v22, 1.0, v22
	v_add_f32_e32 v23, 1.0, v23
	v_add_f32_e32 v24, 1.0, v24
	v_add_f32_e32 v25, 1.0, v25
	v_add_f32_e32 v18, 1.0, v18
	v_mul_f32_e32 v10, v0, v10
	v_mul_f32_e32 v11, v0, v11
	v_rcp_f32_e32 v22, v22
	v_rcp_f32_e32 v23, v23
	v_rcp_f32_e32 v24, v24
	v_rcp_f32_e32 v25, v25
	v_rcp_f32_e32 v21, v18
	v_exp_f32_e32 v10, v10
	v_lshl_add_u64 v[34:35], v[142:143], 0, s[22:23]
	v_cvt_pk_bf16_f32 v18, v22, v23
	v_cvt_pk_bf16_f32 v19, v24, v25
	v_cvt_pk_bf16_f32 v21, v27, v21
	v_add_f32_e32 v10, 1.0, v10
	global_store_dwordx4 v[34:35], v[18:21], off offset:256
	v_mul_f32_e32 v12, v0, v12
	v_mul_f32_e32 v13, v0, v13
	v_mul_f32_e32 v14, v0, v14
	v_mul_f32_e32 v15, v0, v15
	v_rcp_f32_e32 v20, v10
	v_exp_f32_e32 v10, v11
	v_mul_f32_e32 v16, v0, v16
	v_mul_f32_e32 v17, v0, v17
	v_exp_f32_e32 v14, v14
	v_exp_f32_e32 v15, v15
	v_add_f32_e32 v10, 1.0, v10
	v_rcp_f32_e32 v21, v10
	v_exp_f32_e32 v10, v12
	v_exp_f32_e32 v16, v16
	v_exp_f32_e32 v17, v17
	v_add_f32_e32 v14, 1.0, v14
	v_add_f32_e32 v10, 1.0, v10
	v_rcp_f32_e32 v22, v10
	v_exp_f32_e32 v10, v13
	v_add_f32_e32 v15, 1.0, v15
	v_rcp_f32_e32 v14, v14
	v_rcp_f32_e32 v15, v15
	v_add_f32_e32 v16, 1.0, v16
	v_add_f32_e32 v17, 1.0, v17
	v_add_f32_e32 v10, 1.0, v10
	v_mul_f32_e32 v2, v0, v2
	v_mul_f32_e32 v3, v0, v3
	v_rcp_f32_e32 v16, v16
	v_rcp_f32_e32 v17, v17
	v_rcp_f32_e32 v13, v10
	v_mul_f32_e32 v8, v0, v8
	v_mul_f32_e32 v9, v0, v9
	v_mul_f32_e32 v6, v0, v6
	v_mul_f32_e32 v7, v0, v7
	v_mul_f32_e32 v4, v0, v4
	v_mul_f32_e32 v5, v0, v5
	v_exp_f32_e32 v0, v2
	v_exp_f32_e32 v2, v3
	s_mov_b32 s29, 0x58000
	v_cvt_pk_bf16_f32 v10, v14, v15
	v_add_co_u32_e32 v14, vcc, s29, v142
	v_cvt_pk_bf16_f32 v11, v16, v17
	v_cvt_pk_bf16_f32 v12, v20, v21
	v_cvt_pk_bf16_f32 v13, v22, v13
	v_addc_co_u32_e32 v15, vcc, 0, v143, vcc
	v_add_f32_e32 v2, 1.0, v2
	global_store_dwordx4 v[14:15], v[10:13], off
	v_exp_f32_e32 v6, v6
	v_exp_f32_e32 v7, v7
	v_rcp_f32_e32 v10, v2
	v_exp_f32_e32 v2, v4
	v_exp_f32_e32 v8, v8
	v_exp_f32_e32 v9, v9
	v_add_f32_e32 v6, 1.0, v6
	v_add_f32_e32 v2, 1.0, v2
	v_rcp_f32_e32 v11, v2
	v_exp_f32_e32 v2, v5
	v_add_f32_e32 v7, 1.0, v7
	v_add_f32_e32 v8, 1.0, v8
	v_add_f32_e32 v9, 1.0, v9
	v_add_f32_e32 v0, 1.0, v0
	v_add_f32_e32 v2, 1.0, v2
	v_rcp_f32_e32 v6, v6
	v_rcp_f32_e32 v7, v7
	v_rcp_f32_e32 v8, v8
	v_rcp_f32_e32 v9, v9
	v_rcp_f32_e32 v0, v0
	v_rcp_f32_e32 v5, v2
	s_mov_b64 s[36:37], 0x58000
	v_lshl_add_u64 v[18:19], v[142:143], 0, s[36:37]
	v_cvt_pk_bf16_f32 v2, v6, v7
	v_cvt_pk_bf16_f32 v3, v8, v9
	v_cvt_pk_bf16_f32 v4, v0, v10
	v_cvt_pk_bf16_f32 v5, v11, v5
	s_mov_b64 s[36:37], -1
	s_andn2_b64 vcc, exec, s[46:47]
	global_store_dwordx4 v[18:19], v[2:5], off offset:256
	s_cbranch_vccnz .LBB0_1054
	s_nop 0
	v_lshl_add_u32 v2, s38, 8, v160
	v_ashrrev_i32_e32 v3, 31, v2
	v_lshl_add_u64 v[2:3], v[2:3], 3, s[0:1]
	global_load_dwordx2 v[156:157], v[2:3], off nt
	global_load_dwordx2 v[154:155], v[2:3], off offset:128 nt
	global_load_dwordx2 v[152:153], v[2:3], off offset:256 nt
	global_load_dwordx2 v[150:151], v[2:3], off offset:384 nt
	global_load_dwordx2 v[148:149], v[2:3], off offset:1024 nt
	global_load_dwordx2 v[146:147], v[2:3], off offset:1152 nt
	global_load_dwordx2 v[144:145], v[2:3], off offset:1280 nt
	global_load_dwordx2 v[142:143], v[2:3], off offset:1408 nt
	s_andn2_b64 vcc, exec, s[14:15]
	s_cbranch_vccnz .LBB0_1053
	s_barrier
	s_branch .LBB0_1053

.LBB0_1072:
	s_and_b64 s[38:39], s[52:53], exec
	v_readfirstlane_b32 s41, v235
	s_cselect_b32 s40, s92, s93
	s_ashr_i32 s31, s41, 6
	s_lshl_b32 s42, s40, 8
	s_lshl_b32 s43, s31, 5
	s_or_b32 s29, s16, s42
	s_ashr_i32 s39, s43, 31
	s_add_u32 s38, s29, s43
	s_addc_u32 s39, s17, s39
	s_lshl_b64 s[38:39], s[38:39], 10
	s_add_u32 s50, s94, s38
	s_addc_u32 s51, s95, s39
	s_lshl_b32 s38, s31, 3
	s_lshl_b32 s29, s31, 4
	s_ashr_i32 s39, s38, 31
	v_and_or_b32 v0, s29, 48, v237
	s_ashr_i32 s29, s41, 3
	v_lshl_add_u64 v[216:217], s[38:39], 1, v[214:215]
	v_lshlrev_b32_e32 v0, 10, v0
	s_and_b32 s38, s29, 0xffffffe0
	v_lshl_add_u64 v[2:3], s[44:45], 0, v[0:1]
	s_ashr_i32 s39, s38, 31
	v_lshl_add_u64 v[2:3], s[38:39], 1, v[2:3]
	v_mov_b32_e32 v203, v1
	s_lshl_b32 s63, s31, 10
	s_mov_b32 s29, m0
	s_mov_b32 m0, s63
	s_nop 0
	global_load_lds_dwordx4 v[216:217], off
	s_mov_b32 m0, s29
	v_lshl_add_u64 v[218:219], v[2:3], 0, v[202:203]
	s_add_i32 s62, s63, 0x6000
	s_mov_b32 s29, m0
	s_mov_b32 m0, s62
	s_nop 0
	global_load_lds_dwordx4 v[218:219], off
	s_mov_b32 m0, s29
	v_lshl_add_u64 v[2:3], v[216:217], 0, s[12:13]
	s_add_i32 s29, s63, 0x2000
	s_mov_b32 s38, m0
	s_mov_b32 m0, s29
	s_nop 0
	global_load_lds_dwordx4 v[2:3], off
	s_mov_b32 m0, s38
	global_load_dwordx4 v[124:127], v247, s[50:51]
	global_load_dwordx4 v[120:123], v247, s[50:51] offset:32
	global_load_dwordx4 v[116:119], v247, s[50:51] offset:64
	global_load_dwordx4 v[112:115], v247, s[50:51] offset:96
	s_add_i32 s43, s43, s42
	v_or_b32_e32 v34, s43, v236
	v_ashrrev_i32_e32 v35, 31, v34
	v_lshl_add_u64 v[2:3], v[34:35], 2, s[0:1]
	v_add_co_u32_e32 v4, vcc, s10, v2
	global_load_dword v0, v[2:3], off
	s_nop 0
	v_addc_co_u32_e32 v5, vcc, 0, v3, vcc
	global_load_dword v36, v[4:5], off
	v_mov_b32_e32 v180, v1
	s_add_i32 s29, s63, 0x4000
	v_ashrrev_i32_e32 v181, 31, v180
	s_mov_b32 s57, 0
	s_waitcnt vmcnt(5)
	v_and_b32_e32 v5, 0xffff0000, v124
	v_lshlrev_b32_e32 v4, 16, v124
	v_mul_f32_e32 v6, v5, v5
	v_fmac_f32_e32 v6, v4, v4
	v_lshlrev_b32_e32 v4, 16, v125
	v_fmac_f32_e32 v6, v4, v4
	v_and_b32_e32 v4, 0xffff0000, v125
	v_fmac_f32_e32 v6, v4, v4
	v_lshlrev_b32_e32 v4, 16, v126
	v_fmac_f32_e32 v6, v4, v4
	v_and_b32_e32 v4, 0xffff0000, v126
	v_fmac_f32_e32 v6, v4, v4
	v_lshlrev_b32_e32 v4, 16, v127
	v_fmac_f32_e32 v6, v4, v4
	v_and_b32_e32 v4, 0xffff0000, v127
	v_fmac_f32_e32 v6, v4, v4
	s_waitcnt vmcnt(4)
	v_lshlrev_b32_e32 v4, 16, v120
	v_fmac_f32_e32 v6, v4, v4
	v_and_b32_e32 v4, 0xffff0000, v120
	v_fmac_f32_e32 v6, v4, v4
	v_lshlrev_b32_e32 v4, 16, v121
	v_fmac_f32_e32 v6, v4, v4
	v_and_b32_e32 v4, 0xffff0000, v121
	v_fmac_f32_e32 v6, v4, v4
	v_lshlrev_b32_e32 v4, 16, v122
	v_fmac_f32_e32 v6, v4, v4
	v_and_b32_e32 v4, 0xffff0000, v122
	v_fmac_f32_e32 v6, v4, v4
	v_lshlrev_b32_e32 v4, 16, v123
	v_fmac_f32_e32 v6, v4, v4
	v_and_b32_e32 v4, 0xffff0000, v123
	v_fmac_f32_e32 v6, v4, v4
	s_waitcnt vmcnt(3)
	v_lshlrev_b32_e32 v4, 16, v116
	v_fmac_f32_e32 v6, v4, v4
	v_and_b32_e32 v4, 0xffff0000, v116
	v_fmac_f32_e32 v6, v4, v4
	v_lshlrev_b32_e32 v4, 16, v117
	v_fmac_f32_e32 v6, v4, v4
	v_and_b32_e32 v4, 0xffff0000, v117
	v_fmac_f32_e32 v6, v4, v4
	v_lshlrev_b32_e32 v4, 16, v118
	v_fmac_f32_e32 v6, v4, v4
	v_and_b32_e32 v4, 0xffff0000, v118
	v_fmac_f32_e32 v6, v4, v4
	v_lshlrev_b32_e32 v4, 16, v119
	v_fmac_f32_e32 v6, v4, v4
	v_and_b32_e32 v4, 0xffff0000, v119
	v_fmac_f32_e32 v6, v4, v4
	s_waitcnt vmcnt(2)
	v_lshlrev_b32_e32 v4, 16, v112
	v_fmac_f32_e32 v6, v4, v4
	v_and_b32_e32 v4, 0xffff0000, v112
	v_fmac_f32_e32 v6, v4, v4
	v_lshlrev_b32_e32 v4, 16, v113
	v_fmac_f32_e32 v6, v4, v4
	v_and_b32_e32 v4, 0xffff0000, v113
	v_fmac_f32_e32 v6, v4, v4
	v_and_b32_e32 v5, 0xffff0000, v114
	v_lshlrev_b32_e32 v4, 16, v114
	v_mul_f32_e32 v4, v4, v4
	v_mul_f32_e32 v5, v5, v5
	s_nop 0
	v_add_f32_e32 v4, v4, v6
	v_add_f32_e32 v6, v5, v4
	v_and_b32_e32 v5, 0xffff0000, v115
	v_lshlrev_b32_e32 v4, 16, v115
	v_mul_f32_e32 v4, v4, v4
	v_mul_f32_e32 v5, v5, v5
	s_nop 0
	v_add_f32_e32 v4, v4, v6
	v_add_f32_e32 v4, v5, v4
	v_mov_b32_e32 v5, v4
	s_nop 1
	v_permlane32_swap_b32_e32 v4, v5
	v_add_f32_e32 v4, v4, v5
	v_cmp_gt_f32_e32 vcc, s7, v4
	v_mul_f32_e32 v5, 0x4f800000, v4
	s_nop 0
	v_cndmask_b32_e32 v4, v4, v5, vcc
	v_sqrt_f32_e32 v5, v4
	s_nop 0
	v_add_u32_e32 v6, -1, v5
	v_fma_f32 v7, -v6, v5, v4
	v_cmp_ge_f32_e64 s[38:39], 0, v7
	v_add_u32_e32 v7, 1, v5
	s_nop 0
	v_cndmask_b32_e64 v6, v5, v6, s[38:39]
	v_fma_f32 v5, -v7, v5, v4
	v_cmp_lt_f32_e64 s[38:39], 0, v5
	s_nop 1
	v_cndmask_b32_e64 v5, v6, v7, s[38:39]
	v_mul_f32_e32 v6, 0x37800000, v5
	v_cndmask_b32_e32 v5, v5, v6, vcc
	v_cmp_class_f32_e32 vcc, v4, v199
	v_lshl_add_u64 v[6:7], v[216:217], 0, s[24:25]
	s_nop 0
	v_cndmask_b32_e32 v4, v5, v4, vcc
	v_mul_f32_e32 v201, 0x3f8147ae, v4
	v_lshl_add_u64 v[4:5], v[180:181], 2, s[14:15]
	global_load_dword v8, v[4:5], off
	s_mov_b32 s38, m0
	s_mov_b32 m0, s29
	s_nop 0
	global_load_lds_dwordx4 v[6:7], off
	s_mov_b32 m0, s38
	s_mov_b32 s29, 0x10000
	v_add_co_u32_e32 v6, vcc, s29, v2
	s_mov_b32 s29, 0x18000
	s_nop 0
	v_addc_co_u32_e32 v7, vcc, 0, v3, vcc
	v_add_co_u32_e32 v2, vcc, s29, v2
	s_waitcnt vmcnt(3) lgkmcnt(0)
	s_barrier
	global_load_dword v211, v[6:7], off
	s_nop 0
	v_addc_co_u32_e32 v3, vcc, 0, v3, vcc
	global_load_dword v213, v[2:3], off
	global_load_dword v209, v[4:5], off offset:4
	s_waitcnt vmcnt(3)
	v_mul_f32_e32 v2, v8, v201
	v_cmp_nge_f32_e32 vcc, s73, v2
	ds_read_b128 v[18:21], v241 offset:512
	ds_read_b128 v[2:5], v241
	s_waitcnt lgkmcnt(0)
	v_mfma_f32_32x32x16_bf16 v[2:17], v[2:5], v[124:127], 0
	ds_read_b128 v[38:41], v241 offset:2560
	ds_read_b128 v[42:45], v241 offset:2048
	v_mfma_f32_32x32x16_bf16 v[18:33], v[18:21], v[124:127], 0
	s_waitcnt lgkmcnt(0)
	v_mfma_f32_32x32x16_bf16 v[2:17], v[42:45], v[120:123], v[2:17]
	v_mfma_f32_32x32x16_bf16 v[18:33], v[38:41], v[120:123], v[18:33]
	ds_read_b128 v[38:41], v241 offset:4608
	ds_read_b128 v[42:45], v241 offset:4096
	s_waitcnt lgkmcnt(0)
	v_mfma_f32_32x32x16_bf16 v[2:17], v[42:45], v[116:119], v[2:17]
	v_mfma_f32_32x32x16_bf16 v[18:33], v[38:41], v[116:119], v[18:33]
	ds_read_b128 v[38:41], v241 offset:6656
	ds_read_b128 v[42:45], v241 offset:6144
	s_waitcnt lgkmcnt(0)
	v_mfma_f32_32x32x16_bf16 v[2:17], v[42:45], v[112:115], v[2:17]
	v_mfma_f32_32x32x16_bf16 v[18:33], v[38:41], v[112:115], v[18:33]
	v_lshrrev_b32_e32 v38, v238, v0
	v_lshrrev_b32_e32 v39, v238, v36
	s_nop 15
	s_nop 7
	v_bfe_i32 v37, v38, 0, 1
	v_bfe_i32 v40, v39, 0, 1
	s_nop 6
	v_bitop3_b32 v37, v2, s6, v37 bitop3:0xe4
	v_bitop3_b32 v2, v18, s6, v40 bitop3:0xe4
	v_bfe_i32 v18, v38, 1, 1
	v_bfe_i32 v40, v39, 1, 1
	v_bitop3_b32 v18, v3, s6, v18 bitop3:0xe4
	v_bitop3_b32 v3, v19, s6, v40 bitop3:0xe4
	v_bfe_i32 v19, v38, 2, 1
	v_bfe_i32 v40, v39, 2, 1
	v_bitop3_b32 v19, v4, s6, v19 bitop3:0xe4
	v_bitop3_b32 v4, v20, s6, v40 bitop3:0xe4
	v_bfe_i32 v20, v38, 3, 1
	v_bfe_i32 v40, v39, 3, 1
	v_bitop3_b32 v20, v5, s6, v20 bitop3:0xe4
	v_bitop3_b32 v5, v21, s6, v40 bitop3:0xe4
	v_bfe_i32 v21, v38, 8, 1
	v_bfe_i32 v40, v39, 8, 1
	v_bitop3_b32 v21, v6, s6, v21 bitop3:0xe4
	v_bitop3_b32 v6, v22, s6, v40 bitop3:0xe4
	v_bfe_i32 v22, v38, 9, 1
	v_bfe_i32 v40, v39, 9, 1
	v_bitop3_b32 v22, v7, s6, v22 bitop3:0xe4
	v_bitop3_b32 v7, v23, s6, v40 bitop3:0xe4
	v_bfe_i32 v23, v38, 10, 1
	v_bfe_i32 v40, v39, 10, 1
	v_bitop3_b32 v23, v8, s6, v23 bitop3:0xe4
	v_bitop3_b32 v8, v24, s6, v40 bitop3:0xe4
	v_bfe_i32 v24, v38, 11, 1
	v_bfe_i32 v40, v39, 11, 1
	v_bitop3_b32 v24, v9, s6, v24 bitop3:0xe4
	v_bitop3_b32 v9, v25, s6, v40 bitop3:0xe4
	v_bfe_i32 v25, v38, 16, 1
	v_bfe_i32 v40, v39, 16, 1
	v_bitop3_b32 v25, v10, s6, v25 bitop3:0xe4
	v_bitop3_b32 v10, v26, s6, v40 bitop3:0xe4
	v_bfe_i32 v26, v38, 17, 1
	v_bfe_i32 v40, v39, 17, 1
	v_bitop3_b32 v26, v11, s6, v26 bitop3:0xe4
	v_bitop3_b32 v11, v27, s6, v40 bitop3:0xe4
	v_bfe_i32 v27, v38, 18, 1
	v_bfe_i32 v40, v39, 18, 1
	v_bitop3_b32 v27, v12, s6, v27 bitop3:0xe4
	v_bitop3_b32 v12, v28, s6, v40 bitop3:0xe4
	v_bfe_i32 v28, v38, 19, 1
	v_bfe_i32 v40, v39, 19, 1
	v_bitop3_b32 v28, v13, s6, v28 bitop3:0xe4
	v_bitop3_b32 v13, v29, s6, v40 bitop3:0xe4
	v_bfe_i32 v29, v38, 24, 1
	v_bfe_i32 v40, v39, 24, 1
	v_bitop3_b32 v29, v14, s6, v29 bitop3:0xe4
	v_bitop3_b32 v14, v30, s6, v40 bitop3:0xe4
	v_bfe_i32 v30, v38, 25, 1
	v_bfe_i32 v40, v39, 25, 1
	v_bitop3_b32 v30, v15, s6, v30 bitop3:0xe4
	v_bitop3_b32 v15, v31, s6, v40 bitop3:0xe4
	v_bfe_i32 v31, v38, 26, 1
	v_bfe_i32 v40, v39, 26, 1
	v_bitop3_b32 v31, v16, s6, v31 bitop3:0xe4
	v_bitop3_b32 v16, v32, s6, v40 bitop3:0xe4
	v_bfe_i32 v32, v38, 27, 1
	v_bfe_i32 v38, v39, 27, 1
	v_bitop3_b32 v32, v17, s6, v32 bitop3:0xe4
	v_bitop3_b32 v17, v33, s6, v38 bitop3:0xe4
	s_cbranch_vccz .LBB0_1074
	v_max3_f32 v33, v37, v18, v2
	v_max3_f32 v38, v19, v20, v3
	s_nop 0
	v_max3_f32 v33, v33, v4, v5
	v_max3_f32 v38, v38, v23, v24
	s_nop 0
	v_max3_f32 v33, v33, v21, v22
	v_max3_f32 v38, v38, v8, v9
	s_nop 0
	v_max3_f32 v33, v33, v6, v7
	v_max3_f32 v38, v38, v27, v28
	s_nop 0
	v_max3_f32 v33, v33, v25, v26
	v_max3_f32 v38, v38, v12, v13
	s_nop 0
	v_max3_f32 v33, v33, v10, v11
	v_max3_f32 v38, v38, v31, v32
	s_nop 0
	v_max3_f32 v33, v33, v29, v30
	v_max3_f32 v38, v38, v16, v17
	s_nop 0
	v_max3_f32 v33, v33, v14, v15
	s_nop 0
	v_max_f32_e32 v33, v33, v38
	s_nop 0
	v_mov_b32_e32 v38, v33
	s_nop 1
	v_permlane32_swap_b32_e32 v33, v38
	v_max_f32_e32 v33, v33, v38
	s_nop 0
	v_cmp_neq_f32_e32 vcc, s6, v33
	s_nop 1
	v_cndmask_b32_e32 v33, 0, v33, vcc
	v_add_f32_e32 v207, v1, v33
	v_sub_f32_e32 v37, v37, v33
	v_sub_f32_e32 v2, v2, v33
	v_sub_f32_e32 v18, v18, v33
	v_sub_f32_e32 v3, v3, v33
	v_sub_f32_e32 v19, v19, v33
	v_sub_f32_e32 v4, v4, v33
	v_sub_f32_e32 v20, v20, v33
	v_sub_f32_e32 v5, v5, v33
	v_sub_f32_e32 v21, v21, v33
	v_sub_f32_e32 v6, v6, v33
	v_sub_f32_e32 v22, v22, v33
	v_sub_f32_e32 v7, v7, v33
	v_sub_f32_e32 v23, v23, v33
	v_sub_f32_e32 v8, v8, v33
	v_sub_f32_e32 v24, v24, v33
	v_sub_f32_e32 v9, v9, v33
	v_sub_f32_e32 v25, v25, v33
	v_sub_f32_e32 v10, v10, v33
	v_sub_f32_e32 v26, v26, v33
	v_sub_f32_e32 v11, v11, v33
	v_sub_f32_e32 v27, v27, v33
	v_sub_f32_e32 v12, v12, v33
	v_sub_f32_e32 v28, v28, v33
	v_sub_f32_e32 v13, v13, v33
	v_sub_f32_e32 v29, v29, v33
	v_sub_f32_e32 v14, v14, v33
	v_sub_f32_e32 v30, v30, v33
	v_sub_f32_e32 v15, v15, v33
	v_sub_f32_e32 v31, v31, v33
	v_sub_f32_e32 v16, v16, v33
	v_sub_f32_e32 v32, v32, v33
	v_sub_f32_e32 v17, v17, v33
	s_branch .LBB0_1075

.LBB0_1080:
	s_waitcnt lgkmcnt(14)
	v_mfma_f32_32x32x16_bf16 v[32:47], v[140:143], v[176:179], v[32:47]
	v_exp_f32_e32 v64, v80
	v_exp_f32_e32 v65, v81
	v_exp_f32_e32 v66, v82
	v_exp_f32_e32 v67, v83
	s_waitcnt lgkmcnt(12)
	v_mfma_f32_32x32x16_bf16 v[16:31], v[140:143], v[172:175], v[16:31]
	v_exp_f32_e32 v68, v84
	v_exp_f32_e32 v69, v85
	v_exp_f32_e32 v70, v86
	v_exp_f32_e32 v71, v87
	v_add_u32_e32 v84, s57, v241
	ds_read_b128 v[140:143], v84
	ds_read_b128 v[148:151], v84 offset:2048
	s_waitcnt lgkmcnt(12)
	v_mfma_f32_32x32x16_bf16 v[32:47], v[136:139], v[164:167], v[32:47]
	v_exp_f32_e32 v72, v88
	v_exp_f32_e32 v73, v89
	v_exp_f32_e32 v74, v90
	v_exp_f32_e32 v75, v91
	ds_read_b128 v[176:179], v84 offset:2560
	ds_read_b128 v[172:175], v84 offset:4096
	s_waitcnt lgkmcnt(12)
	v_mfma_f32_32x32x16_bf16 v[16:31], v[136:139], v[168:171], v[16:31]
	v_exp_f32_e32 v76, v92
	v_exp_f32_e32 v77, v93
	v_exp_f32_e32 v78, v94
	v_exp_f32_e32 v79, v95
	ds_read_b128 v[136:139], v84 offset:512
	ds_read_b128 v[164:167], v84 offset:4608
	s_waitcnt lgkmcnt(12)
	v_mfma_f32_32x32x16_bf16 v[32:47], v[132:135], v[160:163], v[32:47]
	v_exp_f32_e32 v48, v96
	v_exp_f32_e32 v49, v97
	v_exp_f32_e32 v50, v98
	v_exp_f32_e32 v51, v99
	ds_read_b128 v[168:171], v84 offset:6144
	ds_read_b128 v[160:163], v84 offset:6656
	s_waitcnt lgkmcnt(12)
	v_mfma_f32_32x32x16_bf16 v[16:31], v[132:135], v[2:5], v[16:31]
	v_exp_f32_e32 v52, v100
	v_exp_f32_e32 v53, v101
	v_exp_f32_e32 v54, v102
	v_exp_f32_e32 v55, v103
	s_waitcnt lgkmcnt(10)
	v_mfma_f32_32x32x16_bf16 v[32:47], v[128:131], v[6:9], v[32:47]
	v_exp_f32_e32 v56, v104
	v_exp_f32_e32 v57, v105
	v_exp_f32_e32 v58, v106
	v_exp_f32_e32 v59, v107
	s_waitcnt lgkmcnt(8)
	v_mfma_f32_32x32x16_bf16 v[16:31], v[128:131], v[10:13], v[16:31]
	v_exp_f32_e32 v60, v108
	v_exp_f32_e32 v61, v109
	v_exp_f32_e32 v62, v110
	v_exp_f32_e32 v63, v111
	s_waitcnt vmcnt(2) lgkmcnt(0)
	s_barrier
	s_andn2_b64 vcc, exec, s[40:41]
	s_cbranch_vccnz .LBB0_1082
	s_waitcnt lgkmcnt(0)
	ds_read_b128 v[2:5], v203 offset:49248
	ds_read_b128 v[6:9], v203 offset:49216
	ds_read_b128 v[10:13], v203 offset:49184
	ds_read_b128 v[84:87], v203 offset:49152
	s_waitcnt lgkmcnt(3)
	v_mul_f32_e32 v46, v46, v4
	v_mul_f32_e32 v47, v47, v5
	s_waitcnt lgkmcnt(2)
	v_mul_f32_e32 v42, v42, v8
	v_mul_f32_e32 v43, v43, v9
	s_waitcnt lgkmcnt(1)
	v_mul_f32_e32 v38, v38, v12
	v_mul_f32_e32 v39, v39, v13
	s_waitcnt lgkmcnt(0)
	v_mul_f32_e32 v34, v34, v86
	v_mul_f32_e32 v35, v35, v87
	v_mul_f32_e32 v44, v44, v2
	v_mul_f32_e32 v45, v45, v3
	v_mul_f32_e32 v40, v40, v6
	v_mul_f32_e32 v41, v41, v7
	v_mul_f32_e32 v36, v36, v10
	v_mul_f32_e32 v37, v37, v11
	v_mul_f32_e32 v32, v32, v84
	v_mul_f32_e32 v33, v33, v85
	v_mul_f32_e32 v30, v30, v4
	v_mul_f32_e32 v31, v31, v5
	v_mul_f32_e32 v26, v26, v8
	v_mul_f32_e32 v27, v27, v9
	v_mul_f32_e32 v22, v22, v12
	v_mul_f32_e32 v23, v23, v13
	v_mul_f32_e32 v18, v18, v86
	v_mul_f32_e32 v19, v19, v87
	v_mul_f32_e32 v28, v28, v2
	v_mul_f32_e32 v29, v29, v3
	v_mul_f32_e32 v24, v24, v6
	v_mul_f32_e32 v25, v25, v7
	v_mul_f32_e32 v20, v20, v10
	v_mul_f32_e32 v21, v21, v11
	v_mul_f32_e32 v16, v16, v84
	v_mul_f32_e32 v17, v17, v85

.LBB0_1085:
	s_waitcnt lgkmcnt(14)
	v_mfma_f32_32x32x16_bf16 v[32:47], v[140:143], v[156:159], v[32:47]
	v_exp_f32_e32 v64, v80
	v_exp_f32_e32 v65, v81
	v_exp_f32_e32 v66, v82
	v_exp_f32_e32 v67, v83
	s_waitcnt lgkmcnt(12)
	v_mfma_f32_32x32x16_bf16 v[16:31], v[140:143], v[152:155], v[16:31]
	v_exp_f32_e32 v68, v84
	v_exp_f32_e32 v69, v85
	v_exp_f32_e32 v70, v86
	v_exp_f32_e32 v71, v87
	v_add_u32_e32 v80, s65, v241
	ds_read_b128 v[172:175], v80
	ds_read_b128 v[164:167], v80 offset:512
	s_waitcnt lgkmcnt(12)
	v_mfma_f32_32x32x16_bf16 v[32:47], v[136:139], v[144:147], v[32:47]
	v_exp_f32_e32 v72, v88
	v_exp_f32_e32 v73, v89
	v_exp_f32_e32 v74, v90
	v_exp_f32_e32 v75, v91
	ds_read_b128 v[168:171], v80 offset:2048
	ds_read_b128 v[160:163], v80 offset:2560
	s_waitcnt lgkmcnt(12)
	v_mfma_f32_32x32x16_bf16 v[16:31], v[136:139], v[148:151], v[16:31]
	v_exp_f32_e32 v76, v92
	v_exp_f32_e32 v77, v93
	v_exp_f32_e32 v78, v94
	v_exp_f32_e32 v79, v95
	ds_read_b128 v[156:159], v80 offset:4096
	ds_read_b128 v[152:155], v80 offset:4608
	s_waitcnt lgkmcnt(12)
	v_mfma_f32_32x32x16_bf16 v[32:47], v[132:135], v[176:179], v[32:47]
	v_exp_f32_e32 v48, v96
	v_exp_f32_e32 v49, v97
	v_exp_f32_e32 v50, v98
	v_exp_f32_e32 v51, v99
	ds_read_b128 v[148:151], v80 offset:6144
	ds_read_b128 v[144:147], v80 offset:6656
	s_waitcnt lgkmcnt(12)
	v_mfma_f32_32x32x16_bf16 v[16:31], v[132:135], v[2:5], v[16:31]
	v_exp_f32_e32 v52, v100
	v_exp_f32_e32 v53, v101
	v_exp_f32_e32 v54, v102
	v_exp_f32_e32 v55, v103
	s_waitcnt lgkmcnt(10)
	v_mfma_f32_32x32x16_bf16 v[32:47], v[128:131], v[6:9], v[32:47]
	v_exp_f32_e32 v56, v104
	v_exp_f32_e32 v57, v105
	v_exp_f32_e32 v58, v106
	v_exp_f32_e32 v59, v107
	s_waitcnt lgkmcnt(8)
	v_mfma_f32_32x32x16_bf16 v[16:31], v[128:131], v[10:13], v[16:31]
	v_exp_f32_e32 v60, v108
	v_exp_f32_e32 v61, v109
	v_exp_f32_e32 v62, v110
	v_exp_f32_e32 v63, v111
	s_waitcnt vmcnt(2) lgkmcnt(0)
	s_barrier
	s_andn2_b64 vcc, exec, s[40:41]
	s_cbranch_vccnz .LBB0_1087
	s_waitcnt lgkmcnt(0)
	ds_read_b128 v[2:5], v203 offset:49248
	ds_read_b128 v[6:9], v203 offset:49216
	ds_read_b128 v[10:13], v203 offset:49184
	ds_read_b128 v[80:83], v203 offset:49152
	s_waitcnt lgkmcnt(3)
	v_mul_f32_e32 v46, v46, v4
	v_mul_f32_e32 v47, v47, v5
	s_waitcnt lgkmcnt(2)
	v_mul_f32_e32 v42, v42, v8
	v_mul_f32_e32 v43, v43, v9
	s_waitcnt lgkmcnt(1)
	v_mul_f32_e32 v38, v38, v12
	v_mul_f32_e32 v39, v39, v13
	s_waitcnt lgkmcnt(0)
	v_mul_f32_e32 v34, v34, v82
	v_mul_f32_e32 v35, v35, v83
	v_mul_f32_e32 v44, v44, v2
	v_mul_f32_e32 v45, v45, v3
	v_mul_f32_e32 v40, v40, v6
	v_mul_f32_e32 v41, v41, v7
	v_mul_f32_e32 v36, v36, v10
	v_mul_f32_e32 v37, v37, v11
	v_mul_f32_e32 v32, v32, v80
	v_mul_f32_e32 v33, v33, v81
	v_mul_f32_e32 v30, v30, v4
	v_mul_f32_e32 v31, v31, v5
	v_mul_f32_e32 v26, v26, v8
	v_mul_f32_e32 v27, v27, v9
	v_mul_f32_e32 v22, v22, v12
	v_mul_f32_e32 v23, v23, v13
	v_mul_f32_e32 v18, v18, v82
	v_mul_f32_e32 v19, v19, v83
	v_mul_f32_e32 v28, v28, v2
	v_mul_f32_e32 v29, v29, v3
	v_mul_f32_e32 v24, v24, v6
	v_mul_f32_e32 v25, v25, v7
	v_mul_f32_e32 v20, v20, v10
	v_mul_f32_e32 v21, v21, v11
	v_mul_f32_e32 v16, v16, v80
	v_mul_f32_e32 v17, v17, v81

.LBB0_1111:
	s_waitcnt lgkmcnt(0)
	ds_read_b128 v[2:5], v203 offset:49248
	ds_read_b128 v[6:9], v203 offset:49216
	ds_read_b128 v[10:13], v203 offset:49184
	ds_read_b128 v[80:83], v203 offset:49152
	s_waitcnt lgkmcnt(3)
	v_mul_f32_e32 v46, v46, v4
	v_mul_f32_e32 v47, v47, v5
	s_waitcnt lgkmcnt(2)
	v_mul_f32_e32 v42, v42, v8
	v_mul_f32_e32 v43, v43, v9
	s_waitcnt lgkmcnt(1)
	v_mul_f32_e32 v38, v38, v12
	v_mul_f32_e32 v39, v39, v13
	s_waitcnt lgkmcnt(0)
	v_mul_f32_e32 v34, v34, v82
	v_mul_f32_e32 v35, v35, v83
	v_mul_f32_e32 v44, v44, v2
	v_mul_f32_e32 v45, v45, v3
	v_mul_f32_e32 v40, v40, v6
	v_mul_f32_e32 v41, v41, v7
	v_mul_f32_e32 v36, v36, v10
	v_mul_f32_e32 v37, v37, v11
	v_mul_f32_e32 v32, v32, v80
	v_mul_f32_e32 v33, v33, v81
	v_mul_f32_e32 v30, v30, v4
	v_mul_f32_e32 v31, v31, v5
	v_mul_f32_e32 v26, v26, v8
	v_mul_f32_e32 v27, v27, v9
	v_mul_f32_e32 v22, v22, v12
	v_mul_f32_e32 v23, v23, v13
	v_mul_f32_e32 v18, v18, v82
	v_mul_f32_e32 v19, v19, v83
	v_mul_f32_e32 v28, v28, v2
	v_mul_f32_e32 v29, v29, v3
	v_mul_f32_e32 v24, v24, v6
	v_mul_f32_e32 v25, v25, v7
	v_mul_f32_e32 v20, v20, v10
	v_mul_f32_e32 v21, v21, v11
	v_mul_f32_e32 v16, v16, v80
	v_mul_f32_e32 v17, v17, v81

.LBB0_1156:
	s_waitcnt lgkmcnt(14)
	v_mfma_f32_32x32x16_bf16 v[32:47], v[140:143], v[176:179], v[32:47]
	v_exp_f32_e32 v64, v48
	v_exp_f32_e32 v65, v49
	v_exp_f32_e32 v66, v66
	v_exp_f32_e32 v67, v67
	s_waitcnt lgkmcnt(12)
	v_mfma_f32_32x32x16_bf16 v[16:31], v[140:143], v[10:13], v[16:31]
	v_exp_f32_e32 v68, v68
	v_exp_f32_e32 v69, v69
	v_exp_f32_e32 v70, v70
	v_exp_f32_e32 v71, v71
	s_waitcnt lgkmcnt(10)
	v_mfma_f32_32x32x16_bf16 v[32:47], v[136:139], v[6:9], v[32:47]
	v_exp_f32_e32 v72, v72
	v_exp_f32_e32 v73, v73
	v_exp_f32_e32 v74, v74
	v_exp_f32_e32 v75, v75
	s_waitcnt lgkmcnt(8)
	v_mfma_f32_32x32x16_bf16 v[16:31], v[136:139], v[124:127], v[16:31]
	v_exp_f32_e32 v76, v76
	v_exp_f32_e32 v77, v77
	v_exp_f32_e32 v78, v78
	v_exp_f32_e32 v79, v79
	s_waitcnt lgkmcnt(6)
	v_mfma_f32_32x32x16_bf16 v[32:47], v[132:135], v[160:163], v[32:47]
	v_exp_f32_e32 v48, v14
	v_exp_f32_e32 v49, v15
	v_exp_f32_e32 v50, v50
	v_exp_f32_e32 v51, v51
	s_waitcnt lgkmcnt(4)
	v_mfma_f32_32x32x16_bf16 v[16:31], v[132:135], v[2:5], v[16:31]
	v_exp_f32_e32 v52, v52
	v_exp_f32_e32 v53, v53
	v_exp_f32_e32 v54, v54
	v_exp_f32_e32 v55, v55
	s_waitcnt lgkmcnt(2)
	v_mfma_f32_32x32x16_bf16 v[32:47], v[128:131], v[116:119], v[32:47]
	v_exp_f32_e32 v56, v56
	v_exp_f32_e32 v57, v57
	v_exp_f32_e32 v58, v58
	v_exp_f32_e32 v59, v59
	s_waitcnt lgkmcnt(0)
	v_mfma_f32_32x32x16_bf16 v[16:31], v[128:131], v[120:123], v[16:31]
	v_exp_f32_e32 v60, v60
	v_exp_f32_e32 v61, v61
	v_exp_f32_e32 v62, v62
	v_exp_f32_e32 v63, v63
	s_andn2_b64 vcc, exec, s[40:41]
	s_cbranch_vccnz .LBB0_1158
	s_waitcnt lgkmcnt(0)
	ds_read_b128 v[2:5], v203 offset:49248
	ds_read_b128 v[6:9], v203 offset:49216
	ds_read_b128 v[10:13], v203 offset:49184
	ds_read_b128 v[80:83], v203 offset:49152
	s_waitcnt lgkmcnt(3)
	v_mul_f32_e32 v46, v46, v4
	v_mul_f32_e32 v47, v47, v5
	s_waitcnt lgkmcnt(2)
	v_mul_f32_e32 v42, v42, v8
	v_mul_f32_e32 v43, v43, v9
	s_waitcnt lgkmcnt(1)
	v_mul_f32_e32 v38, v38, v12
	v_mul_f32_e32 v39, v39, v13
	s_waitcnt lgkmcnt(0)
	v_mul_f32_e32 v34, v34, v82
	v_mul_f32_e32 v35, v35, v83
	v_mul_f32_e32 v44, v44, v2
	v_mul_f32_e32 v45, v45, v3
	v_mul_f32_e32 v40, v40, v6
	v_mul_f32_e32 v41, v41, v7
	v_mul_f32_e32 v36, v36, v10
	v_mul_f32_e32 v37, v37, v11
	v_mul_f32_e32 v32, v32, v80
	v_mul_f32_e32 v33, v33, v81
	v_mul_f32_e32 v30, v30, v4
	v_mul_f32_e32 v31, v31, v5
	v_mul_f32_e32 v26, v26, v8
	v_mul_f32_e32 v27, v27, v9
	v_mul_f32_e32 v22, v22, v12
	v_mul_f32_e32 v23, v23, v13
	v_mul_f32_e32 v18, v18, v82
	v_mul_f32_e32 v19, v19, v83
	v_mul_f32_e32 v28, v28, v2
	v_mul_f32_e32 v29, v29, v3
	v_mul_f32_e32 v24, v24, v6
	v_mul_f32_e32 v25, v25, v7
	v_mul_f32_e32 v20, v20, v10
	v_mul_f32_e32 v21, v21, v11
	v_mul_f32_e32 v16, v16, v80
	v_mul_f32_e32 v17, v17, v81

.LBB0_1175:
	s_or_b64 exec, exec, s[16:17]
	v_lshlrev_b64 v[28:29], 9, v[98:99]
	v_lshl_add_u64 v[102:103], v[28:29], 1, v[96:97]
	global_load_dwordx4 v[82:85], v[26:27], off
	global_load_dwordx4 v[110:113], v[102:103], off
	global_load_dwordx4 v[74:77], v[26:27], off offset:1024
	global_load_dwordx4 v[78:81], v[102:103], off offset:1024
	global_load_dwordx4 v[66:69], v[26:27], off offset:2048
	global_load_dwordx4 v[70:73], v[102:103], off offset:2048
	global_load_dwordx4 v[58:61], v[26:27], off offset:3072
	global_load_dwordx4 v[62:65], v[102:103], off offset:3072
	s_movk_i32 s16, 0x1000
	v_add_co_u32_e32 v26, vcc, s16, v26
	s_waitcnt vmcnt(8)
	v_lshlrev_b32_e32 v114, 16, v90
	v_addc_co_u32_e32 v27, vcc, 0, v27, vcc
	global_load_dwordx4 v[50:53], v[26:27], off
	v_add_co_u32_e32 v100, vcc, s16, v102
	v_and_b32_e32 v115, 0xffff0000, v90
	s_nop 0
	v_addc_co_u32_e32 v101, vcc, 0, v103, vcc
	global_load_dwordx4 v[54:57], v[100:101], off
	global_load_dwordx4 v[42:45], v[26:27], off offset:1024
	global_load_dwordx4 v[46:49], v[100:101], off offset:1024
	global_load_dwordx4 v[34:37], v[26:27], off offset:2048
	global_load_dwordx4 v[38:41], v[100:101], off offset:2048
	s_nop 0
	global_load_dwordx4 v[26:29], v[26:27], off offset:3072
	s_nop 0
	global_load_dwordx4 v[30:33], v[100:101], off offset:3072
	v_lshlrev_b32_e32 v104, 16, v86
	v_and_b32_e32 v105, 0xffff0000, v86
	v_mul_f32_e32 v116, v10, v114
	v_mul_f32_e32 v117, v11, v115
	v_lshlrev_b32_e32 v90, 16, v91
	v_fma_f32 v116, v18, v104, v116
	v_fma_f32 v117, v19, v105, v117
	v_and_b32_e32 v91, 0xffff0000, v91
	v_lshlrev_b32_e32 v86, 16, v87
	v_and_b32_e32 v87, 0xffff0000, v87
	v_readlane_b32 s16, v253, 8
	v_add_u32_e32 v108, s72, v108
	s_waitcnt vmcnt(15)
	v_lshlrev_b32_e32 v104, 16, v82
	v_and_b32_e32 v105, 0xffff0000, v82
	s_waitcnt vmcnt(14)
	v_lshlrev_b32_e32 v106, 16, v110
	v_and_b32_e32 v107, 0xffff0000, v110
	v_fma_f32 v116, v2, v104, v116
	v_fma_f32 v117, v3, v105, v117
	v_lshlrev_b32_e32 v82, 16, v83
	v_mul_f32_e32 v116, v116, v106
	v_mul_f32_e32 v117, v117, v107
	v_lshlrev_b32_e32 v106, 16, v111
	v_and_b32_e32 v107, 0xffff0000, v111
	v_mul_f32_e32 v110, v12, v90
	v_mul_f32_e32 v111, v13, v91
	v_and_b32_e32 v83, 0xffff0000, v83
	v_fma_f32 v86, v20, v86, v110
	v_fma_f32 v87, v21, v87, v111
	v_lshlrev_b32_e32 v110, 16, v112
	v_fma_f32 v86, v4, v82, v86
	v_fma_f32 v87, v5, v83, v87
	v_and_b32_e32 v111, 0xffff0000, v112
	v_mul_f32_e32 v118, v86, v106
	v_mul_f32_e32 v119, v87, v107
	v_lshlrev_b32_e32 v106, 16, v92
	v_and_b32_e32 v107, 0xffff0000, v92
	v_lshlrev_b32_e32 v86, 16, v88
	v_and_b32_e32 v87, 0xffff0000, v88
	v_mul_f32_e32 v120, v14, v106
	v_mul_f32_e32 v121, v15, v107
	v_lshlrev_b32_e32 v92, 16, v93
	v_fma_f32 v120, v22, v86, v120
	v_fma_f32 v121, v23, v87, v121
	v_lshlrev_b32_e32 v86, 16, v84
	v_and_b32_e32 v87, 0xffff0000, v84
	v_fma_f32 v120, v6, v86, v120
	v_fma_f32 v121, v7, v87, v121
	v_and_b32_e32 v93, 0xffff0000, v93
	v_mul_f32_e32 v120, v120, v110
	v_mul_f32_e32 v121, v121, v111
	v_lshlrev_b32_e32 v110, 16, v113
	v_and_b32_e32 v111, 0xffff0000, v113
	v_lshlrev_b32_e32 v88, 16, v89
	v_and_b32_e32 v89, 0xffff0000, v89
	v_mul_f32_e32 v112, v16, v92
	v_mul_f32_e32 v113, v17, v93
	v_lshlrev_b32_e32 v84, 16, v85
	v_fma_f32 v88, v24, v88, v112
	v_fma_f32 v89, v25, v89, v113
	v_and_b32_e32 v85, 0xffff0000, v85
	v_fma_f32 v88, v8, v84, v88
	v_fma_f32 v89, v9, v85, v89
	v_cvt_pk_bf16_f32 v112, v120, v121
	v_mul_f32_e32 v88, v88, v110
	v_mul_f32_e32 v89, v89, v111
	v_cvt_pk_bf16_f32 v110, v116, v117
	v_cvt_pk_bf16_f32 v111, v118, v119
	v_cvt_pk_bf16_f32 v113, v88, v89
	global_store_dwordx4 v[102:103], v[110:113], off
	s_waitcnt vmcnt(13)
	v_lshlrev_b32_e32 v88, 16, v78
	v_and_b32_e32 v89, 0xffff0000, v78
	v_mul_f32_e32 v110, v10, v104
	v_mul_f32_e32 v111, v11, v105
	v_lshlrev_b32_e32 v112, 16, v74
	v_fma_f32 v110, v18, v114, v110
	v_fma_f32 v111, v19, v115, v111
	v_and_b32_e32 v113, 0xffff0000, v74
	v_fma_f32 v110, v2, v112, v110
	v_fma_f32 v111, v3, v113, v111
	v_lshlrev_b32_e32 v78, 16, v79
	v_mul_f32_e32 v88, v110, v88
	v_mul_f32_e32 v89, v111, v89
	v_mul_f32_e32 v110, v12, v82
	v_mul_f32_e32 v111, v13, v83
	v_and_b32_e32 v79, 0xffff0000, v79
	v_fma_f32 v90, v20, v90, v110
	v_fma_f32 v91, v21, v91, v111
	v_lshlrev_b32_e32 v110, 16, v75
	v_and_b32_e32 v111, 0xffff0000, v75
	v_fma_f32 v74, v4, v110, v90
	v_fma_f32 v75, v5, v111, v91
	v_mul_f32_e32 v90, v14, v86
	v_mul_f32_e32 v91, v15, v87
	v_mul_f32_e32 v78, v74, v78
	v_mul_f32_e32 v79, v75, v79
	v_fma_f32 v90, v22, v106, v90
	v_fma_f32 v91, v23, v107, v91
	v_lshlrev_b32_e32 v106, 16, v76
	v_and_b32_e32 v107, 0xffff0000, v76
	v_lshlrev_b32_e32 v74, 16, v80
	v_and_b32_e32 v75, 0xffff0000, v80
	v_fma_f32 v90, v6, v106, v90
	v_fma_f32 v91, v7, v107, v91
	v_add_u32_e32 v98, s16, v98
	v_mul_f32_e32 v90, v90, v74
	v_mul_f32_e32 v91, v91, v75
	v_lshlrev_b32_e32 v74, 16, v81
	v_and_b32_e32 v75, 0xffff0000, v81
	v_mul_f32_e32 v80, v16, v84
	v_mul_f32_e32 v81, v17, v85
	s_movk_i32 s16, 0x7ff
	v_fma_f32 v80, v24, v92, v80
	v_fma_f32 v81, v25, v93, v81
	v_lshlrev_b32_e32 v92, 16, v77
	v_and_b32_e32 v93, 0xffff0000, v77
	v_fma_f32 v76, v8, v92, v80
	v_fma_f32 v77, v9, v93, v81
	v_cmp_lt_i32_e32 vcc, s16, v108
	v_mul_f32_e32 v80, v76, v74
	v_mul_f32_e32 v81, v77, v75
	v_cvt_pk_bf16_f32 v74, v88, v89
	v_cvt_pk_bf16_f32 v75, v78, v79
	v_cvt_pk_bf16_f32 v76, v90, v91
	v_cvt_pk_bf16_f32 v77, v80, v81
	global_store_dwordx4 v[102:103], v[74:77], off offset:1024
	s_waitcnt vmcnt(13)
	v_lshlrev_b32_e32 v78, 16, v66
	v_and_b32_e32 v79, 0xffff0000, v66
	v_mul_f32_e32 v76, v10, v112
	v_mul_f32_e32 v77, v11, v113
	s_waitcnt vmcnt(12)
	v_lshlrev_b32_e32 v74, 16, v70
	v_fma_f32 v76, v18, v104, v76
	v_fma_f32 v77, v19, v105, v77
	v_and_b32_e32 v75, 0xffff0000, v70
	v_fma_f32 v76, v2, v78, v76
	v_fma_f32 v77, v3, v79, v77
	v_lshlrev_b32_e32 v80, 16, v67
	v_mul_f32_e32 v74, v76, v74
	v_mul_f32_e32 v75, v77, v75
	v_mul_f32_e32 v76, v12, v110
	v_mul_f32_e32 v77, v13, v111
	v_and_b32_e32 v81, 0xffff0000, v67
	v_fma_f32 v76, v20, v82, v76
	v_fma_f32 v77, v21, v83, v77
	v_lshlrev_b32_e32 v70, 16, v71
	v_fma_f32 v66, v4, v80, v76
	v_fma_f32 v67, v5, v81, v77
	v_mul_f32_e32 v76, v14, v106
	v_mul_f32_e32 v77, v15, v107
	v_and_b32_e32 v71, 0xffff0000, v71
	v_fma_f32 v76, v22, v86, v76
	v_fma_f32 v77, v23, v87, v77
	v_lshlrev_b32_e32 v82, 16, v68
	v_and_b32_e32 v83, 0xffff0000, v68
	v_mul_f32_e32 v70, v66, v70
	v_mul_f32_e32 v71, v67, v71
	v_lshlrev_b32_e32 v66, 16, v72
	v_and_b32_e32 v67, 0xffff0000, v72
	v_fma_f32 v76, v6, v82, v76
	v_fma_f32 v77, v7, v83, v77
	s_or_b64 s[14:15], vcc, s[14:15]
	v_mul_f32_e32 v76, v76, v66
	v_mul_f32_e32 v77, v77, v67
	v_lshlrev_b32_e32 v66, 16, v73
	v_and_b32_e32 v67, 0xffff0000, v73
	v_mul_f32_e32 v72, v16, v92
	v_mul_f32_e32 v73, v17, v93
	s_nop 0
	v_fma_f32 v72, v24, v84, v72
	v_fma_f32 v73, v25, v85, v73
	v_lshlrev_b32_e32 v84, 16, v69
	v_and_b32_e32 v85, 0xffff0000, v69
	v_fma_f32 v68, v8, v84, v72
	v_fma_f32 v69, v9, v85, v73
	s_nop 0
	v_mul_f32_e32 v72, v68, v66
	v_mul_f32_e32 v73, v69, v67
	v_cvt_pk_bf16_f32 v66, v74, v75
	v_cvt_pk_bf16_f32 v67, v70, v71
	v_cvt_pk_bf16_f32 v68, v76, v77
	v_cvt_pk_bf16_f32 v69, v72, v73
	global_store_dwordx4 v[102:103], v[66:69], off offset:2048
	s_waitcnt vmcnt(12)
	v_lshlrev_b32_e32 v70, 16, v58
	v_and_b32_e32 v71, 0xffff0000, v58
	v_mul_f32_e32 v68, v10, v78
	v_mul_f32_e32 v69, v11, v79
	s_waitcnt vmcnt(11)
	v_lshlrev_b32_e32 v66, 16, v62
	v_fma_f32 v68, v18, v112, v68
	v_fma_f32 v69, v19, v113, v69
	v_and_b32_e32 v67, 0xffff0000, v62
	v_fma_f32 v68, v2, v70, v68
	v_fma_f32 v69, v3, v71, v69
	v_lshlrev_b32_e32 v72, 16, v59
	v_mul_f32_e32 v66, v68, v66
	v_mul_f32_e32 v67, v69, v67
	v_mul_f32_e32 v68, v12, v80
	v_mul_f32_e32 v69, v13, v81
	v_and_b32_e32 v73, 0xffff0000, v59
	v_fma_f32 v68, v20, v110, v68
	v_fma_f32 v69, v21, v111, v69
	v_lshlrev_b32_e32 v62, 16, v63
	v_fma_f32 v58, v4, v72, v68
	v_fma_f32 v59, v5, v73, v69
	v_mul_f32_e32 v68, v14, v82
	v_mul_f32_e32 v69, v15, v83
	v_and_b32_e32 v63, 0xffff0000, v63
	v_fma_f32 v68, v22, v106, v68
	v_fma_f32 v69, v23, v107, v69
	v_lshlrev_b32_e32 v74, 16, v60
	v_and_b32_e32 v75, 0xffff0000, v60
	v_mul_f32_e32 v62, v58, v62
	v_mul_f32_e32 v63, v59, v63
	v_lshlrev_b32_e32 v58, 16, v64
	v_and_b32_e32 v59, 0xffff0000, v64
	v_fma_f32 v68, v6, v74, v68
	v_fma_f32 v69, v7, v75, v69
	v_lshlrev_b32_e32 v76, 16, v61
	v_mul_f32_e32 v68, v68, v58
	v_mul_f32_e32 v69, v69, v59
	v_lshlrev_b32_e32 v58, 16, v65
	v_and_b32_e32 v59, 0xffff0000, v65
	v_mul_f32_e32 v64, v16, v84
	v_mul_f32_e32 v65, v17, v85
	v_and_b32_e32 v77, 0xffff0000, v61
	v_fma_f32 v64, v24, v92, v64
	v_fma_f32 v65, v25, v93, v65
	s_nop 0
	v_fma_f32 v60, v8, v76, v64
	v_fma_f32 v61, v9, v77, v65
	s_nop 0
	v_mul_f32_e32 v64, v60, v58
	v_mul_f32_e32 v65, v61, v59
	v_cvt_pk_bf16_f32 v58, v66, v67
	v_cvt_pk_bf16_f32 v59, v62, v63
	v_cvt_pk_bf16_f32 v60, v68, v69
	v_cvt_pk_bf16_f32 v61, v64, v65
	global_store_dwordx4 v[102:103], v[58:61], off offset:3072
	s_waitcnt vmcnt(11)
	v_lshlrev_b32_e32 v62, 16, v50
	v_and_b32_e32 v63, 0xffff0000, v50
	v_mul_f32_e32 v60, v10, v70
	v_mul_f32_e32 v61, v11, v71
	s_waitcnt vmcnt(10)
	v_lshlrev_b32_e32 v58, 16, v54
	v_fma_f32 v60, v18, v78, v60
	v_fma_f32 v61, v19, v79, v61
	v_and_b32_e32 v59, 0xffff0000, v54
	v_fma_f32 v60, v2, v62, v60
	v_fma_f32 v61, v3, v63, v61
	v_lshlrev_b32_e32 v64, 16, v51
	v_mul_f32_e32 v58, v60, v58
	v_mul_f32_e32 v59, v61, v59
	v_mul_f32_e32 v60, v12, v72
	v_mul_f32_e32 v61, v13, v73
	v_and_b32_e32 v65, 0xffff0000, v51
	v_fma_f32 v60, v20, v80, v60
	v_fma_f32 v61, v21, v81, v61
	v_lshlrev_b32_e32 v54, 16, v55
	v_fma_f32 v50, v4, v64, v60
	v_fma_f32 v51, v5, v65, v61
	v_mul_f32_e32 v60, v14, v74
	v_mul_f32_e32 v61, v15, v75
	v_and_b32_e32 v55, 0xffff0000, v55
	v_fma_f32 v60, v22, v82, v60
	v_fma_f32 v61, v23, v83, v61
	v_lshlrev_b32_e32 v66, 16, v52
	v_and_b32_e32 v67, 0xffff0000, v52
	v_mul_f32_e32 v54, v50, v54
	v_mul_f32_e32 v55, v51, v55
	v_lshlrev_b32_e32 v50, 16, v56
	v_and_b32_e32 v51, 0xffff0000, v56
	v_fma_f32 v60, v6, v66, v60
	v_fma_f32 v61, v7, v67, v61
	v_lshlrev_b32_e32 v68, 16, v53
	v_mul_f32_e32 v60, v60, v50
	v_mul_f32_e32 v61, v61, v51
	v_lshlrev_b32_e32 v50, 16, v57
	v_and_b32_e32 v51, 0xffff0000, v57
	v_mul_f32_e32 v56, v16, v76
	v_mul_f32_e32 v57, v17, v77
	v_and_b32_e32 v69, 0xffff0000, v53
	v_fma_f32 v56, v24, v84, v56
	v_fma_f32 v57, v25, v85, v57
	s_nop 0
	v_fma_f32 v52, v8, v68, v56
	v_fma_f32 v53, v9, v69, v57
	s_nop 0
	v_mul_f32_e32 v56, v52, v50
	v_mul_f32_e32 v57, v53, v51
	v_cvt_pk_bf16_f32 v50, v58, v59
	v_cvt_pk_bf16_f32 v51, v54, v55
	v_cvt_pk_bf16_f32 v52, v60, v61
	v_cvt_pk_bf16_f32 v53, v56, v57
	global_store_dwordx4 v[100:101], v[50:53], off
	s_waitcnt vmcnt(10)
	v_lshlrev_b32_e32 v54, 16, v42
	v_and_b32_e32 v55, 0xffff0000, v42
	v_mul_f32_e32 v52, v10, v62
	v_mul_f32_e32 v53, v11, v63
	s_waitcnt vmcnt(9)
	v_lshlrev_b32_e32 v50, 16, v46
	v_fma_f32 v52, v18, v70, v52
	v_fma_f32 v53, v19, v71, v53
	v_and_b32_e32 v51, 0xffff0000, v46
	v_fma_f32 v52, v2, v54, v52
	v_fma_f32 v53, v3, v55, v53
	v_lshlrev_b32_e32 v56, 16, v43
	v_mul_f32_e32 v50, v52, v50
	v_mul_f32_e32 v51, v53, v51
	v_mul_f32_e32 v52, v12, v64
	v_mul_f32_e32 v53, v13, v65
	v_and_b32_e32 v57, 0xffff0000, v43
	v_fma_f32 v52, v20, v72, v52
	v_fma_f32 v53, v21, v73, v53
	v_lshlrev_b32_e32 v46, 16, v47
	v_fma_f32 v42, v4, v56, v52
	v_fma_f32 v43, v5, v57, v53
	v_mul_f32_e32 v52, v14, v66
	v_mul_f32_e32 v53, v15, v67
	v_and_b32_e32 v47, 0xffff0000, v47
	v_fma_f32 v52, v22, v74, v52
	v_fma_f32 v53, v23, v75, v53
	v_lshlrev_b32_e32 v58, 16, v44
	v_and_b32_e32 v59, 0xffff0000, v44
	v_mul_f32_e32 v46, v42, v46
	v_mul_f32_e32 v47, v43, v47
	v_lshlrev_b32_e32 v42, 16, v48
	v_and_b32_e32 v43, 0xffff0000, v48
	v_fma_f32 v52, v6, v58, v52
	v_fma_f32 v53, v7, v59, v53
	v_lshlrev_b32_e32 v60, 16, v45
	v_mul_f32_e32 v52, v52, v42
	v_mul_f32_e32 v53, v53, v43
	v_lshlrev_b32_e32 v42, 16, v49
	v_and_b32_e32 v43, 0xffff0000, v49
	v_mul_f32_e32 v48, v16, v68
	v_mul_f32_e32 v49, v17, v69
	v_and_b32_e32 v61, 0xffff0000, v45
	v_fma_f32 v48, v24, v76, v48
	v_fma_f32 v49, v25, v77, v49
	s_nop 0
	v_fma_f32 v44, v8, v60, v48
	v_fma_f32 v45, v9, v61, v49
	s_nop 0
	v_mul_f32_e32 v48, v44, v42
	v_mul_f32_e32 v49, v45, v43
	v_cvt_pk_bf16_f32 v42, v50, v51
	v_cvt_pk_bf16_f32 v43, v46, v47
	v_cvt_pk_bf16_f32 v44, v52, v53
	v_cvt_pk_bf16_f32 v45, v48, v49
	global_store_dwordx4 v[100:101], v[42:45], off offset:1024
	s_waitcnt vmcnt(9)
	v_lshlrev_b32_e32 v46, 16, v34
	v_and_b32_e32 v47, 0xffff0000, v34
	v_mul_f32_e32 v44, v10, v54
	v_mul_f32_e32 v45, v11, v55
	s_waitcnt vmcnt(8)
	v_lshlrev_b32_e32 v42, 16, v38
	v_fma_f32 v44, v18, v62, v44
	v_fma_f32 v45, v19, v63, v45
	v_and_b32_e32 v43, 0xffff0000, v38
	v_fma_f32 v44, v2, v46, v44
	v_fma_f32 v45, v3, v47, v45
	v_lshlrev_b32_e32 v48, 16, v35
	v_mul_f32_e32 v42, v44, v42
	v_mul_f32_e32 v43, v45, v43
	v_mul_f32_e32 v44, v12, v56
	v_mul_f32_e32 v45, v13, v57
	v_and_b32_e32 v49, 0xffff0000, v35
	v_fma_f32 v44, v20, v64, v44
	v_fma_f32 v45, v21, v65, v45
	v_lshlrev_b32_e32 v38, 16, v39
	v_fma_f32 v34, v4, v48, v44
	v_fma_f32 v35, v5, v49, v45
	v_mul_f32_e32 v44, v14, v58
	v_mul_f32_e32 v45, v15, v59
	v_and_b32_e32 v39, 0xffff0000, v39
	v_fma_f32 v44, v22, v66, v44
	v_fma_f32 v45, v23, v67, v45
	v_lshlrev_b32_e32 v50, 16, v36
	v_and_b32_e32 v51, 0xffff0000, v36
	v_mul_f32_e32 v38, v34, v38
	v_mul_f32_e32 v39, v35, v39
	v_lshlrev_b32_e32 v34, 16, v40
	v_and_b32_e32 v35, 0xffff0000, v40
	v_fma_f32 v44, v6, v50, v44
	v_fma_f32 v45, v7, v51, v45
	v_lshlrev_b32_e32 v52, 16, v37
	v_mul_f32_e32 v44, v44, v34
	v_mul_f32_e32 v45, v45, v35
	v_lshlrev_b32_e32 v34, 16, v41
	v_and_b32_e32 v35, 0xffff0000, v41
	v_mul_f32_e32 v40, v16, v60
	v_mul_f32_e32 v41, v17, v61
	v_and_b32_e32 v53, 0xffff0000, v37
	v_fma_f32 v40, v24, v68, v40
	v_fma_f32 v41, v25, v69, v41
	s_nop 0
	v_fma_f32 v36, v8, v52, v40
	v_fma_f32 v37, v9, v53, v41
	s_nop 0
	v_mul_f32_e32 v40, v36, v34
	v_mul_f32_e32 v41, v37, v35
	v_cvt_pk_bf16_f32 v34, v42, v43
	v_cvt_pk_bf16_f32 v35, v38, v39
	v_cvt_pk_bf16_f32 v36, v44, v45
	v_cvt_pk_bf16_f32 v37, v40, v41
	global_store_dwordx4 v[100:101], v[34:37], off offset:2048
	s_waitcnt vmcnt(8)
	v_lshlrev_b32_e32 v38, 16, v26
	v_and_b32_e32 v39, 0xffff0000, v26
	v_mul_f32_e32 v36, v10, v46
	v_mul_f32_e32 v37, v11, v47
	s_waitcnt vmcnt(7)
	v_lshlrev_b32_e32 v34, 16, v30
	v_fma_f32 v36, v18, v54, v36
	v_fma_f32 v37, v19, v55, v37
	v_and_b32_e32 v35, 0xffff0000, v30
	v_fma_f32 v36, v2, v38, v36
	v_fma_f32 v37, v3, v39, v37
	v_lshlrev_b32_e32 v26, 16, v27
	v_mul_f32_e32 v34, v36, v34
	v_mul_f32_e32 v35, v37, v35
	v_mul_f32_e32 v36, v12, v48
	v_mul_f32_e32 v37, v13, v49
	v_and_b32_e32 v27, 0xffff0000, v27
	v_fma_f32 v36, v20, v56, v36
	v_fma_f32 v37, v21, v57, v37
	v_lshlrev_b32_e32 v30, 16, v31
	v_fma_f32 v26, v4, v26, v36
	v_fma_f32 v27, v5, v27, v37
	v_mul_f32_e32 v36, v14, v50
	v_mul_f32_e32 v37, v15, v51
	v_and_b32_e32 v31, 0xffff0000, v31
	v_fma_f32 v36, v22, v58, v36
	v_fma_f32 v37, v23, v59, v37
	v_lshlrev_b32_e32 v38, 16, v28
	v_and_b32_e32 v39, 0xffff0000, v28
	v_mul_f32_e32 v30, v26, v30
	v_mul_f32_e32 v31, v27, v31
	v_lshlrev_b32_e32 v26, 16, v32
	v_and_b32_e32 v27, 0xffff0000, v32
	v_fma_f32 v36, v6, v38, v36
	v_fma_f32 v37, v7, v39, v37
	v_lshlrev_b32_e32 v28, 16, v29
	v_mul_f32_e32 v36, v36, v26
	v_mul_f32_e32 v37, v37, v27
	v_lshlrev_b32_e32 v26, 16, v33
	v_and_b32_e32 v27, 0xffff0000, v33
	v_mul_f32_e32 v32, v16, v52
	v_mul_f32_e32 v33, v17, v53
	v_and_b32_e32 v29, 0xffff0000, v29
	v_fma_f32 v32, v24, v60, v32
	v_fma_f32 v33, v25, v61, v33
	s_nop 0
	v_fma_f32 v28, v8, v28, v32
	v_fma_f32 v29, v9, v29, v33
	s_nop 0
	v_mul_f32_e32 v32, v28, v26
	v_mul_f32_e32 v33, v29, v27
	v_cvt_pk_bf16_f32 v26, v34, v35
	v_cvt_pk_bf16_f32 v27, v30, v31
	v_cvt_pk_bf16_f32 v28, v36, v37
	v_cvt_pk_bf16_f32 v29, v32, v33
	global_store_dwordx4 v[100:101], v[26:29], off offset:3072
	s_andn2_b64 exec, exec, s[14:15]
	s_cbranch_execz .LBB0_1178

.LBB0_1198:
	s_ashr_i32 s42, s47, 2
	s_mov_b32 s17, -1
	s_ashr_i32 s43, s42, 31
	s_lshl_b64 s[42:43], s[42:43], 21
	v_mbcnt_lo_u32_b32 v0, s17, 0
	v_mbcnt_hi_u32_b32 v138, s17, v0
	s_add_u32 s17, s93, s42
	s_addc_u32 s29, s94, s43
	s_lshl_b32 s42, s47, 19
	s_and_b32 s42, s42, 0x180000
	s_add_u32 s17, s17, s42
	s_addc_u32 s29, s29, 0
	s_ashr_i32 s47, s46, 31
	s_lshl_b64 s[42:43], s[46:47], 9
	s_add_u32 s17, s17, s42
	s_addc_u32 s29, s29, s43
	s_add_u32 s42, s17, s35
	s_addc_u32 s43, s29, 0
	v_and_b32_e32 v0, 0x70, v138
	v_lshl_add_u64 v[142:143], s[42:43], 0, v[0:1]
	v_and_or_b32 v0, v138, 15, s84
	v_lshl_add_u32 v144, s1, 8, v0
	v_ashrrev_i32_e32 v145, 31, v144
	v_lshlrev_b64 v[138:139], 11, v[144:145]
	v_mul_f32_e32 v128, s26, v128
	v_mul_f32_e32 v129, s26, v129
	v_mul_f32_e32 v126, s26, v126
	v_mul_f32_e32 v127, s26, v127
	v_mul_f32_e32 v146, s26, v124
	v_mul_f32_e32 v147, s26, v125
	v_mul_f32_e32 v124, s26, v122
	v_mul_f32_e32 v125, s26, v123
	v_lshl_add_u64 v[138:139], v[142:143], 0, v[138:139]
	v_cvt_pk_bf16_f32 v122, v126, v127
	v_cvt_pk_bf16_f32 v123, v128, v129
	v_cvt_pk_bf16_f32 v124, v124, v125
	v_cvt_pk_bf16_f32 v125, v146, v147
	global_store_dwordx4 v[138:139], v[122:125], off
	v_mul_f32_e32 v116, s26, v116
	v_mul_f32_e32 v117, s26, v117
	v_mul_f32_e32 v114, s26, v114
	v_mul_f32_e32 v115, s26, v115
	v_mul_f32_e32 v122, s26, v108
	v_mul_f32_e32 v123, s26, v109
	v_mul_f32_e32 v108, s26, v106
	v_mul_f32_e32 v109, s26, v107
	v_cvt_pk_bf16_f32 v106, v114, v115
	v_cvt_pk_bf16_f32 v107, v116, v117
	v_cvt_pk_bf16_f32 v108, v108, v109
	v_cvt_pk_bf16_f32 v109, v122, v123
	global_store_dwordx4 v[138:139], v[106:109], off offset:256
	v_mul_f32_e32 v112, s26, v112
	v_mul_f32_e32 v113, s26, v113
	v_mul_f32_e32 v110, s26, v110
	v_mul_f32_e32 v111, s26, v111
	v_or_b32_e32 v106, 16, v144
	v_ashrrev_i32_e32 v107, 31, v106
	v_lshlrev_b64 v[106:107], 11, v[106:107]
	v_lshl_add_u64 v[114:115], v[142:143], 0, v[106:107]
	v_mul_f32_e32 v108, s26, v120
	v_mul_f32_e32 v109, s26, v121
	v_mul_f32_e32 v106, s26, v118
	v_mul_f32_e32 v107, s26, v119
	v_mul_f32_e32 v100, s26, v100
	v_mul_f32_e32 v101, s26, v101
	v_cvt_pk_bf16_f32 v106, v106, v107
	v_cvt_pk_bf16_f32 v107, v108, v109
	v_cvt_pk_bf16_f32 v108, v110, v111
	v_cvt_pk_bf16_f32 v109, v112, v113
	global_store_dwordx4 v[114:115], v[106:109], off
	v_mul_f32_e32 v98, s26, v98
	v_mul_f32_e32 v99, s26, v99
	v_mul_f32_e32 v96, s26, v96
	v_mul_f32_e32 v97, s26, v97
	v_mul_f32_e32 v106, s26, v92
	v_mul_f32_e32 v107, s26, v93
	v_mul_f32_e32 v92, s26, v90
	v_mul_f32_e32 v93, s26, v91
	v_cvt_pk_bf16_f32 v90, v98, v99
	v_cvt_pk_bf16_f32 v91, v100, v101
	v_cvt_pk_bf16_f32 v92, v92, v93
	v_cvt_pk_bf16_f32 v93, v106, v107
	global_store_dwordx4 v[114:115], v[90:93], off offset:256
	v_mul_f32_e32 v94, s26, v94
	v_mul_f32_e32 v95, s26, v95
	v_mul_f32_e32 v84, s26, v84
	v_mul_f32_e32 v85, s26, v85
	v_or_b32_e32 v90, 32, v144
	v_ashrrev_i32_e32 v91, 31, v90
	v_lshlrev_b64 v[90:91], 11, v[90:91]
	v_lshl_add_u64 v[98:99], v[142:143], 0, v[90:91]
	v_mul_f32_e32 v92, s26, v104
	v_mul_f32_e32 v93, s26, v105
	v_mul_f32_e32 v90, s26, v102
	v_mul_f32_e32 v91, s26, v103
	v_mul_f32_e32 v82, s26, v82
	v_mul_f32_e32 v83, s26, v83
	v_cvt_pk_bf16_f32 v90, v90, v91
	v_cvt_pk_bf16_f32 v91, v92, v93
	v_cvt_pk_bf16_f32 v92, v94, v95
	v_cvt_pk_bf16_f32 v93, v96, v97
	global_store_dwordx4 v[98:99], v[90:93], off
	v_mul_f32_e32 v80, s26, v80
	v_mul_f32_e32 v81, s26, v81
	v_mul_f32_e32 v78, s26, v78
	v_mul_f32_e32 v79, s26, v79
	v_mul_f32_e32 v90, s26, v76
	v_mul_f32_e32 v91, s26, v77
	v_mul_f32_e32 v76, s26, v74
	v_mul_f32_e32 v77, s26, v75
	v_cvt_pk_bf16_f32 v74, v82, v83
	v_cvt_pk_bf16_f32 v75, v84, v85
	v_cvt_pk_bf16_f32 v76, v76, v77
	v_cvt_pk_bf16_f32 v77, v90, v91
	global_store_dwordx4 v[98:99], v[74:77], off offset:256
	v_mul_f32_e32 v72, s26, v72
	v_mul_f32_e32 v73, s26, v73
	v_mul_f32_e32 v70, s26, v70
	v_mul_f32_e32 v71, s26, v71
	v_or_b32_e32 v74, 48, v144
	v_ashrrev_i32_e32 v75, 31, v74
	v_lshlrev_b64 v[74:75], 11, v[74:75]
	v_lshl_add_u64 v[82:83], v[142:143], 0, v[74:75]
	v_mul_f32_e32 v76, s26, v88
	v_mul_f32_e32 v77, s26, v89
	v_mul_f32_e32 v74, s26, v86
	v_mul_f32_e32 v75, s26, v87
	v_mul_f32_e32 v62, s26, v62
	v_mul_f32_e32 v63, s26, v63
	v_cvt_pk_bf16_f32 v74, v74, v75
	v_cvt_pk_bf16_f32 v75, v76, v77
	v_cvt_pk_bf16_f32 v76, v78, v79
	v_cvt_pk_bf16_f32 v77, v80, v81
	global_store_dwordx4 v[82:83], v[74:77], off
	s_mov_b32 s1, 0x40000
	v_mul_f32_e32 v64, s26, v64
	v_mul_f32_e32 v65, s26, v65
	v_mul_f32_e32 v74, s26, v68
	v_mul_f32_e32 v75, s26, v69
	v_mul_f32_e32 v68, s26, v66
	v_mul_f32_e32 v69, s26, v67
	v_cvt_pk_bf16_f32 v66, v70, v71
	v_cvt_pk_bf16_f32 v67, v72, v73
	v_cvt_pk_bf16_f32 v68, v68, v69
	v_cvt_pk_bf16_f32 v69, v74, v75
	global_store_dwordx4 v[82:83], v[66:69], off offset:256
	v_mul_f32_e32 v52, s26, v52
	v_mul_f32_e32 v53, s26, v53
	v_mul_f32_e32 v50, s26, v50
	v_mul_f32_e32 v51, s26, v51
	v_mul_f32_e32 v68, s26, v60
	v_mul_f32_e32 v69, s26, v61
	v_mul_f32_e32 v60, s26, v58
	v_mul_f32_e32 v61, s26, v59
	v_cvt_pk_bf16_f32 v58, v62, v63
	v_add_co_u32_e32 v62, vcc, s1, v138
	v_cvt_pk_bf16_f32 v59, v64, v65
	v_cvt_pk_bf16_f32 v60, v60, v61
	v_cvt_pk_bf16_f32 v61, v68, v69
	v_addc_co_u32_e32 v63, vcc, 0, v139, vcc
	global_store_dwordx4 v[62:63], v[58:61], off
	v_lshl_add_u64 v[66:67], v[138:139], 0, s[20:21]
	v_mul_f32_e32 v46, s26, v46
	v_mul_f32_e32 v47, s26, v47
	v_mul_f32_e32 v58, s26, v44
	v_mul_f32_e32 v59, s26, v45
	v_mul_f32_e32 v44, s26, v42
	v_mul_f32_e32 v45, s26, v43
	v_cvt_pk_bf16_f32 v42, v50, v51
	v_cvt_pk_bf16_f32 v43, v52, v53
	v_cvt_pk_bf16_f32 v44, v44, v45
	v_cvt_pk_bf16_f32 v45, v58, v59
	global_store_dwordx4 v[66:67], v[42:45], off offset:256
	s_mov_b32 s1, 0x48000
	v_mul_f32_e32 v48, s26, v48
	v_mul_f32_e32 v49, s26, v49
	v_mul_f32_e32 v44, s26, v56
	v_mul_f32_e32 v45, s26, v57
	v_mul_f32_e32 v42, s26, v54
	v_mul_f32_e32 v43, s26, v55
	s_mov_b64 s[42:43], 0x48000
	v_cvt_pk_bf16_f32 v42, v42, v43
	v_cvt_pk_bf16_f32 v43, v44, v45
	v_cvt_pk_bf16_f32 v44, v46, v47
	v_add_co_u32_e32 v46, vcc, s1, v138
	v_cvt_pk_bf16_f32 v45, v48, v49
	s_nop 0
	v_addc_co_u32_e32 v47, vcc, 0, v139, vcc
	global_store_dwordx4 v[46:47], v[42:45], off
	v_mul_f32_e32 v36, s26, v36
	v_mul_f32_e32 v37, s26, v37
	v_mul_f32_e32 v34, s26, v34
	v_mul_f32_e32 v35, s26, v35
	v_mul_f32_e32 v42, s26, v28
	v_mul_f32_e32 v43, s26, v29
	v_mul_f32_e32 v28, s26, v26
	v_mul_f32_e32 v29, s26, v27
	v_lshl_add_u64 v[50:51], v[138:139], 0, s[42:43]
	v_cvt_pk_bf16_f32 v26, v34, v35
	v_cvt_pk_bf16_f32 v27, v36, v37
	v_cvt_pk_bf16_f32 v28, v28, v29
	v_cvt_pk_bf16_f32 v29, v42, v43
	global_store_dwordx4 v[50:51], v[26:29], off offset:256
	v_mul_f32_e32 v30, s26, v30
	v_mul_f32_e32 v31, s26, v31
	s_mov_b32 s1, 0x50000
	v_mul_f32_e32 v28, s26, v40
	v_mul_f32_e32 v29, s26, v41
	v_mul_f32_e32 v26, s26, v38
	v_mul_f32_e32 v27, s26, v39
	v_mul_f32_e32 v32, s26, v32
	v_mul_f32_e32 v33, s26, v33
	v_cvt_pk_bf16_f32 v26, v26, v27
	v_cvt_pk_bf16_f32 v27, v28, v29
	v_cvt_pk_bf16_f32 v28, v30, v31
	v_add_co_u32_e32 v30, vcc, s1, v138
	v_cvt_pk_bf16_f32 v29, v32, v33
	s_nop 0
	v_addc_co_u32_e32 v31, vcc, 0, v139, vcc
	global_store_dwordx4 v[30:31], v[26:29], off
	v_mul_f32_e32 v20, s26, v20
	v_mul_f32_e32 v21, s26, v21
	v_mul_f32_e32 v18, s26, v18
	v_mul_f32_e32 v19, s26, v19
	v_mul_f32_e32 v26, s26, v12
	v_mul_f32_e32 v27, s26, v13
	v_mul_f32_e32 v12, s26, v10
	v_mul_f32_e32 v13, s26, v11
	v_lshl_add_u64 v[34:35], v[138:139], 0, s[22:23]
	v_cvt_pk_bf16_f32 v10, v18, v19
	v_cvt_pk_bf16_f32 v11, v20, v21
	v_cvt_pk_bf16_f32 v12, v12, v13
	v_cvt_pk_bf16_f32 v13, v26, v27
	global_store_dwordx4 v[34:35], v[10:13], off offset:256
	v_mul_f32_e32 v14, s26, v14
	v_mul_f32_e32 v15, s26, v15
	s_mov_b32 s1, 0x58000
	v_mul_f32_e32 v12, s26, v24
	v_mul_f32_e32 v13, s26, v25
	v_mul_f32_e32 v10, s26, v22
	v_mul_f32_e32 v11, s26, v23
	v_mul_f32_e32 v16, s26, v16
	v_mul_f32_e32 v17, s26, v17
	v_cvt_pk_bf16_f32 v10, v10, v11
	v_cvt_pk_bf16_f32 v11, v12, v13
	v_cvt_pk_bf16_f32 v12, v14, v15
	v_add_co_u32_e32 v14, vcc, s1, v138
	v_cvt_pk_bf16_f32 v13, v16, v17
	s_nop 0
	v_addc_co_u32_e32 v15, vcc, 0, v139, vcc
	s_mov_b64 s[42:43], 0x58000
	global_store_dwordx4 v[14:15], v[10:13], off
	v_mul_f32_e32 v8, s26, v8
	v_mul_f32_e32 v9, s26, v9
	v_mul_f32_e32 v6, s26, v6
	v_mul_f32_e32 v7, s26, v7
	v_mul_f32_e32 v10, s26, v4
	v_mul_f32_e32 v11, s26, v5
	v_mul_f32_e32 v4, s26, v2
	v_mul_f32_e32 v5, s26, v3
	v_lshl_add_u64 v[18:19], v[138:139], 0, s[42:43]
	v_cvt_pk_bf16_f32 v2, v6, v7
	v_cvt_pk_bf16_f32 v3, v8, v9
	v_cvt_pk_bf16_f32 v4, v4, v5
	v_cvt_pk_bf16_f32 v5, v10, v11
	s_and_b64 vcc, exec, s[36:37]
	s_mov_b64 s[36:37], -1
	global_store_dwordx4 v[18:19], v[2:5], off offset:256
	s_cbranch_vccnz .LBB0_1189
	v_readlane_b32 s36, v253, 50
	v_readlane_b32 s37, v253, 51
	s_andn2_b64 vcc, exec, s[36:37]
	s_cbranch_vccnz .LBB0_1188
	s_barrier
	s_branch .LBB0_1188

.LBB0_2009:
	s_waitcnt vmcnt(0)
	v_ffbh_u32_e32 v161, v157
	v_min_u32_e32 v161, 32, v161
	v_lshlrev_b64 v[156:157], v161, v[156:157]
	v_min_u32_e32 v156, 1, v156
	v_or_b32_e32 v156, v157, v156
	v_cvt_f32_u32_e32 v156, v156
	v_sub_u32_e32 v157, 32, v161
	s_mov_b32 s36, 0x358637bd
	v_mov_b64_e32 v[166:167], s[36:37]
	v_ldexp_f32 v157, v156, v157
	v_ffbh_u32_e32 v156, v155
	v_min_u32_e32 v156, 32, v156
	v_lshlrev_b64 v[154:155], v156, v[154:155]
	v_min_u32_e32 v154, 1, v154
	v_or_b32_e32 v154, v155, v154
	v_cvt_f32_u32_e32 v154, v154
	v_sub_u32_e32 v155, 32, v156
	s_mov_b32 s40, 0x32800000
	s_mov_b32 s29, -1
	v_ldexp_f32 v156, v154, v155
	v_fma_f32 v154, v156, s40, v166
	v_fma_f32 v155, v157, s40, v166
	s_movk_i32 s95, 0x100
	v_mul_f32_e32 v156, 0x4b800000, v155
	v_cmp_gt_f32_e64 s[36:37], s96, v155
	v_cmp_gt_f32_e32 vcc, s96, v154
	v_mbcnt_lo_u32_b32 v0, s29, 0
	v_cndmask_b32_e64 v155, v155, v156, s[36:37]
	v_rsq_f32_e32 v155, v155
	v_mbcnt_hi_u32_b32 v159, s29, v0
	s_lshl_b32 s29, s58, 8
	v_lshrrev_b32_e32 v160, 1, v159
	v_mul_f32_e32 v156, 0x45800000, v155
	v_cndmask_b32_e64 v156, v155, v156, s[36:37]
	v_mul_f32_e32 v155, 0x4b800000, v154
	v_cndmask_b32_e32 v154, v154, v155, vcc
	v_rsq_f32_e32 v154, v154
	v_and_b32_e32 v0, 15, v159
	s_add_i32 s29, s29, s34
	v_and_b32_e32 v160, 56, v160
	v_mul_f32_e32 v155, 0x45800000, v154
	v_cndmask_b32_e32 v154, v154, v155, vcc
	v_ffbh_u32_e32 v155, v153
	v_min_u32_e32 v155, 32, v155
	v_lshlrev_b64 v[152:153], v155, v[152:153]
	v_min_u32_e32 v152, 1, v152
	v_or_b32_e32 v152, v153, v152
	v_cvt_f32_u32_e32 v152, v152
	v_sub_u32_e32 v153, 32, v155
	v_or_b32_e32 v158, s29, v0
	v_add_u32_e32 v160, s85, v160
	v_ldexp_f32 v153, v152, v153
	v_ffbh_u32_e32 v152, v151
	v_min_u32_e32 v152, 32, v152
	v_lshlrev_b64 v[150:151], v152, v[150:151]
	v_min_u32_e32 v150, 1, v150
	v_or_b32_e32 v150, v151, v150
	v_cvt_f32_u32_e32 v150, v150
	v_sub_u32_e32 v151, 32, v152
	s_cmp_gt_i32 s50, 15
	v_ldexp_f32 v152, v150, v151
	v_fma_f32 v150, v152, s40, v166
	v_fma_f32 v151, v153, s40, v166
	s_nop 0
	v_mul_f32_e32 v152, 0x4b800000, v151
	v_cmp_gt_f32_e64 s[36:37], s96, v151
	v_cmp_gt_f32_e32 vcc, s96, v150
	s_nop 0
	v_cndmask_b32_e64 v151, v151, v152, s[36:37]
	v_rsq_f32_e32 v151, v151
	s_nop 0
	v_mul_f32_e32 v152, 0x45800000, v151
	v_cndmask_b32_e64 v152, v151, v152, s[36:37]
	v_mul_f32_e32 v151, 0x4b800000, v150
	v_cndmask_b32_e32 v150, v150, v151, vcc
	v_rsq_f32_e32 v150, v150
	s_nop 0
	v_mul_f32_e32 v151, 0x45800000, v150
	v_cndmask_b32_e32 v150, v150, v151, vcc
	v_ffbh_u32_e32 v151, v149
	v_min_u32_e32 v151, 32, v151
	v_lshlrev_b64 v[148:149], v151, v[148:149]
	v_min_u32_e32 v148, 1, v148
	v_or_b32_e32 v148, v149, v148
	v_cvt_f32_u32_e32 v148, v148
	v_sub_u32_e32 v149, 32, v151
	v_ldexp_f32 v149, v148, v149
	v_ffbh_u32_e32 v148, v147
	v_min_u32_e32 v148, 32, v148
	v_lshlrev_b64 v[146:147], v148, v[146:147]
	v_min_u32_e32 v146, 1, v146
	v_or_b32_e32 v146, v147, v146
	v_cvt_f32_u32_e32 v146, v146
	v_sub_u32_e32 v147, 32, v148
	v_ldexp_f32 v148, v146, v147
	v_fma_f32 v146, v148, s40, v166
	v_fma_f32 v147, v149, s40, v166
	s_nop 0
	v_mul_f32_e32 v148, 0x4b800000, v147
	v_cmp_gt_f32_e64 s[36:37], s96, v147
	v_cmp_gt_f32_e32 vcc, s96, v146
	s_nop 0
	v_cndmask_b32_e64 v147, v147, v148, s[36:37]
	v_rsq_f32_e32 v147, v147
	s_nop 0
	v_mul_f32_e32 v148, 0x45800000, v147
	v_cndmask_b32_e64 v148, v147, v148, s[36:37]
	v_mul_f32_e32 v147, 0x4b800000, v146
	v_cndmask_b32_e32 v146, v146, v147, vcc
	v_rsq_f32_e32 v146, v146
	s_nop 0
	v_mul_f32_e32 v147, 0x45800000, v146
	v_cndmask_b32_e32 v146, v146, v147, vcc
	v_ffbh_u32_e32 v147, v145
	v_min_u32_e32 v147, 32, v147
	v_lshlrev_b64 v[144:145], v147, v[144:145]
	v_min_u32_e32 v144, 1, v144
	v_or_b32_e32 v144, v145, v144
	v_cvt_f32_u32_e32 v144, v144
	v_sub_u32_e32 v145, 32, v147
	v_ldexp_f32 v145, v144, v145
	v_ffbh_u32_e32 v144, v143
	v_min_u32_e32 v144, 32, v144
	v_lshlrev_b64 v[142:143], v144, v[142:143]
	v_min_u32_e32 v142, 1, v142
	v_or_b32_e32 v142, v143, v142
	v_cvt_f32_u32_e32 v142, v142
	v_sub_u32_e32 v143, 32, v144
	v_ldexp_f32 v144, v142, v143
	v_fma_f32 v142, v144, s40, v166
	v_fma_f32 v143, v145, s40, v166
	s_nop 0
	v_mul_f32_e32 v144, 0x4b800000, v143
	v_cmp_gt_f32_e64 s[36:37], s96, v143
	v_cmp_gt_f32_e32 vcc, s96, v142
	s_nop 0
	v_cndmask_b32_e64 v143, v143, v144, s[36:37]
	v_rsq_f32_e32 v143, v143
	s_nop 0
	v_mul_f32_e32 v144, 0x45800000, v143
	v_cndmask_b32_e64 v144, v143, v144, s[36:37]
	v_mul_f32_e32 v143, 0x4b800000, v142
	v_cndmask_b32_e32 v142, v142, v143, vcc
	v_rsq_f32_e32 v142, v142
	s_mov_b64 s[36:37], -1
	v_mul_f32_e32 v143, 0x45800000, v142
	v_cndmask_b32_e32 v142, v142, v143, vcc
	s_cbranch_scc0 .LBB0_2021
	s_cmp_gt_u32 s50, 19
	s_cbranch_scc0 .LBB0_2018
	s_and_b64 vcc, exec, s[38:39]
	s_cbranch_vccz .LBB0_2015
	v_readlane_b32 s36, v253, 45
	v_cmp_gt_u32_e32 vcc, 16, v159
	v_readlane_b32 s37, v253, 46
	s_and_b64 s[40:41], s[36:37], vcc
	s_and_saveexec_b64 s[36:37], s[40:41]
	s_cbranch_execz .LBB0_2014
	v_ashrrev_i32_e32 v159, 31, v158
	v_lshlrev_b64 v[166:167], 5, v[158:159]
	v_mul_f32_e32 v172, 0x3d3504f3, v156
	v_lshl_add_u64 v[170:171], s[42:43], 0, v[166:167]
	v_mul_f32_e32 v168, v172, v128
	v_mul_f32_e32 v169, v172, v129
	v_mul_f32_e32 v166, v172, v126
	v_mul_f32_e32 v167, v172, v127
	global_store_dwordx4 v[170:171], v[166:169], off
	v_mul_f32_e32 v174, 0x3d3504f3, v154
	s_mov_b64 s[40:41], 0x1000
	v_mul_f32_e32 v168, v172, v124
	v_mul_f32_e32 v169, v172, v125
	v_mul_f32_e32 v166, v172, v122
	v_mul_f32_e32 v167, v172, v123
	global_store_dwordx4 v[170:171], v[166:169], off offset:16
	s_nop 1
	v_or_b32_e32 v166, 16, v158
	v_ashrrev_i32_e32 v167, 31, v166
	v_lshlrev_b64 v[166:167], 5, v[166:167]
	v_lshl_add_u64 v[172:173], s[42:43], 0, v[166:167]
	v_mul_f32_e32 v168, v174, v116
	v_mul_f32_e32 v169, v174, v117
	v_mul_f32_e32 v166, v174, v114
	v_mul_f32_e32 v167, v174, v115
	global_store_dwordx4 v[172:173], v[166:169], off
	s_nop 1
	v_mul_f32_e32 v168, v174, v108
	v_mul_f32_e32 v169, v174, v109
	v_mul_f32_e32 v166, v174, v106
	v_mul_f32_e32 v167, v174, v107
	global_store_dwordx4 v[172:173], v[166:169], off offset:16
	v_mul_f32_e32 v174, 0x3d3504f3, v152
	s_nop 0
	v_or_b32_e32 v166, 32, v158
	v_ashrrev_i32_e32 v167, 31, v166
	v_lshlrev_b64 v[166:167], 5, v[166:167]
	v_lshl_add_u64 v[172:173], s[42:43], 0, v[166:167]
	v_mul_f32_e32 v168, v174, v100
	v_mul_f32_e32 v169, v174, v101
	v_mul_f32_e32 v166, v174, v98
	v_mul_f32_e32 v167, v174, v99
	global_store_dwordx4 v[172:173], v[166:169], off
	s_nop 1
	v_mul_f32_e32 v168, v174, v92
	v_mul_f32_e32 v169, v174, v93
	v_mul_f32_e32 v166, v174, v90
	v_mul_f32_e32 v167, v174, v91
	global_store_dwordx4 v[172:173], v[166:169], off offset:16
	v_mul_f32_e32 v174, 0x3d3504f3, v150
	s_nop 0
	v_or_b32_e32 v166, 48, v158
	v_ashrrev_i32_e32 v167, 31, v166
	v_lshlrev_b64 v[166:167], 5, v[166:167]
	v_lshl_add_u64 v[172:173], s[42:43], 0, v[166:167]
	v_mul_f32_e32 v168, v174, v84
	v_mul_f32_e32 v169, v174, v85
	v_mul_f32_e32 v166, v174, v82
	v_mul_f32_e32 v167, v174, v83
	global_store_dwordx4 v[172:173], v[166:169], off
	s_nop 1
	v_mul_f32_e32 v168, v174, v76
	v_mul_f32_e32 v169, v174, v77
	v_mul_f32_e32 v166, v174, v74
	v_mul_f32_e32 v167, v174, v75
	global_store_dwordx4 v[172:173], v[166:169], off offset:16
	v_lshl_add_u64 v[172:173], v[170:171], 0, s[40:41]
	s_movk_i32 s40, 0x1000
	v_mul_f32_e32 v174, 0x3d3504f3, v148
	v_add_co_u32_e32 v176, vcc, s40, v170
	v_mul_f32_e32 v168, v174, v64
	v_mul_f32_e32 v169, v174, v65
	v_mul_f32_e32 v166, v174, v62
	v_mul_f32_e32 v167, v174, v63
	v_addc_co_u32_e32 v177, vcc, 0, v171, vcc
	global_store_dwordx4 v[176:177], v[166:169], off
	s_mov_b64 s[40:41], 0x1200
	s_nop 0
	v_mul_f32_e32 v168, v174, v60
	v_mul_f32_e32 v169, v174, v61
	v_mul_f32_e32 v166, v174, v58
	v_mul_f32_e32 v167, v174, v59
	v_mul_f32_e32 v174, 0x3d3504f3, v146
	global_store_dwordx4 v[172:173], v[166:169], off offset:16
	v_lshl_add_u64 v[172:173], v[170:171], 0, s[40:41]
	s_mov_b64 s[40:41], 0x1400
	v_mul_f32_e32 v168, v174, v56
	v_mul_f32_e32 v169, v174, v57
	v_mul_f32_e32 v166, v174, v54
	v_mul_f32_e32 v167, v174, v55
	global_store_dwordx4 v[176:177], v[166:169], off offset:512
	s_nop 1
	v_mul_f32_e32 v168, v174, v48
	v_mul_f32_e32 v169, v174, v49
	v_mul_f32_e32 v166, v174, v46
	v_mul_f32_e32 v167, v174, v47
	v_mul_f32_e32 v174, 0x3d3504f3, v144
	global_store_dwordx4 v[172:173], v[166:169], off offset:16
	v_lshl_add_u64 v[172:173], v[170:171], 0, s[40:41]
	s_mov_b64 s[40:41], 0x1600
	v_mul_f32_e32 v168, v174, v40
	v_mul_f32_e32 v169, v174, v41
	v_mul_f32_e32 v166, v174, v38
	v_mul_f32_e32 v167, v174, v39
	global_store_dwordx4 v[176:177], v[166:169], off offset:1024
	v_lshl_add_u64 v[170:171], v[170:171], 0, s[40:41]
	s_nop 0
	v_mul_f32_e32 v168, v174, v32
	v_mul_f32_e32 v169, v174, v33
	v_mul_f32_e32 v166, v174, v30
	v_mul_f32_e32 v167, v174, v31
	global_store_dwordx4 v[172:173], v[166:169], off offset:16
	v_mul_f32_e32 v172, 0x3d3504f3, v142
	s_nop 0
	v_mul_f32_e32 v168, v172, v24
	v_mul_f32_e32 v169, v172, v25
	v_mul_f32_e32 v166, v172, v22
	v_mul_f32_e32 v167, v172, v23
	global_store_dwordx4 v[176:177], v[166:169], off offset:1536
	s_nop 1
	v_mul_f32_e32 v168, v172, v16
	v_mul_f32_e32 v169, v172, v17
	v_mul_f32_e32 v166, v172, v14
	v_mul_f32_e32 v167, v172, v15
	global_store_dwordx4 v[170:171], v[166:169], off offset:16

.LBB0_2015:
	s_andn2_b64 vcc, exec, s[36:37]
	s_cbranch_vccnz .LBB0_2017
	s_ashr_i32 s36, s29, 5
	s_ashr_i32 s37, s36, 31
	s_lshl_b64 s[40:41], s[36:37], 12
	v_mul_f32_e32 v168, v156, v128
	v_mul_f32_e32 v169, v156, v129
	v_mul_f32_e32 v166, v156, v126
	v_mul_f32_e32 v167, v156, v127
	v_mul_f32_e32 v170, v156, v124
	v_mul_f32_e32 v171, v156, v125
	v_mul_f32_e32 v172, v156, v122
	v_mul_f32_e32 v173, v156, v123
	s_add_u32 s40, s44, s40
	v_lshlrev_b32_e32 v145, 6, v160
	v_cvt_pk_bf16_f32 v166, v166, v167
	v_cvt_pk_bf16_f32 v167, v168, v169
	v_cvt_pk_bf16_f32 v168, v172, v173
	v_cvt_pk_bf16_f32 v169, v170, v171
	s_addc_u32 s41, s45, s41
	v_lshl_or_b32 v145, v0, 4, v145
	s_or_b32 s36, s36, 1
	global_store_dwordx4 v145, v[166:169], s[40:41]
	v_mul_f32_e32 v170, v154, v108
	v_mul_f32_e32 v171, v154, v109
	v_mul_f32_e32 v172, v154, v106
	v_mul_f32_e32 v173, v154, v107
	v_mul_f32_e32 v168, v154, v116
	v_mul_f32_e32 v169, v154, v117
	v_mul_f32_e32 v166, v154, v114
	v_mul_f32_e32 v167, v154, v115
	s_ashr_i32 s37, s36, 31
	v_cvt_pk_bf16_f32 v166, v166, v167
	v_cvt_pk_bf16_f32 v167, v168, v169
	v_cvt_pk_bf16_f32 v168, v172, v173
	v_cvt_pk_bf16_f32 v169, v170, v171
	s_lshl_b64 s[36:37], s[36:37], 12
	global_store_dwordx4 v145, v[166:169], s[40:41] offset:256
	v_mul_f32_e32 v170, v152, v92
	v_mul_f32_e32 v171, v152, v93
	v_mul_f32_e32 v172, v152, v90
	v_mul_f32_e32 v173, v152, v91
	v_mul_f32_e32 v168, v152, v100
	v_mul_f32_e32 v169, v152, v101
	v_mul_f32_e32 v166, v152, v98
	v_mul_f32_e32 v167, v152, v99
	s_add_u32 s36, s44, s36
	v_cvt_pk_bf16_f32 v166, v166, v167
	v_cvt_pk_bf16_f32 v167, v168, v169
	v_cvt_pk_bf16_f32 v168, v172, v173
	v_cvt_pk_bf16_f32 v169, v170, v171
	s_addc_u32 s37, s45, s37
	global_store_dwordx4 v145, v[166:169], s[36:37]
	v_or_b32_e32 v0, 48, v158
	v_mul_f32_e32 v170, v150, v76
	v_mul_f32_e32 v171, v150, v77
	v_mul_f32_e32 v168, v150, v84
	v_mul_f32_e32 v169, v150, v85
	v_mul_f32_e32 v166, v150, v82
	v_mul_f32_e32 v167, v150, v83
	v_cvt_pk_bf16_f32 v166, v166, v167
	v_cvt_pk_bf16_f32 v167, v168, v169
	v_cvt_pk_bf16_f32 v169, v170, v171
	v_ashrrev_i32_e32 v170, 5, v0
	v_lshlrev_b32_e32 v143, 5, v160
	v_ashrrev_i32_e32 v171, 31, v170
	v_lshlrev_b32_e32 v0, 3, v0
	s_movk_i32 s40, 0xf8
	s_add_i32 s36, s29, 0x80
	v_lshlrev_b64 v[170:171], 12, v[170:171]
	v_and_or_b32 v0, v0, s40, v143
	s_ashr_i32 s36, s36, 5
	v_mul_f32_e32 v172, v150, v74
	v_mul_f32_e32 v173, v150, v75
	v_lshl_add_u64 v[170:171], s[44:45], 0, v[170:171]
	v_lshlrev_b32_e32 v0, 1, v0
	s_ashr_i32 s37, s36, 31
	v_cvt_pk_bf16_f32 v168, v172, v173
	v_lshl_add_u64 v[170:171], v[170:171], 0, v[0:1]
	s_lshl_b64 s[36:37], s[36:37], 12
	global_store_dwordx4 v[170:171], v[166:169], off
	v_mul_f32_e32 v170, v148, v60
	v_mul_f32_e32 v171, v148, v61
	v_mul_f32_e32 v172, v148, v58
	v_mul_f32_e32 v173, v148, v59
	v_mul_f32_e32 v168, v148, v64
	v_mul_f32_e32 v169, v148, v65
	v_mul_f32_e32 v166, v148, v62
	v_mul_f32_e32 v167, v148, v63
	s_add_u32 s36, s44, s36
	v_cvt_pk_bf16_f32 v166, v166, v167
	v_cvt_pk_bf16_f32 v167, v168, v169
	v_cvt_pk_bf16_f32 v168, v172, v173
	v_cvt_pk_bf16_f32 v169, v170, v171
	s_addc_u32 s37, s45, s37
	global_store_dwordx4 v145, v[166:169], s[36:37]
	v_add_u32_e32 v0, 0x90, v158
	v_mul_f32_e32 v170, v146, v48
	v_mul_f32_e32 v171, v146, v49
	v_mul_f32_e32 v168, v146, v56
	v_mul_f32_e32 v169, v146, v57
	v_mul_f32_e32 v166, v146, v54
	v_mul_f32_e32 v167, v146, v55
	v_cvt_pk_bf16_f32 v166, v166, v167
	v_cvt_pk_bf16_f32 v167, v168, v169
	v_cvt_pk_bf16_f32 v169, v170, v171
	v_ashrrev_i32_e32 v170, 5, v0
	v_ashrrev_i32_e32 v171, 31, v170
	v_lshlrev_b32_e32 v0, 3, v0
	s_addk_i32 s29, 0xa0
	v_lshlrev_b64 v[170:171], 12, v[170:171]
	v_and_or_b32 v0, v0, s40, v143
	s_ashr_i32 s36, s29, 5
	v_mul_f32_e32 v172, v146, v46
	v_mul_f32_e32 v173, v146, v47
	v_lshl_add_u64 v[170:171], s[44:45], 0, v[170:171]
	v_lshlrev_b32_e32 v0, 1, v0
	s_ashr_i32 s37, s36, 31
	v_cvt_pk_bf16_f32 v168, v172, v173
	v_lshl_add_u64 v[170:171], v[170:171], 0, v[0:1]
	s_lshl_b64 s[36:37], s[36:37], 12
	global_store_dwordx4 v[170:171], v[166:169], off
	v_mul_f32_e32 v170, v144, v32
	v_mul_f32_e32 v171, v144, v33
	v_mul_f32_e32 v172, v144, v30
	v_mul_f32_e32 v173, v144, v31
	v_mul_f32_e32 v168, v144, v40
	v_mul_f32_e32 v169, v144, v41
	v_mul_f32_e32 v166, v144, v38
	v_mul_f32_e32 v167, v144, v39
	s_add_u32 s36, s44, s36
	v_cvt_pk_bf16_f32 v166, v166, v167
	v_cvt_pk_bf16_f32 v167, v168, v169
	v_cvt_pk_bf16_f32 v168, v172, v173
	v_cvt_pk_bf16_f32 v169, v170, v171
	s_addc_u32 s37, s45, s37
	global_store_dwordx4 v145, v[166:169], s[36:37]
	v_add_u32_e32 v0, 0xb0, v158
	v_mul_f32_e32 v170, v142, v16
	v_mul_f32_e32 v171, v142, v17
	v_mul_f32_e32 v168, v142, v24
	v_mul_f32_e32 v169, v142, v25
	v_mul_f32_e32 v166, v142, v22
	v_mul_f32_e32 v167, v142, v23
	v_cvt_pk_bf16_f32 v166, v166, v167
	v_cvt_pk_bf16_f32 v167, v168, v169
	v_cvt_pk_bf16_f32 v169, v170, v171
	v_ashrrev_i32_e32 v170, 5, v0
	v_ashrrev_i32_e32 v171, 31, v170
	v_lshlrev_b32_e32 v0, 3, v0
	v_lshlrev_b64 v[170:171], 12, v[170:171]
	v_and_or_b32 v0, v0, s40, v143
	v_mul_f32_e32 v172, v142, v14
	v_mul_f32_e32 v173, v142, v15
	v_lshl_add_u64 v[170:171], s[44:45], 0, v[170:171]
	v_lshlrev_b32_e32 v0, 1, v0
	v_cvt_pk_bf16_f32 v168, v172, v173
	v_lshl_add_u64 v[170:171], v[170:171], 0, v[0:1]
	global_store_dwordx4 v[170:171], v[166:169], off

.LBB0_2018:
	s_andn2_b64 vcc, exec, s[36:37]
	s_cbranch_vccnz .LBB0_2020
	s_lshl_b32 s29, s50, 8
	s_add_u32 s36, s74, s29
	s_addc_u32 s37, s75, 0
	v_lshlrev_b32_e32 v0, 1, v160
	v_lshl_add_u64 v[166:167], s[36:37], 0, v[0:1]
	s_mov_b64 s[36:37], 0xd7ff000
	v_lshl_add_u64 v[170:171], v[166:167], 0, s[36:37]
	v_mul_f32_e32 v0, v156, v156
	v_mul_f32_e32 v166, v128, v120
	v_mul_f32_e32 v167, v129, v121
	v_mul_f32_e32 v168, v126, v118
	v_mul_f32_e32 v169, v127, v119
	v_mul_f32_e32 v172, v0, v166
	v_mul_f32_e32 v173, v0, v167
	v_mul_f32_e32 v166, v0, v168
	v_mul_f32_e32 v167, v0, v169
	v_mul_f32_e32 v168, v124, v112
	v_mul_f32_e32 v169, v125, v113
	v_mul_f32_e32 v174, v122, v110
	v_mul_f32_e32 v175, v123, v111
	v_ashrrev_i32_e32 v159, 31, v158
	v_mul_f32_e32 v176, v0, v168
	v_mul_f32_e32 v177, v0, v169
	v_mul_f32_e32 v168, v0, v174
	v_mul_f32_e32 v169, v0, v175
	v_cvt_pk_bf16_f32 v166, v166, v167
	v_cvt_pk_bf16_f32 v167, v172, v173
	v_lshlrev_b64 v[172:173], 10, v[158:159]
	v_cvt_pk_bf16_f32 v168, v168, v169
	v_cvt_pk_bf16_f32 v169, v176, v177
	v_lshl_add_u64 v[172:173], v[170:171], 0, v[172:173]
	global_store_dwordx4 v[172:173], v[166:169], off
	v_mul_f32_e32 v0, v154, v154
	v_mul_f32_e32 v176, v106, v94
	v_mul_f32_e32 v177, v107, v95
	v_mul_f32_e32 v166, v116, v104
	v_mul_f32_e32 v167, v117, v105
	v_mul_f32_e32 v168, v114, v102
	v_mul_f32_e32 v169, v115, v103
	v_mul_f32_e32 v174, v0, v166
	v_mul_f32_e32 v175, v0, v167
	v_mul_f32_e32 v166, v0, v168
	v_mul_f32_e32 v167, v0, v169
	v_cvt_pk_bf16_f32 v166, v166, v167
	v_cvt_pk_bf16_f32 v167, v174, v175
	v_or_b32_e32 v174, 16, v158
	v_mul_f32_e32 v168, v108, v96
	v_mul_f32_e32 v169, v109, v97
	v_ashrrev_i32_e32 v175, 31, v174
	v_mul_f32_e32 v178, v0, v168
	v_mul_f32_e32 v179, v0, v169
	v_mul_f32_e32 v168, v0, v176
	v_mul_f32_e32 v169, v0, v177
	v_lshlrev_b64 v[174:175], 10, v[174:175]
	v_cvt_pk_bf16_f32 v168, v168, v169
	v_cvt_pk_bf16_f32 v169, v178, v179
	v_lshl_add_u64 v[174:175], v[170:171], 0, v[174:175]
	global_store_dwordx4 v[174:175], v[166:169], off
	v_mul_f32_e32 v0, v152, v152
	v_mul_f32_e32 v176, v90, v78
	v_mul_f32_e32 v177, v91, v79
	v_mul_f32_e32 v166, v100, v88
	v_mul_f32_e32 v167, v101, v89
	v_mul_f32_e32 v168, v98, v86
	v_mul_f32_e32 v169, v99, v87
	v_mul_f32_e32 v174, v0, v166
	v_mul_f32_e32 v175, v0, v167
	v_mul_f32_e32 v166, v0, v168
	v_mul_f32_e32 v167, v0, v169
	v_cvt_pk_bf16_f32 v166, v166, v167
	v_cvt_pk_bf16_f32 v167, v174, v175
	v_or_b32_e32 v174, 32, v158
	v_mul_f32_e32 v168, v92, v80
	v_mul_f32_e32 v169, v93, v81
	v_ashrrev_i32_e32 v175, 31, v174
	v_mul_f32_e32 v178, v0, v168
	v_mul_f32_e32 v179, v0, v169
	v_mul_f32_e32 v168, v0, v176
	v_mul_f32_e32 v169, v0, v177
	v_lshlrev_b64 v[174:175], 10, v[174:175]
	v_cvt_pk_bf16_f32 v168, v168, v169
	v_cvt_pk_bf16_f32 v169, v178, v179
	v_lshl_add_u64 v[174:175], v[170:171], 0, v[174:175]
	global_store_dwordx4 v[174:175], v[166:169], off
	v_mul_f32_e32 v0, v150, v150
	v_mul_f32_e32 v176, v74, v66
	v_mul_f32_e32 v177, v75, v67
	v_mul_f32_e32 v166, v84, v72
	v_mul_f32_e32 v167, v85, v73
	v_mul_f32_e32 v168, v82, v70
	v_mul_f32_e32 v169, v83, v71
	v_mul_f32_e32 v174, v0, v166
	v_mul_f32_e32 v175, v0, v167
	v_mul_f32_e32 v166, v0, v168
	v_mul_f32_e32 v167, v0, v169
	v_cvt_pk_bf16_f32 v166, v166, v167
	v_cvt_pk_bf16_f32 v167, v174, v175
	v_or_b32_e32 v174, 48, v158
	v_mul_f32_e32 v168, v76, v68
	v_mul_f32_e32 v169, v77, v69
	v_ashrrev_i32_e32 v175, 31, v174
	v_mul_f32_e32 v178, v0, v168
	v_mul_f32_e32 v179, v0, v169
	v_mul_f32_e32 v168, v0, v176
	v_mul_f32_e32 v169, v0, v177
	v_lshlrev_b64 v[174:175], 10, v[174:175]
	v_cvt_pk_bf16_f32 v168, v168, v169
	v_cvt_pk_bf16_f32 v169, v178, v179
	v_lshl_add_u64 v[170:171], v[170:171], 0, v[174:175]
	global_store_dwordx4 v[170:171], v[166:169], off
	v_mul_f32_e32 v0, v148, v148
	v_mul_f32_e32 v174, v58, v42
	v_mul_f32_e32 v175, v59, v43
	v_mul_f32_e32 v166, v64, v52
	v_mul_f32_e32 v167, v65, v53
	v_mul_f32_e32 v168, v62, v50
	v_mul_f32_e32 v169, v63, v51
	v_mul_f32_e32 v170, v0, v166
	v_mul_f32_e32 v171, v0, v167
	v_mul_f32_e32 v166, v0, v168
	v_mul_f32_e32 v167, v0, v169
	v_mul_f32_e32 v168, v60, v44
	v_mul_f32_e32 v169, v61, v45
	s_mov_b32 s29, 0x20000
	v_mul_f32_e32 v176, v0, v168
	v_mul_f32_e32 v177, v0, v169
	v_mul_f32_e32 v168, v0, v174
	v_mul_f32_e32 v169, v0, v175
	v_cvt_pk_bf16_f32 v166, v166, v167
	v_cvt_pk_bf16_f32 v167, v170, v171
	v_add_co_u32_e32 v170, vcc, s29, v172
	v_cvt_pk_bf16_f32 v168, v168, v169
	v_cvt_pk_bf16_f32 v169, v176, v177
	v_addc_co_u32_e32 v171, vcc, 0, v173, vcc
	global_store_dwordx4 v[170:171], v[166:169], off
	v_mul_f32_e32 v0, v146, v146
	v_mul_f32_e32 v174, v46, v26
	v_mul_f32_e32 v175, v47, v27
	v_mul_f32_e32 v166, v56, v36
	v_mul_f32_e32 v167, v57, v37
	v_mul_f32_e32 v168, v54, v34
	v_mul_f32_e32 v169, v55, v35
	v_mul_f32_e32 v170, v0, v166
	v_mul_f32_e32 v171, v0, v167
	v_mul_f32_e32 v166, v0, v168
	v_mul_f32_e32 v167, v0, v169
	v_mul_f32_e32 v168, v48, v28
	v_mul_f32_e32 v169, v49, v29
	s_mov_b32 s29, 0x24000
	v_mul_f32_e32 v176, v0, v168
	v_mul_f32_e32 v177, v0, v169
	v_mul_f32_e32 v168, v0, v174
	v_mul_f32_e32 v169, v0, v175
	v_cvt_pk_bf16_f32 v166, v166, v167
	v_cvt_pk_bf16_f32 v167, v170, v171
	v_add_co_u32_e32 v170, vcc, s29, v172
	v_cvt_pk_bf16_f32 v168, v168, v169
	v_cvt_pk_bf16_f32 v169, v176, v177
	v_addc_co_u32_e32 v171, vcc, 0, v173, vcc
	global_store_dwordx4 v[170:171], v[166:169], off
	v_mul_f32_e32 v0, v144, v144
	v_mul_f32_e32 v174, v30, v10
	v_mul_f32_e32 v175, v31, v11
	v_mul_f32_e32 v166, v40, v20
	v_mul_f32_e32 v167, v41, v21
	v_mul_f32_e32 v168, v38, v18
	v_mul_f32_e32 v169, v39, v19
	v_mul_f32_e32 v170, v0, v166
	v_mul_f32_e32 v171, v0, v167
	v_mul_f32_e32 v166, v0, v168
	v_mul_f32_e32 v167, v0, v169
	v_mul_f32_e32 v168, v32, v12
	v_mul_f32_e32 v169, v33, v13
	s_mov_b32 s29, 0x28000
	v_mul_f32_e32 v176, v0, v168
	v_mul_f32_e32 v177, v0, v169
	v_mul_f32_e32 v168, v0, v174
	v_mul_f32_e32 v169, v0, v175
	v_cvt_pk_bf16_f32 v166, v166, v167
	v_cvt_pk_bf16_f32 v167, v170, v171
	v_add_co_u32_e32 v170, vcc, s29, v172
	v_cvt_pk_bf16_f32 v168, v168, v169
	v_cvt_pk_bf16_f32 v169, v176, v177
	v_addc_co_u32_e32 v171, vcc, 0, v173, vcc
	global_store_dwordx4 v[170:171], v[166:169], off
	v_mul_f32_e32 v0, v142, v142
	v_mul_f32_e32 v174, v14, v2
	v_mul_f32_e32 v175, v15, v3
	v_mul_f32_e32 v166, v24, v8
	v_mul_f32_e32 v167, v25, v9
	v_mul_f32_e32 v168, v22, v6
	v_mul_f32_e32 v169, v23, v7
	v_mul_f32_e32 v170, v0, v166
	v_mul_f32_e32 v171, v0, v167
	v_mul_f32_e32 v166, v0, v168
	v_mul_f32_e32 v167, v0, v169
	v_mul_f32_e32 v168, v16, v4
	v_mul_f32_e32 v169, v17, v5
	v_cvt_pk_bf16_f32 v166, v166, v167
	v_mul_f32_e32 v176, v0, v168
	v_mul_f32_e32 v177, v0, v169
	v_mul_f32_e32 v168, v0, v174
	v_mul_f32_e32 v169, v0, v175
	v_cvt_pk_bf16_f32 v167, v170, v171
	v_add_co_u32_e32 v170, vcc, 0x2c000, v172
	v_cvt_pk_bf16_f32 v168, v168, v169
	v_cvt_pk_bf16_f32 v169, v176, v177
	v_addc_co_u32_e32 v171, vcc, 0, v173, vcc
	global_store_dwordx4 v[170:171], v[166:169], off

.LBB0_2042:
	s_cmp_eq_u32 s29, 3
	s_cselect_b64 s[40:41], -1, 0
	s_or_b64 vcc, s[36:37], s[40:41]
	s_add_u32 s29, s74, s60
	s_addc_u32 s37, s75, s61
	s_lshl_b32 s36, s50, 9
	s_and_b32 s36, s36, 0x200
	v_mov_b32_e32 v0, 0x3e38aa3b
	s_add_u32 s36, s29, s36
	v_cndmask_b32_e32 v143, 1.0, v0, vcc
	s_addc_u32 s37, s37, 0
	v_lshlrev_b32_e32 v0, 1, v160
	v_lshl_add_u64 v[166:167], s[36:37], 0, v[0:1]
	v_ashrrev_i32_e32 v159, 31, v158
	v_mul_f32_e32 v0, v143, v156
	v_lshlrev_b64 v[160:161], 10, v[158:159]
	v_mul_f32_e32 v128, v0, v128
	v_mul_f32_e32 v129, v0, v129
	v_mul_f32_e32 v126, v0, v126
	v_mul_f32_e32 v127, v0, v127
	v_mul_f32_e32 v156, v0, v124
	v_mul_f32_e32 v157, v0, v125
	v_mul_f32_e32 v124, v0, v122
	v_mul_f32_e32 v125, v0, v123
	v_lshl_add_u64 v[160:161], v[166:167], 0, v[160:161]
	v_cvt_pk_bf16_f32 v122, v126, v127
	v_cvt_pk_bf16_f32 v123, v128, v129
	v_cvt_pk_bf16_f32 v124, v124, v125
	v_cvt_pk_bf16_f32 v125, v156, v157
	global_store_dwordx4 v[160:161], v[122:125], off
	v_mul_f32_e32 v120, v0, v120
	v_mul_f32_e32 v121, v0, v121
	v_mul_f32_e32 v118, v0, v118
	v_mul_f32_e32 v119, v0, v119
	v_mul_f32_e32 v122, v0, v112
	v_mul_f32_e32 v123, v0, v113
	v_mul_f32_e32 v112, v0, v110
	v_mul_f32_e32 v113, v0, v111
	v_cvt_pk_bf16_f32 v110, v118, v119
	v_cvt_pk_bf16_f32 v111, v120, v121
	v_cvt_pk_bf16_f32 v112, v112, v113
	v_cvt_pk_bf16_f32 v113, v122, v123
	global_store_dwordx4 v[160:161], v[110:113], off offset:256
	v_mul_f32_e32 v0, v143, v154
	v_mul_f32_e32 v114, v0, v114
	v_mul_f32_e32 v115, v0, v115
	v_or_b32_e32 v110, 16, v158
	v_ashrrev_i32_e32 v111, 31, v110
	v_lshlrev_b64 v[110:111], 10, v[110:111]
	v_mul_f32_e32 v112, v0, v116
	v_mul_f32_e32 v113, v0, v117
	v_mul_f32_e32 v116, v0, v108
	v_mul_f32_e32 v117, v0, v109
	v_mul_f32_e32 v108, v0, v106
	v_mul_f32_e32 v109, v0, v107
	v_lshl_add_u64 v[110:111], v[166:167], 0, v[110:111]
	v_cvt_pk_bf16_f32 v106, v114, v115
	v_cvt_pk_bf16_f32 v107, v112, v113
	v_cvt_pk_bf16_f32 v108, v108, v109
	v_cvt_pk_bf16_f32 v109, v116, v117
	global_store_dwordx4 v[110:111], v[106:109], off
	v_mul_f32_e32 v104, v0, v104
	v_mul_f32_e32 v105, v0, v105
	v_mul_f32_e32 v102, v0, v102
	v_mul_f32_e32 v103, v0, v103
	v_mul_f32_e32 v106, v0, v96
	v_mul_f32_e32 v107, v0, v97
	v_mul_f32_e32 v96, v0, v94
	v_mul_f32_e32 v97, v0, v95
	v_cvt_pk_bf16_f32 v94, v102, v103
	v_cvt_pk_bf16_f32 v95, v104, v105
	v_cvt_pk_bf16_f32 v96, v96, v97
	v_cvt_pk_bf16_f32 v97, v106, v107
	global_store_dwordx4 v[110:111], v[94:97], off offset:256
	v_mul_f32_e32 v0, v143, v152
	v_mul_f32_e32 v98, v0, v98
	v_mul_f32_e32 v99, v0, v99
	v_or_b32_e32 v94, 32, v158
	v_ashrrev_i32_e32 v95, 31, v94
	v_lshlrev_b64 v[94:95], 10, v[94:95]
	v_mul_f32_e32 v96, v0, v100
	v_mul_f32_e32 v97, v0, v101
	v_mul_f32_e32 v100, v0, v92
	v_mul_f32_e32 v101, v0, v93
	v_mul_f32_e32 v92, v0, v90
	v_mul_f32_e32 v93, v0, v91
	v_lshl_add_u64 v[94:95], v[166:167], 0, v[94:95]
	v_cvt_pk_bf16_f32 v90, v98, v99
	v_cvt_pk_bf16_f32 v91, v96, v97
	v_cvt_pk_bf16_f32 v92, v92, v93
	v_cvt_pk_bf16_f32 v93, v100, v101
	global_store_dwordx4 v[94:95], v[90:93], off
	v_mul_f32_e32 v88, v0, v88
	v_mul_f32_e32 v89, v0, v89
	v_mul_f32_e32 v86, v0, v86
	v_mul_f32_e32 v87, v0, v87
	v_mul_f32_e32 v90, v0, v80
	v_mul_f32_e32 v91, v0, v81
	v_mul_f32_e32 v80, v0, v78
	v_mul_f32_e32 v81, v0, v79
	v_cvt_pk_bf16_f32 v78, v86, v87
	v_cvt_pk_bf16_f32 v79, v88, v89
	v_cvt_pk_bf16_f32 v80, v80, v81
	v_cvt_pk_bf16_f32 v81, v90, v91
	global_store_dwordx4 v[94:95], v[78:81], off offset:256
	v_mul_f32_e32 v0, v143, v150
	v_mul_f32_e32 v82, v0, v82
	v_mul_f32_e32 v83, v0, v83
	v_or_b32_e32 v78, 48, v158
	v_ashrrev_i32_e32 v79, 31, v78
	v_lshlrev_b64 v[78:79], 10, v[78:79]
	v_mul_f32_e32 v80, v0, v84
	v_mul_f32_e32 v81, v0, v85
	v_mul_f32_e32 v84, v0, v76
	v_mul_f32_e32 v85, v0, v77
	v_mul_f32_e32 v76, v0, v74
	v_mul_f32_e32 v77, v0, v75
	v_lshl_add_u64 v[78:79], v[166:167], 0, v[78:79]
	v_cvt_pk_bf16_f32 v74, v82, v83
	v_cvt_pk_bf16_f32 v75, v80, v81
	v_cvt_pk_bf16_f32 v76, v76, v77
	v_cvt_pk_bf16_f32 v77, v84, v85
	global_store_dwordx4 v[78:79], v[74:77], off
	v_mul_f32_e32 v72, v0, v72
	v_mul_f32_e32 v73, v0, v73
	v_mul_f32_e32 v70, v0, v70
	v_mul_f32_e32 v71, v0, v71
	v_mul_f32_e32 v74, v0, v68
	v_mul_f32_e32 v75, v0, v69
	v_mul_f32_e32 v68, v0, v66
	v_mul_f32_e32 v69, v0, v67
	v_mul_f32_e32 v0, v143, v148
	v_cvt_pk_bf16_f32 v66, v70, v71
	v_cvt_pk_bf16_f32 v67, v72, v73
	v_cvt_pk_bf16_f32 v68, v68, v69
	v_cvt_pk_bf16_f32 v69, v74, v75
	v_mul_f32_e32 v62, v0, v62
	v_mul_f32_e32 v63, v0, v63
	s_mov_b32 s29, 0x20000
	global_store_dwordx4 v[78:79], v[66:69], off offset:256
	v_mul_f32_e32 v64, v0, v64
	v_mul_f32_e32 v65, v0, v65
	v_mul_f32_e32 v52, v0, v52
	v_mul_f32_e32 v53, v0, v53
	v_mul_f32_e32 v68, v0, v60
	v_mul_f32_e32 v69, v0, v61
	v_mul_f32_e32 v60, v0, v58
	v_mul_f32_e32 v61, v0, v59
	v_cvt_pk_bf16_f32 v58, v62, v63
	v_add_co_u32_e32 v62, vcc, s29, v160
	v_cvt_pk_bf16_f32 v59, v64, v65
	v_cvt_pk_bf16_f32 v60, v60, v61
	v_cvt_pk_bf16_f32 v61, v68, v69
	v_addc_co_u32_e32 v63, vcc, 0, v161, vcc
	global_store_dwordx4 v[62:63], v[58:61], off
	v_mul_f32_e32 v50, v0, v50
	v_mul_f32_e32 v51, v0, v51
	v_lshl_add_u64 v[66:67], v[160:161], 0, s[24:25]
	v_mul_f32_e32 v58, v0, v44
	v_mul_f32_e32 v59, v0, v45
	v_mul_f32_e32 v44, v0, v42
	v_mul_f32_e32 v45, v0, v43
	v_cvt_pk_bf16_f32 v42, v50, v51
	v_cvt_pk_bf16_f32 v43, v52, v53
	v_cvt_pk_bf16_f32 v44, v44, v45
	v_cvt_pk_bf16_f32 v45, v58, v59
	v_mul_f32_e32 v0, v143, v146
	global_store_dwordx4 v[66:67], v[42:45], off offset:256
	v_mul_f32_e32 v46, v0, v46
	v_mul_f32_e32 v47, v0, v47
	s_mov_b32 s29, 0x24000
	v_mul_f32_e32 v44, v0, v56
	v_mul_f32_e32 v45, v0, v57
	v_mul_f32_e32 v42, v0, v54
	v_mul_f32_e32 v43, v0, v55
	v_mul_f32_e32 v48, v0, v48
	v_mul_f32_e32 v49, v0, v49
	v_cvt_pk_bf16_f32 v42, v42, v43
	v_cvt_pk_bf16_f32 v43, v44, v45
	v_cvt_pk_bf16_f32 v44, v46, v47
	v_add_co_u32_e32 v46, vcc, s29, v160
	v_cvt_pk_bf16_f32 v45, v48, v49
	s_nop 0
	v_addc_co_u32_e32 v47, vcc, 0, v161, vcc
	s_mov_b64 s[36:37], 0x24000
	global_store_dwordx4 v[46:47], v[42:45], off
	v_mul_f32_e32 v36, v0, v36
	v_mul_f32_e32 v37, v0, v37
	v_mul_f32_e32 v34, v0, v34
	v_mul_f32_e32 v35, v0, v35
	v_mul_f32_e32 v42, v0, v28
	v_mul_f32_e32 v43, v0, v29
	v_mul_f32_e32 v28, v0, v26
	v_mul_f32_e32 v29, v0, v27
	v_lshl_add_u64 v[50:51], v[160:161], 0, s[36:37]
	v_cvt_pk_bf16_f32 v26, v34, v35
	v_cvt_pk_bf16_f32 v27, v36, v37
	v_cvt_pk_bf16_f32 v28, v28, v29
	v_cvt_pk_bf16_f32 v29, v42, v43
	v_mul_f32_e32 v0, v143, v144
	global_store_dwordx4 v[50:51], v[26:29], off offset:256
	v_mul_f32_e32 v30, v0, v30
	v_mul_f32_e32 v31, v0, v31
	s_mov_b32 s29, 0x28000
	v_mul_f32_e32 v28, v0, v40
	v_mul_f32_e32 v29, v0, v41
	v_mul_f32_e32 v26, v0, v38
	v_mul_f32_e32 v27, v0, v39
	v_mul_f32_e32 v32, v0, v32
	v_mul_f32_e32 v33, v0, v33
	v_cvt_pk_bf16_f32 v26, v26, v27
	v_cvt_pk_bf16_f32 v27, v28, v29
	v_cvt_pk_bf16_f32 v28, v30, v31
	v_add_co_u32_e32 v30, vcc, s29, v160
	v_cvt_pk_bf16_f32 v29, v32, v33
	s_nop 0
	v_addc_co_u32_e32 v31, vcc, 0, v161, vcc
	s_mov_b64 s[36:37], 0x28000
	global_store_dwordx4 v[30:31], v[26:29], off
	v_mul_f32_e32 v20, v0, v20
	v_mul_f32_e32 v21, v0, v21
	v_mul_f32_e32 v18, v0, v18
	v_mul_f32_e32 v19, v0, v19
	v_mul_f32_e32 v26, v0, v12
	v_mul_f32_e32 v27, v0, v13
	v_mul_f32_e32 v12, v0, v10
	v_mul_f32_e32 v13, v0, v11
	v_lshl_add_u64 v[34:35], v[160:161], 0, s[36:37]
	v_cvt_pk_bf16_f32 v10, v18, v19
	v_cvt_pk_bf16_f32 v11, v20, v21
	v_cvt_pk_bf16_f32 v12, v12, v13
	v_cvt_pk_bf16_f32 v13, v26, v27
	v_mul_f32_e32 v0, v143, v142
	global_store_dwordx4 v[34:35], v[10:13], off offset:256
	v_mul_f32_e32 v14, v0, v14
	v_mul_f32_e32 v15, v0, v15
	s_mov_b32 s29, 0x2c000
	v_mul_f32_e32 v12, v0, v24
	v_mul_f32_e32 v13, v0, v25
	v_mul_f32_e32 v10, v0, v22
	v_mul_f32_e32 v11, v0, v23
	v_mul_f32_e32 v16, v0, v16
	v_mul_f32_e32 v17, v0, v17
	v_cvt_pk_bf16_f32 v10, v10, v11
	v_cvt_pk_bf16_f32 v11, v12, v13
	v_cvt_pk_bf16_f32 v12, v14, v15
	v_add_co_u32_e32 v14, vcc, s29, v160
	v_cvt_pk_bf16_f32 v13, v16, v17
	s_nop 0
	v_addc_co_u32_e32 v15, vcc, 0, v161, vcc
	s_mov_b64 s[36:37], 0x2c000
	global_store_dwordx4 v[14:15], v[10:13], off
	v_mul_f32_e32 v8, v0, v8
	v_mul_f32_e32 v9, v0, v9
	v_mul_f32_e32 v6, v0, v6
	v_mul_f32_e32 v7, v0, v7
	v_mul_f32_e32 v10, v0, v4
	v_mul_f32_e32 v11, v0, v5
	v_mul_f32_e32 v4, v0, v2
	v_mul_f32_e32 v5, v0, v3
	v_lshl_add_u64 v[18:19], v[160:161], 0, s[36:37]
	v_cvt_pk_bf16_f32 v2, v6, v7
	v_cvt_pk_bf16_f32 v3, v8, v9
	v_cvt_pk_bf16_f32 v4, v4, v5
	v_cvt_pk_bf16_f32 v5, v10, v11
	global_store_dwordx4 v[18:19], v[2:5], off offset:256
